# speedup vs baseline: 1.0240x; 1.0240x over previous
_Z16closed_form_mainPKfS0_PKiPf:
	s_load_dwordx8 s[16:23], s[0:1], 0x0
	s_lshr_b32 s6, s2, 3
	v_readfirstlane_b32 s0, v0
	s_mul_hi_u32 s7, s6, 0x24924925
	s_lshr_b32 s4, s0, 6
	s_and_b32 s0, s2, 7
	s_mul_i32 s1, s7, 7
	s_bfe_u32 s5, s2, 0x10003
	s_sub_i32 s1, s6, s1
	s_mul_i32 s36, s0, 7
	s_xor_b32 s3, s4, s5
	s_add_i32 s36, s36, s1
	s_waitcnt lgkmcnt(0)
	s_mov_b64 s[28:29], s[22:23]
	v_and_b32_e32 v19, 63, v0
	s_cmp_lt_u32 s36, 52
	s_mov_b64 s[0:1], -1
	s_cbranch_scc0 .LBB0_32
	s_mul_hi_u32 s0, s6, 0x20820821
	s_lshr_b32 s38, s0, 3
	s_mul_hi_u32 s0, s7, 0x1c71c71d
	s_mul_i32 s0, s0, 9
	s_sub_i32 s0, s7, s0
	v_add_u32_e32 v2, -3, v19
	v_mad_u64_u32 v[0:1], s[0:1], s0, 57, v[2:3]
	s_mov_b64 s[24:25], s[18:19]
	v_mov_b32_e32 v1, 0x200
	v_med3_i32 v1, v0, 0, v1
	s_mul_i32 s34, s36, 10
	s_and_b32 s17, s17, 0xffff
	s_and_b32 s25, s25, 0xffff
	v_cmp_gt_u32_e64 s[0:1], 57, v2
	s_mov_b32 s19, 0x20000
	s_mov_b32 s18, 0xe0e038
	s_mov_b32 s26, 0x606018
	s_mul_i32 s35, s38, 0x70701c
	s_mul_i32 s33, s38, 0x30300c
	v_lshlrev_b32_e32 v28, 2, v1
	v_mul_u32_u24_e32 v27, 12, v1
	v_lshlrev_b32_e32 v23, 4, v19
	s_cmp_lg_u32 s4, s5
	v_sub_u32_e64 v29, s34, 2 clamp
	s_cbranch_scc0 .LBB0_15
	s_setprio 2
	s_mov_b32 s27, s19
	s_and_b32 s21, s21, 0xffff
	s_mov_b32 s22, 0x202008
	s_mov_b32 s23, s19
	s_mul_i32 s38, s38, 0x101004
	s_movk_i32 s37, 0x80
	v_add_u32_e32 v18, -1, v0
	s_movk_i32 s4, 0x201
	s_movk_i32 s5, 0x1ff
	v_cmp_gt_u32_e64 s[40:41], s4, v0
	v_cmp_gt_u32_e64 s[42:43], s5, v18
	v_mov_b32_e32 v18, 0x42c80000
	v_mov_b32_e32 v22, 0x3de38e39
	v_mov_b32_e32 v26, 0x3a3d6628
	v_mov_b32_e32 v1, 0
	s_add_i32 s4, s34, -3
	s_max_i32 s4, s4, 0
	s_mul_i32 s4, s4, 0x804
	s_add_i32 s4, s4, s38
	buffer_load_dword v29, v28, s[20:23], s4 offen nt
	s_add_i32 s4, s34, -2
	s_max_i32 s4, s4, 0
	s_mul_i32 s4, s4, 0x804
	s_add_i32 s4, s4, s38
	buffer_load_dword v2, v28, s[20:23], s4 offen nt
	s_add_i32 s5, s34, -2
	s_max_i32 s5, s5, 0
	s_mul_i32 s6, s5, 0x804
	s_add_i32 s6, s6, s35
	s_add_i32 s7, s6, 0x606018
	s_mul_i32 s9, s5, 0x180c
	s_add_i32 s9, s9, s33
	s_add_i32 s4, s34, -1
	s_max_i32 s4, s4, 0
	s_mul_i32 s4, s4, 0x804
	s_add_i32 s4, s4, s38
	buffer_load_dword v3, v28, s[20:23], s4 offen nt
	buffer_load_dwordx3 v[8:10], v27, s[24:27], s9 offen nt
	buffer_load_dword v4, v28, s[16:19], s7 offen nt
	s_add_i32 s5, s34, -1
	s_max_i32 s5, s5, 0
	s_mul_i32 s6, s5, 0x804
	s_add_i32 s6, s6, s35
	s_add_i32 s7, s6, 0x606018
	s_mul_i32 s9, s5, 0x180c
	s_add_i32 s9, s9, s33
	s_add_i32 s4, s34, 0
	s_min_i32 s4, s4, 0x200
	s_mul_i32 s4, s4, 0x804
	s_add_i32 s4, s4, s38
	buffer_load_dword v16, v28, s[20:23], s4 offen nt
	buffer_load_dwordx3 v[12:14], v27, s[24:27], s9 offen nt
	buffer_load_dword v6, v28, s[16:19], s7 offen nt
	s_waitcnt vmcnt(6)
	s_add_i32 s4, s34, -3
	s_cmpk_lt_u32 s4, 0x201
	s_cselect_b64 s[12:13], s[40:41], 0
	v_cmp_eq_u32_e64 s[14:15], s37, v29
	s_and_b64 s[14:15], s[14:15], s[12:13]
	v_cndmask_b32_e64 v17, 0, 1, s[14:15]
	s_add_i32 s4, s34, -2
	s_cmpk_lt_u32 s4, 0x201
	s_cselect_b64 s[12:13], s[40:41], 0
	v_cmp_eq_u32_e64 s[14:15], s37, v2
	s_and_b64 s[14:15], s[14:15], s[12:13]
	v_cndmask_b32_e64 v20, 0, 1, s[14:15]
	s_nop 0
	v_or_b32_dpp v21, v17, v17 wave_shr:1 row_mask:0xf bank_mask:0xf bound_ctrl:1
	v_or_b32_dpp v24, v20, v20 wave_shr:1 row_mask:0xf bank_mask:0xf bound_ctrl:1
	s_nop 1
	v_or_b32_dpp v21, v17, v21 wave_shl:1 row_mask:0xf bank_mask:0xf bound_ctrl:1
	v_or_b32_dpp v24, v20, v24 wave_shl:1 row_mask:0xf bank_mask:0xf bound_ctrl:1
	s_nop 1
	v_or_b32_dpp v25, v21, v21 wave_shr:1 row_mask:0xf bank_mask:0xf bound_ctrl:1
	v_or_b32_dpp v30, v24, v24 wave_shr:1 row_mask:0xf bank_mask:0xf bound_ctrl:1
	s_nop 1
	v_or_b32_dpp v25, v21, v25 wave_shl:1 row_mask:0xf bank_mask:0xf bound_ctrl:1
	v_or_b32_dpp v30, v24, v30 wave_shl:1 row_mask:0xf bank_mask:0xf bound_ctrl:1
	v_mov_b32_e32 v17, 0
	v_mov_b32_e32 v24, 0
	s_add_i32 s5, s34, 0
	s_min_i32 s5, s5, 0x200
	s_mul_i32 s6, s5, 0x804
	s_add_i32 s6, s6, s35
	s_add_i32 s7, s6, 0x606018
	s_mul_i32 s9, s5, 0x180c
	s_add_i32 s9, s9, s33
	s_add_i32 s4, s34, 1
	s_min_i32 s4, s4, 0x200
	s_mul_i32 s4, s4, 0x804
	s_add_i32 s4, s4, s38
	buffer_load_dword v31, v28, s[20:23], s4 offen nt
	buffer_load_dwordx3 v[32:34], v27, s[24:27], s9 offen nt
	buffer_load_dword v20, v28, s[16:19], s7 offen nt
	s_waitcnt vmcnt(6)
	v_mov_b32_dpp v36, v8 wave_shr:1 row_mask:0xf bank_mask:0xf bound_ctrl:1
	v_mov_b32_dpp v37, v9 wave_shr:1 row_mask:0xf bank_mask:0xf bound_ctrl:1
	v_mov_b32_dpp v38, v10 wave_shr:1 row_mask:0xf bank_mask:0xf bound_ctrl:1
	v_mov_b32_dpp v40, v8 wave_shl:1 row_mask:0xf bank_mask:0xf bound_ctrl:1
	v_mov_b32_dpp v41, v9 wave_shl:1 row_mask:0xf bank_mask:0xf bound_ctrl:1
	v_mov_b32_dpp v42, v10 wave_shl:1 row_mask:0xf bank_mask:0xf bound_ctrl:1
	s_add_i32 s4, s34, -1
	s_cmpk_lt_u32 s4, 0x201
	s_cselect_b64 s[12:13], s[40:41], 0
	v_cmp_eq_u32_e64 s[14:15], s37, v3
	s_and_b64 s[14:15], s[14:15], s[12:13]
	v_cndmask_b32_e64 v44, 0, 1, s[14:15]
	v_mul_f32_e64 v46, v8, v8
	v_mul_f32_e64 v47, v8, v9
	v_mul_f32_e64 v48, v8, v10
	v_mul_f32_e64 v49, v9, v9
	v_mul_f32_e64 v50, v9, v10
	v_mul_f32_e64 v51, v10, v10
	v_or_b32_dpp v45, v44, v44 wave_shr:1 row_mask:0xf bank_mask:0xf bound_ctrl:1
	s_nop 1
	v_or_b32_dpp v45, v44, v45 wave_shl:1 row_mask:0xf bank_mask:0xf bound_ctrl:1
	s_nop 1
	v_or_b32_dpp v52, v45, v45 wave_shr:1 row_mask:0xf bank_mask:0xf bound_ctrl:1
	s_nop 1
	v_or_b32_dpp v52, v45, v52 wave_shl:1 row_mask:0xf bank_mask:0xf bound_ctrl:1
	v_or3_b32 v53, v52, v30, v25
	v_or3_b32 v53, v53, v17, v24
	s_add_i32 s4, s34, -4
	s_cmpk_lt_u32 s4, 0x1ff
	s_cselect_b64 s[12:13], s[42:43], 0
	v_cmp_ne_u32_e64 s[30:31], 0, v53
	s_and_b64 s[30:31], s[30:31], s[12:13]
	v_cndmask_b32_e64 v53, 0, 1.0, s[30:31]
	v_add_f32_e64 v44, v8, v36
	v_add_f32_e64 v45, v9, v37
	v_add_f32_e64 v54, v10, v38
	v_fma_f32 v46, v36, v36, v46
	v_fma_f32 v47, v36, v37, v47
	v_fma_f32 v48, v36, v38, v48
	v_fma_f32 v49, v37, v37, v49
	v_fma_f32 v50, v37, v38, v50
	v_fma_f32 v51, v38, v38, v51
	v_add_f32_dpp v61, v53, v53 wave_shr:1 row_mask:0xf bank_mask:0xf bound_ctrl:1
	v_add_f32_e64 v44, v44, v40
	v_add_f32_e64 v45, v45, v41
	v_add_f32_e64 v54, v54, v42
	v_fma_f32 v55, v40, v40, v46
	v_fma_f32 v56, v40, v41, v47
	v_fma_f32 v57, v40, v42, v48
	v_fma_f32 v58, v41, v41, v49
	v_fma_f32 v59, v41, v42, v50
	v_fma_f32 v60, v42, v42, v51
	v_add_f32_dpp v61, v53, v61 wave_shl:1 row_mask:0xf bank_mask:0xf bound_ctrl:1
	s_barrier
	v_mov_b32_dpp v46, v4 wave_shr:1 row_mask:0xf bank_mask:0xf bound_ctrl:1
	v_mov_b32_dpp v48, v4 wave_shl:1 row_mask:0xf bank_mask:0xf bound_ctrl:1
	v_mul_f32_e64 v50, v4, v8
	v_mul_f32_e64 v62, v4, v9
	v_mul_f32_e64 v64, v4, v10
	v_add_f32_e64 v66, v4, v46
	v_fma_f32 v50, v46, v36, v50
	v_fma_f32 v62, v46, v37, v62
	v_fma_f32 v64, v46, v38, v64
	v_add_f32_e64 v66, v66, v48
	v_fma_f32 v50, v48, v40, v50
	v_fma_f32 v62, v48, v41, v62
	v_fma_f32 v64, v48, v42, v64
	s_add_i32 s5, s34, 1
	s_min_i32 s5, s5, 0x200
	s_mul_i32 s6, s5, 0x804
	s_add_i32 s6, s6, s35
	s_add_i32 s7, s6, 0x606018
	s_mul_i32 s9, s5, 0x180c
	s_add_i32 s9, s9, s33
	s_add_i32 s4, s34, 2
	s_min_i32 s4, s4, 0x200
	s_mul_i32 s4, s4, 0x804
	s_add_i32 s4, s4, s38
	buffer_load_dword v24, v28, s[20:23], s4 offen nt
	buffer_load_dwordx3 v[68:70], v27, s[24:27], s9 offen nt
	buffer_load_dword v46, v28, s[16:19], s7 offen nt
	s_waitcnt vmcnt(6)
	v_mov_b32_dpp v72, v12 wave_shr:1 row_mask:0xf bank_mask:0xf bound_ctrl:1
	v_mov_b32_dpp v73, v13 wave_shr:1 row_mask:0xf bank_mask:0xf bound_ctrl:1
	v_mov_b32_dpp v74, v14 wave_shr:1 row_mask:0xf bank_mask:0xf bound_ctrl:1
	v_mov_b32_dpp v76, v12 wave_shl:1 row_mask:0xf bank_mask:0xf bound_ctrl:1
	v_mov_b32_dpp v77, v13 wave_shl:1 row_mask:0xf bank_mask:0xf bound_ctrl:1
	v_mov_b32_dpp v78, v14 wave_shl:1 row_mask:0xf bank_mask:0xf bound_ctrl:1
	s_add_i32 s4, s34, 0
	s_cmpk_lt_u32 s4, 0x201
	s_cselect_b64 s[12:13], s[40:41], 0
	v_cmp_eq_u32_e64 s[14:15], s37, v16
	s_and_b64 s[14:15], s[14:15], s[12:13]
	v_cndmask_b32_e64 v53, 0, 1, s[14:15]
	v_mul_f32_e64 v48, v12, v12
	v_mul_f32_e64 v49, v12, v13
	v_mul_f32_e64 v80, v12, v14
	v_mul_f32_e64 v81, v13, v13
	v_mul_f32_e64 v82, v13, v14
	v_mul_f32_e64 v83, v14, v14
	v_or_b32_dpp v84, v53, v53 wave_shr:1 row_mask:0xf bank_mask:0xf bound_ctrl:1
	s_nop 1
	v_or_b32_dpp v84, v53, v84 wave_shl:1 row_mask:0xf bank_mask:0xf bound_ctrl:1
	s_nop 1
	v_or_b32_dpp v85, v84, v84 wave_shr:1 row_mask:0xf bank_mask:0xf bound_ctrl:1
	s_nop 1
	v_or_b32_dpp v85, v84, v85 wave_shl:1 row_mask:0xf bank_mask:0xf bound_ctrl:1
	v_or3_b32 v53, v85, v52, v30
	v_or3_b32 v53, v53, v25, v17
	s_add_i32 s4, s34, -3
	s_cmpk_lt_u32 s4, 0x1ff
	s_cselect_b64 s[12:13], s[42:43], 0
	v_cmp_ne_u32_e64 s[30:31], 0, v53
	s_and_b64 s[30:31], s[30:31], s[12:13]
	v_cndmask_b32_e64 v53, 0, 1.0, s[30:31]
	v_add_f32_e64 v86, v12, v72
	v_add_f32_e64 v87, v13, v73
	v_add_f32_e64 v88, v14, v74
	v_fma_f32 v48, v72, v72, v48
	v_fma_f32 v49, v72, v73, v49
	v_fma_f32 v80, v72, v74, v80
	v_fma_f32 v81, v73, v73, v81
	v_fma_f32 v82, v73, v74, v82
	v_fma_f32 v83, v74, v74, v83
	v_add_f32_dpp v95, v53, v53 wave_shr:1 row_mask:0xf bank_mask:0xf bound_ctrl:1
	v_add_f32_e64 v86, v86, v76
	v_add_f32_e64 v87, v87, v77
	v_add_f32_e64 v88, v88, v78
	v_fma_f32 v89, v76, v76, v48
	v_fma_f32 v90, v76, v77, v49
	v_fma_f32 v91, v76, v78, v80
	v_fma_f32 v92, v77, v77, v81
	v_fma_f32 v93, v77, v78, v82
	v_fma_f32 v94, v78, v78, v83
	v_add_f32_dpp v95, v53, v95 wave_shl:1 row_mask:0xf bank_mask:0xf bound_ctrl:1
	s_barrier
	v_mov_b32_dpp v48, v6 wave_shr:1 row_mask:0xf bank_mask:0xf bound_ctrl:1
	v_mov_b32_dpp v80, v6 wave_shl:1 row_mask:0xf bank_mask:0xf bound_ctrl:1
	v_mul_f32_e64 v82, v6, v12
	v_mul_f32_e64 v96, v6, v13
	v_mul_f32_e64 v98, v6, v14
	v_add_f32_e64 v100, v6, v48
	v_fma_f32 v82, v48, v72, v82
	v_fma_f32 v96, v48, v73, v96
	v_fma_f32 v98, v48, v74, v98
	v_add_f32_e64 v100, v100, v80
	v_fma_f32 v82, v80, v76, v82
	v_fma_f32 v96, v80, v77, v96
	v_fma_f32 v98, v80, v78, v98
	s_add_i32 s5, s34, 2
	s_min_i32 s5, s5, 0x200
	s_mul_i32 s6, s5, 0x804
	s_add_i32 s6, s6, s35
	s_add_i32 s7, s6, 0x606018
	s_mul_i32 s9, s5, 0x180c
	s_add_i32 s9, s9, s33
	s_add_i32 s4, s34, 3
	s_min_i32 s4, s4, 0x200
	s_mul_i32 s4, s4, 0x804
	s_add_i32 s4, s4, s38
	buffer_load_dword v17, v28, s[20:23], s4 offen nt
	buffer_load_dwordx3 v[104:106], v27, s[24:27], s9 offen nt
	buffer_load_dword v48, v28, s[16:19], s7 offen nt
	s_waitcnt vmcnt(6)
	v_mov_b32_dpp v108, v32 wave_shr:1 row_mask:0xf bank_mask:0xf bound_ctrl:1
	v_mov_b32_dpp v109, v33 wave_shr:1 row_mask:0xf bank_mask:0xf bound_ctrl:1
	v_mov_b32_dpp v110, v34 wave_shr:1 row_mask:0xf bank_mask:0xf bound_ctrl:1
	v_mov_b32_dpp v112, v32 wave_shl:1 row_mask:0xf bank_mask:0xf bound_ctrl:1
	v_mov_b32_dpp v113, v33 wave_shl:1 row_mask:0xf bank_mask:0xf bound_ctrl:1
	v_mov_b32_dpp v114, v34 wave_shl:1 row_mask:0xf bank_mask:0xf bound_ctrl:1
	s_add_i32 s4, s34, 1
	s_cmpk_lt_u32 s4, 0x201
	s_cselect_b64 s[12:13], s[40:41], 0
	v_cmp_eq_u32_e64 s[14:15], s37, v31
	s_and_b64 s[14:15], s[14:15], s[12:13]
	v_cndmask_b32_e64 v29, 0, 1, s[14:15]
	v_mul_f32_e64 v80, v32, v32
	v_mul_f32_e64 v81, v32, v33
	v_mul_f32_e64 v102, v32, v34
	v_mul_f32_e64 v103, v33, v33
	v_mul_f32_e64 v116, v33, v34
	v_mul_f32_e64 v117, v34, v34
	v_or_b32_dpp v53, v29, v29 wave_shr:1 row_mask:0xf bank_mask:0xf bound_ctrl:1
	s_nop 1
	v_or_b32_dpp v53, v29, v53 wave_shl:1 row_mask:0xf bank_mask:0xf bound_ctrl:1
	s_nop 1
	v_or_b32_dpp v84, v53, v53 wave_shr:1 row_mask:0xf bank_mask:0xf bound_ctrl:1
	s_nop 1
	v_or_b32_dpp v84, v53, v84 wave_shl:1 row_mask:0xf bank_mask:0xf bound_ctrl:1
	v_or3_b32 v29, v84, v85, v52
	v_or3_b32 v29, v29, v30, v25
	s_add_i32 s4, s34, -2
	s_cmpk_lt_u32 s4, 0x1ff
	s_cselect_b64 s[12:13], s[42:43], 0
	v_cmp_ne_u32_e64 s[30:31], 0, v29
	s_and_b64 s[30:31], s[30:31], s[12:13]
	v_cndmask_b32_e64 v29, 0, 1.0, s[30:31]
	v_add_f32_e64 v118, v32, v108
	v_add_f32_e64 v119, v33, v109
	v_add_f32_e64 v120, v34, v110
	v_fma_f32 v80, v108, v108, v80
	v_fma_f32 v81, v108, v109, v81
	v_fma_f32 v102, v108, v110, v102
	v_fma_f32 v103, v109, v109, v103
	v_fma_f32 v116, v109, v110, v116
	v_fma_f32 v117, v110, v110, v117
	v_add_f32_dpp v127, v29, v29 wave_shr:1 row_mask:0xf bank_mask:0xf bound_ctrl:1
	v_add_f32_e64 v118, v118, v112
	v_add_f32_e64 v119, v119, v113
	v_add_f32_e64 v120, v120, v114
	v_fma_f32 v121, v112, v112, v80
	v_fma_f32 v122, v112, v113, v81
	v_fma_f32 v123, v112, v114, v102
	v_fma_f32 v124, v113, v113, v103
	v_fma_f32 v125, v113, v114, v116
	v_fma_f32 v126, v114, v114, v117
	v_add_f32_dpp v127, v29, v127 wave_shl:1 row_mask:0xf bank_mask:0xf bound_ctrl:1
	v_pk_add_f32 v[80:81], v[86:87], v[118:119]
	v_pk_add_f32 v[102:103], v[44:45], v[80:81]
	v_pk_add_f32 v[44:45], v[88:89], v[120:121]
	v_pk_add_f32 v[86:87], v[54:55], v[44:45]
	v_pk_add_f32 v[54:55], v[90:91], v[122:123]
	v_pk_add_f32 v[88:89], v[56:57], v[54:55]
	v_pk_add_f32 v[56:57], v[92:93], v[124:125]
	v_pk_add_f32 v[90:91], v[58:59], v[56:57]
	v_pk_add_f32 v[58:59], v[94:95], v[126:127]
	v_pk_add_f32 v[92:93], v[60:61], v[58:59]
	v_mul_f32_e64 v128, v102, v22
	v_mul_f32_e64 v129, v103, v22
	v_mul_f32_e64 v130, v86, v22
	v_fma_f32 v29, v87, v22, v26
	v_mul_f32_e64 v53, v88, v22
	v_mul_f32_e64 v60, v89, v22
	v_fma_f32 v61, v90, v22, v26
	v_mul_f32_e64 v94, v91, v22
	v_fma_f32 v95, v92, v22, v26
	v_fma_f32 v29, -v128, v128, v29
	v_fma_f32 v53, -v128, v129, v53
	v_fma_f32 v60, -v128, v130, v60
	v_fma_f32 v61, -v129, v129, v61
	v_fma_f32 v94, -v129, v130, v94
	v_fma_f32 v95, -v130, v130, v95
	v_mul_f32_e64 v116, v94, v94
	v_mul_f32_e64 v117, v53, v95
	v_mul_f32_e64 v140, v60, v61
	v_mul_f32_e64 v141, v60, v60
	v_mul_f32_e64 v142, v29, v94
	v_mul_f32_e64 v143, v53, v53
	v_fma_f32 v116, v61, v95, -v116
	v_fma_f32 v117, v60, v94, -v117
	v_fma_f32 v140, v53, v94, -v140
	v_fma_f32 v141, v29, v95, -v141
	v_fma_f32 v142, v53, v60, -v142
	v_fma_f32 v143, v29, v61, -v143
	v_mul_f32_e64 v144, v29, v116
	v_fma_f32 v144, v53, v117, v144
	v_fma_f32 v144, v60, v140, v144
	v_rcp_f32_e32 v144, v144
	v_cmp_ne_u32_e64 vcc, s37, v2
	v_mul_f32_e64 v144, v144, v22
	v_cndmask_b32_e64 v144, 0, v144, s[30:31]
	v_cndmask_b32_e64 v29, 0, v18, vcc
	v_cndmask_b32_e64 v137, 0, v22, s[30:31]
	v_mul_f32_e64 v131, v116, v144
	v_mul_f32_e64 v132, v117, v144
	v_mul_f32_e64 v133, v140, v144
	v_mul_f32_e64 v134, v141, v144
	v_mul_f32_e64 v135, v142, v144
	v_mul_f32_e64 v136, v143, v144
	v_add_f32_e64 v138, v93, v29
	v_mov_b32_e32 v139, v2
	ds_write_b128 v23, v[128:131]
	ds_write_b128 v23, v[132:135] offset:1024
	ds_write_b128 v23, v[136:139] offset:2048
	s_waitcnt lgkmcnt(0)
	s_barrier
	v_mov_b32_dpp v60, v20 wave_shr:1 row_mask:0xf bank_mask:0xf bound_ctrl:1
	v_mov_b32_dpp v86, v20 wave_shl:1 row_mask:0xf bank_mask:0xf bound_ctrl:1
	v_mul_f32_e64 v88, v20, v32
	v_mul_f32_e64 v90, v20, v33
	v_mul_f32_e64 v92, v20, v34
	v_add_f32_e64 v94, v20, v60
	v_fma_f32 v88, v60, v108, v88
	v_fma_f32 v90, v60, v109, v90
	v_fma_f32 v92, v60, v110, v92
	v_add_f32_e64 v94, v94, v86
	v_fma_f32 v88, v86, v112, v88
	v_fma_f32 v90, v86, v113, v90
	v_fma_f32 v92, v86, v114, v92
	v_add_f32_e64 v60, v100, v94
	v_add_f32_e64 v86, v66, v60
	v_add_f32_e64 v66, v82, v88
	v_add_f32_e64 v100, v50, v66
	v_add_f32_e64 v50, v96, v90
	v_add_f32_e64 v82, v62, v50
	v_add_f32_e64 v62, v98, v92
	v_add_f32_e64 v96, v64, v62
	v_fma_f32 v100, -v128, v86, v100
	v_fma_f32 v82, -v129, v86, v82
	v_fma_f32 v96, -v130, v86, v96
	v_mul_f32_e64 v64, v131, v100
	v_mul_f32_e64 v98, v132, v100
	v_mul_f32_e64 v102, v133, v100
	v_fma_f32 v64, v132, v82, v64
	v_fma_f32 v98, v134, v82, v98
	v_fma_f32 v102, v135, v82, v102
	v_fma_f32 v64, v133, v96, v64
	v_fma_f32 v98, v135, v96, v98
	v_fma_f32 v102, v136, v96, v102
	v_mul_f32_e64 v116, v128, v64
	v_fma_f32 v116, v129, v98, v116
	v_fma_f32 v116, v130, v102, v116
	v_fma_f32 v116, v137, v86, -v116
	s_add_i32 s5, s34, 3
	s_min_i32 s5, s5, 0x200
	s_mul_i32 s6, s5, 0x804
	s_add_i32 s6, s6, s35
	s_add_i32 s7, s6, 0x606018
	s_mul_i32 s9, s5, 0x180c
	s_add_i32 s9, s9, s33
	s_add_i32 s4, s34, 4
	s_min_i32 s4, s4, 0x200
	s_mul_i32 s4, s4, 0x804
	s_add_i32 s4, s4, s38
	buffer_load_dword v2, v28, s[20:23], s4 offen nt
	buffer_load_dwordx3 v[8:10], v27, s[24:27], s9 offen nt
	buffer_load_dword v4, v28, s[16:19], s7 offen nt
	s_waitcnt vmcnt(6)
	v_mov_b32_dpp v36, v68 wave_shr:1 row_mask:0xf bank_mask:0xf bound_ctrl:1
	v_mov_b32_dpp v37, v69 wave_shr:1 row_mask:0xf bank_mask:0xf bound_ctrl:1
	v_mov_b32_dpp v38, v70 wave_shr:1 row_mask:0xf bank_mask:0xf bound_ctrl:1
	v_mov_b32_dpp v40, v68 wave_shl:1 row_mask:0xf bank_mask:0xf bound_ctrl:1
	v_mov_b32_dpp v41, v69 wave_shl:1 row_mask:0xf bank_mask:0xf bound_ctrl:1
	v_mov_b32_dpp v42, v70 wave_shl:1 row_mask:0xf bank_mask:0xf bound_ctrl:1
	s_add_i32 s4, s34, 2
	s_cmpk_lt_u32 s4, 0x201
	s_cselect_b64 s[12:13], s[40:41], 0
	v_cmp_eq_u32_e64 s[14:15], s37, v24
	s_and_b64 s[14:15], s[14:15], s[12:13]
	v_cndmask_b32_e64 v25, 0, 1, s[14:15]
	v_mul_f32_e64 v82, v68, v68
	v_mul_f32_e64 v83, v68, v69
	v_mul_f32_e64 v86, v68, v70
	v_mul_f32_e64 v87, v69, v69
	v_mul_f32_e64 v96, v69, v70
	v_mul_f32_e64 v97, v70, v70
	v_or_b32_dpp v29, v25, v25 wave_shr:1 row_mask:0xf bank_mask:0xf bound_ctrl:1
	s_nop 1
	v_or_b32_dpp v29, v25, v29 wave_shl:1 row_mask:0xf bank_mask:0xf bound_ctrl:1
	s_nop 1
	v_or_b32_dpp v53, v29, v29 wave_shr:1 row_mask:0xf bank_mask:0xf bound_ctrl:1
	s_nop 1
	v_or_b32_dpp v53, v29, v53 wave_shl:1 row_mask:0xf bank_mask:0xf bound_ctrl:1
	v_or3_b32 v25, v53, v84, v85
	v_or3_b32 v25, v25, v52, v30
	s_add_i32 s4, s34, -1
	s_cmpk_lt_u32 s4, 0x1ff
	s_cselect_b64 s[12:13], s[42:43], 0
	v_cmp_ne_u32_e64 s[30:31], 0, v25
	s_and_b64 s[30:31], s[30:31], s[12:13]
	v_cndmask_b32_e64 v25, 0, 1.0, s[30:31]
	v_add_f32_e64 v100, v68, v36
	v_add_f32_e64 v101, v69, v37
	v_add_f32_e64 v128, v70, v38
	v_fma_f32 v82, v36, v36, v82
	v_fma_f32 v83, v36, v37, v83
	v_fma_f32 v86, v36, v38, v86
	v_fma_f32 v87, v37, v37, v87
	v_fma_f32 v96, v37, v38, v96
	v_fma_f32 v97, v38, v38, v97
	v_add_f32_dpp v135, v25, v25 wave_shr:1 row_mask:0xf bank_mask:0xf bound_ctrl:1
	v_add_f32_e64 v100, v100, v40
	v_add_f32_e64 v101, v101, v41
	v_add_f32_e64 v128, v128, v42
	v_fma_f32 v129, v40, v40, v82
	v_fma_f32 v130, v40, v41, v83
	v_fma_f32 v131, v40, v42, v86
	v_fma_f32 v132, v41, v41, v87
	v_fma_f32 v133, v41, v42, v96
	v_fma_f32 v134, v42, v42, v97
	v_add_f32_dpp v135, v25, v135 wave_shl:1 row_mask:0xf bank_mask:0xf bound_ctrl:1
	v_pk_add_f32 v[82:83], v[80:81], v[100:101]
	v_pk_add_f32 v[80:81], v[44:45], v[128:129]
	v_pk_add_f32 v[44:45], v[54:55], v[130:131]
	v_pk_add_f32 v[54:55], v[56:57], v[132:133]
	v_pk_add_f32 v[56:57], v[58:59], v[134:135]
	v_mul_f32_e64 v136, v82, v22
	v_mul_f32_e64 v137, v83, v22
	v_mul_f32_e64 v138, v80, v22
	v_fma_f32 v25, v81, v22, v26
	v_mul_f32_e64 v29, v44, v22
	v_mul_f32_e64 v58, v45, v22
	v_fma_f32 v59, v54, v22, v26
	v_mul_f32_e64 v86, v55, v22
	v_fma_f32 v87, v56, v22, v26
	v_fma_f32 v25, -v136, v136, v25
	v_fma_f32 v29, -v136, v137, v29
	v_fma_f32 v58, -v136, v138, v58
	v_fma_f32 v59, -v137, v137, v59
	v_fma_f32 v86, -v137, v138, v86
	v_fma_f32 v87, -v138, v138, v87
	v_mul_f32_e64 v96, v86, v86
	v_mul_f32_e64 v97, v29, v87
	v_mul_f32_e64 v148, v58, v59
	v_mul_f32_e64 v149, v58, v58
	v_mul_f32_e64 v150, v25, v86
	v_mul_f32_e64 v151, v29, v29
	v_fma_f32 v96, v59, v87, -v96
	v_fma_f32 v97, v58, v86, -v97
	v_fma_f32 v148, v29, v86, -v148
	v_fma_f32 v149, v25, v87, -v149
	v_fma_f32 v150, v29, v58, -v150
	v_fma_f32 v151, v25, v59, -v151
	v_mul_f32_e64 v152, v25, v96
	v_fma_f32 v152, v29, v97, v152
	v_fma_f32 v152, v58, v148, v152
	v_rcp_f32_e32 v152, v152
	v_cmp_ne_u32_e64 vcc, s37, v3
	v_mul_f32_e64 v152, v152, v22
	v_cndmask_b32_e64 v152, 0, v152, s[30:31]
	v_cndmask_b32_e64 v25, 0, v18, vcc
	v_cndmask_b32_e64 v145, 0, v22, s[30:31]
	v_mul_f32_e64 v139, v96, v152
	v_mul_f32_e64 v140, v97, v152
	v_mul_f32_e64 v141, v148, v152
	v_mul_f32_e64 v142, v149, v152
	v_mul_f32_e64 v143, v150, v152
	v_mul_f32_e64 v144, v151, v152
	v_add_f32_e64 v146, v57, v25
	v_mov_b32_e32 v147, v3
	ds_write_b128 v23, v[136:139] offset:3072
	ds_write_b128 v23, v[140:143] offset:4096
	ds_write_b128 v23, v[144:147] offset:5120
	s_waitcnt lgkmcnt(0)
	s_barrier
	v_mov_b32_dpp v44, v46 wave_shr:1 row_mask:0xf bank_mask:0xf bound_ctrl:1
	v_mov_b32_dpp v54, v46 wave_shl:1 row_mask:0xf bank_mask:0xf bound_ctrl:1
	v_mul_f32_e64 v56, v46, v68
	v_mul_f32_e64 v58, v46, v69
	v_mul_f32_e64 v80, v46, v70
	v_add_f32_e64 v82, v46, v44
	v_fma_f32 v56, v44, v36, v56
	v_fma_f32 v58, v44, v37, v58
	v_fma_f32 v80, v44, v38, v80
	v_add_f32_e64 v82, v82, v54
	v_fma_f32 v56, v54, v40, v56
	v_fma_f32 v58, v54, v41, v58
	v_fma_f32 v80, v54, v42, v80
	v_add_f32_e64 v44, v60, v82
	v_add_f32_e64 v54, v66, v56
	v_add_f32_e64 v60, v50, v58
	v_add_f32_e64 v50, v62, v80
	v_fma_f32 v54, -v136, v44, v54
	v_fma_f32 v60, -v137, v44, v60
	v_fma_f32 v50, -v138, v44, v50
	v_mul_f32_e64 v62, v139, v54
	v_mul_f32_e64 v66, v140, v54
	v_mul_f32_e64 v86, v141, v54
	v_fma_f32 v62, v140, v60, v62
	v_fma_f32 v66, v142, v60, v66
	v_fma_f32 v86, v143, v60, v86
	v_fma_f32 v62, v141, v50, v62
	v_fma_f32 v66, v143, v50, v66
	v_fma_f32 v86, v144, v50, v86
	v_mul_f32_e64 v96, v136, v62
	v_fma_f32 v96, v137, v66, v96
	v_fma_f32 v96, v138, v86, v96
	v_fma_f32 v96, v145, v44, -v96
	s_add_i32 s5, s34, 4
	s_min_i32 s5, s5, 0x200
	s_mul_i32 s6, s5, 0x804
	s_add_i32 s6, s6, s35
	s_add_i32 s7, s6, 0x606018
	s_mul_i32 s9, s5, 0x180c
	s_add_i32 s9, s9, s33
	s_add_i32 s4, s34, 5
	s_min_i32 s4, s4, 0x200
	s_mul_i32 s4, s4, 0x804
	s_add_i32 s4, s4, s38
	buffer_load_dword v3, v28, s[20:23], s4 offen nt
	buffer_load_dwordx3 v[12:14], v27, s[24:27], s9 offen nt
	buffer_load_dword v6, v28, s[16:19], s7 offen nt
	s_waitcnt vmcnt(6)
	v_mov_b32_dpp v72, v104 wave_shr:1 row_mask:0xf bank_mask:0xf bound_ctrl:1
	v_mov_b32_dpp v73, v105 wave_shr:1 row_mask:0xf bank_mask:0xf bound_ctrl:1
	v_mov_b32_dpp v74, v106 wave_shr:1 row_mask:0xf bank_mask:0xf bound_ctrl:1
	v_mov_b32_dpp v76, v104 wave_shl:1 row_mask:0xf bank_mask:0xf bound_ctrl:1
	v_mov_b32_dpp v77, v105 wave_shl:1 row_mask:0xf bank_mask:0xf bound_ctrl:1
	v_mov_b32_dpp v78, v106 wave_shl:1 row_mask:0xf bank_mask:0xf bound_ctrl:1
	s_add_i32 s4, s34, 3
	s_cmpk_lt_u32 s4, 0x201
	s_cselect_b64 s[12:13], s[40:41], 0
	v_cmp_eq_u32_e64 s[14:15], s37, v17
	s_and_b64 s[14:15], s[14:15], s[12:13]
	v_cndmask_b32_e64 v25, 0, 1, s[14:15]
	v_mul_f32_e64 v44, v104, v104
	v_mul_f32_e64 v45, v104, v105
	v_mul_f32_e64 v50, v104, v106
	v_mul_f32_e64 v51, v105, v105
	v_mul_f32_e64 v54, v105, v106
	v_mul_f32_e64 v55, v106, v106
	v_or_b32_dpp v29, v25, v25 wave_shr:1 row_mask:0xf bank_mask:0xf bound_ctrl:1
	s_nop 1
	v_or_b32_dpp v29, v25, v29 wave_shl:1 row_mask:0xf bank_mask:0xf bound_ctrl:1
	s_nop 1
	v_or_b32_dpp v30, v29, v29 wave_shr:1 row_mask:0xf bank_mask:0xf bound_ctrl:1
	s_nop 1
	v_or_b32_dpp v30, v29, v30 wave_shl:1 row_mask:0xf bank_mask:0xf bound_ctrl:1
	v_or3_b32 v25, v30, v53, v84
	v_or3_b32 v25, v25, v85, v52
	s_add_i32 s4, s34, 0
	s_cmpk_lt_u32 s4, 0x1ff
	s_cselect_b64 s[12:13], s[42:43], 0
	v_cmp_ne_u32_e64 s[30:31], 0, v25
	s_and_b64 s[30:31], s[30:31], s[12:13]
	v_cndmask_b32_e64 v25, 0, 1.0, s[30:31]
	v_add_f32_e64 v60, v104, v72
	v_add_f32_e64 v61, v105, v73
	v_add_f32_e64 v136, v106, v74
	v_fma_f32 v44, v72, v72, v44
	v_fma_f32 v45, v72, v73, v45
	v_fma_f32 v50, v72, v74, v50
	v_fma_f32 v51, v73, v73, v51
	v_fma_f32 v54, v73, v74, v54
	v_fma_f32 v55, v74, v74, v55
	v_add_f32_dpp v143, v25, v25 wave_shr:1 row_mask:0xf bank_mask:0xf bound_ctrl:1
	v_add_f32_e64 v60, v60, v76
	v_add_f32_e64 v61, v61, v77
	v_add_f32_e64 v136, v136, v78
	v_fma_f32 v137, v76, v76, v44
	v_fma_f32 v138, v76, v77, v45
	v_fma_f32 v139, v76, v78, v50
	v_fma_f32 v140, v77, v77, v51
	v_fma_f32 v141, v77, v78, v54
	v_fma_f32 v142, v78, v78, v55
	v_add_f32_dpp v143, v25, v143 wave_shl:1 row_mask:0xf bank_mask:0xf bound_ctrl:1
	v_pk_add_f32 v[44:45], v[100:101], v[60:61]
	v_pk_add_f32 v[50:51], v[118:119], v[44:45]
	v_pk_add_f32 v[54:55], v[128:129], v[136:137]
	v_pk_add_f32 v[100:101], v[120:121], v[54:55]
	v_pk_add_f32 v[118:119], v[130:131], v[138:139]
	v_pk_add_f32 v[120:121], v[122:123], v[118:119]
	v_pk_add_f32 v[122:123], v[132:133], v[140:141]
	v_pk_add_f32 v[128:129], v[124:125], v[122:123]
	v_pk_add_f32 v[124:125], v[134:135], v[142:143]
	v_pk_add_f32 v[130:131], v[126:127], v[124:125]
	v_mul_f32_e64 v132, v50, v22
	v_mul_f32_e64 v133, v51, v22
	v_mul_f32_e64 v134, v100, v22
	v_fma_f32 v25, v101, v22, v26
	v_mul_f32_e64 v29, v120, v22
	v_mul_f32_e64 v126, v121, v22
	v_fma_f32 v127, v128, v22, v26
	v_mul_f32_e64 v152, v129, v22
	v_fma_f32 v153, v130, v22, v26
	v_fma_f32 v25, -v132, v132, v25
	v_fma_f32 v29, -v132, v133, v29
	v_fma_f32 v126, -v132, v134, v126
	v_fma_f32 v127, -v133, v133, v127
	v_fma_f32 v152, -v133, v134, v152
	v_fma_f32 v153, -v134, v134, v153
	v_mul_f32_e64 v154, v152, v152
	v_mul_f32_e64 v155, v29, v153
	v_mul_f32_e64 v156, v126, v127
	v_mul_f32_e64 v157, v126, v126
	v_mul_f32_e64 v158, v25, v152
	v_mul_f32_e64 v159, v29, v29
	v_fma_f32 v154, v127, v153, -v154
	v_fma_f32 v155, v126, v152, -v155
	v_fma_f32 v156, v29, v152, -v156
	v_fma_f32 v157, v25, v153, -v157
	v_fma_f32 v158, v29, v126, -v158
	v_fma_f32 v159, v25, v127, -v159
	v_mul_f32_e64 v160, v25, v154
	v_fma_f32 v160, v29, v155, v160
	v_fma_f32 v160, v126, v156, v160
	v_rcp_f32_e32 v160, v160
	v_cmp_ne_u32_e64 vcc, s37, v16
	v_mul_f32_e64 v160, v160, v22
	v_cndmask_b32_e64 v160, 0, v160, s[30:31]
	v_cndmask_b32_e64 v25, 0, v18, vcc
	v_cndmask_b32_e64 v149, 0, v22, s[30:31]
	v_mul_f32_e64 v135, v154, v160
	v_mul_f32_e64 v144, v155, v160
	v_mul_f32_e64 v145, v156, v160
	v_mul_f32_e64 v146, v157, v160
	v_mul_f32_e64 v147, v158, v160
	v_mul_f32_e64 v148, v159, v160
	v_add_f32_e64 v150, v131, v25
	v_mov_b32_e32 v151, v16
	ds_write_b128 v23, v[132:135]
	ds_write_b128 v23, v[144:147] offset:1024
	ds_write_b128 v23, v[148:151] offset:2048
	s_waitcnt lgkmcnt(0)
	s_barrier
	v_mov_b32_dpp v50, v48 wave_shr:1 row_mask:0xf bank_mask:0xf bound_ctrl:1
	v_mov_b32_dpp v100, v48 wave_shl:1 row_mask:0xf bank_mask:0xf bound_ctrl:1
	v_mul_f32_e64 v120, v48, v104
	v_mul_f32_e64 v126, v48, v105
	v_mul_f32_e64 v128, v48, v106
	v_add_f32_e64 v130, v48, v50
	v_fma_f32 v120, v50, v72, v120
	v_fma_f32 v126, v50, v73, v126
	v_fma_f32 v128, v50, v74, v128
	v_add_f32_e64 v130, v130, v100
	v_fma_f32 v120, v100, v76, v120
	v_fma_f32 v126, v100, v77, v126
	v_fma_f32 v128, v100, v78, v128
	v_add_f32_e64 v50, v82, v130
	v_add_f32_e64 v100, v94, v50
	v_add_f32_e64 v82, v56, v120
	v_add_f32_e64 v94, v88, v82
	v_add_f32_e64 v56, v58, v126
	v_add_f32_e64 v88, v90, v56
	v_add_f32_e64 v58, v80, v128
	v_add_f32_e64 v90, v92, v58
	v_fma_f32 v94, -v132, v100, v94
	v_fma_f32 v88, -v133, v100, v88
	v_fma_f32 v90, -v134, v100, v90
	v_mul_f32_e64 v80, v135, v94
	v_mul_f32_e64 v92, v144, v94
	v_mul_f32_e64 v152, v145, v94
	v_fma_f32 v80, v144, v88, v80
	v_fma_f32 v92, v146, v88, v92
	v_fma_f32 v152, v147, v88, v152
	v_fma_f32 v80, v145, v90, v80
	v_fma_f32 v92, v147, v90, v92
	v_fma_f32 v152, v148, v90, v152
	v_mul_f32_e64 v154, v132, v80
	v_fma_f32 v154, v133, v92, v154
	v_fma_f32 v154, v134, v152, v154
	v_fma_f32 v154, v149, v100, -v154
	v_cmp_eq_u32_e64 s[10:11], 7, v151
	v_add_f32_e64 v88, v62, v80
	v_add_f32_e64 v90, v64, v88
	v_add_f32_e64 v62, v66, v92
	v_add_f32_e64 v64, v98, v62
	v_add_f32_e64 v66, v86, v152
	v_add_f32_e64 v94, v102, v66
	v_add_f32_e64 v86, v96, v154
	v_add_f32_e64 v98, v116, v86
	v_fma_f32 v96, v108, v90, v98
	v_fma_f32 v100, v112, v90, v98
	v_fma_f32 v96, v109, v64, v96
	v_fma_f32 v100, v113, v64, v100
	v_fma_f32 v96, v110, v94, v96
	v_fma_f32 v100, v114, v94, v100
	v_fma_f32 v98, v32, v90, v98
	v_fma_f32 v98, v33, v64, v98
	v_fma_f32 v98, v34, v94, v98
	v_cndmask_b32_e64 v102, 0, v18, s[10:11]
	v_add_f32_dpp v98, v96, v98 wave_shl:1 row_mask:0xf bank_mask:0xf bound_ctrl:1
	s_add_i32 s4, s34, 0
	s_cmpk_lt_i32 s4, 0x201
	s_cselect_b64 s[12:13], s[0:1], 0
	v_add_f32_dpp v98, v100, v98 wave_shr:1 row_mask:0xf bank_mask:0xf bound_ctrl:1
	v_fma_f32 v98, v20, v150, -v98
	v_add_f32_e64 v98, v98, -v102
	v_mul_f32_e64 v116, v98, v98
	v_cndmask_b32_e64 v117, 0, v116, s[12:13]
	v_add_f32_e32 v1, v1, v117
	s_add_i32 s5, s34, 5
	s_min_i32 s5, s5, 0x200
	s_mul_i32 s6, s5, 0x804
	s_add_i32 s6, s6, s35
	s_add_i32 s7, s6, 0x606018
	s_mul_i32 s9, s5, 0x180c
	s_add_i32 s9, s9, s33
	s_add_i32 s4, s34, 6
	s_min_i32 s4, s4, 0x200
	s_mul_i32 s4, s4, 0x804
	s_add_i32 s4, s4, s38
	buffer_load_dword v16, v28, s[20:23], s4 offen nt
	buffer_load_dwordx3 v[32:34], v27, s[24:27], s9 offen nt
	buffer_load_dword v20, v28, s[16:19], s7 offen nt
	s_waitcnt vmcnt(6)
	v_mov_b32_dpp v96, v8 wave_shr:1 row_mask:0xf bank_mask:0xf bound_ctrl:1
	v_mov_b32_dpp v97, v9 wave_shr:1 row_mask:0xf bank_mask:0xf bound_ctrl:1
	v_mov_b32_dpp v98, v10 wave_shr:1 row_mask:0xf bank_mask:0xf bound_ctrl:1
	v_mov_b32_dpp v100, v8 wave_shl:1 row_mask:0xf bank_mask:0xf bound_ctrl:1
	v_mov_b32_dpp v101, v9 wave_shl:1 row_mask:0xf bank_mask:0xf bound_ctrl:1
	v_mov_b32_dpp v102, v10 wave_shl:1 row_mask:0xf bank_mask:0xf bound_ctrl:1
	s_add_i32 s4, s34, 4
	s_cmpk_lt_u32 s4, 0x201
	s_cselect_b64 s[12:13], s[40:41], 0
	v_cmp_eq_u32_e64 s[14:15], s37, v2
	s_and_b64 s[14:15], s[14:15], s[12:13]
	v_cndmask_b32_e64 v25, 0, 1, s[14:15]
	v_mul_f32_e64 v64, v8, v8
	v_mul_f32_e64 v65, v8, v9
	v_mul_f32_e64 v90, v8, v10
	v_mul_f32_e64 v91, v9, v9
	v_mul_f32_e64 v94, v9, v10
	v_mul_f32_e64 v95, v10, v10
	v_or_b32_dpp v29, v25, v25 wave_shr:1 row_mask:0xf bank_mask:0xf bound_ctrl:1
	s_nop 1
	v_or_b32_dpp v29, v25, v29 wave_shl:1 row_mask:0xf bank_mask:0xf bound_ctrl:1
	s_nop 1
	v_or_b32_dpp v52, v29, v29 wave_shr:1 row_mask:0xf bank_mask:0xf bound_ctrl:1
	s_nop 1
	v_or_b32_dpp v52, v29, v52 wave_shl:1 row_mask:0xf bank_mask:0xf bound_ctrl:1
	v_or3_b32 v25, v52, v30, v53
	v_or3_b32 v25, v25, v84, v85
	s_add_i32 s4, s34, 1
	s_cmpk_lt_u32 s4, 0x1ff
	s_cselect_b64 s[12:13], s[42:43], 0
	v_cmp_ne_u32_e64 s[30:31], 0, v25
	s_and_b64 s[30:31], s[30:31], s[12:13]
	v_cndmask_b32_e64 v25, 0, 1.0, s[30:31]
	v_add_f32_e64 v108, v8, v96
	v_add_f32_e64 v109, v9, v97
	v_add_f32_e64 v110, v10, v98
	v_fma_f32 v64, v96, v96, v64
	v_fma_f32 v65, v96, v97, v65
	v_fma_f32 v90, v96, v98, v90
	v_fma_f32 v91, v97, v97, v91
	v_fma_f32 v94, v97, v98, v94
	v_fma_f32 v95, v98, v98, v95
	v_add_f32_dpp v117, v25, v25 wave_shr:1 row_mask:0xf bank_mask:0xf bound_ctrl:1
	v_add_f32_e64 v108, v108, v100
	v_add_f32_e64 v109, v109, v101
	v_add_f32_e64 v110, v110, v102
	v_fma_f32 v111, v100, v100, v64
	v_fma_f32 v112, v100, v101, v65
	v_fma_f32 v113, v100, v102, v90
	v_fma_f32 v114, v101, v101, v91
	v_fma_f32 v115, v101, v102, v94
	v_fma_f32 v116, v102, v102, v95
	v_add_f32_dpp v117, v25, v117 wave_shl:1 row_mask:0xf bank_mask:0xf bound_ctrl:1
	v_pk_add_f32 v[64:65], v[44:45], v[108:109]
	v_pk_add_f32 v[44:45], v[54:55], v[110:111]
	v_pk_add_f32 v[54:55], v[118:119], v[112:113]
	v_pk_add_f32 v[90:91], v[122:123], v[114:115]
	v_pk_add_f32 v[94:95], v[124:125], v[116:117]
	v_mul_f32_e64 v132, v64, v22
	v_mul_f32_e64 v133, v65, v22
	v_mul_f32_e64 v134, v44, v22
	v_fma_f32 v25, v45, v22, v26
	v_mul_f32_e64 v29, v54, v22
	v_mul_f32_e64 v118, v55, v22
	v_fma_f32 v119, v90, v22, v26
	v_mul_f32_e64 v122, v91, v22
	v_fma_f32 v123, v94, v22, v26
	v_fma_f32 v25, -v132, v132, v25
	v_fma_f32 v29, -v132, v133, v29
	v_fma_f32 v118, -v132, v134, v118
	v_fma_f32 v119, -v133, v133, v119
	v_fma_f32 v122, -v133, v134, v122
	v_fma_f32 v123, -v134, v134, v123
	v_mul_f32_e64 v124, v122, v122
	v_mul_f32_e64 v125, v29, v123
	v_mul_f32_e64 v156, v118, v119
	v_mul_f32_e64 v157, v118, v118
	v_mul_f32_e64 v158, v25, v122
	v_mul_f32_e64 v159, v29, v29
	v_fma_f32 v124, v119, v123, -v124
	v_fma_f32 v125, v118, v122, -v125
	v_fma_f32 v156, v29, v122, -v156
	v_fma_f32 v157, v25, v123, -v157
	v_fma_f32 v158, v29, v118, -v158
	v_fma_f32 v159, v25, v119, -v159
	v_mul_f32_e64 v160, v25, v124
	v_fma_f32 v160, v29, v125, v160
	v_fma_f32 v160, v118, v156, v160
	v_rcp_f32_e32 v160, v160
	v_cmp_ne_u32_e64 vcc, s37, v31
	v_mul_f32_e64 v160, v160, v22
	v_cndmask_b32_e64 v160, 0, v160, s[30:31]
	v_cndmask_b32_e64 v25, 0, v18, vcc
	v_cndmask_b32_e64 v149, 0, v22, s[30:31]
	v_mul_f32_e64 v135, v124, v160
	v_mul_f32_e64 v144, v125, v160
	v_mul_f32_e64 v145, v156, v160
	v_mul_f32_e64 v146, v157, v160
	v_mul_f32_e64 v147, v158, v160
	v_mul_f32_e64 v148, v159, v160
	v_add_f32_e64 v150, v95, v25
	v_mov_b32_e32 v151, v31
	ds_write_b128 v23, v[132:135] offset:3072
	ds_write_b128 v23, v[144:147] offset:4096
	ds_write_b128 v23, v[148:151] offset:5120
	s_waitcnt lgkmcnt(0)
	s_barrier
	v_mov_b32_dpp v44, v4 wave_shr:1 row_mask:0xf bank_mask:0xf bound_ctrl:1
	v_mov_b32_dpp v54, v4 wave_shl:1 row_mask:0xf bank_mask:0xf bound_ctrl:1
	v_mul_f32_e64 v64, v4, v8
	v_mul_f32_e64 v90, v4, v9
	v_mul_f32_e64 v94, v4, v10
	v_add_f32_e64 v118, v4, v44
	v_fma_f32 v64, v44, v96, v64
	v_fma_f32 v90, v44, v97, v90
	v_fma_f32 v94, v44, v98, v94
	v_add_f32_e64 v118, v118, v54
	v_fma_f32 v64, v54, v100, v64
	v_fma_f32 v90, v54, v101, v90
	v_fma_f32 v94, v54, v102, v94
	v_add_f32_e64 v44, v50, v118
	v_add_f32_e64 v50, v82, v64
	v_add_f32_e64 v54, v56, v90
	v_add_f32_e64 v56, v58, v94
	v_fma_f32 v50, -v132, v44, v50
	v_fma_f32 v54, -v133, v44, v54
	v_fma_f32 v56, -v134, v44, v56
	v_mul_f32_e64 v58, v135, v50
	v_mul_f32_e64 v82, v144, v50
	v_mul_f32_e64 v122, v145, v50
	v_fma_f32 v58, v144, v54, v58
	v_fma_f32 v82, v146, v54, v82
	v_fma_f32 v122, v147, v54, v122
	v_fma_f32 v58, v145, v56, v58
	v_fma_f32 v82, v147, v56, v82
	v_fma_f32 v122, v148, v56, v122
	v_mul_f32_e64 v124, v132, v58
	v_fma_f32 v124, v133, v82, v124
	v_fma_f32 v124, v134, v122, v124
	v_fma_f32 v124, v149, v44, -v124
	v_cmp_eq_u32_e64 s[10:11], 7, v151
	v_add_f32_e64 v44, v88, v58
	v_add_f32_e64 v50, v62, v82
	v_add_f32_e64 v54, v66, v122
	v_add_f32_e64 v56, v86, v124
	v_fma_f32 v62, v36, v44, v56
	v_fma_f32 v66, v40, v44, v56
	v_fma_f32 v62, v37, v50, v62
	v_fma_f32 v66, v41, v50, v66
	v_fma_f32 v62, v38, v54, v62
	v_fma_f32 v66, v42, v54, v66
	v_fma_f32 v56, v68, v44, v56
	v_fma_f32 v56, v69, v50, v56
	v_fma_f32 v56, v70, v54, v56
	v_cndmask_b32_e64 v86, 0, v18, s[10:11]
	v_add_f32_dpp v56, v62, v56 wave_shl:1 row_mask:0xf bank_mask:0xf bound_ctrl:1
	s_add_i32 s4, s34, 1
	s_cmpk_lt_i32 s4, 0x201
	s_cselect_b64 s[12:13], s[0:1], 0
	v_add_f32_dpp v56, v66, v56 wave_shr:1 row_mask:0xf bank_mask:0xf bound_ctrl:1
	v_fma_f32 v56, v46, v150, -v56
	v_add_f32_e64 v56, v56, -v86
	v_mul_f32_e64 v88, v56, v56
	v_cndmask_b32_e64 v89, 0, v88, s[12:13]
	v_add_f32_e32 v1, v1, v89
	s_add_i32 s5, s34, 6
	s_min_i32 s5, s5, 0x200
	s_mul_i32 s6, s5, 0x804
	s_add_i32 s6, s6, s35
	s_add_i32 s7, s6, 0x606018
	s_mul_i32 s9, s5, 0x180c
	s_add_i32 s9, s9, s33
	s_add_i32 s4, s34, 7
	s_min_i32 s4, s4, 0x200
	s_mul_i32 s4, s4, 0x804
	s_add_i32 s4, s4, s38
	buffer_load_dword v25, v28, s[20:23], s4 offen nt
	buffer_load_dwordx3 v[40:42], v27, s[24:27], s9 offen nt
	buffer_load_dword v36, v28, s[16:19], s7 offen nt
	s_waitcnt vmcnt(6)
	v_mov_b32_dpp v44, v12 wave_shr:1 row_mask:0xf bank_mask:0xf bound_ctrl:1
	v_mov_b32_dpp v45, v13 wave_shr:1 row_mask:0xf bank_mask:0xf bound_ctrl:1
	v_mov_b32_dpp v46, v14 wave_shr:1 row_mask:0xf bank_mask:0xf bound_ctrl:1
	v_mov_b32_dpp v68, v12 wave_shl:1 row_mask:0xf bank_mask:0xf bound_ctrl:1
	v_mov_b32_dpp v69, v13 wave_shl:1 row_mask:0xf bank_mask:0xf bound_ctrl:1
	v_mov_b32_dpp v70, v14 wave_shl:1 row_mask:0xf bank_mask:0xf bound_ctrl:1
	s_add_i32 s4, s34, 5
	s_cmpk_lt_u32 s4, 0x201
	s_cselect_b64 s[12:13], s[40:41], 0
	v_cmp_eq_u32_e64 s[14:15], s37, v3
	s_and_b64 s[14:15], s[14:15], s[12:13]
	v_cndmask_b32_e64 v29, 0, 1, s[14:15]
	v_mul_f32_e64 v38, v12, v12
	v_mul_f32_e64 v39, v12, v13
	v_mul_f32_e64 v50, v12, v14
	v_mul_f32_e64 v51, v13, v13
	v_mul_f32_e64 v54, v13, v14
	v_mul_f32_e64 v55, v14, v14
	v_or_b32_dpp v31, v29, v29 wave_shr:1 row_mask:0xf bank_mask:0xf bound_ctrl:1
	s_nop 1
	v_or_b32_dpp v31, v29, v31 wave_shl:1 row_mask:0xf bank_mask:0xf bound_ctrl:1
	s_nop 1
	v_or_b32_dpp v85, v31, v31 wave_shr:1 row_mask:0xf bank_mask:0xf bound_ctrl:1
	s_nop 1
	v_or_b32_dpp v85, v31, v85 wave_shl:1 row_mask:0xf bank_mask:0xf bound_ctrl:1
	v_or3_b32 v29, v85, v52, v30
	v_or3_b32 v29, v29, v53, v84
	s_add_i32 s4, s34, 2
	s_cmpk_lt_u32 s4, 0x1ff
	s_cselect_b64 s[12:13], s[42:43], 0
	v_cmp_ne_u32_e64 s[30:31], 0, v29
	s_and_b64 s[30:31], s[30:31], s[12:13]
	v_cndmask_b32_e64 v29, 0, 1.0, s[30:31]
	v_add_f32_e64 v56, v12, v44
	v_add_f32_e64 v57, v13, v45
	v_add_f32_e64 v62, v14, v46
	v_fma_f32 v38, v44, v44, v38
	v_fma_f32 v39, v44, v45, v39
	v_fma_f32 v50, v44, v46, v50
	v_fma_f32 v51, v45, v45, v51
	v_fma_f32 v54, v45, v46, v54
	v_fma_f32 v55, v46, v46, v55
	v_add_f32_dpp v89, v29, v29 wave_shr:1 row_mask:0xf bank_mask:0xf bound_ctrl:1
	v_add_f32_e64 v56, v56, v68
	v_add_f32_e64 v57, v57, v69
	v_add_f32_e64 v62, v62, v70
	v_fma_f32 v63, v68, v68, v38
	v_fma_f32 v66, v68, v69, v39
	v_fma_f32 v67, v68, v70, v50
	v_fma_f32 v86, v69, v69, v51
	v_fma_f32 v87, v69, v70, v54
	v_fma_f32 v88, v70, v70, v55
	v_add_f32_dpp v89, v29, v89 wave_shl:1 row_mask:0xf bank_mask:0xf bound_ctrl:1
	v_pk_add_f32 v[38:39], v[108:109], v[56:57]
	v_pk_add_f32 v[50:51], v[60:61], v[38:39]
	v_pk_add_f32 v[54:55], v[110:111], v[62:63]
	v_pk_add_f32 v[60:61], v[136:137], v[54:55]
	v_pk_add_f32 v[108:109], v[112:113], v[66:67]
	v_pk_add_f32 v[110:111], v[138:139], v[108:109]
	v_pk_add_f32 v[112:113], v[114:115], v[86:87]
	v_pk_add_f32 v[132:133], v[140:141], v[112:113]
	v_pk_add_f32 v[114:115], v[116:117], v[88:89]
	v_pk_add_f32 v[134:135], v[142:143], v[114:115]
	v_mul_f32_e64 v136, v50, v22
	v_mul_f32_e64 v137, v51, v22
	v_mul_f32_e64 v138, v60, v22
	v_fma_f32 v29, v61, v22, v26
	v_mul_f32_e64 v31, v110, v22
	v_mul_f32_e64 v116, v111, v22
	v_fma_f32 v117, v132, v22, v26
	v_mul_f32_e64 v148, v133, v22
	v_fma_f32 v149, v134, v22, v26
	v_fma_f32 v29, -v136, v136, v29
	v_fma_f32 v31, -v136, v137, v31
	v_fma_f32 v116, -v136, v138, v116
	v_fma_f32 v117, -v137, v137, v117
	v_fma_f32 v148, -v137, v138, v148
	v_fma_f32 v149, -v138, v138, v149
	v_mul_f32_e64 v150, v148, v148
	v_mul_f32_e64 v151, v31, v149
	v_mul_f32_e64 v156, v116, v117
	v_mul_f32_e64 v157, v116, v116
	v_mul_f32_e64 v158, v29, v148
	v_mul_f32_e64 v159, v31, v31
	v_fma_f32 v150, v117, v149, -v150
	v_fma_f32 v151, v116, v148, -v151
	v_fma_f32 v156, v31, v148, -v156
	v_fma_f32 v157, v29, v149, -v157
	v_fma_f32 v158, v31, v116, -v158
	v_fma_f32 v159, v29, v117, -v159
	v_mul_f32_e64 v160, v29, v150
	v_fma_f32 v160, v31, v151, v160
	v_fma_f32 v160, v116, v156, v160
	v_rcp_f32_e32 v160, v160
	v_cmp_ne_u32_e64 vcc, s37, v24
	v_mul_f32_e64 v160, v160, v22
	v_cndmask_b32_e64 v160, 0, v160, s[30:31]
	v_cndmask_b32_e64 v29, 0, v18, vcc
	v_cndmask_b32_e64 v145, 0, v22, s[30:31]
	v_mul_f32_e64 v139, v150, v160
	v_mul_f32_e64 v140, v151, v160
	v_mul_f32_e64 v141, v156, v160
	v_mul_f32_e64 v142, v157, v160
	v_mul_f32_e64 v143, v158, v160
	v_mul_f32_e64 v144, v159, v160
	v_add_f32_e64 v146, v135, v29
	v_mov_b32_e32 v147, v24
	ds_write_b128 v23, v[136:139]
	ds_write_b128 v23, v[140:143] offset:1024
	ds_write_b128 v23, v[144:147] offset:2048
	s_waitcnt lgkmcnt(0)
	s_barrier
	v_mov_b32_dpp v50, v6 wave_shr:1 row_mask:0xf bank_mask:0xf bound_ctrl:1
	v_mov_b32_dpp v60, v6 wave_shl:1 row_mask:0xf bank_mask:0xf bound_ctrl:1
	v_mul_f32_e64 v110, v6, v12
	v_mul_f32_e64 v116, v6, v13
	v_mul_f32_e64 v132, v6, v14
	v_add_f32_e64 v134, v6, v50
	v_fma_f32 v110, v50, v44, v110
	v_fma_f32 v116, v50, v45, v116
	v_fma_f32 v132, v50, v46, v132
	v_add_f32_e64 v134, v134, v60
	v_fma_f32 v110, v60, v68, v110
	v_fma_f32 v116, v60, v69, v116
	v_fma_f32 v132, v60, v70, v132
	v_add_f32_e64 v50, v118, v134
	v_add_f32_e64 v60, v130, v50
	v_add_f32_e64 v118, v64, v110
	v_add_f32_e64 v130, v120, v118
	v_add_f32_e64 v64, v90, v116
	v_add_f32_e64 v120, v126, v64
	v_add_f32_e64 v90, v94, v132
	v_add_f32_e64 v126, v128, v90
	v_fma_f32 v130, -v136, v60, v130
	v_fma_f32 v120, -v137, v60, v120
	v_fma_f32 v126, -v138, v60, v126
	v_mul_f32_e64 v94, v139, v130
	v_mul_f32_e64 v128, v140, v130
	v_mul_f32_e64 v148, v141, v130
	v_fma_f32 v94, v140, v120, v94
	v_fma_f32 v128, v142, v120, v128
	v_fma_f32 v148, v143, v120, v148
	v_fma_f32 v94, v141, v126, v94
	v_fma_f32 v128, v143, v126, v128
	v_fma_f32 v148, v144, v126, v148
	v_mul_f32_e64 v150, v136, v94
	v_fma_f32 v150, v137, v128, v150
	v_fma_f32 v150, v138, v148, v150
	v_fma_f32 v150, v145, v60, -v150
	v_cmp_eq_u32_e64 s[10:11], 7, v147
	v_add_f32_e64 v60, v58, v94
	v_add_f32_e64 v120, v80, v60
	v_add_f32_e64 v58, v82, v128
	v_add_f32_e64 v80, v92, v58
	v_add_f32_e64 v82, v122, v148
	v_add_f32_e64 v92, v152, v82
	v_add_f32_e64 v122, v124, v150
	v_add_f32_e64 v126, v154, v122
	v_fma_f32 v124, v72, v120, v126
	v_fma_f32 v130, v76, v120, v126
	v_fma_f32 v124, v73, v80, v124
	v_fma_f32 v130, v77, v80, v130
	v_fma_f32 v124, v74, v92, v124
	v_fma_f32 v130, v78, v92, v130
	v_fma_f32 v126, v104, v120, v126
	v_fma_f32 v126, v105, v80, v126
	v_fma_f32 v126, v106, v92, v126
	v_cndmask_b32_e64 v152, 0, v18, s[10:11]
	v_add_f32_dpp v126, v124, v126 wave_shl:1 row_mask:0xf bank_mask:0xf bound_ctrl:1
	s_add_i32 s4, s34, 2
	s_cmpk_lt_i32 s4, 0x201
	s_cselect_b64 s[12:13], s[0:1], 0
	v_add_f32_dpp v126, v130, v126 wave_shr:1 row_mask:0xf bank_mask:0xf bound_ctrl:1
	v_fma_f32 v126, v48, v146, -v126
	v_add_f32_e64 v126, v126, -v152
	v_mul_f32_e64 v154, v126, v126
	v_cndmask_b32_e64 v155, 0, v154, s[12:13]
	v_add_f32_e32 v1, v1, v155
	s_add_i32 s5, s34, 7
	s_min_i32 s5, s5, 0x200
	s_mul_i32 s6, s5, 0x804
	s_add_i32 s6, s6, s35
	s_add_i32 s7, s6, 0x606018
	s_mul_i32 s9, s5, 0x180c
	s_add_i32 s9, s9, s33
	s_add_i32 s4, s34, 8
	s_min_i32 s4, s4, 0x200
	s_mul_i32 s4, s4, 0x804
	s_add_i32 s4, s4, s38
	buffer_load_dword v24, v28, s[20:23], s4 offen nt
	buffer_load_dwordx3 v[72:74], v27, s[24:27], s9 offen nt
	buffer_load_dword v48, v28, s[16:19], s7 offen nt
	s_waitcnt vmcnt(6)
	v_mov_b32_dpp v76, v32 wave_shr:1 row_mask:0xf bank_mask:0xf bound_ctrl:1
	v_mov_b32_dpp v77, v33 wave_shr:1 row_mask:0xf bank_mask:0xf bound_ctrl:1
	v_mov_b32_dpp v78, v34 wave_shr:1 row_mask:0xf bank_mask:0xf bound_ctrl:1
	v_mov_b32_dpp v104, v32 wave_shl:1 row_mask:0xf bank_mask:0xf bound_ctrl:1
	v_mov_b32_dpp v105, v33 wave_shl:1 row_mask:0xf bank_mask:0xf bound_ctrl:1
	v_mov_b32_dpp v106, v34 wave_shl:1 row_mask:0xf bank_mask:0xf bound_ctrl:1
	s_add_i32 s4, s34, 6
	s_cmpk_lt_u32 s4, 0x201
	s_cselect_b64 s[12:13], s[40:41], 0
	v_cmp_eq_u32_e64 s[14:15], s37, v16
	s_and_b64 s[14:15], s[14:15], s[12:13]
	v_cndmask_b32_e64 v29, 0, 1, s[14:15]
	v_mul_f32_e64 v80, v32, v32
	v_mul_f32_e64 v81, v32, v33
	v_mul_f32_e64 v92, v32, v34
	v_mul_f32_e64 v93, v33, v33
	v_mul_f32_e64 v120, v33, v34
	v_mul_f32_e64 v121, v34, v34
	v_or_b32_dpp v31, v29, v29 wave_shr:1 row_mask:0xf bank_mask:0xf bound_ctrl:1
	s_nop 1
	v_or_b32_dpp v31, v29, v31 wave_shl:1 row_mask:0xf bank_mask:0xf bound_ctrl:1
	s_nop 1
	v_or_b32_dpp v84, v31, v31 wave_shr:1 row_mask:0xf bank_mask:0xf bound_ctrl:1
	s_nop 1
	v_or_b32_dpp v84, v31, v84 wave_shl:1 row_mask:0xf bank_mask:0xf bound_ctrl:1
	v_or3_b32 v29, v84, v85, v52
	v_or3_b32 v29, v29, v30, v53
	s_add_i32 s4, s34, 3
	s_cmpk_lt_u32 s4, 0x1ff
	s_cselect_b64 s[12:13], s[42:43], 0
	v_cmp_ne_u32_e64 s[30:31], 0, v29
	s_and_b64 s[30:31], s[30:31], s[12:13]
	v_cndmask_b32_e64 v29, 0, 1.0, s[30:31]
	v_add_f32_e64 v124, v32, v76
	v_add_f32_e64 v125, v33, v77
	v_add_f32_e64 v126, v34, v78
	v_fma_f32 v80, v76, v76, v80
	v_fma_f32 v81, v76, v77, v81
	v_fma_f32 v92, v76, v78, v92
	v_fma_f32 v93, v77, v77, v93
	v_fma_f32 v120, v77, v78, v120
	v_fma_f32 v121, v78, v78, v121
	v_add_f32_dpp v139, v29, v29 wave_shr:1 row_mask:0xf bank_mask:0xf bound_ctrl:1
	v_add_f32_e64 v124, v124, v104
	v_add_f32_e64 v125, v125, v105
	v_add_f32_e64 v126, v126, v106
	v_fma_f32 v127, v104, v104, v80
	v_fma_f32 v130, v104, v105, v81
	v_fma_f32 v131, v104, v106, v92
	v_fma_f32 v136, v105, v105, v93
	v_fma_f32 v137, v105, v106, v120
	v_fma_f32 v138, v106, v106, v121
	v_add_f32_dpp v139, v29, v139 wave_shl:1 row_mask:0xf bank_mask:0xf bound_ctrl:1
	v_pk_add_f32 v[80:81], v[38:39], v[124:125]
	v_pk_add_f32 v[38:39], v[54:55], v[126:127]
	v_pk_add_f32 v[54:55], v[108:109], v[130:131]
	v_pk_add_f32 v[92:93], v[112:113], v[136:137]
	v_pk_add_f32 v[108:109], v[114:115], v[138:139]
	v_mul_f32_e64 v112, v80, v22
	v_mul_f32_e64 v113, v81, v22
	v_mul_f32_e64 v114, v38, v22
	v_fma_f32 v29, v39, v22, v26
	v_mul_f32_e64 v31, v54, v22
	v_mul_f32_e64 v120, v55, v22
	v_fma_f32 v121, v92, v22, v26
	v_mul_f32_e64 v152, v93, v22
	v_fma_f32 v153, v108, v22, v26
	v_fma_f32 v29, -v112, v112, v29
	v_fma_f32 v31, -v112, v113, v31
	v_fma_f32 v120, -v112, v114, v120
	v_fma_f32 v121, -v113, v113, v121
	v_fma_f32 v152, -v113, v114, v152
	v_fma_f32 v153, -v114, v114, v153
	v_mul_f32_e64 v154, v152, v152
	v_mul_f32_e64 v155, v31, v153
	v_mul_f32_e64 v156, v120, v121
	v_mul_f32_e64 v157, v120, v120
	v_mul_f32_e64 v158, v29, v152
	v_mul_f32_e64 v159, v31, v31
	v_fma_f32 v154, v121, v153, -v154
	v_fma_f32 v155, v120, v152, -v155
	v_fma_f32 v156, v31, v152, -v156
	v_fma_f32 v157, v29, v153, -v157
	v_fma_f32 v158, v31, v120, -v158
	v_fma_f32 v159, v29, v121, -v159
	v_mul_f32_e64 v160, v29, v154
	v_fma_f32 v160, v31, v155, v160
	v_fma_f32 v160, v120, v156, v160
	v_rcp_f32_e32 v160, v160
	v_cmp_ne_u32_e64 vcc, s37, v17
	v_mul_f32_e64 v160, v160, v22
	v_cndmask_b32_e64 v160, 0, v160, s[30:31]
	v_cndmask_b32_e64 v29, 0, v18, vcc
	v_cndmask_b32_e64 v145, 0, v22, s[30:31]
	v_mul_f32_e64 v115, v154, v160
	v_mul_f32_e64 v140, v155, v160
	v_mul_f32_e64 v141, v156, v160
	v_mul_f32_e64 v142, v157, v160
	v_mul_f32_e64 v143, v158, v160
	v_mul_f32_e64 v144, v159, v160
	v_add_f32_e64 v146, v109, v29
	v_mov_b32_e32 v147, v17
	ds_write_b128 v23, v[112:115] offset:3072
	ds_write_b128 v23, v[140:143] offset:4096
	ds_write_b128 v23, v[144:147] offset:5120
	s_waitcnt lgkmcnt(0)
	s_barrier
	v_mov_b32_dpp v38, v20 wave_shr:1 row_mask:0xf bank_mask:0xf bound_ctrl:1
	v_mov_b32_dpp v54, v20 wave_shl:1 row_mask:0xf bank_mask:0xf bound_ctrl:1
	v_mul_f32_e64 v80, v20, v32
	v_mul_f32_e64 v92, v20, v33
	v_mul_f32_e64 v108, v20, v34
	v_add_f32_e64 v120, v20, v38
	v_fma_f32 v80, v38, v76, v80
	v_fma_f32 v92, v38, v77, v92
	v_fma_f32 v108, v38, v78, v108
	v_add_f32_e64 v120, v120, v54
	v_fma_f32 v80, v54, v104, v80
	v_fma_f32 v92, v54, v105, v92
	v_fma_f32 v108, v54, v106, v108
	v_add_f32_e64 v38, v50, v120
	v_add_f32_e64 v50, v118, v80
	v_add_f32_e64 v54, v64, v92
	v_add_f32_e64 v64, v90, v108
	v_fma_f32 v50, -v112, v38, v50
	v_fma_f32 v54, -v113, v38, v54
	v_fma_f32 v64, -v114, v38, v64
	v_mul_f32_e64 v90, v115, v50
	v_mul_f32_e64 v118, v140, v50
	v_mul_f32_e64 v152, v141, v50
	v_fma_f32 v90, v140, v54, v90
	v_fma_f32 v118, v142, v54, v118
	v_fma_f32 v152, v143, v54, v152
	v_fma_f32 v90, v141, v64, v90
	v_fma_f32 v118, v143, v64, v118
	v_fma_f32 v152, v144, v64, v152
	v_mul_f32_e64 v154, v112, v90
	v_fma_f32 v154, v113, v118, v154
	v_fma_f32 v154, v114, v152, v154
	v_fma_f32 v154, v145, v38, -v154
	v_cmp_eq_u32_e64 s[10:11], 7, v147
	v_add_f32_e64 v38, v60, v90
	v_add_f32_e64 v50, v58, v118
	v_add_f32_e64 v54, v82, v152
	v_add_f32_e64 v58, v122, v154
	v_fma_f32 v60, v96, v38, v58
	v_fma_f32 v64, v100, v38, v58
	v_fma_f32 v60, v97, v50, v60
	v_fma_f32 v64, v101, v50, v64
	v_fma_f32 v60, v98, v54, v60
	v_fma_f32 v64, v102, v54, v64
	v_fma_f32 v58, v8, v38, v58
	v_fma_f32 v58, v9, v50, v58
	v_fma_f32 v58, v10, v54, v58
	v_cndmask_b32_e64 v82, 0, v18, s[10:11]
	v_add_f32_dpp v58, v60, v58 wave_shl:1 row_mask:0xf bank_mask:0xf bound_ctrl:1
	s_add_i32 s4, s34, 3
	s_cmpk_lt_i32 s4, 0x201
	s_cselect_b64 s[12:13], s[0:1], 0
	v_add_f32_dpp v58, v64, v58 wave_shr:1 row_mask:0xf bank_mask:0xf bound_ctrl:1
	v_fma_f32 v58, v4, v146, -v58
	v_add_f32_e64 v58, v58, -v82
	v_mul_f32_e64 v122, v58, v58
	v_cndmask_b32_e64 v123, 0, v122, s[12:13]
	v_add_f32_e32 v1, v1, v123
	s_add_i32 s5, s34, 8
	s_min_i32 s5, s5, 0x200
	s_mul_i32 s6, s5, 0x804
	s_add_i32 s6, s6, s35
	s_add_i32 s7, s6, 0x606018
	s_mul_i32 s9, s5, 0x180c
	s_add_i32 s9, s9, s33
	s_add_i32 s4, s34, 9
	s_min_i32 s4, s4, 0x200
	s_mul_i32 s4, s4, 0x804
	s_add_i32 s4, s4, s38
	buffer_load_dword v17, v28, s[20:23], s4 offen nt
	buffer_load_dwordx3 v[8:10], v27, s[24:27], s9 offen nt
	buffer_load_dword v4, v28, s[16:19], s7 offen nt
	s_waitcnt vmcnt(6)
	v_mov_b32_dpp v96, v40 wave_shr:1 row_mask:0xf bank_mask:0xf bound_ctrl:1
	v_mov_b32_dpp v97, v41 wave_shr:1 row_mask:0xf bank_mask:0xf bound_ctrl:1
	v_mov_b32_dpp v98, v42 wave_shr:1 row_mask:0xf bank_mask:0xf bound_ctrl:1
	v_mov_b32_dpp v100, v40 wave_shl:1 row_mask:0xf bank_mask:0xf bound_ctrl:1
	v_mov_b32_dpp v101, v41 wave_shl:1 row_mask:0xf bank_mask:0xf bound_ctrl:1
	v_mov_b32_dpp v102, v42 wave_shl:1 row_mask:0xf bank_mask:0xf bound_ctrl:1
	s_add_i32 s4, s34, 7
	s_cmpk_lt_u32 s4, 0x201
	s_cselect_b64 s[12:13], s[40:41], 0
	v_cmp_eq_u32_e64 s[14:15], s37, v25
	s_and_b64 s[14:15], s[14:15], s[12:13]
	v_cndmask_b32_e64 v29, 0, 1, s[14:15]
	v_mul_f32_e64 v38, v40, v40
	v_mul_f32_e64 v39, v40, v41
	v_mul_f32_e64 v50, v40, v42
	v_mul_f32_e64 v51, v41, v41
	v_mul_f32_e64 v54, v41, v42
	v_mul_f32_e64 v55, v42, v42
	v_or_b32_dpp v31, v29, v29 wave_shr:1 row_mask:0xf bank_mask:0xf bound_ctrl:1
	s_nop 1
	v_or_b32_dpp v31, v29, v31 wave_shl:1 row_mask:0xf bank_mask:0xf bound_ctrl:1
	s_nop 1
	v_or_b32_dpp v53, v31, v31 wave_shr:1 row_mask:0xf bank_mask:0xf bound_ctrl:1
	s_nop 1
	v_or_b32_dpp v53, v31, v53 wave_shl:1 row_mask:0xf bank_mask:0xf bound_ctrl:1
	v_or3_b32 v29, v53, v84, v85
	v_or3_b32 v29, v29, v52, v30
	s_add_i32 s4, s34, 4
	s_cmpk_lt_u32 s4, 0x1ff
	s_cselect_b64 s[12:13], s[42:43], 0
	v_cmp_ne_u32_e64 s[30:31], 0, v29
	s_and_b64 s[30:31], s[30:31], s[12:13]
	v_cndmask_b32_e64 v29, 0, 1.0, s[30:31]
	v_add_f32_e64 v58, v40, v96
	v_add_f32_e64 v59, v41, v97
	v_add_f32_e64 v60, v42, v98
	v_fma_f32 v38, v96, v96, v38
	v_fma_f32 v39, v96, v97, v39
	v_fma_f32 v50, v96, v98, v50
	v_fma_f32 v51, v97, v97, v51
	v_fma_f32 v54, v97, v98, v54
	v_fma_f32 v55, v98, v98, v55
	v_add_f32_dpp v113, v29, v29 wave_shr:1 row_mask:0xf bank_mask:0xf bound_ctrl:1
	v_add_f32_e64 v58, v58, v100
	v_add_f32_e64 v59, v59, v101
	v_add_f32_e64 v60, v60, v102
	v_fma_f32 v61, v100, v100, v38
	v_fma_f32 v64, v100, v101, v39
	v_fma_f32 v65, v100, v102, v50
	v_fma_f32 v82, v101, v101, v51
	v_fma_f32 v83, v101, v102, v54
	v_fma_f32 v112, v102, v102, v55
	v_add_f32_dpp v113, v29, v113 wave_shl:1 row_mask:0xf bank_mask:0xf bound_ctrl:1
	v_pk_add_f32 v[38:39], v[124:125], v[58:59]
	v_pk_add_f32 v[50:51], v[56:57], v[38:39]
	v_pk_add_f32 v[54:55], v[126:127], v[60:61]
	v_pk_add_f32 v[56:57], v[62:63], v[54:55]
	v_pk_add_f32 v[62:63], v[130:131], v[64:65]
	v_pk_add_f32 v[114:115], v[66:67], v[62:63]
	v_pk_add_f32 v[66:67], v[136:137], v[82:83]
	v_pk_add_f32 v[122:123], v[86:87], v[66:67]
	v_pk_add_f32 v[86:87], v[138:139], v[112:113]
	v_pk_add_f32 v[124:125], v[88:89], v[86:87]
	v_mul_f32_e64 v136, v50, v22
	v_mul_f32_e64 v137, v51, v22
	v_mul_f32_e64 v138, v56, v22
	v_fma_f32 v29, v57, v22, v26
	v_mul_f32_e64 v31, v114, v22
	v_mul_f32_e64 v88, v115, v22
	v_fma_f32 v89, v122, v22, v26
	v_mul_f32_e64 v126, v123, v22
	v_fma_f32 v127, v124, v22, v26
	v_fma_f32 v29, -v136, v136, v29
	v_fma_f32 v31, -v136, v137, v31
	v_fma_f32 v88, -v136, v138, v88
	v_fma_f32 v89, -v137, v137, v89
	v_fma_f32 v126, -v137, v138, v126
	v_fma_f32 v127, -v138, v138, v127
	v_mul_f32_e64 v130, v126, v126
	v_mul_f32_e64 v131, v31, v127
	v_mul_f32_e64 v156, v88, v89
	v_mul_f32_e64 v157, v88, v88
	v_mul_f32_e64 v158, v29, v126
	v_mul_f32_e64 v159, v31, v31
	v_fma_f32 v130, v89, v127, -v130
	v_fma_f32 v131, v88, v126, -v131
	v_fma_f32 v156, v31, v126, -v156
	v_fma_f32 v157, v29, v127, -v157
	v_fma_f32 v158, v31, v88, -v158
	v_fma_f32 v159, v29, v89, -v159
	v_mul_f32_e64 v160, v29, v130
	v_fma_f32 v160, v31, v131, v160
	v_fma_f32 v160, v88, v156, v160
	v_rcp_f32_e32 v160, v160
	v_cmp_ne_u32_e64 vcc, s37, v2
	v_mul_f32_e64 v160, v160, v22
	v_cndmask_b32_e64 v160, 0, v160, s[30:31]
	v_cndmask_b32_e64 v29, 0, v18, vcc
	v_cndmask_b32_e64 v145, 0, v22, s[30:31]
	v_mul_f32_e64 v139, v130, v160
	v_mul_f32_e64 v140, v131, v160
	v_mul_f32_e64 v141, v156, v160
	v_mul_f32_e64 v142, v157, v160
	v_mul_f32_e64 v143, v158, v160
	v_mul_f32_e64 v144, v159, v160
	v_add_f32_e64 v146, v125, v29
	v_mov_b32_e32 v147, v2
	ds_write_b128 v23, v[136:139]
	ds_write_b128 v23, v[140:143] offset:1024
	ds_write_b128 v23, v[144:147] offset:2048
	s_waitcnt lgkmcnt(0)
	s_barrier
	v_mov_b32_dpp v30, v36 wave_shr:1 row_mask:0xf bank_mask:0xf bound_ctrl:1
	v_mov_b32_dpp v50, v36 wave_shl:1 row_mask:0xf bank_mask:0xf bound_ctrl:1
	v_mul_f32_e64 v56, v36, v40
	v_mul_f32_e64 v88, v36, v41
	v_mul_f32_e64 v114, v36, v42
	v_add_f32_e64 v122, v36, v30
	v_fma_f32 v56, v30, v96, v56
	v_fma_f32 v88, v30, v97, v88
	v_fma_f32 v114, v30, v98, v114
	v_add_f32_e64 v122, v122, v50
	v_fma_f32 v56, v50, v100, v56
	v_fma_f32 v88, v50, v101, v88
	v_fma_f32 v114, v50, v102, v114
	v_add_f32_e64 v30, v120, v122
	v_add_f32_e64 v50, v134, v30
	v_add_f32_e64 v120, v80, v56
	v_add_f32_e64 v124, v110, v120
	v_add_f32_e64 v80, v92, v88
	v_add_f32_e64 v110, v116, v80
	v_add_f32_e64 v92, v108, v114
	v_add_f32_e64 v116, v132, v92
	v_fma_f32 v124, -v136, v50, v124
	v_fma_f32 v110, -v137, v50, v110
	v_fma_f32 v116, -v138, v50, v116
	v_mul_f32_e64 v108, v139, v124
	v_mul_f32_e64 v126, v140, v124
	v_mul_f32_e64 v130, v141, v124
	v_fma_f32 v108, v140, v110, v108
	v_fma_f32 v126, v142, v110, v126
	v_fma_f32 v130, v143, v110, v130
	v_fma_f32 v108, v141, v116, v108
	v_fma_f32 v126, v143, v116, v126
	v_fma_f32 v130, v144, v116, v130
	v_mul_f32_e64 v132, v136, v108
	v_fma_f32 v132, v137, v126, v132
	v_fma_f32 v132, v138, v130, v132
	v_fma_f32 v132, v145, v50, -v132
	v_cmp_eq_u32_e64 s[10:11], 7, v147
	v_add_f32_e64 v50, v90, v108
	v_add_f32_e64 v110, v94, v50
	v_add_f32_e64 v90, v118, v126
	v_add_f32_e64 v94, v128, v90
	v_add_f32_e64 v116, v152, v130
	v_add_f32_e64 v118, v148, v116
	v_add_f32_e64 v124, v154, v132
	v_add_f32_e64 v128, v150, v124
	v_fma_f32 v134, v44, v110, v128
	v_fma_f32 v148, v68, v110, v128
	v_fma_f32 v134, v45, v94, v134
	v_fma_f32 v148, v69, v94, v148
	v_fma_f32 v134, v46, v118, v134
	v_fma_f32 v148, v70, v118, v148
	v_fma_f32 v128, v12, v110, v128
	v_fma_f32 v128, v13, v94, v128
	v_fma_f32 v128, v14, v118, v128
	v_cndmask_b32_e64 v150, 0, v18, s[10:11]
	v_add_f32_dpp v128, v134, v128 wave_shl:1 row_mask:0xf bank_mask:0xf bound_ctrl:1
	s_add_i32 s4, s34, 4
	s_cmpk_lt_i32 s4, 0x201
	s_cselect_b64 s[12:13], s[0:1], 0
	v_add_f32_dpp v128, v148, v128 wave_shr:1 row_mask:0xf bank_mask:0xf bound_ctrl:1
	v_fma_f32 v128, v6, v146, -v128
	v_add_f32_e64 v128, v128, -v150
	v_mul_f32_e64 v152, v128, v128
	v_cndmask_b32_e64 v153, 0, v152, s[12:13]
	v_add_f32_e32 v1, v1, v153
	s_add_i32 s5, s34, 9
	s_min_i32 s5, s5, 0x200
	s_mul_i32 s6, s5, 0x804
	s_add_i32 s6, s6, s35
	s_add_i32 s7, s6, 0x606018
	s_mul_i32 s9, s5, 0x180c
	s_add_i32 s9, s9, s33
	s_add_i32 s4, s34, 10
	s_min_i32 s4, s4, 0x200
	s_mul_i32 s4, s4, 0x804
	s_add_i32 s4, s4, s38
	buffer_load_dword v2, v28, s[20:23], s4 offen nt
	buffer_load_dwordx3 v[12:14], v27, s[24:27], s9 offen nt
	buffer_load_dword v6, v28, s[16:19], s7 offen nt
	s_waitcnt vmcnt(6)
	v_mov_b32_dpp v44, v72 wave_shr:1 row_mask:0xf bank_mask:0xf bound_ctrl:1
	v_mov_b32_dpp v45, v73 wave_shr:1 row_mask:0xf bank_mask:0xf bound_ctrl:1
	v_mov_b32_dpp v46, v74 wave_shr:1 row_mask:0xf bank_mask:0xf bound_ctrl:1
	v_mov_b32_dpp v68, v72 wave_shl:1 row_mask:0xf bank_mask:0xf bound_ctrl:1
	v_mov_b32_dpp v69, v73 wave_shl:1 row_mask:0xf bank_mask:0xf bound_ctrl:1
	v_mov_b32_dpp v70, v74 wave_shl:1 row_mask:0xf bank_mask:0xf bound_ctrl:1
	s_add_i32 s4, s34, 8
	s_cmpk_lt_u32 s4, 0x201
	s_cselect_b64 s[12:13], s[40:41], 0
	v_cmp_eq_u32_e64 s[14:15], s37, v24
	s_and_b64 s[14:15], s[14:15], s[12:13]
	v_cndmask_b32_e64 v29, 0, 1, s[14:15]
	v_mul_f32_e64 v94, v72, v72
	v_mul_f32_e64 v95, v72, v73
	v_mul_f32_e64 v110, v72, v74
	v_mul_f32_e64 v111, v73, v73
	v_mul_f32_e64 v118, v73, v74
	v_mul_f32_e64 v119, v74, v74
	v_or_b32_dpp v128, v29, v29 wave_shr:1 row_mask:0xf bank_mask:0xf bound_ctrl:1
	s_nop 1
	v_or_b32_dpp v128, v29, v128 wave_shl:1 row_mask:0xf bank_mask:0xf bound_ctrl:1
	s_nop 1
	v_or_b32_dpp v129, v128, v128 wave_shr:1 row_mask:0xf bank_mask:0xf bound_ctrl:1
	s_nop 1
	v_or_b32_dpp v129, v128, v129 wave_shl:1 row_mask:0xf bank_mask:0xf bound_ctrl:1
	v_or3_b32 v29, v129, v53, v84
	v_or3_b32 v29, v29, v85, v52
	s_add_i32 s4, s34, 5
	s_cmpk_lt_u32 s4, 0x1ff
	s_cselect_b64 s[12:13], s[42:43], 0
	v_cmp_ne_u32_e64 s[30:31], 0, v29
	s_and_b64 s[30:31], s[30:31], s[12:13]
	v_cndmask_b32_e64 v29, 0, 1.0, s[30:31]
	v_add_f32_e64 v134, v72, v44
	v_add_f32_e64 v135, v73, v45
	v_add_f32_e64 v136, v74, v46
	v_fma_f32 v94, v44, v44, v94
	v_fma_f32 v95, v44, v45, v95
	v_fma_f32 v110, v44, v46, v110
	v_fma_f32 v111, v45, v45, v111
	v_fma_f32 v118, v45, v46, v118
	v_fma_f32 v119, v46, v46, v119
	v_add_f32_dpp v143, v29, v29 wave_shr:1 row_mask:0xf bank_mask:0xf bound_ctrl:1
	v_add_f32_e64 v134, v134, v68
	v_add_f32_e64 v135, v135, v69
	v_add_f32_e64 v136, v136, v70
	v_fma_f32 v137, v68, v68, v94
	v_fma_f32 v138, v68, v69, v95
	v_fma_f32 v139, v68, v70, v110
	v_fma_f32 v140, v69, v69, v111
	v_fma_f32 v141, v69, v70, v118
	v_fma_f32 v142, v70, v70, v119
	v_add_f32_dpp v143, v29, v143 wave_shl:1 row_mask:0xf bank_mask:0xf bound_ctrl:1
	v_pk_add_f32 v[94:95], v[38:39], v[134:135]
	v_pk_add_f32 v[38:39], v[54:55], v[136:137]
	v_pk_add_f32 v[54:55], v[62:63], v[138:139]
	v_pk_add_f32 v[62:63], v[66:67], v[140:141]
	v_pk_add_f32 v[66:67], v[86:87], v[142:143]
	v_mul_f32_e64 v144, v94, v22
	v_mul_f32_e64 v145, v95, v22
	v_mul_f32_e64 v146, v38, v22
	v_fma_f32 v29, v39, v22, v26
	v_mul_f32_e64 v128, v54, v22
	v_mul_f32_e64 v86, v55, v22
	v_fma_f32 v87, v62, v22, v26
	v_mul_f32_e64 v110, v63, v22
	v_fma_f32 v111, v66, v22, v26
	v_fma_f32 v29, -v144, v144, v29
	v_fma_f32 v128, -v144, v145, v128
	v_fma_f32 v86, -v144, v146, v86
	v_fma_f32 v87, -v145, v145, v87
	v_fma_f32 v110, -v145, v146, v110
	v_fma_f32 v111, -v146, v146, v111
	v_mul_f32_e64 v118, v110, v110
	v_mul_f32_e64 v119, v128, v111
	v_mul_f32_e64 v156, v86, v87
	v_mul_f32_e64 v157, v86, v86
	v_mul_f32_e64 v158, v29, v110
	v_mul_f32_e64 v159, v128, v128
	v_fma_f32 v118, v87, v111, -v118
	v_fma_f32 v119, v86, v110, -v119
	v_fma_f32 v156, v128, v110, -v156
	v_fma_f32 v157, v29, v111, -v157
	v_fma_f32 v158, v128, v86, -v158
	v_fma_f32 v159, v29, v87, -v159
	v_mul_f32_e64 v160, v29, v118
	v_fma_f32 v160, v128, v119, v160
	v_fma_f32 v160, v86, v156, v160
	v_rcp_f32_e32 v160, v160
	v_cmp_ne_u32_e64 vcc, s37, v3
	v_mul_f32_e64 v160, v160, v22
	v_cndmask_b32_e64 v160, 0, v160, s[30:31]
	v_cndmask_b32_e64 v29, 0, v18, vcc
	v_cndmask_b32_e64 v153, 0, v22, s[30:31]
	v_mul_f32_e64 v147, v118, v160
	v_mul_f32_e64 v148, v119, v160
	v_mul_f32_e64 v149, v156, v160
	v_mul_f32_e64 v150, v157, v160
	v_mul_f32_e64 v151, v158, v160
	v_mul_f32_e64 v152, v159, v160
	v_add_f32_e64 v154, v67, v29
	v_mov_b32_e32 v155, v3
	ds_write_b128 v23, v[144:147] offset:3072
	ds_write_b128 v23, v[148:151] offset:4096
	ds_write_b128 v23, v[152:155] offset:5120
	s_waitcnt lgkmcnt(0)
	s_barrier
	v_mov_b32_dpp v38, v48 wave_shr:1 row_mask:0xf bank_mask:0xf bound_ctrl:1
	v_mov_b32_dpp v54, v48 wave_shl:1 row_mask:0xf bank_mask:0xf bound_ctrl:1
	v_mul_f32_e64 v62, v48, v72
	v_mul_f32_e64 v66, v48, v73
	v_mul_f32_e64 v86, v48, v74
	v_add_f32_e64 v94, v48, v38
	v_fma_f32 v62, v38, v44, v62
	v_fma_f32 v66, v38, v45, v66
	v_fma_f32 v86, v38, v46, v86
	v_add_f32_e64 v94, v94, v54
	v_fma_f32 v62, v54, v68, v62
	v_fma_f32 v66, v54, v69, v66
	v_fma_f32 v86, v54, v70, v86
	v_add_f32_e64 v38, v30, v94
	v_add_f32_e64 v30, v120, v62
	v_add_f32_e64 v54, v80, v66
	v_add_f32_e64 v80, v92, v86
	v_fma_f32 v30, -v144, v38, v30
	v_fma_f32 v54, -v145, v38, v54
	v_fma_f32 v80, -v146, v38, v80
	v_mul_f32_e64 v92, v147, v30
	v_mul_f32_e64 v110, v148, v30
	v_mul_f32_e64 v118, v149, v30
	v_fma_f32 v92, v148, v54, v92
	v_fma_f32 v110, v150, v54, v110
	v_fma_f32 v118, v151, v54, v118
	v_fma_f32 v92, v149, v80, v92
	v_fma_f32 v110, v151, v80, v110
	v_fma_f32 v118, v152, v80, v118
	v_mul_f32_e64 v120, v144, v92
	v_fma_f32 v120, v145, v110, v120
	v_fma_f32 v120, v146, v118, v120
	v_fma_f32 v120, v153, v38, -v120
	v_cmp_eq_u32_e64 s[10:11], 7, v155
	v_add_f32_e64 v30, v50, v92
	v_add_f32_e64 v38, v90, v110
	v_add_f32_e64 v50, v116, v118
	v_add_f32_e64 v54, v124, v120
	v_fma_f32 v80, v76, v30, v54
	v_fma_f32 v90, v104, v30, v54
	v_fma_f32 v80, v77, v38, v80
	v_fma_f32 v90, v105, v38, v90
	v_fma_f32 v80, v78, v50, v80
	v_fma_f32 v90, v106, v50, v90
	v_fma_f32 v54, v32, v30, v54
	v_fma_f32 v54, v33, v38, v54
	v_fma_f32 v54, v34, v50, v54
	v_cndmask_b32_e64 v116, 0, v18, s[10:11]
	v_add_f32_dpp v54, v80, v54 wave_shl:1 row_mask:0xf bank_mask:0xf bound_ctrl:1
	s_add_i32 s4, s34, 5
	s_cmpk_lt_i32 s4, 0x201
	s_cselect_b64 s[12:13], s[0:1], 0
	v_add_f32_dpp v54, v90, v54 wave_shr:1 row_mask:0xf bank_mask:0xf bound_ctrl:1
	v_fma_f32 v54, v20, v154, -v54
	v_add_f32_e64 v54, v54, -v116
	v_mul_f32_e64 v124, v54, v54
	v_cndmask_b32_e64 v125, 0, v124, s[12:13]
	v_add_f32_e32 v1, v1, v125
	s_add_i32 s5, s34, 10
	s_min_i32 s5, s5, 0x200
	s_mul_i32 s6, s5, 0x804
	s_add_i32 s6, s6, s35
	s_add_i32 s7, s6, 0x606018
	s_mul_i32 s9, s5, 0x180c
	s_add_i32 s9, s9, s33
	s_add_i32 s4, s34, 11
	s_min_i32 s4, s4, 0x200
	s_mul_i32 s4, s4, 0x804
	s_add_i32 s4, s4, s38
	buffer_load_dword v3, v28, s[20:23], s4 offen nt
	buffer_load_dwordx3 v[32:34], v27, s[24:27], s9 offen nt
	buffer_load_dword v20, v28, s[16:19], s7 offen nt
	s_waitcnt vmcnt(6)
	v_mov_b32_dpp v76, v8 wave_shr:1 row_mask:0xf bank_mask:0xf bound_ctrl:1
	v_mov_b32_dpp v77, v9 wave_shr:1 row_mask:0xf bank_mask:0xf bound_ctrl:1
	v_mov_b32_dpp v78, v10 wave_shr:1 row_mask:0xf bank_mask:0xf bound_ctrl:1
	v_mov_b32_dpp v104, v8 wave_shl:1 row_mask:0xf bank_mask:0xf bound_ctrl:1
	v_mov_b32_dpp v105, v9 wave_shl:1 row_mask:0xf bank_mask:0xf bound_ctrl:1
	v_mov_b32_dpp v106, v10 wave_shl:1 row_mask:0xf bank_mask:0xf bound_ctrl:1
	s_add_i32 s4, s34, 9
	s_cmpk_lt_u32 s4, 0x201
	s_cselect_b64 s[12:13], s[40:41], 0
	v_cmp_eq_u32_e64 s[14:15], s37, v17
	s_and_b64 s[14:15], s[14:15], s[12:13]
	v_cndmask_b32_e64 v29, 0, 1, s[14:15]
	v_mul_f32_e64 v30, v8, v8
	v_mul_f32_e64 v31, v8, v9
	v_mul_f32_e64 v38, v8, v10
	v_mul_f32_e64 v39, v9, v9
	v_mul_f32_e64 v50, v9, v10
	v_mul_f32_e64 v51, v10, v10
	v_or_b32_dpp v52, v29, v29 wave_shr:1 row_mask:0xf bank_mask:0xf bound_ctrl:1
	s_nop 1
	v_or_b32_dpp v52, v29, v52 wave_shl:1 row_mask:0xf bank_mask:0xf bound_ctrl:1
	s_nop 1
	v_or_b32_dpp v128, v52, v52 wave_shr:1 row_mask:0xf bank_mask:0xf bound_ctrl:1
	s_nop 1
	v_or_b32_dpp v128, v52, v128 wave_shl:1 row_mask:0xf bank_mask:0xf bound_ctrl:1
	v_or3_b32 v29, v128, v129, v53
	v_or3_b32 v29, v29, v84, v85
	s_add_i32 s4, s34, 6
	s_cmpk_lt_u32 s4, 0x1ff
	s_cselect_b64 s[12:13], s[42:43], 0
	v_cmp_ne_u32_e64 s[30:31], 0, v29
	s_and_b64 s[30:31], s[30:31], s[12:13]
	v_cndmask_b32_e64 v29, 0, 1.0, s[30:31]
	v_add_f32_e64 v54, v8, v76
	v_add_f32_e64 v55, v9, v77
	v_add_f32_e64 v80, v10, v78
	v_fma_f32 v30, v76, v76, v30
	v_fma_f32 v31, v76, v77, v31
	v_fma_f32 v38, v76, v78, v38
	v_fma_f32 v39, v77, v77, v39
	v_fma_f32 v50, v77, v78, v50
	v_fma_f32 v51, v78, v78, v51
	v_add_f32_dpp v125, v29, v29 wave_shr:1 row_mask:0xf bank_mask:0xf bound_ctrl:1
	v_add_f32_e64 v54, v54, v104
	v_add_f32_e64 v55, v55, v105
	v_add_f32_e64 v80, v80, v106
	v_fma_f32 v81, v104, v104, v30
	v_fma_f32 v90, v104, v105, v31
	v_fma_f32 v91, v104, v106, v38
	v_fma_f32 v116, v105, v105, v39
	v_fma_f32 v117, v105, v106, v50
	v_fma_f32 v124, v106, v106, v51
	v_add_f32_dpp v125, v29, v125 wave_shl:1 row_mask:0xf bank_mask:0xf bound_ctrl:1
	v_pk_add_f32 v[30:31], v[134:135], v[54:55]
	v_pk_add_f32 v[38:39], v[58:59], v[30:31]
	v_pk_add_f32 v[50:51], v[136:137], v[80:81]
	v_pk_add_f32 v[58:59], v[60:61], v[50:51]
	v_pk_add_f32 v[60:61], v[138:139], v[90:91]
	v_pk_add_f32 v[134:135], v[64:65], v[60:61]
	v_pk_add_f32 v[64:65], v[140:141], v[116:117]
	v_pk_add_f32 v[136:137], v[82:83], v[64:65]
	v_pk_add_f32 v[82:83], v[142:143], v[124:125]
	v_pk_add_f32 v[138:139], v[112:113], v[82:83]
	v_mul_f32_e64 v140, v38, v22
	v_mul_f32_e64 v141, v39, v22
	v_mul_f32_e64 v142, v58, v22
	v_fma_f32 v29, v59, v22, v26
	v_mul_f32_e64 v52, v134, v22
	v_mul_f32_e64 v112, v135, v22
	v_fma_f32 v113, v136, v22, v26
	v_mul_f32_e64 v152, v137, v22
	v_fma_f32 v153, v138, v22, v26
	v_fma_f32 v29, -v140, v140, v29
	v_fma_f32 v52, -v140, v141, v52
	v_fma_f32 v112, -v140, v142, v112
	v_fma_f32 v113, -v141, v141, v113
	v_fma_f32 v152, -v141, v142, v152
	v_fma_f32 v153, -v142, v142, v153
	v_mul_f32_e64 v154, v152, v152
	v_mul_f32_e64 v155, v52, v153
	v_mul_f32_e64 v156, v112, v113
	v_mul_f32_e64 v157, v112, v112
	v_mul_f32_e64 v158, v29, v152
	v_mul_f32_e64 v159, v52, v52
	v_fma_f32 v154, v113, v153, -v154
	v_fma_f32 v155, v112, v152, -v155
	v_fma_f32 v156, v52, v152, -v156
	v_fma_f32 v157, v29, v153, -v157
	v_fma_f32 v158, v52, v112, -v158
	v_fma_f32 v159, v29, v113, -v159
	v_mul_f32_e64 v160, v29, v154
	v_fma_f32 v160, v52, v155, v160
	v_fma_f32 v160, v112, v156, v160
	v_rcp_f32_e32 v160, v160
	v_cmp_ne_u32_e64 vcc, s37, v16
	v_mul_f32_e64 v160, v160, v22
	v_cndmask_b32_e64 v160, 0, v160, s[30:31]
	v_cndmask_b32_e64 v29, 0, v18, vcc
	v_cndmask_b32_e64 v149, 0, v22, s[30:31]
	v_mul_f32_e64 v143, v154, v160
	v_mul_f32_e64 v144, v155, v160
	v_mul_f32_e64 v145, v156, v160
	v_mul_f32_e64 v146, v157, v160
	v_mul_f32_e64 v147, v158, v160
	v_mul_f32_e64 v148, v159, v160
	v_add_f32_e64 v150, v139, v29
	v_mov_b32_e32 v151, v16
	ds_write_b128 v23, v[140:143]
	ds_write_b128 v23, v[144:147] offset:1024
	ds_write_b128 v23, v[148:151] offset:2048
	s_waitcnt lgkmcnt(0)
	s_barrier
	v_mov_b32_dpp v38, v4 wave_shr:1 row_mask:0xf bank_mask:0xf bound_ctrl:1
	v_mov_b32_dpp v58, v4 wave_shl:1 row_mask:0xf bank_mask:0xf bound_ctrl:1
	v_mul_f32_e64 v112, v4, v8
	v_mul_f32_e64 v134, v4, v9
	v_mul_f32_e64 v136, v4, v10
	v_add_f32_e64 v138, v4, v38
	v_fma_f32 v112, v38, v76, v112
	v_fma_f32 v134, v38, v77, v134
	v_fma_f32 v136, v38, v78, v136
	v_add_f32_e64 v138, v138, v58
	v_fma_f32 v112, v58, v104, v112
	v_fma_f32 v134, v58, v105, v134
	v_fma_f32 v136, v58, v106, v136
	v_add_f32_e64 v38, v94, v138
	v_add_f32_e64 v58, v122, v38
	v_add_f32_e64 v94, v62, v112
	v_add_f32_e64 v122, v56, v94
	v_add_f32_e64 v56, v66, v134
	v_add_f32_e64 v62, v88, v56
	v_add_f32_e64 v66, v86, v136
	v_add_f32_e64 v88, v114, v66
	v_fma_f32 v122, -v140, v58, v122
	v_fma_f32 v62, -v141, v58, v62
	v_fma_f32 v88, -v142, v58, v88
	v_mul_f32_e64 v86, v143, v122
	v_mul_f32_e64 v114, v144, v122
	v_mul_f32_e64 v152, v145, v122
	v_fma_f32 v86, v144, v62, v86
	v_fma_f32 v114, v146, v62, v114
	v_fma_f32 v152, v147, v62, v152
	v_fma_f32 v86, v145, v88, v86
	v_fma_f32 v114, v147, v88, v114
	v_fma_f32 v152, v148, v88, v152
	v_mul_f32_e64 v154, v140, v86
	v_fma_f32 v154, v141, v114, v154
	v_fma_f32 v154, v142, v152, v154
	v_fma_f32 v154, v149, v58, -v154
	v_cmp_eq_u32_e64 s[10:11], 7, v151
	v_add_f32_e64 v58, v92, v86
	v_add_f32_e64 v62, v108, v58
	v_add_f32_e64 v88, v110, v114
	v_add_f32_e64 v92, v126, v88
	v_add_f32_e64 v108, v118, v152
	v_add_f32_e64 v110, v130, v108
	v_add_f32_e64 v118, v120, v154
	v_add_f32_e64 v122, v132, v118
	v_fma_f32 v120, v96, v62, v122
	v_fma_f32 v126, v100, v62, v122
	v_fma_f32 v120, v97, v92, v120
	v_fma_f32 v126, v101, v92, v126
	v_fma_f32 v120, v98, v110, v120
	v_fma_f32 v126, v102, v110, v126
	v_fma_f32 v122, v40, v62, v122
	v_fma_f32 v122, v41, v92, v122
	v_fma_f32 v122, v42, v110, v122
	v_cndmask_b32_e64 v130, 0, v18, s[10:11]
	v_add_f32_dpp v122, v120, v122 wave_shl:1 row_mask:0xf bank_mask:0xf bound_ctrl:1
	s_add_i32 s4, s34, 6
	s_cmpk_lt_i32 s4, 0x201
	s_cselect_b64 s[12:13], s[0:1], 0
	v_add_f32_dpp v122, v126, v122 wave_shr:1 row_mask:0xf bank_mask:0xf bound_ctrl:1
	v_fma_f32 v122, v36, v150, -v122
	v_add_f32_e64 v122, v122, -v130
	v_mul_f32_e64 v132, v122, v122
	v_cndmask_b32_e64 v133, 0, v132, s[12:13]
	v_add_f32_e32 v1, v1, v133
	s_add_i32 s5, s34, 11
	s_min_i32 s5, s5, 0x200
	s_mul_i32 s6, s5, 0x804
	s_add_i32 s6, s6, s35
	s_add_i32 s7, s6, 0x606018
	s_mul_i32 s9, s5, 0x180c
	s_add_i32 s9, s9, s33
	s_add_i32 s4, s34, 12
	s_min_i32 s4, s4, 0x200
	s_mul_i32 s4, s4, 0x804
	s_add_i32 s4, s4, s38
	buffer_load_dword v16, v28, s[20:23], s4 offen nt
	buffer_load_dwordx3 v[40:42], v27, s[24:27], s9 offen nt
	buffer_load_dword v36, v28, s[16:19], s7 offen nt
	s_waitcnt vmcnt(6)
	v_mov_b32_dpp v96, v12 wave_shr:1 row_mask:0xf bank_mask:0xf bound_ctrl:1
	v_mov_b32_dpp v97, v13 wave_shr:1 row_mask:0xf bank_mask:0xf bound_ctrl:1
	v_mov_b32_dpp v98, v14 wave_shr:1 row_mask:0xf bank_mask:0xf bound_ctrl:1
	v_mov_b32_dpp v100, v12 wave_shl:1 row_mask:0xf bank_mask:0xf bound_ctrl:1
	v_mov_b32_dpp v101, v13 wave_shl:1 row_mask:0xf bank_mask:0xf bound_ctrl:1
	v_mov_b32_dpp v102, v14 wave_shl:1 row_mask:0xf bank_mask:0xf bound_ctrl:1
	s_add_i32 s4, s34, 10
	s_cmpk_lt_u32 s4, 0x201
	s_cselect_b64 s[12:13], s[40:41], 0
	v_cmp_eq_u32_e64 s[14:15], s37, v2
	s_and_b64 s[14:15], s[14:15], s[12:13]
	v_cndmask_b32_e64 v29, 0, 1, s[14:15]
	v_mul_f32_e64 v62, v12, v12
	v_mul_f32_e64 v63, v12, v13
	v_mul_f32_e64 v92, v12, v14
	v_mul_f32_e64 v93, v13, v13
	v_mul_f32_e64 v110, v13, v14
	v_mul_f32_e64 v111, v14, v14
	v_or_b32_dpp v52, v29, v29 wave_shr:1 row_mask:0xf bank_mask:0xf bound_ctrl:1
	s_nop 1
	v_or_b32_dpp v52, v29, v52 wave_shl:1 row_mask:0xf bank_mask:0xf bound_ctrl:1
	s_nop 1
	v_or_b32_dpp v85, v52, v52 wave_shr:1 row_mask:0xf bank_mask:0xf bound_ctrl:1
	s_nop 1
	v_or_b32_dpp v85, v52, v85 wave_shl:1 row_mask:0xf bank_mask:0xf bound_ctrl:1
	v_or3_b32 v29, v85, v128, v129
	v_or3_b32 v29, v29, v53, v84
	s_add_i32 s4, s34, 7
	s_cmpk_lt_u32 s4, 0x1ff
	s_cselect_b64 s[12:13], s[42:43], 0
	v_cmp_ne_u32_e64 s[30:31], 0, v29
	s_and_b64 s[30:31], s[30:31], s[12:13]
	v_cndmask_b32_e64 v29, 0, 1.0, s[30:31]
	v_add_f32_e64 v120, v12, v96
	v_add_f32_e64 v121, v13, v97
	v_add_f32_e64 v122, v14, v98
	v_fma_f32 v62, v96, v96, v62
	v_fma_f32 v63, v96, v97, v63
	v_fma_f32 v92, v96, v98, v92
	v_fma_f32 v93, v97, v97, v93
	v_fma_f32 v110, v97, v98, v110
	v_fma_f32 v111, v98, v98, v111
	v_add_f32_dpp v133, v29, v29 wave_shr:1 row_mask:0xf bank_mask:0xf bound_ctrl:1
	v_add_f32_e64 v120, v120, v100
	v_add_f32_e64 v121, v121, v101
	v_add_f32_e64 v122, v122, v102
	v_fma_f32 v123, v100, v100, v62
	v_fma_f32 v126, v100, v101, v63
	v_fma_f32 v127, v100, v102, v92
	v_fma_f32 v130, v101, v101, v93
	v_fma_f32 v131, v101, v102, v110
	v_fma_f32 v132, v102, v102, v111
	v_add_f32_dpp v133, v29, v133 wave_shl:1 row_mask:0xf bank_mask:0xf bound_ctrl:1
	v_pk_add_f32 v[62:63], v[30:31], v[120:121]
	v_pk_add_f32 v[30:31], v[50:51], v[122:123]
	v_pk_add_f32 v[50:51], v[60:61], v[126:127]
	v_pk_add_f32 v[60:61], v[64:65], v[130:131]
	v_pk_add_f32 v[64:65], v[82:83], v[132:133]
	v_mul_f32_e64 v140, v62, v22
	v_mul_f32_e64 v141, v63, v22
	v_mul_f32_e64 v142, v30, v22
	v_fma_f32 v29, v31, v22, v26
	v_mul_f32_e64 v52, v50, v22
	v_mul_f32_e64 v82, v51, v22
	v_fma_f32 v83, v60, v22, v26
	v_mul_f32_e64 v92, v61, v22
	v_fma_f32 v93, v64, v22, v26
	v_fma_f32 v29, -v140, v140, v29
	v_fma_f32 v52, -v140, v141, v52
	v_fma_f32 v82, -v140, v142, v82
	v_fma_f32 v83, -v141, v141, v83
	v_fma_f32 v92, -v141, v142, v92
	v_fma_f32 v93, -v142, v142, v93
	v_mul_f32_e64 v110, v92, v92
	v_mul_f32_e64 v111, v52, v93
	v_mul_f32_e64 v156, v82, v83
	v_mul_f32_e64 v157, v82, v82
	v_mul_f32_e64 v158, v29, v92
	v_mul_f32_e64 v159, v52, v52
	v_fma_f32 v110, v83, v93, -v110
	v_fma_f32 v111, v82, v92, -v111
	v_fma_f32 v156, v52, v92, -v156
	v_fma_f32 v157, v29, v93, -v157
	v_fma_f32 v158, v52, v82, -v158
	v_fma_f32 v159, v29, v83, -v159
	v_mul_f32_e64 v160, v29, v110
	v_fma_f32 v160, v52, v111, v160
	v_fma_f32 v160, v82, v156, v160
	v_rcp_f32_e32 v160, v160
	v_cmp_ne_u32_e64 vcc, s37, v25
	v_mul_f32_e64 v160, v160, v22
	v_cndmask_b32_e64 v160, 0, v160, s[30:31]
	v_cndmask_b32_e64 v29, 0, v18, vcc
	v_cndmask_b32_e64 v149, 0, v22, s[30:31]
	v_mul_f32_e64 v143, v110, v160
	v_mul_f32_e64 v144, v111, v160
	v_mul_f32_e64 v145, v156, v160
	v_mul_f32_e64 v146, v157, v160
	v_mul_f32_e64 v147, v158, v160
	v_mul_f32_e64 v148, v159, v160
	v_add_f32_e64 v150, v65, v29
	v_mov_b32_e32 v151, v25
	ds_write_b128 v23, v[140:143] offset:3072
	ds_write_b128 v23, v[144:147] offset:4096
	ds_write_b128 v23, v[148:151] offset:5120
	s_waitcnt lgkmcnt(0)
	s_barrier
	v_mov_b32_dpp v30, v6 wave_shr:1 row_mask:0xf bank_mask:0xf bound_ctrl:1
	v_mov_b32_dpp v50, v6 wave_shl:1 row_mask:0xf bank_mask:0xf bound_ctrl:1
	v_mul_f32_e64 v60, v6, v12
	v_mul_f32_e64 v62, v6, v13
	v_mul_f32_e64 v64, v6, v14
	v_add_f32_e64 v82, v6, v30
	v_fma_f32 v60, v30, v96, v60
	v_fma_f32 v62, v30, v97, v62
	v_fma_f32 v64, v30, v98, v64
	v_add_f32_e64 v82, v82, v50
	v_fma_f32 v60, v50, v100, v60
	v_fma_f32 v62, v50, v101, v62
	v_fma_f32 v64, v50, v102, v64
	v_add_f32_e64 v30, v38, v82
	v_add_f32_e64 v38, v94, v60
	v_add_f32_e64 v50, v56, v62
	v_add_f32_e64 v56, v66, v64
	v_fma_f32 v38, -v140, v30, v38
	v_fma_f32 v50, -v141, v30, v50
	v_fma_f32 v56, -v142, v30, v56
	v_mul_f32_e64 v66, v143, v38
	v_mul_f32_e64 v92, v144, v38
	v_mul_f32_e64 v94, v145, v38
	v_fma_f32 v66, v144, v50, v66
	v_fma_f32 v92, v146, v50, v92
	v_fma_f32 v94, v147, v50, v94
	v_fma_f32 v66, v145, v56, v66
	v_fma_f32 v92, v147, v56, v92
	v_fma_f32 v94, v148, v56, v94
	v_mul_f32_e64 v110, v140, v66
	v_fma_f32 v110, v141, v92, v110
	v_fma_f32 v110, v142, v94, v110
	v_fma_f32 v110, v149, v30, -v110
	v_cmp_eq_u32_e64 s[10:11], 7, v151
	v_add_f32_e64 v30, v58, v66
	v_add_f32_e64 v38, v88, v92
	v_add_f32_e64 v50, v108, v94
	v_add_f32_e64 v56, v118, v110
	v_fma_f32 v58, v44, v30, v56
	v_fma_f32 v88, v68, v30, v56
	v_fma_f32 v58, v45, v38, v58
	v_fma_f32 v88, v69, v38, v88
	v_fma_f32 v58, v46, v50, v58
	v_fma_f32 v88, v70, v50, v88
	v_fma_f32 v56, v72, v30, v56
	v_fma_f32 v56, v73, v38, v56
	v_fma_f32 v56, v74, v50, v56
	v_cndmask_b32_e64 v108, 0, v18, s[10:11]
	v_add_f32_dpp v56, v58, v56 wave_shl:1 row_mask:0xf bank_mask:0xf bound_ctrl:1
	s_add_i32 s4, s34, 7
	s_cmpk_lt_i32 s4, 0x201
	s_cselect_b64 s[12:13], s[0:1], 0
	v_add_f32_dpp v56, v88, v56 wave_shr:1 row_mask:0xf bank_mask:0xf bound_ctrl:1
	v_fma_f32 v56, v48, v150, -v56
	v_add_f32_e64 v56, v56, -v108
	v_mul_f32_e64 v118, v56, v56
	v_cndmask_b32_e64 v119, 0, v118, s[12:13]
	v_add_f32_e32 v1, v1, v119
	s_waitcnt vmcnt(3)
	v_mov_b32_dpp v44, v32 wave_shr:1 row_mask:0xf bank_mask:0xf bound_ctrl:1
	v_mov_b32_dpp v45, v33 wave_shr:1 row_mask:0xf bank_mask:0xf bound_ctrl:1
	v_mov_b32_dpp v46, v34 wave_shr:1 row_mask:0xf bank_mask:0xf bound_ctrl:1
	v_mov_b32_dpp v48, v32 wave_shl:1 row_mask:0xf bank_mask:0xf bound_ctrl:1
	v_mov_b32_dpp v49, v33 wave_shl:1 row_mask:0xf bank_mask:0xf bound_ctrl:1
	v_mov_b32_dpp v50, v34 wave_shl:1 row_mask:0xf bank_mask:0xf bound_ctrl:1
	s_add_i32 s4, s34, 11
	s_cmpk_lt_u32 s4, 0x201
	s_cselect_b64 s[12:13], s[40:41], 0
	v_cmp_eq_u32_e64 s[14:15], s37, v3
	s_and_b64 s[14:15], s[14:15], s[12:13]
	v_cndmask_b32_e64 v25, 0, 1, s[14:15]
	v_mul_f32_e64 v30, v32, v32
	v_mul_f32_e64 v31, v32, v33
	v_mul_f32_e64 v38, v32, v34
	v_mul_f32_e64 v39, v33, v33
	v_mul_f32_e64 v56, v33, v34
	v_mul_f32_e64 v57, v34, v34
	v_or_b32_dpp v29, v25, v25 wave_shr:1 row_mask:0xf bank_mask:0xf bound_ctrl:1
	s_nop 1
	v_or_b32_dpp v29, v25, v29 wave_shl:1 row_mask:0xf bank_mask:0xf bound_ctrl:1
	s_nop 1
	v_or_b32_dpp v52, v29, v29 wave_shr:1 row_mask:0xf bank_mask:0xf bound_ctrl:1
	s_nop 1
	v_or_b32_dpp v52, v29, v52 wave_shl:1 row_mask:0xf bank_mask:0xf bound_ctrl:1
	v_or3_b32 v25, v52, v85, v128
	v_or3_b32 v25, v25, v129, v53
	s_add_i32 s4, s34, 8
	s_cmpk_lt_u32 s4, 0x1ff
	s_cselect_b64 s[12:13], s[42:43], 0
	v_cmp_ne_u32_e64 s[30:31], 0, v25
	s_and_b64 s[30:31], s[30:31], s[12:13]
	v_cndmask_b32_e64 v25, 0, 1.0, s[30:31]
	v_add_f32_e64 v58, v32, v44
	v_add_f32_e64 v59, v33, v45
	v_add_f32_e64 v68, v34, v46
	v_fma_f32 v30, v44, v44, v30
	v_fma_f32 v31, v44, v45, v31
	v_fma_f32 v38, v44, v46, v38
	v_fma_f32 v39, v45, v45, v39
	v_fma_f32 v56, v45, v46, v56
	v_fma_f32 v57, v46, v46, v57
	v_add_f32_dpp v75, v25, v25 wave_shr:1 row_mask:0xf bank_mask:0xf bound_ctrl:1
	v_add_f32_e64 v58, v58, v48
	v_add_f32_e64 v59, v59, v49
	v_add_f32_e64 v68, v68, v50
	v_fma_f32 v69, v48, v48, v30
	v_fma_f32 v70, v48, v49, v31
	v_fma_f32 v71, v48, v50, v38
	v_fma_f32 v72, v49, v49, v39
	v_fma_f32 v73, v49, v50, v56
	v_fma_f32 v74, v50, v50, v57
	v_add_f32_dpp v75, v25, v75 wave_shl:1 row_mask:0xf bank_mask:0xf bound_ctrl:1
	v_pk_add_f32 v[30:31], v[120:121], v[58:59]
	v_pk_add_f32 v[38:39], v[54:55], v[30:31]
	v_pk_add_f32 v[54:55], v[122:123], v[68:69]
	v_pk_add_f32 v[56:57], v[80:81], v[54:55]
	v_pk_add_f32 v[80:81], v[126:127], v[70:71]
	v_pk_add_f32 v[88:89], v[90:91], v[80:81]
	v_pk_add_f32 v[90:91], v[130:131], v[72:73]
	v_pk_add_f32 v[108:109], v[116:117], v[90:91]
	v_pk_add_f32 v[116:117], v[132:133], v[74:75]
	v_pk_add_f32 v[118:119], v[124:125], v[116:117]
	v_mul_f32_e64 v120, v38, v22
	v_mul_f32_e64 v121, v39, v22
	v_mul_f32_e64 v122, v56, v22
	v_fma_f32 v25, v57, v22, v26
	v_mul_f32_e64 v29, v88, v22
	v_mul_f32_e64 v84, v89, v22
	v_fma_f32 v130, v108, v22, v26
	v_mul_f32_e64 v131, v109, v22
	v_fma_f32 v132, v118, v22, v26
	v_fma_f32 v25, -v120, v120, v25
	v_fma_f32 v29, -v120, v121, v29
	v_fma_f32 v84, -v120, v122, v84
	v_fma_f32 v130, -v121, v121, v130
	v_fma_f32 v131, -v121, v122, v131
	v_fma_f32 v132, -v122, v122, v132
	v_mul_f32_e64 v133, v131, v131
	v_mul_f32_e64 v144, v29, v132
	v_mul_f32_e64 v145, v84, v130
	v_mul_f32_e64 v146, v84, v84
	v_mul_f32_e64 v147, v25, v131
	v_mul_f32_e64 v148, v29, v29
	v_fma_f32 v133, v130, v132, -v133
	v_fma_f32 v144, v84, v131, -v144
	v_fma_f32 v145, v29, v131, -v145
	v_fma_f32 v146, v25, v132, -v146
	v_fma_f32 v147, v29, v84, -v147
	v_fma_f32 v148, v25, v130, -v148
	v_mul_f32_e64 v149, v25, v133
	v_fma_f32 v149, v29, v144, v149
	v_fma_f32 v149, v84, v145, v149
	v_rcp_f32_e32 v149, v149
	v_cmp_ne_u32_e64 vcc, s37, v24
	v_mul_f32_e64 v149, v149, v22
	v_cndmask_b32_e64 v149, 0, v149, s[30:31]
	v_cndmask_b32_e64 v25, 0, v18, vcc
	v_cndmask_b32_e64 v141, 0, v22, s[30:31]
	v_mul_f32_e64 v123, v133, v149
	v_mul_f32_e64 v124, v144, v149
	v_mul_f32_e64 v125, v145, v149
	v_mul_f32_e64 v126, v146, v149
	v_mul_f32_e64 v127, v147, v149
	v_mul_f32_e64 v140, v148, v149
	v_add_f32_e64 v142, v119, v25
	v_mov_b32_e32 v143, v24
	ds_write_b128 v23, v[120:123]
	ds_write_b128 v23, v[124:127] offset:1024
	ds_write_b128 v23, v[140:143] offset:2048
	s_waitcnt lgkmcnt(0)
	s_barrier
	v_mov_b32_dpp v24, v20 wave_shr:1 row_mask:0xf bank_mask:0xf bound_ctrl:1
	v_mov_b32_dpp v38, v20 wave_shl:1 row_mask:0xf bank_mask:0xf bound_ctrl:1
	v_mul_f32_e64 v56, v20, v32
	v_mul_f32_e64 v88, v20, v33
	v_mul_f32_e64 v108, v20, v34
	v_add_f32_e64 v118, v20, v24
	v_fma_f32 v56, v24, v44, v56
	v_fma_f32 v88, v24, v45, v88
	v_fma_f32 v108, v24, v46, v108
	v_add_f32_e64 v118, v118, v38
	v_fma_f32 v56, v38, v48, v56
	v_fma_f32 v88, v38, v49, v88
	v_fma_f32 v108, v38, v50, v108
	v_add_f32_e64 v24, v82, v118
	v_add_f32_e64 v38, v138, v24
	v_add_f32_e64 v82, v60, v56
	v_add_f32_e64 v130, v112, v82
	v_add_f32_e64 v60, v62, v88
	v_add_f32_e64 v112, v134, v60
	v_add_f32_e64 v62, v64, v108
	v_add_f32_e64 v132, v136, v62
	v_fma_f32 v130, -v120, v38, v130
	v_fma_f32 v112, -v121, v38, v112
	v_fma_f32 v132, -v122, v38, v132
	v_mul_f32_e64 v64, v123, v130
	v_mul_f32_e64 v134, v124, v130
	v_mul_f32_e64 v136, v125, v130
	v_fma_f32 v64, v124, v112, v64
	v_fma_f32 v134, v126, v112, v134
	v_fma_f32 v136, v127, v112, v136
	v_fma_f32 v64, v125, v132, v64
	v_fma_f32 v134, v127, v132, v134
	v_fma_f32 v136, v140, v132, v136
	v_mul_f32_e64 v138, v120, v64
	v_fma_f32 v138, v121, v134, v138
	v_fma_f32 v138, v122, v136, v138
	v_fma_f32 v138, v141, v38, -v138
	v_cmp_eq_u32_e64 s[10:11], 7, v143
	v_add_f32_e64 v38, v66, v64
	v_add_f32_e64 v112, v86, v38
	v_add_f32_e64 v66, v92, v134
	v_add_f32_e64 v86, v114, v66
	v_add_f32_e64 v92, v94, v136
	v_add_f32_e64 v114, v152, v92
	v_add_f32_e64 v94, v110, v138
	v_add_f32_e64 v130, v154, v94
	v_fma_f32 v110, v76, v112, v130
	v_fma_f32 v132, v104, v112, v130
	v_fma_f32 v110, v77, v86, v110
	v_fma_f32 v132, v105, v86, v132
	v_fma_f32 v110, v78, v114, v110
	v_fma_f32 v132, v106, v114, v132
	v_fma_f32 v130, v8, v112, v130
	v_fma_f32 v130, v9, v86, v130
	v_fma_f32 v130, v10, v114, v130
	v_cndmask_b32_e64 v144, 0, v18, s[10:11]
	v_add_f32_dpp v130, v110, v130 wave_shl:1 row_mask:0xf bank_mask:0xf bound_ctrl:1
	s_add_i32 s4, s34, 8
	s_cmpk_lt_i32 s4, 0x201
	s_cselect_b64 s[12:13], s[0:1], 0
	v_add_f32_dpp v130, v132, v130 wave_shr:1 row_mask:0xf bank_mask:0xf bound_ctrl:1
	v_fma_f32 v130, v4, v142, -v130
	v_add_f32_e64 v130, v130, -v144
	v_mul_f32_e64 v146, v130, v130
	v_cndmask_b32_e64 v147, 0, v146, s[12:13]
	v_add_f32_e32 v1, v1, v147
	s_waitcnt vmcnt(0)
	v_mov_b32_dpp v8, v40 wave_shr:1 row_mask:0xf bank_mask:0xf bound_ctrl:1
	v_mov_b32_dpp v9, v41 wave_shr:1 row_mask:0xf bank_mask:0xf bound_ctrl:1
	v_mov_b32_dpp v10, v42 wave_shr:1 row_mask:0xf bank_mask:0xf bound_ctrl:1
	v_mov_b32_dpp v76, v40 wave_shl:1 row_mask:0xf bank_mask:0xf bound_ctrl:1
	v_mov_b32_dpp v77, v41 wave_shl:1 row_mask:0xf bank_mask:0xf bound_ctrl:1
	v_mov_b32_dpp v78, v42 wave_shl:1 row_mask:0xf bank_mask:0xf bound_ctrl:1
	s_add_i32 s4, s34, 12
	s_cmpk_lt_u32 s4, 0x201
	s_cselect_b64 s[12:13], s[40:41], 0
	v_cmp_eq_u32_e64 s[14:15], s37, v16
	s_and_b64 s[14:15], s[14:15], s[12:13]
	v_cndmask_b32_e64 v29, 0, 1, s[14:15]
	v_mul_f32_e64 v4, v40, v40
	v_mul_f32_e64 v5, v40, v41
	v_mul_f32_e64 v86, v40, v42
	v_mul_f32_e64 v87, v41, v41
	v_mul_f32_e64 v104, v41, v42
	v_mul_f32_e64 v105, v42, v42
	v_or_b32_dpp v53, v29, v29 wave_shr:1 row_mask:0xf bank_mask:0xf bound_ctrl:1
	s_nop 1
	v_or_b32_dpp v53, v29, v53 wave_shl:1 row_mask:0xf bank_mask:0xf bound_ctrl:1
	s_nop 1
	v_or_b32_dpp v84, v53, v53 wave_shr:1 row_mask:0xf bank_mask:0xf bound_ctrl:1
	s_nop 1
	v_or_b32_dpp v84, v53, v84 wave_shl:1 row_mask:0xf bank_mask:0xf bound_ctrl:1
	v_or3_b32 v29, v84, v52, v85
	v_or3_b32 v29, v29, v128, v129
	s_add_i32 s4, s34, 9
	s_cmpk_lt_u32 s4, 0x1ff
	s_cselect_b64 s[12:13], s[42:43], 0
	v_cmp_ne_u32_e64 s[30:31], 0, v29
	s_and_b64 s[30:31], s[30:31], s[12:13]
	v_cndmask_b32_e64 v29, 0, 1.0, s[30:31]
	v_add_f32_e64 v106, v40, v8
	v_add_f32_e64 v107, v41, v9
	v_add_f32_e64 v110, v42, v10
	v_fma_f32 v4, v8, v8, v4
	v_fma_f32 v5, v8, v9, v5
	v_fma_f32 v86, v8, v10, v86
	v_fma_f32 v87, v9, v9, v87
	v_fma_f32 v104, v9, v10, v104
	v_fma_f32 v105, v10, v10, v105
	v_add_f32_dpp v121, v29, v29 wave_shr:1 row_mask:0xf bank_mask:0xf bound_ctrl:1
	v_add_f32_e64 v106, v106, v76
	v_add_f32_e64 v107, v107, v77
	v_add_f32_e64 v110, v110, v78
	v_fma_f32 v111, v76, v76, v4
	v_fma_f32 v112, v76, v77, v5
	v_fma_f32 v113, v76, v78, v86
	v_fma_f32 v114, v77, v77, v87
	v_fma_f32 v115, v77, v78, v104
	v_fma_f32 v120, v78, v78, v105
	v_add_f32_dpp v121, v29, v121 wave_shl:1 row_mask:0xf bank_mask:0xf bound_ctrl:1
	v_pk_add_f32 v[4:5], v[30:31], v[106:107]
	v_pk_add_f32 v[30:31], v[54:55], v[110:111]
	v_pk_add_f32 v[54:55], v[80:81], v[112:113]
	v_pk_add_f32 v[80:81], v[90:91], v[114:115]
	v_pk_add_f32 v[86:87], v[116:117], v[120:121]
	v_mul_f32_e64 v124, v4, v22
	v_mul_f32_e64 v125, v5, v22
	v_mul_f32_e64 v126, v30, v22
	v_fma_f32 v29, v31, v22, v26
	v_mul_f32_e64 v53, v54, v22
	v_mul_f32_e64 v90, v55, v22
	v_fma_f32 v91, v80, v22, v26
	v_mul_f32_e64 v104, v81, v22
	v_fma_f32 v105, v86, v22, v26
	v_fma_f32 v29, -v124, v124, v29
	v_fma_f32 v53, -v124, v125, v53
	v_fma_f32 v90, -v124, v126, v90
	v_fma_f32 v91, -v125, v125, v91
	v_fma_f32 v104, -v125, v126, v104
	v_fma_f32 v105, -v126, v126, v105
	v_mul_f32_e64 v116, v104, v104
	v_mul_f32_e64 v117, v53, v105
	v_mul_f32_e64 v122, v90, v91
	v_mul_f32_e64 v123, v90, v90
	v_mul_f32_e64 v130, v29, v104
	v_mul_f32_e64 v131, v53, v53
	v_fma_f32 v116, v91, v105, -v116
	v_fma_f32 v117, v90, v104, -v117
	v_fma_f32 v122, v53, v104, -v122
	v_fma_f32 v123, v29, v105, -v123
	v_fma_f32 v130, v53, v90, -v130
	v_fma_f32 v131, v29, v91, -v131
	v_mul_f32_e64 v132, v29, v116
	v_fma_f32 v132, v53, v117, v132
	v_fma_f32 v132, v90, v122, v132
	v_rcp_f32_e32 v132, v132
	v_cmp_ne_u32_e64 vcc, s37, v17
	v_mul_f32_e64 v132, v132, v22
	v_cndmask_b32_e64 v132, 0, v132, s[30:31]
	v_cndmask_b32_e64 v29, 0, v18, vcc
	v_cndmask_b32_e64 v145, 0, v22, s[30:31]
	v_mul_f32_e64 v127, v116, v132
	v_mul_f32_e64 v140, v117, v132
	v_mul_f32_e64 v141, v122, v132
	v_mul_f32_e64 v142, v123, v132
	v_mul_f32_e64 v143, v130, v132
	v_mul_f32_e64 v144, v131, v132
	v_add_f32_e64 v146, v87, v29
	v_mov_b32_e32 v147, v17
	ds_write_b128 v23, v[124:127] offset:3072
	ds_write_b128 v23, v[140:143] offset:4096
	ds_write_b128 v23, v[144:147] offset:5120
	s_waitcnt lgkmcnt(0)
	s_barrier
	v_mov_b32_dpp v4, v36 wave_shr:1 row_mask:0xf bank_mask:0xf bound_ctrl:1
	v_mov_b32_dpp v30, v36 wave_shl:1 row_mask:0xf bank_mask:0xf bound_ctrl:1
	v_mul_f32_e64 v54, v36, v40
	v_mul_f32_e64 v80, v36, v41
	v_mul_f32_e64 v86, v36, v42
	v_add_f32_e64 v90, v36, v4
	v_fma_f32 v54, v4, v8, v54
	v_fma_f32 v80, v4, v9, v80
	v_fma_f32 v86, v4, v10, v86
	v_add_f32_e64 v90, v90, v30
	v_fma_f32 v54, v30, v76, v54
	v_fma_f32 v80, v30, v77, v80
	v_fma_f32 v86, v30, v78, v86
	v_add_f32_e64 v4, v24, v90
	v_add_f32_e64 v24, v82, v54
	v_add_f32_e64 v30, v60, v80
	v_add_f32_e64 v60, v62, v86
	v_fma_f32 v24, -v124, v4, v24
	v_fma_f32 v30, -v125, v4, v30
	v_fma_f32 v60, -v126, v4, v60
	v_mul_f32_e64 v62, v127, v24
	v_mul_f32_e64 v82, v140, v24
	v_mul_f32_e64 v104, v141, v24
	v_fma_f32 v62, v140, v30, v62
	v_fma_f32 v82, v142, v30, v82
	v_fma_f32 v104, v143, v30, v104
	v_fma_f32 v62, v141, v60, v62
	v_fma_f32 v82, v143, v60, v82
	v_fma_f32 v104, v144, v60, v104
	v_mul_f32_e64 v116, v124, v62
	v_fma_f32 v116, v125, v82, v116
	v_fma_f32 v116, v126, v104, v116
	v_fma_f32 v116, v145, v4, -v116
	v_cmp_eq_u32_e64 s[10:11], 7, v147
	v_add_f32_e64 v4, v38, v62
	v_add_f32_e64 v24, v66, v82
	v_add_f32_e64 v30, v92, v104
	v_add_f32_e64 v38, v94, v116
	v_fma_f32 v60, v96, v4, v38
	v_fma_f32 v66, v100, v4, v38
	v_fma_f32 v60, v97, v24, v60
	v_fma_f32 v66, v101, v24, v66
	v_fma_f32 v60, v98, v30, v60
	v_fma_f32 v66, v102, v30, v66
	v_fma_f32 v38, v12, v4, v38
	v_fma_f32 v38, v13, v24, v38
	v_fma_f32 v38, v14, v30, v38
	v_cndmask_b32_e64 v92, 0, v18, s[10:11]
	v_add_f32_dpp v38, v60, v38 wave_shl:1 row_mask:0xf bank_mask:0xf bound_ctrl:1
	s_add_i32 s4, s34, 9
	s_cmpk_lt_i32 s4, 0x201
	s_cselect_b64 s[12:13], s[0:1], 0
	v_add_f32_dpp v38, v66, v38 wave_shr:1 row_mask:0xf bank_mask:0xf bound_ctrl:1
	v_fma_f32 v38, v6, v146, -v38
	v_add_f32_e64 v38, v38, -v92
	v_mul_f32_e64 v94, v38, v38
	v_cndmask_b32_e64 v95, 0, v94, s[12:13]
	v_add_f32_e32 v1, v1, v95
	v_mov_b32_e32 v0, v1
	s_branch .LBB0_29
.LBB0_15:
.LBB0_16:
	s_mov_b32 s27, s19
	v_mov_b32_e32 v1, 0x42c80000
	v_mov_b32_e32 v0, 0
	s_add_i32 s4, s34, -2
	s_max_i32 s4, s4, 0
	s_mul_i32 s5, s4, 0x804
	s_add_i32 s5, s5, s35
	s_add_i32 s6, s5, 0x0
	s_add_i32 s7, s5, 0x101004
	s_add_i32 s8, s5, 0x202008
	s_add_i32 s11, s5, 0x30300c
	s_add_i32 s15, s5, 0x404010
	s_add_i32 s31, s5, 0x505014
	s_mul_i32 s9, s4, 0x180c
	s_add_i32 s9, s9, s33
	buffer_load_dword v2, v28, s[16:19], s6 offen nt
	buffer_load_dword v3, v28, s[16:19], s7 offen nt
	buffer_load_dword v4, v28, s[16:19], s8 offen nt
	buffer_load_dword v5, v28, s[16:19], s11 offen nt
	buffer_load_dword v6, v28, s[16:19], s15 offen nt
	buffer_load_dword v7, v28, s[16:19], s31 offen nt
	buffer_load_dwordx3 v[8:10], v27, s[24:27], s9 offen nt
	s_add_i32 s4, s34, -1
	s_max_i32 s4, s4, 0
	s_mul_i32 s5, s4, 0x804
	s_add_i32 s5, s5, s35
	s_add_i32 s6, s5, 0x0
	s_add_i32 s7, s5, 0x101004
	s_add_i32 s8, s5, 0x202008
	s_add_i32 s11, s5, 0x30300c
	s_add_i32 s15, s5, 0x404010
	s_add_i32 s31, s5, 0x505014
	s_mul_i32 s9, s4, 0x180c
	s_add_i32 s9, s9, s33
	buffer_load_dword v12, v28, s[16:19], s6 offen nt
	buffer_load_dword v13, v28, s[16:19], s7 offen nt
	buffer_load_dword v14, v28, s[16:19], s8 offen nt
	buffer_load_dword v15, v28, s[16:19], s11 offen nt
	buffer_load_dword v16, v28, s[16:19], s15 offen nt
	buffer_load_dword v17, v28, s[16:19], s31 offen nt
	buffer_load_dwordx3 v[32:34], v27, s[24:27], s9 offen nt
	s_add_i32 s4, s34, 0
	s_min_i32 s4, s4, 0x200
	s_mul_i32 s5, s4, 0x804
	s_add_i32 s5, s5, s35
	s_add_i32 s6, s5, 0x0
	s_add_i32 s7, s5, 0x101004
	s_add_i32 s8, s5, 0x202008
	s_add_i32 s11, s5, 0x30300c
	s_add_i32 s15, s5, 0x404010
	s_add_i32 s31, s5, 0x505014
	s_mul_i32 s9, s4, 0x180c
	s_add_i32 s9, s9, s33
	buffer_load_dword v20, v28, s[16:19], s6 offen nt
	buffer_load_dword v21, v28, s[16:19], s7 offen nt
	buffer_load_dword v24, v28, s[16:19], s8 offen nt
	buffer_load_dword v25, v28, s[16:19], s11 offen nt
	buffer_load_dword v30, v28, s[16:19], s15 offen nt
	buffer_load_dword v31, v28, s[16:19], s31 offen nt
	buffer_load_dwordx3 v[36:38], v27, s[24:27], s9 offen nt
	s_waitcnt vmcnt(14)
	v_mov_b32_dpp v40, v8 wave_shr:1 row_mask:0xf bank_mask:0xf bound_ctrl:1
	v_mov_b32_dpp v41, v9 wave_shr:1 row_mask:0xf bank_mask:0xf bound_ctrl:1
	v_mov_b32_dpp v42, v10 wave_shr:1 row_mask:0xf bank_mask:0xf bound_ctrl:1
	v_mov_b32_dpp v44, v8 wave_shl:1 row_mask:0xf bank_mask:0xf bound_ctrl:1
	v_mov_b32_dpp v45, v9 wave_shl:1 row_mask:0xf bank_mask:0xf bound_ctrl:1
	v_mov_b32_dpp v46, v10 wave_shl:1 row_mask:0xf bank_mask:0xf bound_ctrl:1
	v_mov_b32_dpp v48, v2 wave_shr:1 row_mask:0xf bank_mask:0xf bound_ctrl:1
	v_mov_b32_dpp v49, v3 wave_shr:1 row_mask:0xf bank_mask:0xf bound_ctrl:1
	v_mov_b32_dpp v50, v4 wave_shr:1 row_mask:0xf bank_mask:0xf bound_ctrl:1
	v_mov_b32_dpp v51, v5 wave_shr:1 row_mask:0xf bank_mask:0xf bound_ctrl:1
	v_mov_b32_dpp v52, v6 wave_shr:1 row_mask:0xf bank_mask:0xf bound_ctrl:1
	v_mov_b32_dpp v53, v7 wave_shr:1 row_mask:0xf bank_mask:0xf bound_ctrl:1
	v_mov_b32_dpp v54, v2 wave_shl:1 row_mask:0xf bank_mask:0xf bound_ctrl:1
	v_mov_b32_dpp v55, v3 wave_shl:1 row_mask:0xf bank_mask:0xf bound_ctrl:1
	v_mov_b32_dpp v56, v4 wave_shl:1 row_mask:0xf bank_mask:0xf bound_ctrl:1
	v_mov_b32_dpp v57, v5 wave_shl:1 row_mask:0xf bank_mask:0xf bound_ctrl:1
	v_mov_b32_dpp v58, v6 wave_shl:1 row_mask:0xf bank_mask:0xf bound_ctrl:1
	v_mov_b32_dpp v59, v7 wave_shl:1 row_mask:0xf bank_mask:0xf bound_ctrl:1
	v_pk_mul_f32 v[60:61], v[2:3], v[8:9] op_sel_hi:[1,0]
	v_pk_mul_f32 v[62:63], v[4:5], v[8:9] op_sel_hi:[1,0]
	v_pk_mul_f32 v[64:65], v[6:7], v[8:9] op_sel_hi:[1,0]
	v_pk_mul_f32 v[66:67], v[2:3], v[8:9] op_sel:[0,1]
	v_pk_mul_f32 v[68:69], v[4:5], v[8:9] op_sel:[0,1]
	v_pk_mul_f32 v[70:71], v[6:7], v[8:9] op_sel:[0,1]
	v_pk_mul_f32 v[72:73], v[2:3], v[10:11] op_sel_hi:[1,0]
	v_pk_mul_f32 v[74:75], v[4:5], v[10:11] op_sel_hi:[1,0]
	v_pk_mul_f32 v[76:77], v[6:7], v[10:11] op_sel_hi:[1,0]
	v_pk_add_f32 v[78:79], v[2:3], v[48:49]
	v_pk_add_f32 v[80:81], v[4:5], v[50:51]
	v_pk_add_f32 v[82:83], v[6:7], v[52:53]
	v_pk_fma_f32 v[60:61], v[48:49], v[40:41], v[60:61] op_sel_hi:[1,0,1]
	v_pk_fma_f32 v[62:63], v[50:51], v[40:41], v[62:63] op_sel_hi:[1,0,1]
	v_pk_fma_f32 v[64:65], v[52:53], v[40:41], v[64:65] op_sel_hi:[1,0,1]
	v_pk_fma_f32 v[66:67], v[48:49], v[40:41], v[66:67] op_sel:[0,1,0]
	v_pk_fma_f32 v[68:69], v[50:51], v[40:41], v[68:69] op_sel:[0,1,0]
	v_pk_fma_f32 v[70:71], v[52:53], v[40:41], v[70:71] op_sel:[0,1,0]
	v_pk_fma_f32 v[72:73], v[48:49], v[42:43], v[72:73] op_sel_hi:[1,0,1]
	v_pk_fma_f32 v[74:75], v[50:51], v[42:43], v[74:75] op_sel_hi:[1,0,1]
	v_pk_fma_f32 v[76:77], v[52:53], v[42:43], v[76:77] op_sel_hi:[1,0,1]
	v_pk_add_f32 v[78:79], v[78:79], v[54:55]
	v_pk_add_f32 v[80:81], v[80:81], v[56:57]
	v_pk_add_f32 v[82:83], v[82:83], v[58:59]
	v_pk_fma_f32 v[60:61], v[54:55], v[44:45], v[60:61] op_sel_hi:[1,0,1]
	v_pk_fma_f32 v[62:63], v[56:57], v[44:45], v[62:63] op_sel_hi:[1,0,1]
	v_pk_fma_f32 v[64:65], v[58:59], v[44:45], v[64:65] op_sel_hi:[1,0,1]
	v_pk_fma_f32 v[66:67], v[54:55], v[44:45], v[66:67] op_sel:[0,1,0]
	v_pk_fma_f32 v[68:69], v[56:57], v[44:45], v[68:69] op_sel:[0,1,0]
	v_pk_fma_f32 v[70:71], v[58:59], v[44:45], v[70:71] op_sel:[0,1,0]
	v_pk_fma_f32 v[72:73], v[54:55], v[46:47], v[72:73] op_sel_hi:[1,0,1]
	v_pk_fma_f32 v[74:75], v[56:57], v[46:47], v[74:75] op_sel_hi:[1,0,1]
	v_pk_fma_f32 v[76:77], v[58:59], v[46:47], v[76:77] op_sel_hi:[1,0,1]
	s_barrier
	s_add_i32 s4, s34, 1
	s_min_i32 s4, s4, 0x200
	s_mul_i32 s5, s4, 0x804
	s_add_i32 s5, s5, s35
	s_add_i32 s6, s5, 0x0
	s_add_i32 s7, s5, 0x101004
	s_add_i32 s8, s5, 0x202008
	s_add_i32 s11, s5, 0x30300c
	s_add_i32 s15, s5, 0x404010
	s_add_i32 s31, s5, 0x505014
	s_mul_i32 s9, s4, 0x180c
	s_add_i32 s9, s9, s33
	buffer_load_dword v48, v28, s[16:19], s6 offen nt
	buffer_load_dword v49, v28, s[16:19], s7 offen nt
	buffer_load_dword v50, v28, s[16:19], s8 offen nt
	buffer_load_dword v51, v28, s[16:19], s11 offen nt
	buffer_load_dword v52, v28, s[16:19], s15 offen nt
	buffer_load_dword v53, v28, s[16:19], s31 offen nt
	buffer_load_dwordx3 v[56:58], v27, s[24:27], s9 offen nt
	s_waitcnt vmcnt(14)
	v_mov_b32_dpp v84, v32 wave_shr:1 row_mask:0xf bank_mask:0xf bound_ctrl:1
	v_mov_b32_dpp v85, v33 wave_shr:1 row_mask:0xf bank_mask:0xf bound_ctrl:1
	v_mov_b32_dpp v86, v34 wave_shr:1 row_mask:0xf bank_mask:0xf bound_ctrl:1
	v_mov_b32_dpp v88, v32 wave_shl:1 row_mask:0xf bank_mask:0xf bound_ctrl:1
	v_mov_b32_dpp v89, v33 wave_shl:1 row_mask:0xf bank_mask:0xf bound_ctrl:1
	v_mov_b32_dpp v90, v34 wave_shl:1 row_mask:0xf bank_mask:0xf bound_ctrl:1
	v_mov_b32_dpp v54, v12 wave_shr:1 row_mask:0xf bank_mask:0xf bound_ctrl:1
	v_mov_b32_dpp v55, v13 wave_shr:1 row_mask:0xf bank_mask:0xf bound_ctrl:1
	v_mov_b32_dpp v92, v14 wave_shr:1 row_mask:0xf bank_mask:0xf bound_ctrl:1
	v_mov_b32_dpp v93, v15 wave_shr:1 row_mask:0xf bank_mask:0xf bound_ctrl:1
	v_mov_b32_dpp v94, v16 wave_shr:1 row_mask:0xf bank_mask:0xf bound_ctrl:1
	v_mov_b32_dpp v95, v17 wave_shr:1 row_mask:0xf bank_mask:0xf bound_ctrl:1
	v_mov_b32_dpp v96, v12 wave_shl:1 row_mask:0xf bank_mask:0xf bound_ctrl:1
	v_mov_b32_dpp v97, v13 wave_shl:1 row_mask:0xf bank_mask:0xf bound_ctrl:1
	v_mov_b32_dpp v98, v14 wave_shl:1 row_mask:0xf bank_mask:0xf bound_ctrl:1
	v_mov_b32_dpp v99, v15 wave_shl:1 row_mask:0xf bank_mask:0xf bound_ctrl:1
	v_mov_b32_dpp v100, v16 wave_shl:1 row_mask:0xf bank_mask:0xf bound_ctrl:1
	v_mov_b32_dpp v101, v17 wave_shl:1 row_mask:0xf bank_mask:0xf bound_ctrl:1
	v_pk_mul_f32 v[102:103], v[12:13], v[32:33] op_sel_hi:[1,0]
	v_pk_mul_f32 v[104:105], v[14:15], v[32:33] op_sel_hi:[1,0]
	v_pk_mul_f32 v[106:107], v[16:17], v[32:33] op_sel_hi:[1,0]
	v_pk_mul_f32 v[108:109], v[12:13], v[32:33] op_sel:[0,1]
	v_pk_mul_f32 v[110:111], v[14:15], v[32:33] op_sel:[0,1]
	v_pk_mul_f32 v[112:113], v[16:17], v[32:33] op_sel:[0,1]
	v_pk_mul_f32 v[114:115], v[12:13], v[34:35] op_sel_hi:[1,0]
	v_pk_mul_f32 v[116:117], v[14:15], v[34:35] op_sel_hi:[1,0]
	v_pk_mul_f32 v[118:119], v[16:17], v[34:35] op_sel_hi:[1,0]
	v_pk_add_f32 v[120:121], v[12:13], v[54:55]
	v_pk_add_f32 v[122:123], v[14:15], v[92:93]
	v_pk_add_f32 v[124:125], v[16:17], v[94:95]
	v_pk_fma_f32 v[102:103], v[54:55], v[84:85], v[102:103] op_sel_hi:[1,0,1]
	v_pk_fma_f32 v[104:105], v[92:93], v[84:85], v[104:105] op_sel_hi:[1,0,1]
	v_pk_fma_f32 v[106:107], v[94:95], v[84:85], v[106:107] op_sel_hi:[1,0,1]
	v_pk_fma_f32 v[108:109], v[54:55], v[84:85], v[108:109] op_sel:[0,1,0]
	v_pk_fma_f32 v[110:111], v[92:93], v[84:85], v[110:111] op_sel:[0,1,0]
	v_pk_fma_f32 v[112:113], v[94:95], v[84:85], v[112:113] op_sel:[0,1,0]
	v_pk_fma_f32 v[114:115], v[54:55], v[86:87], v[114:115] op_sel_hi:[1,0,1]
	v_pk_fma_f32 v[116:117], v[92:93], v[86:87], v[116:117] op_sel_hi:[1,0,1]
	v_pk_fma_f32 v[118:119], v[94:95], v[86:87], v[118:119] op_sel_hi:[1,0,1]
	v_pk_add_f32 v[120:121], v[120:121], v[96:97]
	v_pk_add_f32 v[122:123], v[122:123], v[98:99]
	v_pk_add_f32 v[124:125], v[124:125], v[100:101]
	v_pk_fma_f32 v[102:103], v[96:97], v[88:89], v[102:103] op_sel_hi:[1,0,1]
	v_pk_fma_f32 v[104:105], v[98:99], v[88:89], v[104:105] op_sel_hi:[1,0,1]
	v_pk_fma_f32 v[106:107], v[100:101], v[88:89], v[106:107] op_sel_hi:[1,0,1]
	v_pk_fma_f32 v[108:109], v[96:97], v[88:89], v[108:109] op_sel:[0,1,0]
	v_pk_fma_f32 v[110:111], v[98:99], v[88:89], v[110:111] op_sel:[0,1,0]
	v_pk_fma_f32 v[112:113], v[100:101], v[88:89], v[112:113] op_sel:[0,1,0]
	v_pk_fma_f32 v[114:115], v[96:97], v[90:91], v[114:115] op_sel_hi:[1,0,1]
	v_pk_fma_f32 v[116:117], v[98:99], v[90:91], v[116:117] op_sel_hi:[1,0,1]
	v_pk_fma_f32 v[118:119], v[100:101], v[90:91], v[118:119] op_sel_hi:[1,0,1]
	s_barrier
	s_add_i32 s4, s34, 2
	s_min_i32 s4, s4, 0x200
	s_mul_i32 s5, s4, 0x804
	s_add_i32 s5, s5, s35
	s_add_i32 s6, s5, 0x0
	s_add_i32 s7, s5, 0x101004
	s_add_i32 s8, s5, 0x202008
	s_add_i32 s11, s5, 0x30300c
	s_add_i32 s15, s5, 0x404010
	s_add_i32 s31, s5, 0x505014
	s_mul_i32 s9, s4, 0x180c
	s_add_i32 s9, s9, s33
	buffer_load_dword v54, v28, s[16:19], s6 offen nt
	buffer_load_dword v55, v28, s[16:19], s7 offen nt
	buffer_load_dword v92, v28, s[16:19], s8 offen nt
	buffer_load_dword v93, v28, s[16:19], s11 offen nt
	buffer_load_dword v94, v28, s[16:19], s15 offen nt
	buffer_load_dword v95, v28, s[16:19], s31 offen nt
	buffer_load_dwordx3 v[96:98], v27, s[24:27], s9 offen nt
	s_waitcnt vmcnt(14)
	v_mov_b32_dpp v128, v36 wave_shr:1 row_mask:0xf bank_mask:0xf bound_ctrl:1
	v_mov_b32_dpp v129, v37 wave_shr:1 row_mask:0xf bank_mask:0xf bound_ctrl:1
	v_mov_b32_dpp v130, v38 wave_shr:1 row_mask:0xf bank_mask:0xf bound_ctrl:1
	v_mov_b32_dpp v132, v36 wave_shl:1 row_mask:0xf bank_mask:0xf bound_ctrl:1
	v_mov_b32_dpp v133, v37 wave_shl:1 row_mask:0xf bank_mask:0xf bound_ctrl:1
	v_mov_b32_dpp v134, v38 wave_shl:1 row_mask:0xf bank_mask:0xf bound_ctrl:1
	v_mov_b32_dpp v100, v20 wave_shr:1 row_mask:0xf bank_mask:0xf bound_ctrl:1
	v_mov_b32_dpp v101, v21 wave_shr:1 row_mask:0xf bank_mask:0xf bound_ctrl:1
	v_mov_b32_dpp v126, v24 wave_shr:1 row_mask:0xf bank_mask:0xf bound_ctrl:1
	v_mov_b32_dpp v127, v25 wave_shr:1 row_mask:0xf bank_mask:0xf bound_ctrl:1
	v_mov_b32_dpp v136, v30 wave_shr:1 row_mask:0xf bank_mask:0xf bound_ctrl:1
	v_mov_b32_dpp v137, v31 wave_shr:1 row_mask:0xf bank_mask:0xf bound_ctrl:1
	v_mov_b32_dpp v138, v20 wave_shl:1 row_mask:0xf bank_mask:0xf bound_ctrl:1
	v_mov_b32_dpp v139, v21 wave_shl:1 row_mask:0xf bank_mask:0xf bound_ctrl:1
	v_mov_b32_dpp v140, v24 wave_shl:1 row_mask:0xf bank_mask:0xf bound_ctrl:1
	v_mov_b32_dpp v141, v25 wave_shl:1 row_mask:0xf bank_mask:0xf bound_ctrl:1
	v_mov_b32_dpp v142, v30 wave_shl:1 row_mask:0xf bank_mask:0xf bound_ctrl:1
	v_mov_b32_dpp v143, v31 wave_shl:1 row_mask:0xf bank_mask:0xf bound_ctrl:1
	v_pk_mul_f32 v[144:145], v[20:21], v[36:37] op_sel_hi:[1,0]
	v_pk_mul_f32 v[146:147], v[24:25], v[36:37] op_sel_hi:[1,0]
	v_pk_mul_f32 v[148:149], v[30:31], v[36:37] op_sel_hi:[1,0]
	v_pk_mul_f32 v[150:151], v[20:21], v[36:37] op_sel:[0,1]
	v_pk_mul_f32 v[152:153], v[24:25], v[36:37] op_sel:[0,1]
	v_pk_mul_f32 v[154:155], v[30:31], v[36:37] op_sel:[0,1]
	v_pk_mul_f32 v[156:157], v[20:21], v[38:39] op_sel_hi:[1,0]
	v_pk_mul_f32 v[158:159], v[24:25], v[38:39] op_sel_hi:[1,0]
	v_pk_mul_f32 v[160:161], v[30:31], v[38:39] op_sel_hi:[1,0]
	v_pk_add_f32 v[162:163], v[20:21], v[100:101]
	v_pk_add_f32 v[164:165], v[24:25], v[126:127]
	v_pk_add_f32 v[166:167], v[30:31], v[136:137]
	v_pk_fma_f32 v[144:145], v[100:101], v[128:129], v[144:145] op_sel_hi:[1,0,1]
	v_pk_fma_f32 v[146:147], v[126:127], v[128:129], v[146:147] op_sel_hi:[1,0,1]
	v_pk_fma_f32 v[148:149], v[136:137], v[128:129], v[148:149] op_sel_hi:[1,0,1]
	v_pk_fma_f32 v[150:151], v[100:101], v[128:129], v[150:151] op_sel:[0,1,0]
	v_pk_fma_f32 v[152:153], v[126:127], v[128:129], v[152:153] op_sel:[0,1,0]
	v_pk_fma_f32 v[154:155], v[136:137], v[128:129], v[154:155] op_sel:[0,1,0]
	v_pk_fma_f32 v[156:157], v[100:101], v[130:131], v[156:157] op_sel_hi:[1,0,1]
	v_pk_fma_f32 v[158:159], v[126:127], v[130:131], v[158:159] op_sel_hi:[1,0,1]
	v_pk_fma_f32 v[160:161], v[136:137], v[130:131], v[160:161] op_sel_hi:[1,0,1]
	v_pk_add_f32 v[162:163], v[162:163], v[138:139]
	v_pk_add_f32 v[164:165], v[164:165], v[140:141]
	v_pk_add_f32 v[166:167], v[166:167], v[142:143]
	v_pk_fma_f32 v[144:145], v[138:139], v[132:133], v[144:145] op_sel_hi:[1,0,1]
	v_pk_fma_f32 v[146:147], v[140:141], v[132:133], v[146:147] op_sel_hi:[1,0,1]
	v_pk_fma_f32 v[148:149], v[142:143], v[132:133], v[148:149] op_sel_hi:[1,0,1]
	v_pk_fma_f32 v[150:151], v[138:139], v[132:133], v[150:151] op_sel:[0,1,0]
	v_pk_fma_f32 v[152:153], v[140:141], v[132:133], v[152:153] op_sel:[0,1,0]
	v_pk_fma_f32 v[154:155], v[142:143], v[132:133], v[154:155] op_sel:[0,1,0]
	v_pk_fma_f32 v[156:157], v[138:139], v[134:135], v[156:157] op_sel_hi:[1,0,1]
	v_pk_fma_f32 v[158:159], v[140:141], v[134:135], v[158:159] op_sel_hi:[1,0,1]
	v_pk_fma_f32 v[160:161], v[142:143], v[134:135], v[160:161] op_sel_hi:[1,0,1]
	s_barrier
	ds_read_b128 v[136:139], v23 offset:0
	ds_read_b128 v[140:143], v23 offset:1024
	ds_read_b128 v[168:171], v23 offset:2048
	v_pk_add_f32 v[100:101], v[120:121], v[162:163]
	v_pk_add_f32 v[126:127], v[78:79], v[100:101]
	v_pk_add_f32 v[78:79], v[122:123], v[164:165]
	v_pk_add_f32 v[120:121], v[80:81], v[78:79]
	v_pk_add_f32 v[80:81], v[124:125], v[166:167]
	v_pk_add_f32 v[122:123], v[82:83], v[80:81]
	v_pk_add_f32 v[82:83], v[102:103], v[144:145]
	v_pk_add_f32 v[124:125], v[60:61], v[82:83]
	v_pk_add_f32 v[60:61], v[104:105], v[146:147]
	v_pk_add_f32 v[102:103], v[62:63], v[60:61]
	v_pk_add_f32 v[62:63], v[106:107], v[148:149]
	v_pk_add_f32 v[104:105], v[64:65], v[62:63]
	v_pk_add_f32 v[64:65], v[108:109], v[150:151]
	v_pk_add_f32 v[106:107], v[66:67], v[64:65]
	v_pk_add_f32 v[66:67], v[110:111], v[152:153]
	v_pk_add_f32 v[108:109], v[68:69], v[66:67]
	v_pk_add_f32 v[68:69], v[112:113], v[154:155]
	v_pk_add_f32 v[110:111], v[70:71], v[68:69]
	v_pk_add_f32 v[70:71], v[114:115], v[156:157]
	v_pk_add_f32 v[112:113], v[72:73], v[70:71]
	v_pk_add_f32 v[72:73], v[116:117], v[158:159]
	v_pk_add_f32 v[114:115], v[74:75], v[72:73]
	v_pk_add_f32 v[74:75], v[118:119], v[160:161]
	v_pk_add_f32 v[116:117], v[76:77], v[74:75]
	s_waitcnt lgkmcnt(2)
	v_pk_fma_f32 v[124:125], v[136:137], v[126:127], v[124:125] op_sel_hi:[0,1,1] neg_lo:[1,0,0] neg_hi:[1,0,0]
	v_pk_fma_f32 v[102:103], v[136:137], v[120:121], v[102:103] op_sel_hi:[0,1,1] neg_lo:[1,0,0] neg_hi:[1,0,0]
	v_pk_fma_f32 v[104:105], v[136:137], v[122:123], v[104:105] op_sel_hi:[0,1,1] neg_lo:[1,0,0] neg_hi:[1,0,0]
	v_pk_fma_f32 v[106:107], v[136:137], v[126:127], v[106:107] op_sel:[1,0,0] neg_lo:[1,0,0] neg_hi:[1,0,0]
	v_pk_fma_f32 v[108:109], v[136:137], v[120:121], v[108:109] op_sel:[1,0,0] neg_lo:[1,0,0] neg_hi:[1,0,0]
	v_pk_fma_f32 v[110:111], v[136:137], v[122:123], v[110:111] op_sel:[1,0,0] neg_lo:[1,0,0] neg_hi:[1,0,0]
	v_pk_fma_f32 v[112:113], v[138:139], v[126:127], v[112:113] op_sel_hi:[0,1,1] neg_lo:[1,0,0] neg_hi:[1,0,0]
	v_pk_fma_f32 v[114:115], v[138:139], v[120:121], v[114:115] op_sel_hi:[0,1,1] neg_lo:[1,0,0] neg_hi:[1,0,0]
	v_pk_fma_f32 v[116:117], v[138:139], v[122:123], v[116:117] op_sel_hi:[0,1,1] neg_lo:[1,0,0] neg_hi:[1,0,0]
	v_pk_mul_f32 v[76:77], v[138:139], v[124:125] op_sel:[1,0]
	v_pk_mul_f32 v[174:175], v[138:139], v[102:103] op_sel:[1,0]
	v_pk_mul_f32 v[180:181], v[138:139], v[104:105] op_sel:[1,0]
	s_waitcnt lgkmcnt(1)
	v_pk_mul_f32 v[118:119], v[140:141], v[124:125] op_sel_hi:[0,1]
	v_pk_mul_f32 v[176:177], v[140:141], v[102:103] op_sel_hi:[0,1]
	v_pk_mul_f32 v[182:183], v[140:141], v[104:105] op_sel_hi:[0,1]
	v_pk_mul_f32 v[172:173], v[140:141], v[124:125] op_sel:[1,0]
	v_pk_mul_f32 v[178:179], v[140:141], v[102:103] op_sel:[1,0]
	v_pk_mul_f32 v[184:185], v[140:141], v[104:105] op_sel:[1,0]
	v_pk_fma_f32 v[76:77], v[140:141], v[106:107], v[76:77] op_sel_hi:[0,1,1]
	v_pk_fma_f32 v[174:175], v[140:141], v[108:109], v[174:175] op_sel_hi:[0,1,1]
	v_pk_fma_f32 v[180:181], v[140:141], v[110:111], v[180:181] op_sel_hi:[0,1,1]
	v_pk_fma_f32 v[118:119], v[142:143], v[106:107], v[118:119] op_sel_hi:[0,1,1]
	v_pk_fma_f32 v[176:177], v[142:143], v[108:109], v[176:177] op_sel_hi:[0,1,1]
	v_pk_fma_f32 v[182:183], v[142:143], v[110:111], v[182:183] op_sel_hi:[0,1,1]
	v_pk_fma_f32 v[172:173], v[142:143], v[106:107], v[172:173] op_sel:[1,0,0]
	v_pk_fma_f32 v[178:179], v[142:143], v[108:109], v[178:179] op_sel:[1,0,0]
	v_pk_fma_f32 v[184:185], v[142:143], v[110:111], v[184:185] op_sel:[1,0,0]
	v_pk_fma_f32 v[76:77], v[140:141], v[112:113], v[76:77] op_sel:[1,0,0]
	v_pk_fma_f32 v[174:175], v[140:141], v[114:115], v[174:175] op_sel:[1,0,0]
	v_pk_fma_f32 v[180:181], v[140:141], v[116:117], v[180:181] op_sel:[1,0,0]
	v_pk_fma_f32 v[118:119], v[142:143], v[112:113], v[118:119] op_sel:[1,0,0]
	v_pk_fma_f32 v[176:177], v[142:143], v[114:115], v[176:177] op_sel:[1,0,0]
	v_pk_fma_f32 v[182:183], v[142:143], v[116:117], v[182:183] op_sel:[1,0,0]
	s_waitcnt lgkmcnt(0)
	v_pk_fma_f32 v[172:173], v[168:169], v[112:113], v[172:173] op_sel_hi:[0,1,1]
	v_pk_fma_f32 v[178:179], v[168:169], v[114:115], v[178:179] op_sel_hi:[0,1,1]
	v_pk_fma_f32 v[184:185], v[168:169], v[116:117], v[184:185] op_sel_hi:[0,1,1]
	v_pk_mul_f32 v[186:187], v[136:137], v[76:77] op_sel_hi:[0,1]
	v_pk_mul_f32 v[188:189], v[136:137], v[174:175] op_sel_hi:[0,1]
	v_pk_mul_f32 v[190:191], v[136:137], v[180:181] op_sel_hi:[0,1]
	v_pk_fma_f32 v[186:187], v[136:137], v[118:119], v[186:187] op_sel:[1,0,0]
	v_pk_fma_f32 v[188:189], v[136:137], v[176:177], v[188:189] op_sel:[1,0,0]
	v_pk_fma_f32 v[190:191], v[136:137], v[182:183], v[190:191] op_sel:[1,0,0]
	v_pk_fma_f32 v[186:187], v[138:139], v[172:173], v[186:187] op_sel_hi:[0,1,1]
	v_pk_fma_f32 v[188:189], v[138:139], v[178:179], v[188:189] op_sel_hi:[0,1,1]
	v_pk_fma_f32 v[190:191], v[138:139], v[184:185], v[190:191] op_sel_hi:[0,1,1]
	v_pk_fma_f32 v[186:187], v[168:169], v[126:127], v[186:187] op_sel:[1,0,0] neg_lo:[0,0,1] neg_hi:[0,0,1]
	v_pk_fma_f32 v[188:189], v[168:169], v[120:121], v[188:189] op_sel:[1,0,0] neg_lo:[0,0,1] neg_hi:[0,0,1]
	v_pk_fma_f32 v[190:191], v[168:169], v[122:123], v[190:191] op_sel:[1,0,0] neg_lo:[0,0,1] neg_hi:[0,0,1]
	s_add_i32 s4, s34, 3
	s_min_i32 s4, s4, 0x200
	s_mul_i32 s5, s4, 0x804
	s_add_i32 s5, s5, s35
	s_add_i32 s6, s5, 0x0
	s_add_i32 s7, s5, 0x101004
	s_add_i32 s8, s5, 0x202008
	s_add_i32 s11, s5, 0x30300c
	s_add_i32 s15, s5, 0x404010
	s_add_i32 s31, s5, 0x505014
	s_mul_i32 s9, s4, 0x180c
	s_add_i32 s9, s9, s33
	buffer_load_dword v2, v28, s[16:19], s6 offen nt
	buffer_load_dword v3, v28, s[16:19], s7 offen nt
	buffer_load_dword v4, v28, s[16:19], s8 offen nt
	buffer_load_dword v5, v28, s[16:19], s11 offen nt
	buffer_load_dword v6, v28, s[16:19], s15 offen nt
	buffer_load_dword v7, v28, s[16:19], s31 offen nt
	buffer_load_dwordx3 v[8:10], v27, s[24:27], s9 offen nt
	s_waitcnt vmcnt(14)
	v_mov_b32_dpp v40, v56 wave_shr:1 row_mask:0xf bank_mask:0xf bound_ctrl:1
	v_mov_b32_dpp v41, v57 wave_shr:1 row_mask:0xf bank_mask:0xf bound_ctrl:1
	v_mov_b32_dpp v42, v58 wave_shr:1 row_mask:0xf bank_mask:0xf bound_ctrl:1
	v_mov_b32_dpp v44, v56 wave_shl:1 row_mask:0xf bank_mask:0xf bound_ctrl:1
	v_mov_b32_dpp v45, v57 wave_shl:1 row_mask:0xf bank_mask:0xf bound_ctrl:1
	v_mov_b32_dpp v46, v58 wave_shl:1 row_mask:0xf bank_mask:0xf bound_ctrl:1
	v_mov_b32_dpp v102, v48 wave_shr:1 row_mask:0xf bank_mask:0xf bound_ctrl:1
	v_mov_b32_dpp v103, v49 wave_shr:1 row_mask:0xf bank_mask:0xf bound_ctrl:1
	v_mov_b32_dpp v104, v50 wave_shr:1 row_mask:0xf bank_mask:0xf bound_ctrl:1
	v_mov_b32_dpp v105, v51 wave_shr:1 row_mask:0xf bank_mask:0xf bound_ctrl:1
	v_mov_b32_dpp v106, v52 wave_shr:1 row_mask:0xf bank_mask:0xf bound_ctrl:1
	v_mov_b32_dpp v107, v53 wave_shr:1 row_mask:0xf bank_mask:0xf bound_ctrl:1
	v_mov_b32_dpp v108, v48 wave_shl:1 row_mask:0xf bank_mask:0xf bound_ctrl:1
	v_mov_b32_dpp v109, v49 wave_shl:1 row_mask:0xf bank_mask:0xf bound_ctrl:1
	v_mov_b32_dpp v110, v50 wave_shl:1 row_mask:0xf bank_mask:0xf bound_ctrl:1
	v_mov_b32_dpp v111, v51 wave_shl:1 row_mask:0xf bank_mask:0xf bound_ctrl:1
	v_mov_b32_dpp v112, v52 wave_shl:1 row_mask:0xf bank_mask:0xf bound_ctrl:1
	v_mov_b32_dpp v113, v53 wave_shl:1 row_mask:0xf bank_mask:0xf bound_ctrl:1
	v_pk_mul_f32 v[114:115], v[48:49], v[56:57] op_sel_hi:[1,0]
	v_pk_mul_f32 v[116:117], v[50:51], v[56:57] op_sel_hi:[1,0]
	v_pk_mul_f32 v[120:121], v[52:53], v[56:57] op_sel_hi:[1,0]
	v_pk_mul_f32 v[122:123], v[48:49], v[56:57] op_sel:[0,1]
	v_pk_mul_f32 v[124:125], v[50:51], v[56:57] op_sel:[0,1]
	v_pk_mul_f32 v[126:127], v[52:53], v[56:57] op_sel:[0,1]
	v_pk_mul_f32 v[136:137], v[48:49], v[58:59] op_sel_hi:[1,0]
	v_pk_mul_f32 v[138:139], v[50:51], v[58:59] op_sel_hi:[1,0]
	v_pk_mul_f32 v[140:141], v[52:53], v[58:59] op_sel_hi:[1,0]
	v_pk_add_f32 v[142:143], v[48:49], v[102:103]
	v_pk_add_f32 v[168:169], v[50:51], v[104:105]
	v_pk_add_f32 v[170:171], v[52:53], v[106:107]
	v_pk_fma_f32 v[114:115], v[102:103], v[40:41], v[114:115] op_sel_hi:[1,0,1]
	v_pk_fma_f32 v[116:117], v[104:105], v[40:41], v[116:117] op_sel_hi:[1,0,1]
	v_pk_fma_f32 v[120:121], v[106:107], v[40:41], v[120:121] op_sel_hi:[1,0,1]
	v_pk_fma_f32 v[122:123], v[102:103], v[40:41], v[122:123] op_sel:[0,1,0]
	v_pk_fma_f32 v[124:125], v[104:105], v[40:41], v[124:125] op_sel:[0,1,0]
	v_pk_fma_f32 v[126:127], v[106:107], v[40:41], v[126:127] op_sel:[0,1,0]
	v_pk_fma_f32 v[136:137], v[102:103], v[42:43], v[136:137] op_sel_hi:[1,0,1]
	v_pk_fma_f32 v[138:139], v[104:105], v[42:43], v[138:139] op_sel_hi:[1,0,1]
	v_pk_fma_f32 v[140:141], v[106:107], v[42:43], v[140:141] op_sel_hi:[1,0,1]
	v_pk_add_f32 v[142:143], v[142:143], v[108:109]
	v_pk_add_f32 v[168:169], v[168:169], v[110:111]
	v_pk_add_f32 v[170:171], v[170:171], v[112:113]
	v_pk_fma_f32 v[114:115], v[108:109], v[44:45], v[114:115] op_sel_hi:[1,0,1]
	v_pk_fma_f32 v[116:117], v[110:111], v[44:45], v[116:117] op_sel_hi:[1,0,1]
	v_pk_fma_f32 v[120:121], v[112:113], v[44:45], v[120:121] op_sel_hi:[1,0,1]
	v_pk_fma_f32 v[122:123], v[108:109], v[44:45], v[122:123] op_sel:[0,1,0]
	v_pk_fma_f32 v[124:125], v[110:111], v[44:45], v[124:125] op_sel:[0,1,0]
	v_pk_fma_f32 v[126:127], v[112:113], v[44:45], v[126:127] op_sel:[0,1,0]
	v_pk_fma_f32 v[136:137], v[108:109], v[46:47], v[136:137] op_sel_hi:[1,0,1]
	v_pk_fma_f32 v[138:139], v[110:111], v[46:47], v[138:139] op_sel_hi:[1,0,1]
	v_pk_fma_f32 v[140:141], v[112:113], v[46:47], v[140:141] op_sel_hi:[1,0,1]
	s_barrier
	ds_read_b128 v[104:107], v23 offset:3072
	ds_read_b128 v[108:111], v23 offset:4096
	ds_read_b128 v[192:195], v23 offset:5120
	v_pk_add_f32 v[102:103], v[100:101], v[142:143]
	v_pk_add_f32 v[100:101], v[78:79], v[168:169]
	v_pk_add_f32 v[78:79], v[80:81], v[170:171]
	v_pk_add_f32 v[80:81], v[82:83], v[114:115]
	v_pk_add_f32 v[82:83], v[60:61], v[116:117]
	v_pk_add_f32 v[60:61], v[62:63], v[120:121]
	v_pk_add_f32 v[62:63], v[64:65], v[122:123]
	v_pk_add_f32 v[64:65], v[66:67], v[124:125]
	v_pk_add_f32 v[66:67], v[68:69], v[126:127]
	v_pk_add_f32 v[68:69], v[70:71], v[136:137]
	v_pk_add_f32 v[70:71], v[72:73], v[138:139]
	v_pk_add_f32 v[72:73], v[74:75], v[140:141]
	s_waitcnt lgkmcnt(2)
	v_pk_fma_f32 v[80:81], v[104:105], v[102:103], v[80:81] op_sel_hi:[0,1,1] neg_lo:[1,0,0] neg_hi:[1,0,0]
	v_pk_fma_f32 v[82:83], v[104:105], v[100:101], v[82:83] op_sel_hi:[0,1,1] neg_lo:[1,0,0] neg_hi:[1,0,0]
	v_pk_fma_f32 v[60:61], v[104:105], v[78:79], v[60:61] op_sel_hi:[0,1,1] neg_lo:[1,0,0] neg_hi:[1,0,0]
	v_pk_fma_f32 v[62:63], v[104:105], v[102:103], v[62:63] op_sel:[1,0,0] neg_lo:[1,0,0] neg_hi:[1,0,0]
	v_pk_fma_f32 v[64:65], v[104:105], v[100:101], v[64:65] op_sel:[1,0,0] neg_lo:[1,0,0] neg_hi:[1,0,0]
	v_pk_fma_f32 v[66:67], v[104:105], v[78:79], v[66:67] op_sel:[1,0,0] neg_lo:[1,0,0] neg_hi:[1,0,0]
	v_pk_fma_f32 v[68:69], v[106:107], v[102:103], v[68:69] op_sel_hi:[0,1,1] neg_lo:[1,0,0] neg_hi:[1,0,0]
	v_pk_fma_f32 v[70:71], v[106:107], v[100:101], v[70:71] op_sel_hi:[0,1,1] neg_lo:[1,0,0] neg_hi:[1,0,0]
	v_pk_fma_f32 v[72:73], v[106:107], v[78:79], v[72:73] op_sel_hi:[0,1,1] neg_lo:[1,0,0] neg_hi:[1,0,0]
	v_pk_mul_f32 v[74:75], v[106:107], v[80:81] op_sel:[1,0]
	v_pk_mul_f32 v[198:199], v[106:107], v[82:83] op_sel:[1,0]
	v_pk_mul_f32 v[204:205], v[106:107], v[60:61] op_sel:[1,0]
	s_waitcnt lgkmcnt(1)
	v_pk_mul_f32 v[112:113], v[108:109], v[80:81] op_sel_hi:[0,1]
	v_pk_mul_f32 v[200:201], v[108:109], v[82:83] op_sel_hi:[0,1]
	v_pk_mul_f32 v[206:207], v[108:109], v[60:61] op_sel_hi:[0,1]
	v_pk_mul_f32 v[196:197], v[108:109], v[80:81] op_sel:[1,0]
	v_pk_mul_f32 v[202:203], v[108:109], v[82:83] op_sel:[1,0]
	v_pk_mul_f32 v[208:209], v[108:109], v[60:61] op_sel:[1,0]
	v_pk_fma_f32 v[74:75], v[108:109], v[62:63], v[74:75] op_sel_hi:[0,1,1]
	v_pk_fma_f32 v[198:199], v[108:109], v[64:65], v[198:199] op_sel_hi:[0,1,1]
	v_pk_fma_f32 v[204:205], v[108:109], v[66:67], v[204:205] op_sel_hi:[0,1,1]
	v_pk_fma_f32 v[112:113], v[110:111], v[62:63], v[112:113] op_sel_hi:[0,1,1]
	v_pk_fma_f32 v[200:201], v[110:111], v[64:65], v[200:201] op_sel_hi:[0,1,1]
	v_pk_fma_f32 v[206:207], v[110:111], v[66:67], v[206:207] op_sel_hi:[0,1,1]
	v_pk_fma_f32 v[196:197], v[110:111], v[62:63], v[196:197] op_sel:[1,0,0]
	v_pk_fma_f32 v[202:203], v[110:111], v[64:65], v[202:203] op_sel:[1,0,0]
	v_pk_fma_f32 v[208:209], v[110:111], v[66:67], v[208:209] op_sel:[1,0,0]
	v_pk_fma_f32 v[74:75], v[108:109], v[68:69], v[74:75] op_sel:[1,0,0]
	v_pk_fma_f32 v[198:199], v[108:109], v[70:71], v[198:199] op_sel:[1,0,0]
	v_pk_fma_f32 v[204:205], v[108:109], v[72:73], v[204:205] op_sel:[1,0,0]
	v_pk_fma_f32 v[112:113], v[110:111], v[68:69], v[112:113] op_sel:[1,0,0]
	v_pk_fma_f32 v[200:201], v[110:111], v[70:71], v[200:201] op_sel:[1,0,0]
	v_pk_fma_f32 v[206:207], v[110:111], v[72:73], v[206:207] op_sel:[1,0,0]
	s_waitcnt lgkmcnt(0)
	v_pk_fma_f32 v[196:197], v[192:193], v[68:69], v[196:197] op_sel_hi:[0,1,1]
	v_pk_fma_f32 v[202:203], v[192:193], v[70:71], v[202:203] op_sel_hi:[0,1,1]
	v_pk_fma_f32 v[208:209], v[192:193], v[72:73], v[208:209] op_sel_hi:[0,1,1]
	v_pk_mul_f32 v[210:211], v[104:105], v[74:75] op_sel_hi:[0,1]
	v_pk_mul_f32 v[212:213], v[104:105], v[198:199] op_sel_hi:[0,1]
	v_pk_mul_f32 v[214:215], v[104:105], v[204:205] op_sel_hi:[0,1]
	v_pk_fma_f32 v[210:211], v[104:105], v[112:113], v[210:211] op_sel:[1,0,0]
	v_pk_fma_f32 v[212:213], v[104:105], v[200:201], v[212:213] op_sel:[1,0,0]
	v_pk_fma_f32 v[214:215], v[104:105], v[206:207], v[214:215] op_sel:[1,0,0]
	v_pk_fma_f32 v[210:211], v[106:107], v[196:197], v[210:211] op_sel_hi:[0,1,1]
	v_pk_fma_f32 v[212:213], v[106:107], v[202:203], v[212:213] op_sel_hi:[0,1,1]
	v_pk_fma_f32 v[214:215], v[106:107], v[208:209], v[214:215] op_sel_hi:[0,1,1]
	v_pk_fma_f32 v[210:211], v[192:193], v[102:103], v[210:211] op_sel:[1,0,0] neg_lo:[0,0,1] neg_hi:[0,0,1]
	v_pk_fma_f32 v[212:213], v[192:193], v[100:101], v[212:213] op_sel:[1,0,0] neg_lo:[0,0,1] neg_hi:[0,0,1]
	v_pk_fma_f32 v[214:215], v[192:193], v[78:79], v[214:215] op_sel:[1,0,0] neg_lo:[0,0,1] neg_hi:[0,0,1]
	s_add_i32 s4, s34, 4
	s_min_i32 s4, s4, 0x200
	s_mul_i32 s5, s4, 0x804
	s_add_i32 s5, s5, s35
	s_add_i32 s6, s5, 0x0
	s_add_i32 s7, s5, 0x101004
	s_add_i32 s8, s5, 0x202008
	s_add_i32 s11, s5, 0x30300c
	s_add_i32 s15, s5, 0x404010
	s_add_i32 s31, s5, 0x505014
	s_mul_i32 s9, s4, 0x180c
	s_add_i32 s9, s9, s33
	buffer_load_dword v12, v28, s[16:19], s6 offen nt
	buffer_load_dword v13, v28, s[16:19], s7 offen nt
	buffer_load_dword v14, v28, s[16:19], s8 offen nt
	buffer_load_dword v15, v28, s[16:19], s11 offen nt
	buffer_load_dword v16, v28, s[16:19], s15 offen nt
	buffer_load_dword v17, v28, s[16:19], s31 offen nt
	buffer_load_dwordx3 v[32:34], v27, s[24:27], s9 offen nt
	s_waitcnt vmcnt(14)
	v_mov_b32_dpp v60, v96 wave_shr:1 row_mask:0xf bank_mask:0xf bound_ctrl:1
	v_mov_b32_dpp v61, v97 wave_shr:1 row_mask:0xf bank_mask:0xf bound_ctrl:1
	v_mov_b32_dpp v62, v98 wave_shr:1 row_mask:0xf bank_mask:0xf bound_ctrl:1
	v_mov_b32_dpp v64, v96 wave_shl:1 row_mask:0xf bank_mask:0xf bound_ctrl:1
	v_mov_b32_dpp v65, v97 wave_shl:1 row_mask:0xf bank_mask:0xf bound_ctrl:1
	v_mov_b32_dpp v66, v98 wave_shl:1 row_mask:0xf bank_mask:0xf bound_ctrl:1
	v_mov_b32_dpp v68, v54 wave_shr:1 row_mask:0xf bank_mask:0xf bound_ctrl:1
	v_mov_b32_dpp v69, v55 wave_shr:1 row_mask:0xf bank_mask:0xf bound_ctrl:1
	v_mov_b32_dpp v70, v92 wave_shr:1 row_mask:0xf bank_mask:0xf bound_ctrl:1
	v_mov_b32_dpp v71, v93 wave_shr:1 row_mask:0xf bank_mask:0xf bound_ctrl:1
	v_mov_b32_dpp v72, v94 wave_shr:1 row_mask:0xf bank_mask:0xf bound_ctrl:1
	v_mov_b32_dpp v73, v95 wave_shr:1 row_mask:0xf bank_mask:0xf bound_ctrl:1
	v_mov_b32_dpp v78, v54 wave_shl:1 row_mask:0xf bank_mask:0xf bound_ctrl:1
	v_mov_b32_dpp v79, v55 wave_shl:1 row_mask:0xf bank_mask:0xf bound_ctrl:1
	v_mov_b32_dpp v80, v92 wave_shl:1 row_mask:0xf bank_mask:0xf bound_ctrl:1
	v_mov_b32_dpp v81, v93 wave_shl:1 row_mask:0xf bank_mask:0xf bound_ctrl:1
	v_mov_b32_dpp v82, v94 wave_shl:1 row_mask:0xf bank_mask:0xf bound_ctrl:1
	v_mov_b32_dpp v83, v95 wave_shl:1 row_mask:0xf bank_mask:0xf bound_ctrl:1
	v_pk_mul_f32 v[84:85], v[54:55], v[96:97] op_sel_hi:[1,0]
	v_pk_mul_f32 v[86:87], v[92:93], v[96:97] op_sel_hi:[1,0]
	v_pk_mul_f32 v[88:89], v[94:95], v[96:97] op_sel_hi:[1,0]
	v_pk_mul_f32 v[90:91], v[54:55], v[96:97] op_sel:[0,1]
	v_pk_mul_f32 v[100:101], v[92:93], v[96:97] op_sel:[0,1]
	v_pk_mul_f32 v[102:103], v[94:95], v[96:97] op_sel:[0,1]
	v_pk_mul_f32 v[104:105], v[54:55], v[98:99] op_sel_hi:[1,0]
	v_pk_mul_f32 v[106:107], v[92:93], v[98:99] op_sel_hi:[1,0]
	v_pk_mul_f32 v[108:109], v[94:95], v[98:99] op_sel_hi:[1,0]
	v_pk_add_f32 v[110:111], v[54:55], v[68:69]
	v_pk_add_f32 v[192:193], v[92:93], v[70:71]
	v_pk_add_f32 v[194:195], v[94:95], v[72:73]
	v_pk_fma_f32 v[84:85], v[68:69], v[60:61], v[84:85] op_sel_hi:[1,0,1]
	v_pk_fma_f32 v[86:87], v[70:71], v[60:61], v[86:87] op_sel_hi:[1,0,1]
	v_pk_fma_f32 v[88:89], v[72:73], v[60:61], v[88:89] op_sel_hi:[1,0,1]
	v_pk_fma_f32 v[90:91], v[68:69], v[60:61], v[90:91] op_sel:[0,1,0]
	v_pk_fma_f32 v[100:101], v[70:71], v[60:61], v[100:101] op_sel:[0,1,0]
	v_pk_fma_f32 v[102:103], v[72:73], v[60:61], v[102:103] op_sel:[0,1,0]
	v_pk_fma_f32 v[104:105], v[68:69], v[62:63], v[104:105] op_sel_hi:[1,0,1]
	v_pk_fma_f32 v[106:107], v[70:71], v[62:63], v[106:107] op_sel_hi:[1,0,1]
	v_pk_fma_f32 v[108:109], v[72:73], v[62:63], v[108:109] op_sel_hi:[1,0,1]
	v_pk_add_f32 v[110:111], v[110:111], v[78:79]
	v_pk_add_f32 v[192:193], v[192:193], v[80:81]
	v_pk_add_f32 v[194:195], v[194:195], v[82:83]
	v_pk_fma_f32 v[84:85], v[78:79], v[64:65], v[84:85] op_sel_hi:[1,0,1]
	v_pk_fma_f32 v[86:87], v[80:81], v[64:65], v[86:87] op_sel_hi:[1,0,1]
	v_pk_fma_f32 v[88:89], v[82:83], v[64:65], v[88:89] op_sel_hi:[1,0,1]
	v_pk_fma_f32 v[90:91], v[78:79], v[64:65], v[90:91] op_sel:[0,1,0]
	v_pk_fma_f32 v[100:101], v[80:81], v[64:65], v[100:101] op_sel:[0,1,0]
	v_pk_fma_f32 v[102:103], v[82:83], v[64:65], v[102:103] op_sel:[0,1,0]
	v_pk_fma_f32 v[104:105], v[78:79], v[66:67], v[104:105] op_sel_hi:[1,0,1]
	v_pk_fma_f32 v[106:107], v[80:81], v[66:67], v[106:107] op_sel_hi:[1,0,1]
	v_pk_fma_f32 v[108:109], v[82:83], v[66:67], v[108:109] op_sel_hi:[1,0,1]
	s_barrier
	ds_read_b128 v[68:71], v23 offset:0
	ds_read_b128 v[80:83], v23 offset:1024
	ds_read_b128 v[216:219], v23 offset:2048
	v_pk_add_f32 v[72:73], v[142:143], v[110:111]
	v_pk_add_f32 v[78:79], v[162:163], v[72:73]
	v_pk_add_f32 v[142:143], v[168:169], v[192:193]
	v_pk_add_f32 v[162:163], v[164:165], v[142:143]
	v_pk_add_f32 v[164:165], v[170:171], v[194:195]
	v_pk_add_f32 v[168:169], v[166:167], v[164:165]
	v_pk_add_f32 v[166:167], v[114:115], v[84:85]
	v_pk_add_f32 v[170:171], v[144:145], v[166:167]
	v_pk_add_f32 v[114:115], v[116:117], v[86:87]
	v_pk_add_f32 v[144:145], v[146:147], v[114:115]
	v_pk_add_f32 v[116:117], v[120:121], v[88:89]
	v_pk_add_f32 v[146:147], v[148:149], v[116:117]
	v_pk_add_f32 v[120:121], v[122:123], v[90:91]
	v_pk_add_f32 v[148:149], v[150:151], v[120:121]
	v_pk_add_f32 v[122:123], v[124:125], v[100:101]
	v_pk_add_f32 v[150:151], v[152:153], v[122:123]
	v_pk_add_f32 v[124:125], v[126:127], v[102:103]
	v_pk_add_f32 v[152:153], v[154:155], v[124:125]
	v_pk_add_f32 v[126:127], v[136:137], v[104:105]
	v_pk_add_f32 v[154:155], v[156:157], v[126:127]
	v_pk_add_f32 v[136:137], v[138:139], v[106:107]
	v_pk_add_f32 v[156:157], v[158:159], v[136:137]
	v_pk_add_f32 v[138:139], v[140:141], v[108:109]
	v_pk_add_f32 v[158:159], v[160:161], v[138:139]
	s_waitcnt lgkmcnt(2)
	v_pk_fma_f32 v[170:171], v[68:69], v[78:79], v[170:171] op_sel_hi:[0,1,1] neg_lo:[1,0,0] neg_hi:[1,0,0]
	v_pk_fma_f32 v[144:145], v[68:69], v[162:163], v[144:145] op_sel_hi:[0,1,1] neg_lo:[1,0,0] neg_hi:[1,0,0]
	v_pk_fma_f32 v[146:147], v[68:69], v[168:169], v[146:147] op_sel_hi:[0,1,1] neg_lo:[1,0,0] neg_hi:[1,0,0]
	v_pk_fma_f32 v[148:149], v[68:69], v[78:79], v[148:149] op_sel:[1,0,0] neg_lo:[1,0,0] neg_hi:[1,0,0]
	v_pk_fma_f32 v[150:151], v[68:69], v[162:163], v[150:151] op_sel:[1,0,0] neg_lo:[1,0,0] neg_hi:[1,0,0]
	v_pk_fma_f32 v[152:153], v[68:69], v[168:169], v[152:153] op_sel:[1,0,0] neg_lo:[1,0,0] neg_hi:[1,0,0]
	v_pk_fma_f32 v[154:155], v[70:71], v[78:79], v[154:155] op_sel_hi:[0,1,1] neg_lo:[1,0,0] neg_hi:[1,0,0]
	v_pk_fma_f32 v[156:157], v[70:71], v[162:163], v[156:157] op_sel_hi:[0,1,1] neg_lo:[1,0,0] neg_hi:[1,0,0]
	v_pk_fma_f32 v[158:159], v[70:71], v[168:169], v[158:159] op_sel_hi:[0,1,1] neg_lo:[1,0,0] neg_hi:[1,0,0]
	v_pk_mul_f32 v[140:141], v[70:71], v[170:171] op_sel:[1,0]
	v_pk_mul_f32 v[222:223], v[70:71], v[144:145] op_sel:[1,0]
	v_pk_mul_f32 v[228:229], v[70:71], v[146:147] op_sel:[1,0]
	s_waitcnt lgkmcnt(1)
	v_pk_mul_f32 v[160:161], v[80:81], v[170:171] op_sel_hi:[0,1]
	v_pk_mul_f32 v[224:225], v[80:81], v[144:145] op_sel_hi:[0,1]
	v_pk_mul_f32 v[230:231], v[80:81], v[146:147] op_sel_hi:[0,1]
	v_pk_mul_f32 v[220:221], v[80:81], v[170:171] op_sel:[1,0]
	v_pk_mul_f32 v[226:227], v[80:81], v[144:145] op_sel:[1,0]
	v_pk_mul_f32 v[232:233], v[80:81], v[146:147] op_sel:[1,0]
	v_pk_fma_f32 v[140:141], v[80:81], v[148:149], v[140:141] op_sel_hi:[0,1,1]
	v_pk_fma_f32 v[222:223], v[80:81], v[150:151], v[222:223] op_sel_hi:[0,1,1]
	v_pk_fma_f32 v[228:229], v[80:81], v[152:153], v[228:229] op_sel_hi:[0,1,1]
	v_pk_fma_f32 v[160:161], v[82:83], v[148:149], v[160:161] op_sel_hi:[0,1,1]
	v_pk_fma_f32 v[224:225], v[82:83], v[150:151], v[224:225] op_sel_hi:[0,1,1]
	v_pk_fma_f32 v[230:231], v[82:83], v[152:153], v[230:231] op_sel_hi:[0,1,1]
	v_pk_fma_f32 v[220:221], v[82:83], v[148:149], v[220:221] op_sel:[1,0,0]
	v_pk_fma_f32 v[226:227], v[82:83], v[150:151], v[226:227] op_sel:[1,0,0]
	v_pk_fma_f32 v[232:233], v[82:83], v[152:153], v[232:233] op_sel:[1,0,0]
	v_pk_fma_f32 v[140:141], v[80:81], v[154:155], v[140:141] op_sel:[1,0,0]
	v_pk_fma_f32 v[222:223], v[80:81], v[156:157], v[222:223] op_sel:[1,0,0]
	v_pk_fma_f32 v[228:229], v[80:81], v[158:159], v[228:229] op_sel:[1,0,0]
	v_pk_fma_f32 v[160:161], v[82:83], v[154:155], v[160:161] op_sel:[1,0,0]
	v_pk_fma_f32 v[224:225], v[82:83], v[156:157], v[224:225] op_sel:[1,0,0]
	v_pk_fma_f32 v[230:231], v[82:83], v[158:159], v[230:231] op_sel:[1,0,0]
	s_waitcnt lgkmcnt(0)
	v_pk_fma_f32 v[220:221], v[216:217], v[154:155], v[220:221] op_sel_hi:[0,1,1]
	v_pk_fma_f32 v[226:227], v[216:217], v[156:157], v[226:227] op_sel_hi:[0,1,1]
	v_pk_fma_f32 v[232:233], v[216:217], v[158:159], v[232:233] op_sel_hi:[0,1,1]
	v_pk_mul_f32 v[234:235], v[68:69], v[140:141] op_sel_hi:[0,1]
	v_pk_mul_f32 v[236:237], v[68:69], v[222:223] op_sel_hi:[0,1]
	v_pk_mul_f32 v[238:239], v[68:69], v[228:229] op_sel_hi:[0,1]
	v_pk_fma_f32 v[234:235], v[68:69], v[160:161], v[234:235] op_sel:[1,0,0]
	v_pk_fma_f32 v[236:237], v[68:69], v[224:225], v[236:237] op_sel:[1,0,0]
	v_pk_fma_f32 v[238:239], v[68:69], v[230:231], v[238:239] op_sel:[1,0,0]
	v_pk_fma_f32 v[234:235], v[70:71], v[220:221], v[234:235] op_sel_hi:[0,1,1]
	v_pk_fma_f32 v[236:237], v[70:71], v[226:227], v[236:237] op_sel_hi:[0,1,1]
	v_pk_fma_f32 v[238:239], v[70:71], v[232:233], v[238:239] op_sel_hi:[0,1,1]
	v_pk_fma_f32 v[234:235], v[216:217], v[78:79], v[234:235] op_sel:[1,0,0] neg_lo:[0,0,1] neg_hi:[0,0,1]
	v_pk_fma_f32 v[236:237], v[216:217], v[162:163], v[236:237] op_sel:[1,0,0] neg_lo:[0,0,1] neg_hi:[0,0,1]
	v_pk_fma_f32 v[238:239], v[216:217], v[168:169], v[238:239] op_sel:[1,0,0] neg_lo:[0,0,1] neg_hi:[0,0,1]
	v_cmp_eq_u32_e64 s[10:11], 1, v219
	v_cmp_eq_u32_e64 s[14:15], 2, v219
	v_cmp_eq_u32_e64 s[20:21], 3, v219
	v_cmp_eq_u32_e64 s[22:23], 4, v219
	v_cmp_eq_u32_e64 s[30:31], 5, v219
	v_cmp_eq_u32_e64 s[38:39], 6, v219
	v_pk_add_f32 v[78:79], v[74:75], v[140:141]
	v_pk_add_f32 v[144:145], v[76:77], v[78:79]
	v_pk_add_f32 v[74:75], v[198:199], v[222:223]
	v_pk_add_f32 v[76:77], v[174:175], v[74:75]
	v_pk_add_f32 v[146:147], v[204:205], v[228:229]
	v_pk_add_f32 v[148:149], v[180:181], v[146:147]
	v_pk_add_f32 v[150:151], v[112:113], v[160:161]
	v_pk_add_f32 v[152:153], v[118:119], v[150:151]
	v_pk_add_f32 v[112:113], v[200:201], v[224:225]
	v_pk_add_f32 v[118:119], v[176:177], v[112:113]
	v_pk_add_f32 v[154:155], v[206:207], v[230:231]
	v_pk_add_f32 v[156:157], v[182:183], v[154:155]
	v_pk_add_f32 v[158:159], v[196:197], v[220:221]
	v_pk_add_f32 v[162:163], v[172:173], v[158:159]
	v_pk_add_f32 v[168:169], v[202:203], v[226:227]
	v_pk_add_f32 v[170:171], v[178:179], v[168:169]
	v_pk_add_f32 v[172:173], v[208:209], v[232:233]
	v_pk_add_f32 v[174:175], v[184:185], v[172:173]
	v_pk_add_f32 v[176:177], v[210:211], v[234:235]
	v_pk_add_f32 v[178:179], v[186:187], v[176:177]
	v_pk_add_f32 v[180:181], v[212:213], v[236:237]
	v_pk_add_f32 v[182:183], v[188:189], v[180:181]
	v_pk_add_f32 v[184:185], v[214:215], v[238:239]
	v_pk_add_f32 v[186:187], v[190:191], v[184:185]
	v_pk_fma_f32 v[188:189], v[128:129], v[144:145], v[178:179] op_sel_hi:[0,1,1]
	v_pk_fma_f32 v[190:191], v[128:129], v[76:77], v[182:183] op_sel_hi:[0,1,1]
	v_pk_fma_f32 v[196:197], v[128:129], v[148:149], v[186:187] op_sel_hi:[0,1,1]
	v_pk_fma_f32 v[198:199], v[132:133], v[144:145], v[178:179] op_sel_hi:[0,1,1]
	v_pk_fma_f32 v[200:201], v[132:133], v[76:77], v[182:183] op_sel_hi:[0,1,1]
	v_pk_fma_f32 v[202:203], v[132:133], v[148:149], v[186:187] op_sel_hi:[0,1,1]
	v_pk_fma_f32 v[188:189], v[128:129], v[152:153], v[188:189] op_sel:[1,0,0]
	v_pk_fma_f32 v[190:191], v[128:129], v[118:119], v[190:191] op_sel:[1,0,0]
	v_pk_fma_f32 v[196:197], v[128:129], v[156:157], v[196:197] op_sel:[1,0,0]
	v_pk_fma_f32 v[198:199], v[132:133], v[152:153], v[198:199] op_sel:[1,0,0]
	v_pk_fma_f32 v[200:201], v[132:133], v[118:119], v[200:201] op_sel:[1,0,0]
	v_pk_fma_f32 v[202:203], v[132:133], v[156:157], v[202:203] op_sel:[1,0,0]
	v_pk_fma_f32 v[188:189], v[130:131], v[162:163], v[188:189] op_sel_hi:[0,1,1]
	v_pk_fma_f32 v[190:191], v[130:131], v[170:171], v[190:191] op_sel_hi:[0,1,1]
	v_pk_fma_f32 v[196:197], v[130:131], v[174:175], v[196:197] op_sel_hi:[0,1,1]
	v_pk_fma_f32 v[198:199], v[134:135], v[162:163], v[198:199] op_sel_hi:[0,1,1]
	v_pk_fma_f32 v[200:201], v[134:135], v[170:171], v[200:201] op_sel_hi:[0,1,1]
	v_pk_fma_f32 v[202:203], v[134:135], v[174:175], v[202:203] op_sel_hi:[0,1,1]
	v_pk_fma_f32 v[178:179], v[36:37], v[144:145], v[178:179] op_sel_hi:[0,1,1]
	v_pk_fma_f32 v[182:183], v[36:37], v[76:77], v[182:183] op_sel_hi:[0,1,1]
	v_pk_fma_f32 v[186:187], v[36:37], v[148:149], v[186:187] op_sel_hi:[0,1,1]
	v_pk_fma_f32 v[178:179], v[36:37], v[152:153], v[178:179] op_sel:[1,0,0]
	v_pk_fma_f32 v[182:183], v[36:37], v[118:119], v[182:183] op_sel:[1,0,0]
	v_pk_fma_f32 v[186:187], v[36:37], v[156:157], v[186:187] op_sel:[1,0,0]
	v_pk_fma_f32 v[178:179], v[38:39], v[162:163], v[178:179] op_sel_hi:[0,1,1]
	v_pk_fma_f32 v[182:183], v[38:39], v[170:171], v[182:183] op_sel_hi:[0,1,1]
	v_pk_fma_f32 v[186:187], v[38:39], v[174:175], v[186:187] op_sel_hi:[0,1,1]
	v_cndmask_b32_e64 v204, 0, v1, s[10:11]
	v_cndmask_b32_e64 v205, 0, v1, s[14:15]
	v_cndmask_b32_e64 v206, 0, v1, s[20:21]
	v_cndmask_b32_e64 v207, 0, v1, s[22:23]
	v_cndmask_b32_e64 v208, 0, v1, s[30:31]
	v_cndmask_b32_e64 v209, 0, v1, s[38:39]
	v_add_f32_dpp v178, v188, v178 wave_shl:1 row_mask:0xf bank_mask:0xf bound_ctrl:1
	v_add_f32_dpp v179, v189, v179 wave_shl:1 row_mask:0xf bank_mask:0xf bound_ctrl:1
	v_add_f32_dpp v182, v190, v182 wave_shl:1 row_mask:0xf bank_mask:0xf bound_ctrl:1
	v_add_f32_dpp v183, v191, v183 wave_shl:1 row_mask:0xf bank_mask:0xf bound_ctrl:1
	v_add_f32_dpp v186, v196, v186 wave_shl:1 row_mask:0xf bank_mask:0xf bound_ctrl:1
	v_add_f32_dpp v187, v197, v187 wave_shl:1 row_mask:0xf bank_mask:0xf bound_ctrl:1
	s_add_i32 s4, s34, 0
	s_cmpk_lt_i32 s4, 0x201
	s_cselect_b64 s[12:13], s[0:1], 0
	v_add_f32_dpp v178, v198, v178 wave_shr:1 row_mask:0xf bank_mask:0xf bound_ctrl:1
	v_add_f32_dpp v179, v199, v179 wave_shr:1 row_mask:0xf bank_mask:0xf bound_ctrl:1
	v_add_f32_dpp v182, v200, v182 wave_shr:1 row_mask:0xf bank_mask:0xf bound_ctrl:1
	v_add_f32_dpp v183, v201, v183 wave_shr:1 row_mask:0xf bank_mask:0xf bound_ctrl:1
	v_add_f32_dpp v186, v202, v186 wave_shr:1 row_mask:0xf bank_mask:0xf bound_ctrl:1
	v_add_f32_dpp v187, v203, v187 wave_shr:1 row_mask:0xf bank_mask:0xf bound_ctrl:1
	v_pk_fma_f32 v[178:179], v[20:21], v[218:219], v[178:179] op_sel_hi:[1,0,1] neg_lo:[0,0,1] neg_hi:[0,0,1]
	v_pk_fma_f32 v[182:183], v[24:25], v[218:219], v[182:183] op_sel_hi:[1,0,1] neg_lo:[0,0,1] neg_hi:[0,0,1]
	v_pk_fma_f32 v[186:187], v[30:31], v[218:219], v[186:187] op_sel_hi:[1,0,1] neg_lo:[0,0,1] neg_hi:[0,0,1]
	v_pk_add_f32 v[178:179], v[178:179], v[204:205] neg_lo:[0,1] neg_hi:[0,1]
	v_pk_add_f32 v[182:183], v[182:183], v[206:207] neg_lo:[0,1] neg_hi:[0,1]
	v_pk_add_f32 v[186:187], v[186:187], v[208:209] neg_lo:[0,1] neg_hi:[0,1]
	v_pk_mul_f32 v[210:211], v[178:179], v[178:179]
	v_pk_fma_f32 v[210:211], v[182:183], v[182:183], v[210:211]
	v_pk_fma_f32 v[210:211], v[186:187], v[186:187], v[210:211]
	v_add_f32_e32 v210, v210, v211
	v_cndmask_b32_e64 v211, 0, v210, s[12:13]
	v_add_f32_e32 v0, v0, v211
	s_add_i32 s4, s34, 5
	s_min_i32 s4, s4, 0x200
	s_mul_i32 s5, s4, 0x804
	s_add_i32 s5, s5, s35
	s_add_i32 s6, s5, 0x0
	s_add_i32 s7, s5, 0x101004
	s_add_i32 s8, s5, 0x202008
	s_add_i32 s11, s5, 0x30300c
	s_add_i32 s15, s5, 0x404010
	s_add_i32 s31, s5, 0x505014
	s_mul_i32 s9, s4, 0x180c
	s_add_i32 s9, s9, s33
	buffer_load_dword v20, v28, s[16:19], s6 offen nt
	buffer_load_dword v21, v28, s[16:19], s7 offen nt
	buffer_load_dword v24, v28, s[16:19], s8 offen nt
	buffer_load_dword v25, v28, s[16:19], s11 offen nt
	buffer_load_dword v30, v28, s[16:19], s15 offen nt
	buffer_load_dword v31, v28, s[16:19], s31 offen nt
	buffer_load_dwordx3 v[36:38], v27, s[24:27], s9 offen nt
	s_waitcnt vmcnt(14)
	v_mov_b32_dpp v68, v8 wave_shr:1 row_mask:0xf bank_mask:0xf bound_ctrl:1
	v_mov_b32_dpp v69, v9 wave_shr:1 row_mask:0xf bank_mask:0xf bound_ctrl:1
	v_mov_b32_dpp v70, v10 wave_shr:1 row_mask:0xf bank_mask:0xf bound_ctrl:1
	v_mov_b32_dpp v80, v8 wave_shl:1 row_mask:0xf bank_mask:0xf bound_ctrl:1
	v_mov_b32_dpp v81, v9 wave_shl:1 row_mask:0xf bank_mask:0xf bound_ctrl:1
	v_mov_b32_dpp v82, v10 wave_shl:1 row_mask:0xf bank_mask:0xf bound_ctrl:1
	v_mov_b32_dpp v76, v2 wave_shr:1 row_mask:0xf bank_mask:0xf bound_ctrl:1
	v_mov_b32_dpp v77, v3 wave_shr:1 row_mask:0xf bank_mask:0xf bound_ctrl:1
	v_mov_b32_dpp v118, v4 wave_shr:1 row_mask:0xf bank_mask:0xf bound_ctrl:1
	v_mov_b32_dpp v119, v5 wave_shr:1 row_mask:0xf bank_mask:0xf bound_ctrl:1
	v_mov_b32_dpp v128, v6 wave_shr:1 row_mask:0xf bank_mask:0xf bound_ctrl:1
	v_mov_b32_dpp v129, v7 wave_shr:1 row_mask:0xf bank_mask:0xf bound_ctrl:1
	v_mov_b32_dpp v130, v2 wave_shl:1 row_mask:0xf bank_mask:0xf bound_ctrl:1
	v_mov_b32_dpp v131, v3 wave_shl:1 row_mask:0xf bank_mask:0xf bound_ctrl:1
	v_mov_b32_dpp v132, v4 wave_shl:1 row_mask:0xf bank_mask:0xf bound_ctrl:1
	v_mov_b32_dpp v133, v5 wave_shl:1 row_mask:0xf bank_mask:0xf bound_ctrl:1
	v_mov_b32_dpp v134, v6 wave_shl:1 row_mask:0xf bank_mask:0xf bound_ctrl:1
	v_mov_b32_dpp v135, v7 wave_shl:1 row_mask:0xf bank_mask:0xf bound_ctrl:1
	v_pk_mul_f32 v[144:145], v[2:3], v[8:9] op_sel_hi:[1,0]
	v_pk_mul_f32 v[148:149], v[4:5], v[8:9] op_sel_hi:[1,0]
	v_pk_mul_f32 v[152:153], v[6:7], v[8:9] op_sel_hi:[1,0]
	v_pk_mul_f32 v[156:157], v[2:3], v[8:9] op_sel:[0,1]
	v_pk_mul_f32 v[162:163], v[4:5], v[8:9] op_sel:[0,1]
	v_pk_mul_f32 v[170:171], v[6:7], v[8:9] op_sel:[0,1]
	v_pk_mul_f32 v[174:175], v[2:3], v[10:11] op_sel_hi:[1,0]
	v_pk_mul_f32 v[178:179], v[4:5], v[10:11] op_sel_hi:[1,0]
	v_pk_mul_f32 v[182:183], v[6:7], v[10:11] op_sel_hi:[1,0]
	v_pk_add_f32 v[186:187], v[2:3], v[76:77]
	v_pk_add_f32 v[188:189], v[4:5], v[118:119]
	v_pk_add_f32 v[190:191], v[6:7], v[128:129]
	v_pk_fma_f32 v[144:145], v[76:77], v[68:69], v[144:145] op_sel_hi:[1,0,1]
	v_pk_fma_f32 v[148:149], v[118:119], v[68:69], v[148:149] op_sel_hi:[1,0,1]
	v_pk_fma_f32 v[152:153], v[128:129], v[68:69], v[152:153] op_sel_hi:[1,0,1]
	v_pk_fma_f32 v[156:157], v[76:77], v[68:69], v[156:157] op_sel:[0,1,0]
	v_pk_fma_f32 v[162:163], v[118:119], v[68:69], v[162:163] op_sel:[0,1,0]
	v_pk_fma_f32 v[170:171], v[128:129], v[68:69], v[170:171] op_sel:[0,1,0]
	v_pk_fma_f32 v[174:175], v[76:77], v[70:71], v[174:175] op_sel_hi:[1,0,1]
	v_pk_fma_f32 v[178:179], v[118:119], v[70:71], v[178:179] op_sel_hi:[1,0,1]
	v_pk_fma_f32 v[182:183], v[128:129], v[70:71], v[182:183] op_sel_hi:[1,0,1]
	v_pk_add_f32 v[186:187], v[186:187], v[130:131]
	v_pk_add_f32 v[188:189], v[188:189], v[132:133]
	v_pk_add_f32 v[190:191], v[190:191], v[134:135]
	v_pk_fma_f32 v[144:145], v[130:131], v[80:81], v[144:145] op_sel_hi:[1,0,1]
	v_pk_fma_f32 v[148:149], v[132:133], v[80:81], v[148:149] op_sel_hi:[1,0,1]
	v_pk_fma_f32 v[152:153], v[134:135], v[80:81], v[152:153] op_sel_hi:[1,0,1]
	v_pk_fma_f32 v[156:157], v[130:131], v[80:81], v[156:157] op_sel:[0,1,0]
	v_pk_fma_f32 v[162:163], v[132:133], v[80:81], v[162:163] op_sel:[0,1,0]
	v_pk_fma_f32 v[170:171], v[134:135], v[80:81], v[170:171] op_sel:[0,1,0]
	v_pk_fma_f32 v[174:175], v[130:131], v[82:83], v[174:175] op_sel_hi:[1,0,1]
	v_pk_fma_f32 v[178:179], v[132:133], v[82:83], v[178:179] op_sel_hi:[1,0,1]
	v_pk_fma_f32 v[182:183], v[134:135], v[82:83], v[182:183] op_sel_hi:[1,0,1]
	s_barrier
	ds_read_b128 v[128:131], v23 offset:3072
	ds_read_b128 v[132:135], v23 offset:4096
	ds_read_b128 v[196:199], v23 offset:5120
	v_pk_add_f32 v[76:77], v[72:73], v[186:187]
	v_pk_add_f32 v[72:73], v[142:143], v[188:189]
	v_pk_add_f32 v[118:119], v[164:165], v[190:191]
	v_pk_add_f32 v[142:143], v[166:167], v[144:145]
	v_pk_add_f32 v[164:165], v[114:115], v[148:149]
	v_pk_add_f32 v[114:115], v[116:117], v[152:153]
	v_pk_add_f32 v[116:117], v[120:121], v[156:157]
	v_pk_add_f32 v[120:121], v[122:123], v[162:163]
	v_pk_add_f32 v[122:123], v[124:125], v[170:171]
	v_pk_add_f32 v[124:125], v[126:127], v[174:175]
	v_pk_add_f32 v[126:127], v[136:137], v[178:179]
	v_pk_add_f32 v[136:137], v[138:139], v[182:183]
	s_waitcnt lgkmcnt(2)
	v_pk_fma_f32 v[142:143], v[128:129], v[76:77], v[142:143] op_sel_hi:[0,1,1] neg_lo:[1,0,0] neg_hi:[1,0,0]
	v_pk_fma_f32 v[164:165], v[128:129], v[72:73], v[164:165] op_sel_hi:[0,1,1] neg_lo:[1,0,0] neg_hi:[1,0,0]
	v_pk_fma_f32 v[114:115], v[128:129], v[118:119], v[114:115] op_sel_hi:[0,1,1] neg_lo:[1,0,0] neg_hi:[1,0,0]
	v_pk_fma_f32 v[116:117], v[128:129], v[76:77], v[116:117] op_sel:[1,0,0] neg_lo:[1,0,0] neg_hi:[1,0,0]
	v_pk_fma_f32 v[120:121], v[128:129], v[72:73], v[120:121] op_sel:[1,0,0] neg_lo:[1,0,0] neg_hi:[1,0,0]
	v_pk_fma_f32 v[122:123], v[128:129], v[118:119], v[122:123] op_sel:[1,0,0] neg_lo:[1,0,0] neg_hi:[1,0,0]
	v_pk_fma_f32 v[124:125], v[130:131], v[76:77], v[124:125] op_sel_hi:[0,1,1] neg_lo:[1,0,0] neg_hi:[1,0,0]
	v_pk_fma_f32 v[126:127], v[130:131], v[72:73], v[126:127] op_sel_hi:[0,1,1] neg_lo:[1,0,0] neg_hi:[1,0,0]
	v_pk_fma_f32 v[136:137], v[130:131], v[118:119], v[136:137] op_sel_hi:[0,1,1] neg_lo:[1,0,0] neg_hi:[1,0,0]
	v_pk_mul_f32 v[138:139], v[130:131], v[142:143] op_sel:[1,0]
	v_pk_mul_f32 v[202:203], v[130:131], v[164:165] op_sel:[1,0]
	v_pk_mul_f32 v[208:209], v[130:131], v[114:115] op_sel:[1,0]
	s_waitcnt lgkmcnt(1)
	v_pk_mul_f32 v[166:167], v[132:133], v[142:143] op_sel_hi:[0,1]
	v_pk_mul_f32 v[204:205], v[132:133], v[164:165] op_sel_hi:[0,1]
	v_pk_mul_f32 v[210:211], v[132:133], v[114:115] op_sel_hi:[0,1]
	v_pk_mul_f32 v[200:201], v[132:133], v[142:143] op_sel:[1,0]
	v_pk_mul_f32 v[206:207], v[132:133], v[164:165] op_sel:[1,0]
	v_pk_mul_f32 v[212:213], v[132:133], v[114:115] op_sel:[1,0]
	v_pk_fma_f32 v[138:139], v[132:133], v[116:117], v[138:139] op_sel_hi:[0,1,1]
	v_pk_fma_f32 v[202:203], v[132:133], v[120:121], v[202:203] op_sel_hi:[0,1,1]
	v_pk_fma_f32 v[208:209], v[132:133], v[122:123], v[208:209] op_sel_hi:[0,1,1]
	v_pk_fma_f32 v[166:167], v[134:135], v[116:117], v[166:167] op_sel_hi:[0,1,1]
	v_pk_fma_f32 v[204:205], v[134:135], v[120:121], v[204:205] op_sel_hi:[0,1,1]
	v_pk_fma_f32 v[210:211], v[134:135], v[122:123], v[210:211] op_sel_hi:[0,1,1]
	v_pk_fma_f32 v[200:201], v[134:135], v[116:117], v[200:201] op_sel:[1,0,0]
	v_pk_fma_f32 v[206:207], v[134:135], v[120:121], v[206:207] op_sel:[1,0,0]
	v_pk_fma_f32 v[212:213], v[134:135], v[122:123], v[212:213] op_sel:[1,0,0]
	v_pk_fma_f32 v[138:139], v[132:133], v[124:125], v[138:139] op_sel:[1,0,0]
	v_pk_fma_f32 v[202:203], v[132:133], v[126:127], v[202:203] op_sel:[1,0,0]
	v_pk_fma_f32 v[208:209], v[132:133], v[136:137], v[208:209] op_sel:[1,0,0]
	v_pk_fma_f32 v[166:167], v[134:135], v[124:125], v[166:167] op_sel:[1,0,0]
	v_pk_fma_f32 v[204:205], v[134:135], v[126:127], v[204:205] op_sel:[1,0,0]
	v_pk_fma_f32 v[210:211], v[134:135], v[136:137], v[210:211] op_sel:[1,0,0]
	s_waitcnt lgkmcnt(0)
	v_pk_fma_f32 v[200:201], v[196:197], v[124:125], v[200:201] op_sel_hi:[0,1,1]
	v_pk_fma_f32 v[206:207], v[196:197], v[126:127], v[206:207] op_sel_hi:[0,1,1]
	v_pk_fma_f32 v[212:213], v[196:197], v[136:137], v[212:213] op_sel_hi:[0,1,1]
	v_pk_mul_f32 v[214:215], v[128:129], v[138:139] op_sel_hi:[0,1]
	v_pk_mul_f32 v[216:217], v[128:129], v[202:203] op_sel_hi:[0,1]
	v_pk_mul_f32 v[218:219], v[128:129], v[208:209] op_sel_hi:[0,1]
	v_pk_fma_f32 v[214:215], v[128:129], v[166:167], v[214:215] op_sel:[1,0,0]
	v_pk_fma_f32 v[216:217], v[128:129], v[204:205], v[216:217] op_sel:[1,0,0]
	v_pk_fma_f32 v[218:219], v[128:129], v[210:211], v[218:219] op_sel:[1,0,0]
	v_pk_fma_f32 v[214:215], v[130:131], v[200:201], v[214:215] op_sel_hi:[0,1,1]
	v_pk_fma_f32 v[216:217], v[130:131], v[206:207], v[216:217] op_sel_hi:[0,1,1]
	v_pk_fma_f32 v[218:219], v[130:131], v[212:213], v[218:219] op_sel_hi:[0,1,1]
	v_pk_fma_f32 v[214:215], v[196:197], v[76:77], v[214:215] op_sel:[1,0,0] neg_lo:[0,0,1] neg_hi:[0,0,1]
	v_pk_fma_f32 v[216:217], v[196:197], v[72:73], v[216:217] op_sel:[1,0,0] neg_lo:[0,0,1] neg_hi:[0,0,1]
	v_pk_fma_f32 v[218:219], v[196:197], v[118:119], v[218:219] op_sel:[1,0,0] neg_lo:[0,0,1] neg_hi:[0,0,1]
	v_cmp_eq_u32_e64 s[10:11], 1, v199
	v_cmp_eq_u32_e64 s[14:15], 2, v199
	v_cmp_eq_u32_e64 s[20:21], 3, v199
	v_cmp_eq_u32_e64 s[22:23], 4, v199
	v_cmp_eq_u32_e64 s[30:31], 5, v199
	v_cmp_eq_u32_e64 s[38:39], 6, v199
	v_pk_add_f32 v[72:73], v[78:79], v[138:139]
	v_pk_add_f32 v[76:77], v[74:75], v[202:203]
	v_pk_add_f32 v[74:75], v[146:147], v[208:209]
	v_pk_add_f32 v[78:79], v[150:151], v[166:167]
	v_pk_add_f32 v[114:115], v[112:113], v[204:205]
	v_pk_add_f32 v[112:113], v[154:155], v[210:211]
	v_pk_add_f32 v[116:117], v[158:159], v[200:201]
	v_pk_add_f32 v[118:119], v[168:169], v[206:207]
	v_pk_add_f32 v[120:121], v[172:173], v[212:213]
	v_pk_add_f32 v[122:123], v[176:177], v[214:215]
	v_pk_add_f32 v[124:125], v[180:181], v[216:217]
	v_pk_add_f32 v[126:127], v[184:185], v[218:219]
	v_pk_fma_f32 v[136:137], v[40:41], v[72:73], v[122:123] op_sel_hi:[0,1,1]
	v_pk_fma_f32 v[142:143], v[40:41], v[76:77], v[124:125] op_sel_hi:[0,1,1]
	v_pk_fma_f32 v[146:147], v[40:41], v[74:75], v[126:127] op_sel_hi:[0,1,1]
	v_pk_fma_f32 v[150:151], v[44:45], v[72:73], v[122:123] op_sel_hi:[0,1,1]
	v_pk_fma_f32 v[154:155], v[44:45], v[76:77], v[124:125] op_sel_hi:[0,1,1]
	v_pk_fma_f32 v[158:159], v[44:45], v[74:75], v[126:127] op_sel_hi:[0,1,1]
	v_pk_fma_f32 v[136:137], v[40:41], v[78:79], v[136:137] op_sel:[1,0,0]
	v_pk_fma_f32 v[142:143], v[40:41], v[114:115], v[142:143] op_sel:[1,0,0]
	v_pk_fma_f32 v[146:147], v[40:41], v[112:113], v[146:147] op_sel:[1,0,0]
	v_pk_fma_f32 v[150:151], v[44:45], v[78:79], v[150:151] op_sel:[1,0,0]
	v_pk_fma_f32 v[154:155], v[44:45], v[114:115], v[154:155] op_sel:[1,0,0]
	v_pk_fma_f32 v[158:159], v[44:45], v[112:113], v[158:159] op_sel:[1,0,0]
	v_pk_fma_f32 v[136:137], v[42:43], v[116:117], v[136:137] op_sel_hi:[0,1,1]
	v_pk_fma_f32 v[142:143], v[42:43], v[118:119], v[142:143] op_sel_hi:[0,1,1]
	v_pk_fma_f32 v[146:147], v[42:43], v[120:121], v[146:147] op_sel_hi:[0,1,1]
	v_pk_fma_f32 v[150:151], v[46:47], v[116:117], v[150:151] op_sel_hi:[0,1,1]
	v_pk_fma_f32 v[154:155], v[46:47], v[118:119], v[154:155] op_sel_hi:[0,1,1]
	v_pk_fma_f32 v[158:159], v[46:47], v[120:121], v[158:159] op_sel_hi:[0,1,1]
	v_pk_fma_f32 v[122:123], v[56:57], v[72:73], v[122:123] op_sel_hi:[0,1,1]
	v_pk_fma_f32 v[124:125], v[56:57], v[76:77], v[124:125] op_sel_hi:[0,1,1]
	v_pk_fma_f32 v[126:127], v[56:57], v[74:75], v[126:127] op_sel_hi:[0,1,1]
	v_pk_fma_f32 v[122:123], v[56:57], v[78:79], v[122:123] op_sel:[1,0,0]
	v_pk_fma_f32 v[124:125], v[56:57], v[114:115], v[124:125] op_sel:[1,0,0]
	v_pk_fma_f32 v[126:127], v[56:57], v[112:113], v[126:127] op_sel:[1,0,0]
	v_pk_fma_f32 v[122:123], v[58:59], v[116:117], v[122:123] op_sel_hi:[0,1,1]
	v_pk_fma_f32 v[124:125], v[58:59], v[118:119], v[124:125] op_sel_hi:[0,1,1]
	v_pk_fma_f32 v[126:127], v[58:59], v[120:121], v[126:127] op_sel_hi:[0,1,1]
	v_cndmask_b32_e64 v164, 0, v1, s[10:11]
	v_cndmask_b32_e64 v165, 0, v1, s[14:15]
	v_cndmask_b32_e64 v168, 0, v1, s[20:21]
	v_cndmask_b32_e64 v169, 0, v1, s[22:23]
	v_cndmask_b32_e64 v172, 0, v1, s[30:31]
	v_cndmask_b32_e64 v173, 0, v1, s[38:39]
	v_add_f32_dpp v122, v136, v122 wave_shl:1 row_mask:0xf bank_mask:0xf bound_ctrl:1
	v_add_f32_dpp v123, v137, v123 wave_shl:1 row_mask:0xf bank_mask:0xf bound_ctrl:1
	v_add_f32_dpp v124, v142, v124 wave_shl:1 row_mask:0xf bank_mask:0xf bound_ctrl:1
	v_add_f32_dpp v125, v143, v125 wave_shl:1 row_mask:0xf bank_mask:0xf bound_ctrl:1
	v_add_f32_dpp v126, v146, v126 wave_shl:1 row_mask:0xf bank_mask:0xf bound_ctrl:1
	v_add_f32_dpp v127, v147, v127 wave_shl:1 row_mask:0xf bank_mask:0xf bound_ctrl:1
	s_add_i32 s4, s34, 1
	s_cmpk_lt_i32 s4, 0x201
	s_cselect_b64 s[12:13], s[0:1], 0
	v_add_f32_dpp v122, v150, v122 wave_shr:1 row_mask:0xf bank_mask:0xf bound_ctrl:1
	v_add_f32_dpp v123, v151, v123 wave_shr:1 row_mask:0xf bank_mask:0xf bound_ctrl:1
	v_add_f32_dpp v124, v154, v124 wave_shr:1 row_mask:0xf bank_mask:0xf bound_ctrl:1
	v_add_f32_dpp v125, v155, v125 wave_shr:1 row_mask:0xf bank_mask:0xf bound_ctrl:1
	v_add_f32_dpp v126, v158, v126 wave_shr:1 row_mask:0xf bank_mask:0xf bound_ctrl:1
	v_add_f32_dpp v127, v159, v127 wave_shr:1 row_mask:0xf bank_mask:0xf bound_ctrl:1
	v_pk_fma_f32 v[122:123], v[48:49], v[198:199], v[122:123] op_sel_hi:[1,0,1] neg_lo:[0,0,1] neg_hi:[0,0,1]
	v_pk_fma_f32 v[124:125], v[50:51], v[198:199], v[124:125] op_sel_hi:[1,0,1] neg_lo:[0,0,1] neg_hi:[0,0,1]
	v_pk_fma_f32 v[126:127], v[52:53], v[198:199], v[126:127] op_sel_hi:[1,0,1] neg_lo:[0,0,1] neg_hi:[0,0,1]
	v_pk_add_f32 v[122:123], v[122:123], v[164:165] neg_lo:[0,1] neg_hi:[0,1]
	v_pk_add_f32 v[124:125], v[124:125], v[168:169] neg_lo:[0,1] neg_hi:[0,1]
	v_pk_add_f32 v[126:127], v[126:127], v[172:173] neg_lo:[0,1] neg_hi:[0,1]
	v_pk_mul_f32 v[176:177], v[122:123], v[122:123]
	v_pk_fma_f32 v[176:177], v[124:125], v[124:125], v[176:177]
	v_pk_fma_f32 v[176:177], v[126:127], v[126:127], v[176:177]
	v_add_f32_e32 v176, v176, v177
	v_cndmask_b32_e64 v177, 0, v176, s[12:13]
	v_add_f32_e32 v0, v0, v177
	s_add_i32 s4, s34, 6
	s_min_i32 s4, s4, 0x200
	s_mul_i32 s5, s4, 0x804
	s_add_i32 s5, s5, s35
	s_add_i32 s6, s5, 0x0
	s_add_i32 s7, s5, 0x101004
	s_add_i32 s8, s5, 0x202008
	s_add_i32 s11, s5, 0x30300c
	s_add_i32 s15, s5, 0x404010
	s_add_i32 s31, s5, 0x505014
	s_mul_i32 s9, s4, 0x180c
	s_add_i32 s9, s9, s33
	buffer_load_dword v40, v28, s[16:19], s6 offen nt
	buffer_load_dword v41, v28, s[16:19], s7 offen nt
	buffer_load_dword v42, v28, s[16:19], s8 offen nt
	buffer_load_dword v43, v28, s[16:19], s11 offen nt
	buffer_load_dword v44, v28, s[16:19], s15 offen nt
	buffer_load_dword v45, v28, s[16:19], s31 offen nt
	buffer_load_dwordx3 v[48:50], v27, s[24:27], s9 offen nt
	s_waitcnt vmcnt(14)
	v_mov_b32_dpp v56, v32 wave_shr:1 row_mask:0xf bank_mask:0xf bound_ctrl:1
	v_mov_b32_dpp v57, v33 wave_shr:1 row_mask:0xf bank_mask:0xf bound_ctrl:1
	v_mov_b32_dpp v58, v34 wave_shr:1 row_mask:0xf bank_mask:0xf bound_ctrl:1
	v_mov_b32_dpp v72, v32 wave_shl:1 row_mask:0xf bank_mask:0xf bound_ctrl:1
	v_mov_b32_dpp v73, v33 wave_shl:1 row_mask:0xf bank_mask:0xf bound_ctrl:1
	v_mov_b32_dpp v74, v34 wave_shl:1 row_mask:0xf bank_mask:0xf bound_ctrl:1
	v_mov_b32_dpp v46, v12 wave_shr:1 row_mask:0xf bank_mask:0xf bound_ctrl:1
	v_mov_b32_dpp v47, v13 wave_shr:1 row_mask:0xf bank_mask:0xf bound_ctrl:1
	v_mov_b32_dpp v52, v14 wave_shr:1 row_mask:0xf bank_mask:0xf bound_ctrl:1
	v_mov_b32_dpp v53, v15 wave_shr:1 row_mask:0xf bank_mask:0xf bound_ctrl:1
	v_mov_b32_dpp v76, v16 wave_shr:1 row_mask:0xf bank_mask:0xf bound_ctrl:1
	v_mov_b32_dpp v77, v17 wave_shr:1 row_mask:0xf bank_mask:0xf bound_ctrl:1
	v_mov_b32_dpp v78, v12 wave_shl:1 row_mask:0xf bank_mask:0xf bound_ctrl:1
	v_mov_b32_dpp v79, v13 wave_shl:1 row_mask:0xf bank_mask:0xf bound_ctrl:1
	v_mov_b32_dpp v112, v14 wave_shl:1 row_mask:0xf bank_mask:0xf bound_ctrl:1
	v_mov_b32_dpp v113, v15 wave_shl:1 row_mask:0xf bank_mask:0xf bound_ctrl:1
	v_mov_b32_dpp v114, v16 wave_shl:1 row_mask:0xf bank_mask:0xf bound_ctrl:1
	v_mov_b32_dpp v115, v17 wave_shl:1 row_mask:0xf bank_mask:0xf bound_ctrl:1
	v_pk_mul_f32 v[116:117], v[12:13], v[32:33] op_sel_hi:[1,0]
	v_pk_mul_f32 v[118:119], v[14:15], v[32:33] op_sel_hi:[1,0]
	v_pk_mul_f32 v[120:121], v[16:17], v[32:33] op_sel_hi:[1,0]
	v_pk_mul_f32 v[122:123], v[12:13], v[32:33] op_sel:[0,1]
	v_pk_mul_f32 v[124:125], v[14:15], v[32:33] op_sel:[0,1]
	v_pk_mul_f32 v[126:127], v[16:17], v[32:33] op_sel:[0,1]
	v_pk_mul_f32 v[128:129], v[12:13], v[34:35] op_sel_hi:[1,0]
	v_pk_mul_f32 v[130:131], v[14:15], v[34:35] op_sel_hi:[1,0]
	v_pk_mul_f32 v[132:133], v[16:17], v[34:35] op_sel_hi:[1,0]
	v_pk_add_f32 v[134:135], v[12:13], v[46:47]
	v_pk_add_f32 v[136:137], v[14:15], v[52:53]
	v_pk_add_f32 v[142:143], v[16:17], v[76:77]
	v_pk_fma_f32 v[116:117], v[46:47], v[56:57], v[116:117] op_sel_hi:[1,0,1]
	v_pk_fma_f32 v[118:119], v[52:53], v[56:57], v[118:119] op_sel_hi:[1,0,1]
	v_pk_fma_f32 v[120:121], v[76:77], v[56:57], v[120:121] op_sel_hi:[1,0,1]
	v_pk_fma_f32 v[122:123], v[46:47], v[56:57], v[122:123] op_sel:[0,1,0]
	v_pk_fma_f32 v[124:125], v[52:53], v[56:57], v[124:125] op_sel:[0,1,0]
	v_pk_fma_f32 v[126:127], v[76:77], v[56:57], v[126:127] op_sel:[0,1,0]
	v_pk_fma_f32 v[128:129], v[46:47], v[58:59], v[128:129] op_sel_hi:[1,0,1]
	v_pk_fma_f32 v[130:131], v[52:53], v[58:59], v[130:131] op_sel_hi:[1,0,1]
	v_pk_fma_f32 v[132:133], v[76:77], v[58:59], v[132:133] op_sel_hi:[1,0,1]
	v_pk_add_f32 v[134:135], v[134:135], v[78:79]
	v_pk_add_f32 v[136:137], v[136:137], v[112:113]
	v_pk_add_f32 v[142:143], v[142:143], v[114:115]
	v_pk_fma_f32 v[116:117], v[78:79], v[72:73], v[116:117] op_sel_hi:[1,0,1]
	v_pk_fma_f32 v[118:119], v[112:113], v[72:73], v[118:119] op_sel_hi:[1,0,1]
	v_pk_fma_f32 v[120:121], v[114:115], v[72:73], v[120:121] op_sel_hi:[1,0,1]
	v_pk_fma_f32 v[122:123], v[78:79], v[72:73], v[122:123] op_sel:[0,1,0]
	v_pk_fma_f32 v[124:125], v[112:113], v[72:73], v[124:125] op_sel:[0,1,0]
	v_pk_fma_f32 v[126:127], v[114:115], v[72:73], v[126:127] op_sel:[0,1,0]
	v_pk_fma_f32 v[128:129], v[78:79], v[74:75], v[128:129] op_sel_hi:[1,0,1]
	v_pk_fma_f32 v[130:131], v[112:113], v[74:75], v[130:131] op_sel_hi:[1,0,1]
	v_pk_fma_f32 v[132:133], v[114:115], v[74:75], v[132:133] op_sel_hi:[1,0,1]
	s_barrier
	ds_read_b128 v[76:79], v23 offset:0
	ds_read_b128 v[112:115], v23 offset:1024
	ds_read_b128 v[196:199], v23 offset:2048
	v_pk_add_f32 v[46:47], v[186:187], v[134:135]
	v_pk_add_f32 v[52:53], v[110:111], v[46:47]
	v_pk_add_f32 v[110:111], v[188:189], v[136:137]
	v_pk_add_f32 v[146:147], v[192:193], v[110:111]
	v_pk_add_f32 v[150:151], v[190:191], v[142:143]
	v_pk_add_f32 v[154:155], v[194:195], v[150:151]
	v_pk_add_f32 v[158:159], v[144:145], v[116:117]
	v_pk_add_f32 v[164:165], v[84:85], v[158:159]
	v_pk_add_f32 v[84:85], v[148:149], v[118:119]
	v_pk_add_f32 v[144:145], v[86:87], v[84:85]
	v_pk_add_f32 v[86:87], v[152:153], v[120:121]
	v_pk_add_f32 v[148:149], v[88:89], v[86:87]
	v_pk_add_f32 v[88:89], v[156:157], v[122:123]
	v_pk_add_f32 v[152:153], v[90:91], v[88:89]
	v_pk_add_f32 v[90:91], v[162:163], v[124:125]
	v_pk_add_f32 v[156:157], v[100:101], v[90:91]
	v_pk_add_f32 v[100:101], v[170:171], v[126:127]
	v_pk_add_f32 v[162:163], v[102:103], v[100:101]
	v_pk_add_f32 v[102:103], v[174:175], v[128:129]
	v_pk_add_f32 v[168:169], v[104:105], v[102:103]
	v_pk_add_f32 v[104:105], v[178:179], v[130:131]
	v_pk_add_f32 v[170:171], v[106:107], v[104:105]
	v_pk_add_f32 v[106:107], v[182:183], v[132:133]
	v_pk_add_f32 v[172:173], v[108:109], v[106:107]
	s_waitcnt lgkmcnt(2)
	v_pk_fma_f32 v[164:165], v[76:77], v[52:53], v[164:165] op_sel_hi:[0,1,1] neg_lo:[1,0,0] neg_hi:[1,0,0]
	v_pk_fma_f32 v[144:145], v[76:77], v[146:147], v[144:145] op_sel_hi:[0,1,1] neg_lo:[1,0,0] neg_hi:[1,0,0]
	v_pk_fma_f32 v[148:149], v[76:77], v[154:155], v[148:149] op_sel_hi:[0,1,1] neg_lo:[1,0,0] neg_hi:[1,0,0]
	v_pk_fma_f32 v[152:153], v[76:77], v[52:53], v[152:153] op_sel:[1,0,0] neg_lo:[1,0,0] neg_hi:[1,0,0]
	v_pk_fma_f32 v[156:157], v[76:77], v[146:147], v[156:157] op_sel:[1,0,0] neg_lo:[1,0,0] neg_hi:[1,0,0]
	v_pk_fma_f32 v[162:163], v[76:77], v[154:155], v[162:163] op_sel:[1,0,0] neg_lo:[1,0,0] neg_hi:[1,0,0]
	v_pk_fma_f32 v[168:169], v[78:79], v[52:53], v[168:169] op_sel_hi:[0,1,1] neg_lo:[1,0,0] neg_hi:[1,0,0]
	v_pk_fma_f32 v[170:171], v[78:79], v[146:147], v[170:171] op_sel_hi:[0,1,1] neg_lo:[1,0,0] neg_hi:[1,0,0]
	v_pk_fma_f32 v[172:173], v[78:79], v[154:155], v[172:173] op_sel_hi:[0,1,1] neg_lo:[1,0,0] neg_hi:[1,0,0]
	v_pk_mul_f32 v[108:109], v[78:79], v[164:165] op_sel:[1,0]
	v_pk_mul_f32 v[178:179], v[78:79], v[144:145] op_sel:[1,0]
	v_pk_mul_f32 v[184:185], v[78:79], v[148:149] op_sel:[1,0]
	s_waitcnt lgkmcnt(1)
	v_pk_mul_f32 v[174:175], v[112:113], v[164:165] op_sel_hi:[0,1]
	v_pk_mul_f32 v[180:181], v[112:113], v[144:145] op_sel_hi:[0,1]
	v_pk_mul_f32 v[186:187], v[112:113], v[148:149] op_sel_hi:[0,1]
	v_pk_mul_f32 v[176:177], v[112:113], v[164:165] op_sel:[1,0]
	v_pk_mul_f32 v[182:183], v[112:113], v[144:145] op_sel:[1,0]
	v_pk_mul_f32 v[188:189], v[112:113], v[148:149] op_sel:[1,0]
	v_pk_fma_f32 v[108:109], v[112:113], v[152:153], v[108:109] op_sel_hi:[0,1,1]
	v_pk_fma_f32 v[178:179], v[112:113], v[156:157], v[178:179] op_sel_hi:[0,1,1]
	v_pk_fma_f32 v[184:185], v[112:113], v[162:163], v[184:185] op_sel_hi:[0,1,1]
	v_pk_fma_f32 v[174:175], v[114:115], v[152:153], v[174:175] op_sel_hi:[0,1,1]
	v_pk_fma_f32 v[180:181], v[114:115], v[156:157], v[180:181] op_sel_hi:[0,1,1]
	v_pk_fma_f32 v[186:187], v[114:115], v[162:163], v[186:187] op_sel_hi:[0,1,1]
	v_pk_fma_f32 v[176:177], v[114:115], v[152:153], v[176:177] op_sel:[1,0,0]
	v_pk_fma_f32 v[182:183], v[114:115], v[156:157], v[182:183] op_sel:[1,0,0]
	v_pk_fma_f32 v[188:189], v[114:115], v[162:163], v[188:189] op_sel:[1,0,0]
	v_pk_fma_f32 v[108:109], v[112:113], v[168:169], v[108:109] op_sel:[1,0,0]
	v_pk_fma_f32 v[178:179], v[112:113], v[170:171], v[178:179] op_sel:[1,0,0]
	v_pk_fma_f32 v[184:185], v[112:113], v[172:173], v[184:185] op_sel:[1,0,0]
	v_pk_fma_f32 v[174:175], v[114:115], v[168:169], v[174:175] op_sel:[1,0,0]
	v_pk_fma_f32 v[180:181], v[114:115], v[170:171], v[180:181] op_sel:[1,0,0]
	v_pk_fma_f32 v[186:187], v[114:115], v[172:173], v[186:187] op_sel:[1,0,0]
	s_waitcnt lgkmcnt(0)
	v_pk_fma_f32 v[176:177], v[196:197], v[168:169], v[176:177] op_sel_hi:[0,1,1]
	v_pk_fma_f32 v[182:183], v[196:197], v[170:171], v[182:183] op_sel_hi:[0,1,1]
	v_pk_fma_f32 v[188:189], v[196:197], v[172:173], v[188:189] op_sel_hi:[0,1,1]
	v_pk_mul_f32 v[190:191], v[76:77], v[108:109] op_sel_hi:[0,1]
	v_pk_mul_f32 v[192:193], v[76:77], v[178:179] op_sel_hi:[0,1]
	v_pk_mul_f32 v[194:195], v[76:77], v[184:185] op_sel_hi:[0,1]
	v_pk_fma_f32 v[190:191], v[76:77], v[174:175], v[190:191] op_sel:[1,0,0]
	v_pk_fma_f32 v[192:193], v[76:77], v[180:181], v[192:193] op_sel:[1,0,0]
	v_pk_fma_f32 v[194:195], v[76:77], v[186:187], v[194:195] op_sel:[1,0,0]
	v_pk_fma_f32 v[190:191], v[78:79], v[176:177], v[190:191] op_sel_hi:[0,1,1]
	v_pk_fma_f32 v[192:193], v[78:79], v[182:183], v[192:193] op_sel_hi:[0,1,1]
	v_pk_fma_f32 v[194:195], v[78:79], v[188:189], v[194:195] op_sel_hi:[0,1,1]
	v_pk_fma_f32 v[190:191], v[196:197], v[52:53], v[190:191] op_sel:[1,0,0] neg_lo:[0,0,1] neg_hi:[0,0,1]
	v_pk_fma_f32 v[192:193], v[196:197], v[146:147], v[192:193] op_sel:[1,0,0] neg_lo:[0,0,1] neg_hi:[0,0,1]
	v_pk_fma_f32 v[194:195], v[196:197], v[154:155], v[194:195] op_sel:[1,0,0] neg_lo:[0,0,1] neg_hi:[0,0,1]
	v_cmp_eq_u32_e64 s[10:11], 1, v199
	v_cmp_eq_u32_e64 s[14:15], 2, v199
	v_cmp_eq_u32_e64 s[20:21], 3, v199
	v_cmp_eq_u32_e64 s[22:23], 4, v199
	v_cmp_eq_u32_e64 s[30:31], 5, v199
	v_cmp_eq_u32_e64 s[38:39], 6, v199
	v_pk_add_f32 v[52:53], v[138:139], v[108:109]
	v_pk_add_f32 v[144:145], v[140:141], v[52:53]
	v_pk_add_f32 v[138:139], v[202:203], v[178:179]
	v_pk_add_f32 v[140:141], v[222:223], v[138:139]
	v_pk_add_f32 v[146:147], v[208:209], v[184:185]
	v_pk_add_f32 v[148:149], v[228:229], v[146:147]
	v_pk_add_f32 v[152:153], v[166:167], v[174:175]
	v_pk_add_f32 v[154:155], v[160:161], v[152:153]
	v_pk_add_f32 v[156:157], v[204:205], v[180:181]
	v_pk_add_f32 v[160:161], v[224:225], v[156:157]
	v_pk_add_f32 v[162:163], v[210:211], v[186:187]
	v_pk_add_f32 v[164:165], v[230:231], v[162:163]
	v_pk_add_f32 v[166:167], v[200:201], v[176:177]
	v_pk_add_f32 v[168:169], v[220:221], v[166:167]
	v_pk_add_f32 v[170:171], v[206:207], v[182:183]
	v_pk_add_f32 v[172:173], v[226:227], v[170:171]
	v_pk_add_f32 v[200:201], v[212:213], v[188:189]
	v_pk_add_f32 v[202:203], v[232:233], v[200:201]
	v_pk_add_f32 v[204:205], v[214:215], v[190:191]
	v_pk_add_f32 v[206:207], v[234:235], v[204:205]
	v_pk_add_f32 v[208:209], v[216:217], v[192:193]
	v_pk_add_f32 v[210:211], v[236:237], v[208:209]
	v_pk_add_f32 v[212:213], v[218:219], v[194:195]
	v_pk_add_f32 v[214:215], v[238:239], v[212:213]
	v_pk_fma_f32 v[216:217], v[60:61], v[144:145], v[206:207] op_sel_hi:[0,1,1]
	v_pk_fma_f32 v[218:219], v[60:61], v[140:141], v[210:211] op_sel_hi:[0,1,1]
	v_pk_fma_f32 v[220:221], v[60:61], v[148:149], v[214:215] op_sel_hi:[0,1,1]
	v_pk_fma_f32 v[222:223], v[64:65], v[144:145], v[206:207] op_sel_hi:[0,1,1]
	v_pk_fma_f32 v[224:225], v[64:65], v[140:141], v[210:211] op_sel_hi:[0,1,1]
	v_pk_fma_f32 v[226:227], v[64:65], v[148:149], v[214:215] op_sel_hi:[0,1,1]
	v_pk_fma_f32 v[216:217], v[60:61], v[154:155], v[216:217] op_sel:[1,0,0]
	v_pk_fma_f32 v[218:219], v[60:61], v[160:161], v[218:219] op_sel:[1,0,0]
	v_pk_fma_f32 v[220:221], v[60:61], v[164:165], v[220:221] op_sel:[1,0,0]
	v_pk_fma_f32 v[222:223], v[64:65], v[154:155], v[222:223] op_sel:[1,0,0]
	v_pk_fma_f32 v[224:225], v[64:65], v[160:161], v[224:225] op_sel:[1,0,0]
	v_pk_fma_f32 v[226:227], v[64:65], v[164:165], v[226:227] op_sel:[1,0,0]
	v_pk_fma_f32 v[216:217], v[62:63], v[168:169], v[216:217] op_sel_hi:[0,1,1]
	v_pk_fma_f32 v[218:219], v[62:63], v[172:173], v[218:219] op_sel_hi:[0,1,1]
	v_pk_fma_f32 v[220:221], v[62:63], v[202:203], v[220:221] op_sel_hi:[0,1,1]
	v_pk_fma_f32 v[222:223], v[66:67], v[168:169], v[222:223] op_sel_hi:[0,1,1]
	v_pk_fma_f32 v[224:225], v[66:67], v[172:173], v[224:225] op_sel_hi:[0,1,1]
	v_pk_fma_f32 v[226:227], v[66:67], v[202:203], v[226:227] op_sel_hi:[0,1,1]
	v_pk_fma_f32 v[206:207], v[96:97], v[144:145], v[206:207] op_sel_hi:[0,1,1]
	v_pk_fma_f32 v[210:211], v[96:97], v[140:141], v[210:211] op_sel_hi:[0,1,1]
	v_pk_fma_f32 v[214:215], v[96:97], v[148:149], v[214:215] op_sel_hi:[0,1,1]
	v_pk_fma_f32 v[206:207], v[96:97], v[154:155], v[206:207] op_sel:[1,0,0]
	v_pk_fma_f32 v[210:211], v[96:97], v[160:161], v[210:211] op_sel:[1,0,0]
	v_pk_fma_f32 v[214:215], v[96:97], v[164:165], v[214:215] op_sel:[1,0,0]
	v_pk_fma_f32 v[206:207], v[98:99], v[168:169], v[206:207] op_sel_hi:[0,1,1]
	v_pk_fma_f32 v[210:211], v[98:99], v[172:173], v[210:211] op_sel_hi:[0,1,1]
	v_pk_fma_f32 v[214:215], v[98:99], v[202:203], v[214:215] op_sel_hi:[0,1,1]
	v_cndmask_b32_e64 v228, 0, v1, s[10:11]
	v_cndmask_b32_e64 v229, 0, v1, s[14:15]
	v_cndmask_b32_e64 v230, 0, v1, s[20:21]
	v_cndmask_b32_e64 v231, 0, v1, s[22:23]
	v_cndmask_b32_e64 v232, 0, v1, s[30:31]
	v_cndmask_b32_e64 v233, 0, v1, s[38:39]
	v_add_f32_dpp v206, v216, v206 wave_shl:1 row_mask:0xf bank_mask:0xf bound_ctrl:1
	v_add_f32_dpp v207, v217, v207 wave_shl:1 row_mask:0xf bank_mask:0xf bound_ctrl:1
	v_add_f32_dpp v210, v218, v210 wave_shl:1 row_mask:0xf bank_mask:0xf bound_ctrl:1
	v_add_f32_dpp v211, v219, v211 wave_shl:1 row_mask:0xf bank_mask:0xf bound_ctrl:1
	v_add_f32_dpp v214, v220, v214 wave_shl:1 row_mask:0xf bank_mask:0xf bound_ctrl:1
	v_add_f32_dpp v215, v221, v215 wave_shl:1 row_mask:0xf bank_mask:0xf bound_ctrl:1
	s_add_i32 s4, s34, 2
	s_cmpk_lt_i32 s4, 0x201
	s_cselect_b64 s[12:13], s[0:1], 0
	v_add_f32_dpp v206, v222, v206 wave_shr:1 row_mask:0xf bank_mask:0xf bound_ctrl:1
	v_add_f32_dpp v207, v223, v207 wave_shr:1 row_mask:0xf bank_mask:0xf bound_ctrl:1
	v_add_f32_dpp v210, v224, v210 wave_shr:1 row_mask:0xf bank_mask:0xf bound_ctrl:1
	v_add_f32_dpp v211, v225, v211 wave_shr:1 row_mask:0xf bank_mask:0xf bound_ctrl:1
	v_add_f32_dpp v214, v226, v214 wave_shr:1 row_mask:0xf bank_mask:0xf bound_ctrl:1
	v_add_f32_dpp v215, v227, v215 wave_shr:1 row_mask:0xf bank_mask:0xf bound_ctrl:1
	v_pk_fma_f32 v[206:207], v[54:55], v[198:199], v[206:207] op_sel_hi:[1,0,1] neg_lo:[0,0,1] neg_hi:[0,0,1]
	v_pk_fma_f32 v[210:211], v[92:93], v[198:199], v[210:211] op_sel_hi:[1,0,1] neg_lo:[0,0,1] neg_hi:[0,0,1]
	v_pk_fma_f32 v[214:215], v[94:95], v[198:199], v[214:215] op_sel_hi:[1,0,1] neg_lo:[0,0,1] neg_hi:[0,0,1]
	v_pk_add_f32 v[206:207], v[206:207], v[228:229] neg_lo:[0,1] neg_hi:[0,1]
	v_pk_add_f32 v[210:211], v[210:211], v[230:231] neg_lo:[0,1] neg_hi:[0,1]
	v_pk_add_f32 v[214:215], v[214:215], v[232:233] neg_lo:[0,1] neg_hi:[0,1]
	v_pk_mul_f32 v[234:235], v[206:207], v[206:207]
	v_pk_fma_f32 v[234:235], v[210:211], v[210:211], v[234:235]
	v_pk_fma_f32 v[234:235], v[214:215], v[214:215], v[234:235]
	v_add_f32_e32 v234, v234, v235
	v_cndmask_b32_e64 v235, 0, v234, s[12:13]
	v_add_f32_e32 v0, v0, v235
	s_add_i32 s4, s34, 7
	s_min_i32 s4, s4, 0x200
	s_mul_i32 s5, s4, 0x804
	s_add_i32 s5, s5, s35
	s_add_i32 s6, s5, 0x0
	s_add_i32 s7, s5, 0x101004
	s_add_i32 s8, s5, 0x202008
	s_add_i32 s11, s5, 0x30300c
	s_add_i32 s15, s5, 0x404010
	s_add_i32 s31, s5, 0x505014
	s_mul_i32 s9, s4, 0x180c
	s_add_i32 s9, s9, s33
	buffer_load_dword v54, v28, s[16:19], s6 offen nt
	buffer_load_dword v55, v28, s[16:19], s7 offen nt
	buffer_load_dword v60, v28, s[16:19], s8 offen nt
	buffer_load_dword v61, v28, s[16:19], s11 offen nt
	buffer_load_dword v62, v28, s[16:19], s15 offen nt
	buffer_load_dword v63, v28, s[16:19], s31 offen nt
	buffer_load_dwordx3 v[64:66], v27, s[24:27], s9 offen nt
	s_waitcnt vmcnt(14)
	v_mov_b32_dpp v76, v36 wave_shr:1 row_mask:0xf bank_mask:0xf bound_ctrl:1
	v_mov_b32_dpp v77, v37 wave_shr:1 row_mask:0xf bank_mask:0xf bound_ctrl:1
	v_mov_b32_dpp v78, v38 wave_shr:1 row_mask:0xf bank_mask:0xf bound_ctrl:1
	v_mov_b32_dpp v92, v36 wave_shl:1 row_mask:0xf bank_mask:0xf bound_ctrl:1
	v_mov_b32_dpp v93, v37 wave_shl:1 row_mask:0xf bank_mask:0xf bound_ctrl:1
	v_mov_b32_dpp v94, v38 wave_shl:1 row_mask:0xf bank_mask:0xf bound_ctrl:1
	v_mov_b32_dpp v96, v20 wave_shr:1 row_mask:0xf bank_mask:0xf bound_ctrl:1
	v_mov_b32_dpp v97, v21 wave_shr:1 row_mask:0xf bank_mask:0xf bound_ctrl:1
	v_mov_b32_dpp v98, v24 wave_shr:1 row_mask:0xf bank_mask:0xf bound_ctrl:1
	v_mov_b32_dpp v99, v25 wave_shr:1 row_mask:0xf bank_mask:0xf bound_ctrl:1
	v_mov_b32_dpp v112, v30 wave_shr:1 row_mask:0xf bank_mask:0xf bound_ctrl:1
	v_mov_b32_dpp v113, v31 wave_shr:1 row_mask:0xf bank_mask:0xf bound_ctrl:1
	v_mov_b32_dpp v114, v20 wave_shl:1 row_mask:0xf bank_mask:0xf bound_ctrl:1
	v_mov_b32_dpp v115, v21 wave_shl:1 row_mask:0xf bank_mask:0xf bound_ctrl:1
	v_mov_b32_dpp v140, v24 wave_shl:1 row_mask:0xf bank_mask:0xf bound_ctrl:1
	v_mov_b32_dpp v141, v25 wave_shl:1 row_mask:0xf bank_mask:0xf bound_ctrl:1
	v_mov_b32_dpp v144, v30 wave_shl:1 row_mask:0xf bank_mask:0xf bound_ctrl:1
	v_mov_b32_dpp v145, v31 wave_shl:1 row_mask:0xf bank_mask:0xf bound_ctrl:1
	v_pk_mul_f32 v[148:149], v[20:21], v[36:37] op_sel_hi:[1,0]
	v_pk_mul_f32 v[154:155], v[24:25], v[36:37] op_sel_hi:[1,0]
	v_pk_mul_f32 v[160:161], v[30:31], v[36:37] op_sel_hi:[1,0]
	v_pk_mul_f32 v[164:165], v[20:21], v[36:37] op_sel:[0,1]
	v_pk_mul_f32 v[168:169], v[24:25], v[36:37] op_sel:[0,1]
	v_pk_mul_f32 v[172:173], v[30:31], v[36:37] op_sel:[0,1]
	v_pk_mul_f32 v[196:197], v[20:21], v[38:39] op_sel_hi:[1,0]
	v_pk_mul_f32 v[198:199], v[24:25], v[38:39] op_sel_hi:[1,0]
	v_pk_mul_f32 v[202:203], v[30:31], v[38:39] op_sel_hi:[1,0]
	v_pk_add_f32 v[206:207], v[20:21], v[96:97]
	v_pk_add_f32 v[210:211], v[24:25], v[98:99]
	v_pk_add_f32 v[214:215], v[30:31], v[112:113]
	v_pk_fma_f32 v[148:149], v[96:97], v[76:77], v[148:149] op_sel_hi:[1,0,1]
	v_pk_fma_f32 v[154:155], v[98:99], v[76:77], v[154:155] op_sel_hi:[1,0,1]
	v_pk_fma_f32 v[160:161], v[112:113], v[76:77], v[160:161] op_sel_hi:[1,0,1]
	v_pk_fma_f32 v[164:165], v[96:97], v[76:77], v[164:165] op_sel:[0,1,0]
	v_pk_fma_f32 v[168:169], v[98:99], v[76:77], v[168:169] op_sel:[0,1,0]
	v_pk_fma_f32 v[172:173], v[112:113], v[76:77], v[172:173] op_sel:[0,1,0]
	v_pk_fma_f32 v[196:197], v[96:97], v[78:79], v[196:197] op_sel_hi:[1,0,1]
	v_pk_fma_f32 v[198:199], v[98:99], v[78:79], v[198:199] op_sel_hi:[1,0,1]
	v_pk_fma_f32 v[202:203], v[112:113], v[78:79], v[202:203] op_sel_hi:[1,0,1]
	v_pk_add_f32 v[206:207], v[206:207], v[114:115]
	v_pk_add_f32 v[210:211], v[210:211], v[140:141]
	v_pk_add_f32 v[214:215], v[214:215], v[144:145]
	v_pk_fma_f32 v[148:149], v[114:115], v[92:93], v[148:149] op_sel_hi:[1,0,1]
	v_pk_fma_f32 v[154:155], v[140:141], v[92:93], v[154:155] op_sel_hi:[1,0,1]
	v_pk_fma_f32 v[160:161], v[144:145], v[92:93], v[160:161] op_sel_hi:[1,0,1]
	v_pk_fma_f32 v[164:165], v[114:115], v[92:93], v[164:165] op_sel:[0,1,0]
	v_pk_fma_f32 v[168:169], v[140:141], v[92:93], v[168:169] op_sel:[0,1,0]
	v_pk_fma_f32 v[172:173], v[144:145], v[92:93], v[172:173] op_sel:[0,1,0]
	v_pk_fma_f32 v[196:197], v[114:115], v[94:95], v[196:197] op_sel_hi:[1,0,1]
	v_pk_fma_f32 v[198:199], v[140:141], v[94:95], v[198:199] op_sel_hi:[1,0,1]
	v_pk_fma_f32 v[202:203], v[144:145], v[94:95], v[202:203] op_sel_hi:[1,0,1]
	s_barrier
	ds_read_b128 v[96:99], v23 offset:3072
	ds_read_b128 v[112:115], v23 offset:4096
	ds_read_b128 v[216:219], v23 offset:5120
	v_pk_add_f32 v[140:141], v[46:47], v[206:207]
	v_pk_add_f32 v[46:47], v[110:111], v[210:211]
	v_pk_add_f32 v[110:111], v[150:151], v[214:215]
	v_pk_add_f32 v[144:145], v[158:159], v[148:149]
	v_pk_add_f32 v[150:151], v[84:85], v[154:155]
	v_pk_add_f32 v[84:85], v[86:87], v[160:161]
	v_pk_add_f32 v[86:87], v[88:89], v[164:165]
	v_pk_add_f32 v[88:89], v[90:91], v[168:169]
	v_pk_add_f32 v[90:91], v[100:101], v[172:173]
	v_pk_add_f32 v[100:101], v[102:103], v[196:197]
	v_pk_add_f32 v[102:103], v[104:105], v[198:199]
	v_pk_add_f32 v[104:105], v[106:107], v[202:203]
	s_waitcnt lgkmcnt(2)
	v_pk_fma_f32 v[144:145], v[96:97], v[140:141], v[144:145] op_sel_hi:[0,1,1] neg_lo:[1,0,0] neg_hi:[1,0,0]
	v_pk_fma_f32 v[150:151], v[96:97], v[46:47], v[150:151] op_sel_hi:[0,1,1] neg_lo:[1,0,0] neg_hi:[1,0,0]
	v_pk_fma_f32 v[84:85], v[96:97], v[110:111], v[84:85] op_sel_hi:[0,1,1] neg_lo:[1,0,0] neg_hi:[1,0,0]
	v_pk_fma_f32 v[86:87], v[96:97], v[140:141], v[86:87] op_sel:[1,0,0] neg_lo:[1,0,0] neg_hi:[1,0,0]
	v_pk_fma_f32 v[88:89], v[96:97], v[46:47], v[88:89] op_sel:[1,0,0] neg_lo:[1,0,0] neg_hi:[1,0,0]
	v_pk_fma_f32 v[90:91], v[96:97], v[110:111], v[90:91] op_sel:[1,0,0] neg_lo:[1,0,0] neg_hi:[1,0,0]
	v_pk_fma_f32 v[100:101], v[98:99], v[140:141], v[100:101] op_sel_hi:[0,1,1] neg_lo:[1,0,0] neg_hi:[1,0,0]
	v_pk_fma_f32 v[102:103], v[98:99], v[46:47], v[102:103] op_sel_hi:[0,1,1] neg_lo:[1,0,0] neg_hi:[1,0,0]
	v_pk_fma_f32 v[104:105], v[98:99], v[110:111], v[104:105] op_sel_hi:[0,1,1] neg_lo:[1,0,0] neg_hi:[1,0,0]
	v_pk_mul_f32 v[106:107], v[98:99], v[144:145] op_sel:[1,0]
	v_pk_mul_f32 v[222:223], v[98:99], v[150:151] op_sel:[1,0]
	v_pk_mul_f32 v[228:229], v[98:99], v[84:85] op_sel:[1,0]
	s_waitcnt lgkmcnt(1)
	v_pk_mul_f32 v[158:159], v[112:113], v[144:145] op_sel_hi:[0,1]
	v_pk_mul_f32 v[224:225], v[112:113], v[150:151] op_sel_hi:[0,1]
	v_pk_mul_f32 v[230:231], v[112:113], v[84:85] op_sel_hi:[0,1]
	v_pk_mul_f32 v[220:221], v[112:113], v[144:145] op_sel:[1,0]
	v_pk_mul_f32 v[226:227], v[112:113], v[150:151] op_sel:[1,0]
	v_pk_mul_f32 v[232:233], v[112:113], v[84:85] op_sel:[1,0]
	v_pk_fma_f32 v[106:107], v[112:113], v[86:87], v[106:107] op_sel_hi:[0,1,1]
	v_pk_fma_f32 v[222:223], v[112:113], v[88:89], v[222:223] op_sel_hi:[0,1,1]
	v_pk_fma_f32 v[228:229], v[112:113], v[90:91], v[228:229] op_sel_hi:[0,1,1]
	v_pk_fma_f32 v[158:159], v[114:115], v[86:87], v[158:159] op_sel_hi:[0,1,1]
	v_pk_fma_f32 v[224:225], v[114:115], v[88:89], v[224:225] op_sel_hi:[0,1,1]
	v_pk_fma_f32 v[230:231], v[114:115], v[90:91], v[230:231] op_sel_hi:[0,1,1]
	v_pk_fma_f32 v[220:221], v[114:115], v[86:87], v[220:221] op_sel:[1,0,0]
	v_pk_fma_f32 v[226:227], v[114:115], v[88:89], v[226:227] op_sel:[1,0,0]
	v_pk_fma_f32 v[232:233], v[114:115], v[90:91], v[232:233] op_sel:[1,0,0]
	v_pk_fma_f32 v[106:107], v[112:113], v[100:101], v[106:107] op_sel:[1,0,0]
	v_pk_fma_f32 v[222:223], v[112:113], v[102:103], v[222:223] op_sel:[1,0,0]
	v_pk_fma_f32 v[228:229], v[112:113], v[104:105], v[228:229] op_sel:[1,0,0]
	v_pk_fma_f32 v[158:159], v[114:115], v[100:101], v[158:159] op_sel:[1,0,0]
	v_pk_fma_f32 v[224:225], v[114:115], v[102:103], v[224:225] op_sel:[1,0,0]
	v_pk_fma_f32 v[230:231], v[114:115], v[104:105], v[230:231] op_sel:[1,0,0]
	s_waitcnt lgkmcnt(0)
	v_pk_fma_f32 v[220:221], v[216:217], v[100:101], v[220:221] op_sel_hi:[0,1,1]
	v_pk_fma_f32 v[226:227], v[216:217], v[102:103], v[226:227] op_sel_hi:[0,1,1]
	v_pk_fma_f32 v[232:233], v[216:217], v[104:105], v[232:233] op_sel_hi:[0,1,1]
	v_pk_mul_f32 v[234:235], v[96:97], v[106:107] op_sel_hi:[0,1]
	v_pk_mul_f32 v[236:237], v[96:97], v[222:223] op_sel_hi:[0,1]
	v_pk_mul_f32 v[238:239], v[96:97], v[228:229] op_sel_hi:[0,1]
	v_pk_fma_f32 v[234:235], v[96:97], v[158:159], v[234:235] op_sel:[1,0,0]
	v_pk_fma_f32 v[236:237], v[96:97], v[224:225], v[236:237] op_sel:[1,0,0]
	v_pk_fma_f32 v[238:239], v[96:97], v[230:231], v[238:239] op_sel:[1,0,0]
	v_pk_fma_f32 v[234:235], v[98:99], v[220:221], v[234:235] op_sel_hi:[0,1,1]
	v_pk_fma_f32 v[236:237], v[98:99], v[226:227], v[236:237] op_sel_hi:[0,1,1]
	v_pk_fma_f32 v[238:239], v[98:99], v[232:233], v[238:239] op_sel_hi:[0,1,1]
	v_pk_fma_f32 v[234:235], v[216:217], v[140:141], v[234:235] op_sel:[1,0,0] neg_lo:[0,0,1] neg_hi:[0,0,1]
	v_pk_fma_f32 v[236:237], v[216:217], v[46:47], v[236:237] op_sel:[1,0,0] neg_lo:[0,0,1] neg_hi:[0,0,1]
	v_pk_fma_f32 v[238:239], v[216:217], v[110:111], v[238:239] op_sel:[1,0,0] neg_lo:[0,0,1] neg_hi:[0,0,1]
	v_cmp_eq_u32_e64 s[10:11], 1, v219
	v_cmp_eq_u32_e64 s[14:15], 2, v219
	v_cmp_eq_u32_e64 s[20:21], 3, v219
	v_cmp_eq_u32_e64 s[22:23], 4, v219
	v_cmp_eq_u32_e64 s[30:31], 5, v219
	v_cmp_eq_u32_e64 s[38:39], 6, v219
	v_pk_add_f32 v[46:47], v[52:53], v[106:107]
	v_pk_add_f32 v[52:53], v[138:139], v[222:223]
	v_pk_add_f32 v[84:85], v[146:147], v[228:229]
	v_pk_add_f32 v[86:87], v[152:153], v[158:159]
	v_pk_add_f32 v[88:89], v[156:157], v[224:225]
	v_pk_add_f32 v[90:91], v[162:163], v[230:231]
	v_pk_add_f32 v[100:101], v[166:167], v[220:221]
	v_pk_add_f32 v[102:103], v[170:171], v[226:227]
	v_pk_add_f32 v[104:105], v[200:201], v[232:233]
	v_pk_add_f32 v[110:111], v[204:205], v[234:235]
	v_pk_add_f32 v[138:139], v[208:209], v[236:237]
	v_pk_add_f32 v[140:141], v[212:213], v[238:239]
	v_pk_fma_f32 v[144:145], v[68:69], v[46:47], v[110:111] op_sel_hi:[0,1,1]
	v_pk_fma_f32 v[146:147], v[68:69], v[52:53], v[138:139] op_sel_hi:[0,1,1]
	v_pk_fma_f32 v[150:151], v[68:69], v[84:85], v[140:141] op_sel_hi:[0,1,1]
	v_pk_fma_f32 v[152:153], v[80:81], v[46:47], v[110:111] op_sel_hi:[0,1,1]
	v_pk_fma_f32 v[156:157], v[80:81], v[52:53], v[138:139] op_sel_hi:[0,1,1]
	v_pk_fma_f32 v[162:163], v[80:81], v[84:85], v[140:141] op_sel_hi:[0,1,1]
	v_pk_fma_f32 v[144:145], v[68:69], v[86:87], v[144:145] op_sel:[1,0,0]
	v_pk_fma_f32 v[146:147], v[68:69], v[88:89], v[146:147] op_sel:[1,0,0]
	v_pk_fma_f32 v[150:151], v[68:69], v[90:91], v[150:151] op_sel:[1,0,0]
	v_pk_fma_f32 v[152:153], v[80:81], v[86:87], v[152:153] op_sel:[1,0,0]
	v_pk_fma_f32 v[156:157], v[80:81], v[88:89], v[156:157] op_sel:[1,0,0]
	v_pk_fma_f32 v[162:163], v[80:81], v[90:91], v[162:163] op_sel:[1,0,0]
	v_pk_fma_f32 v[144:145], v[70:71], v[100:101], v[144:145] op_sel_hi:[0,1,1]
	v_pk_fma_f32 v[146:147], v[70:71], v[102:103], v[146:147] op_sel_hi:[0,1,1]
	v_pk_fma_f32 v[150:151], v[70:71], v[104:105], v[150:151] op_sel_hi:[0,1,1]
	v_pk_fma_f32 v[152:153], v[82:83], v[100:101], v[152:153] op_sel_hi:[0,1,1]
	v_pk_fma_f32 v[156:157], v[82:83], v[102:103], v[156:157] op_sel_hi:[0,1,1]
	v_pk_fma_f32 v[162:163], v[82:83], v[104:105], v[162:163] op_sel_hi:[0,1,1]
	v_pk_fma_f32 v[110:111], v[8:9], v[46:47], v[110:111] op_sel_hi:[0,1,1]
	v_pk_fma_f32 v[138:139], v[8:9], v[52:53], v[138:139] op_sel_hi:[0,1,1]
	v_pk_fma_f32 v[140:141], v[8:9], v[84:85], v[140:141] op_sel_hi:[0,1,1]
	v_pk_fma_f32 v[110:111], v[8:9], v[86:87], v[110:111] op_sel:[1,0,0]
	v_pk_fma_f32 v[138:139], v[8:9], v[88:89], v[138:139] op_sel:[1,0,0]
	v_pk_fma_f32 v[140:141], v[8:9], v[90:91], v[140:141] op_sel:[1,0,0]
	v_pk_fma_f32 v[110:111], v[10:11], v[100:101], v[110:111] op_sel_hi:[0,1,1]
	v_pk_fma_f32 v[138:139], v[10:11], v[102:103], v[138:139] op_sel_hi:[0,1,1]
	v_pk_fma_f32 v[140:141], v[10:11], v[104:105], v[140:141] op_sel_hi:[0,1,1]
	v_cndmask_b32_e64 v166, 0, v1, s[10:11]
	v_cndmask_b32_e64 v167, 0, v1, s[14:15]
	v_cndmask_b32_e64 v170, 0, v1, s[20:21]
	v_cndmask_b32_e64 v171, 0, v1, s[22:23]
	v_cndmask_b32_e64 v200, 0, v1, s[30:31]
	v_cndmask_b32_e64 v201, 0, v1, s[38:39]
	v_add_f32_dpp v110, v144, v110 wave_shl:1 row_mask:0xf bank_mask:0xf bound_ctrl:1
	v_add_f32_dpp v111, v145, v111 wave_shl:1 row_mask:0xf bank_mask:0xf bound_ctrl:1
	v_add_f32_dpp v138, v146, v138 wave_shl:1 row_mask:0xf bank_mask:0xf bound_ctrl:1
	v_add_f32_dpp v139, v147, v139 wave_shl:1 row_mask:0xf bank_mask:0xf bound_ctrl:1
	v_add_f32_dpp v140, v150, v140 wave_shl:1 row_mask:0xf bank_mask:0xf bound_ctrl:1
	v_add_f32_dpp v141, v151, v141 wave_shl:1 row_mask:0xf bank_mask:0xf bound_ctrl:1
	s_add_i32 s4, s34, 3
	s_cmpk_lt_i32 s4, 0x201
	s_cselect_b64 s[12:13], s[0:1], 0
	v_add_f32_dpp v110, v152, v110 wave_shr:1 row_mask:0xf bank_mask:0xf bound_ctrl:1
	v_add_f32_dpp v111, v153, v111 wave_shr:1 row_mask:0xf bank_mask:0xf bound_ctrl:1
	v_add_f32_dpp v138, v156, v138 wave_shr:1 row_mask:0xf bank_mask:0xf bound_ctrl:1
	v_add_f32_dpp v139, v157, v139 wave_shr:1 row_mask:0xf bank_mask:0xf bound_ctrl:1
	v_add_f32_dpp v140, v162, v140 wave_shr:1 row_mask:0xf bank_mask:0xf bound_ctrl:1
	v_add_f32_dpp v141, v163, v141 wave_shr:1 row_mask:0xf bank_mask:0xf bound_ctrl:1
	v_pk_fma_f32 v[110:111], v[2:3], v[218:219], v[110:111] op_sel_hi:[1,0,1] neg_lo:[0,0,1] neg_hi:[0,0,1]
	v_pk_fma_f32 v[138:139], v[4:5], v[218:219], v[138:139] op_sel_hi:[1,0,1] neg_lo:[0,0,1] neg_hi:[0,0,1]
	v_pk_fma_f32 v[140:141], v[6:7], v[218:219], v[140:141] op_sel_hi:[1,0,1] neg_lo:[0,0,1] neg_hi:[0,0,1]
	v_pk_add_f32 v[110:111], v[110:111], v[166:167] neg_lo:[0,1] neg_hi:[0,1]
	v_pk_add_f32 v[138:139], v[138:139], v[170:171] neg_lo:[0,1] neg_hi:[0,1]
	v_pk_add_f32 v[140:141], v[140:141], v[200:201] neg_lo:[0,1] neg_hi:[0,1]
	v_pk_mul_f32 v[204:205], v[110:111], v[110:111]
	v_pk_fma_f32 v[204:205], v[138:139], v[138:139], v[204:205]
	v_pk_fma_f32 v[204:205], v[140:141], v[140:141], v[204:205]
	v_add_f32_e32 v204, v204, v205
	v_cndmask_b32_e64 v205, 0, v204, s[12:13]
	v_add_f32_e32 v0, v0, v205
	s_add_i32 s4, s34, 8
	s_min_i32 s4, s4, 0x200
	s_mul_i32 s5, s4, 0x804
	s_add_i32 s5, s5, s35
	s_add_i32 s6, s5, 0x0
	s_add_i32 s7, s5, 0x101004
	s_add_i32 s8, s5, 0x202008
	s_add_i32 s11, s5, 0x30300c
	s_add_i32 s15, s5, 0x404010
	s_add_i32 s31, s5, 0x505014
	s_mul_i32 s9, s4, 0x180c
	s_add_i32 s9, s9, s33
	buffer_load_dword v2, v28, s[16:19], s6 offen nt
	buffer_load_dword v3, v28, s[16:19], s7 offen nt
	buffer_load_dword v4, v28, s[16:19], s8 offen nt
	buffer_load_dword v5, v28, s[16:19], s11 offen nt
	buffer_load_dword v6, v28, s[16:19], s15 offen nt
	buffer_load_dword v7, v28, s[16:19], s31 offen nt
	buffer_load_dwordx3 v[8:10], v27, s[24:27], s9 offen nt
	s_waitcnt vmcnt(14)
	v_mov_b32_dpp v68, v48 wave_shr:1 row_mask:0xf bank_mask:0xf bound_ctrl:1
	v_mov_b32_dpp v69, v49 wave_shr:1 row_mask:0xf bank_mask:0xf bound_ctrl:1
	v_mov_b32_dpp v70, v50 wave_shr:1 row_mask:0xf bank_mask:0xf bound_ctrl:1
	v_mov_b32_dpp v80, v48 wave_shl:1 row_mask:0xf bank_mask:0xf bound_ctrl:1
	v_mov_b32_dpp v81, v49 wave_shl:1 row_mask:0xf bank_mask:0xf bound_ctrl:1
	v_mov_b32_dpp v82, v50 wave_shl:1 row_mask:0xf bank_mask:0xf bound_ctrl:1
	v_mov_b32_dpp v46, v40 wave_shr:1 row_mask:0xf bank_mask:0xf bound_ctrl:1
	v_mov_b32_dpp v47, v41 wave_shr:1 row_mask:0xf bank_mask:0xf bound_ctrl:1
	v_mov_b32_dpp v52, v42 wave_shr:1 row_mask:0xf bank_mask:0xf bound_ctrl:1
	v_mov_b32_dpp v53, v43 wave_shr:1 row_mask:0xf bank_mask:0xf bound_ctrl:1
	v_mov_b32_dpp v84, v44 wave_shr:1 row_mask:0xf bank_mask:0xf bound_ctrl:1
	v_mov_b32_dpp v85, v45 wave_shr:1 row_mask:0xf bank_mask:0xf bound_ctrl:1
	v_mov_b32_dpp v86, v40 wave_shl:1 row_mask:0xf bank_mask:0xf bound_ctrl:1
	v_mov_b32_dpp v87, v41 wave_shl:1 row_mask:0xf bank_mask:0xf bound_ctrl:1
	v_mov_b32_dpp v88, v42 wave_shl:1 row_mask:0xf bank_mask:0xf bound_ctrl:1
	v_mov_b32_dpp v89, v43 wave_shl:1 row_mask:0xf bank_mask:0xf bound_ctrl:1
	v_mov_b32_dpp v90, v44 wave_shl:1 row_mask:0xf bank_mask:0xf bound_ctrl:1
	v_mov_b32_dpp v91, v45 wave_shl:1 row_mask:0xf bank_mask:0xf bound_ctrl:1
	v_pk_mul_f32 v[96:97], v[40:41], v[48:49] op_sel_hi:[1,0]
	v_pk_mul_f32 v[98:99], v[42:43], v[48:49] op_sel_hi:[1,0]
	v_pk_mul_f32 v[100:101], v[44:45], v[48:49] op_sel_hi:[1,0]
	v_pk_mul_f32 v[102:103], v[40:41], v[48:49] op_sel:[0,1]
	v_pk_mul_f32 v[104:105], v[42:43], v[48:49] op_sel:[0,1]
	v_pk_mul_f32 v[110:111], v[44:45], v[48:49] op_sel:[0,1]
	v_pk_mul_f32 v[112:113], v[40:41], v[50:51] op_sel_hi:[1,0]
	v_pk_mul_f32 v[114:115], v[42:43], v[50:51] op_sel_hi:[1,0]
	v_pk_mul_f32 v[138:139], v[44:45], v[50:51] op_sel_hi:[1,0]
	v_pk_add_f32 v[140:141], v[40:41], v[46:47]
	v_pk_add_f32 v[144:145], v[42:43], v[52:53]
	v_pk_add_f32 v[146:147], v[44:45], v[84:85]
	v_pk_fma_f32 v[96:97], v[46:47], v[68:69], v[96:97] op_sel_hi:[1,0,1]
	v_pk_fma_f32 v[98:99], v[52:53], v[68:69], v[98:99] op_sel_hi:[1,0,1]
	v_pk_fma_f32 v[100:101], v[84:85], v[68:69], v[100:101] op_sel_hi:[1,0,1]
	v_pk_fma_f32 v[102:103], v[46:47], v[68:69], v[102:103] op_sel:[0,1,0]
	v_pk_fma_f32 v[104:105], v[52:53], v[68:69], v[104:105] op_sel:[0,1,0]
	v_pk_fma_f32 v[110:111], v[84:85], v[68:69], v[110:111] op_sel:[0,1,0]
	v_pk_fma_f32 v[112:113], v[46:47], v[70:71], v[112:113] op_sel_hi:[1,0,1]
	v_pk_fma_f32 v[114:115], v[52:53], v[70:71], v[114:115] op_sel_hi:[1,0,1]
	v_pk_fma_f32 v[138:139], v[84:85], v[70:71], v[138:139] op_sel_hi:[1,0,1]
	v_pk_add_f32 v[140:141], v[140:141], v[86:87]
	v_pk_add_f32 v[144:145], v[144:145], v[88:89]
	v_pk_add_f32 v[146:147], v[146:147], v[90:91]
	v_pk_fma_f32 v[96:97], v[86:87], v[80:81], v[96:97] op_sel_hi:[1,0,1]
	v_pk_fma_f32 v[98:99], v[88:89], v[80:81], v[98:99] op_sel_hi:[1,0,1]
	v_pk_fma_f32 v[100:101], v[90:91], v[80:81], v[100:101] op_sel_hi:[1,0,1]
	v_pk_fma_f32 v[102:103], v[86:87], v[80:81], v[102:103] op_sel:[0,1,0]
	v_pk_fma_f32 v[104:105], v[88:89], v[80:81], v[104:105] op_sel:[0,1,0]
	v_pk_fma_f32 v[110:111], v[90:91], v[80:81], v[110:111] op_sel:[0,1,0]
	v_pk_fma_f32 v[112:113], v[86:87], v[82:83], v[112:113] op_sel_hi:[1,0,1]
	v_pk_fma_f32 v[114:115], v[88:89], v[82:83], v[114:115] op_sel_hi:[1,0,1]
	v_pk_fma_f32 v[138:139], v[90:91], v[82:83], v[138:139] op_sel_hi:[1,0,1]
	s_barrier
	ds_read_b128 v[84:87], v23 offset:0
	ds_read_b128 v[88:91], v23 offset:1024
	ds_read_b128 v[216:219], v23 offset:2048
	v_pk_add_f32 v[46:47], v[206:207], v[140:141]
	v_pk_add_f32 v[52:53], v[134:135], v[46:47]
	v_pk_add_f32 v[134:135], v[210:211], v[144:145]
	v_pk_add_f32 v[150:151], v[136:137], v[134:135]
	v_pk_add_f32 v[136:137], v[214:215], v[146:147]
	v_pk_add_f32 v[152:153], v[142:143], v[136:137]
	v_pk_add_f32 v[142:143], v[148:149], v[96:97]
	v_pk_add_f32 v[156:157], v[116:117], v[142:143]
	v_pk_add_f32 v[116:117], v[154:155], v[98:99]
	v_pk_add_f32 v[148:149], v[118:119], v[116:117]
	v_pk_add_f32 v[118:119], v[160:161], v[100:101]
	v_pk_add_f32 v[154:155], v[120:121], v[118:119]
	v_pk_add_f32 v[120:121], v[164:165], v[102:103]
	v_pk_add_f32 v[160:161], v[122:123], v[120:121]
	v_pk_add_f32 v[122:123], v[168:169], v[104:105]
	v_pk_add_f32 v[162:163], v[124:125], v[122:123]
	v_pk_add_f32 v[124:125], v[172:173], v[110:111]
	v_pk_add_f32 v[164:165], v[126:127], v[124:125]
	v_pk_add_f32 v[126:127], v[196:197], v[112:113]
	v_pk_add_f32 v[166:167], v[128:129], v[126:127]
	v_pk_add_f32 v[128:129], v[198:199], v[114:115]
	v_pk_add_f32 v[168:169], v[130:131], v[128:129]
	v_pk_add_f32 v[130:131], v[202:203], v[138:139]
	v_pk_add_f32 v[170:171], v[132:133], v[130:131]
	s_waitcnt lgkmcnt(2)
	v_pk_fma_f32 v[156:157], v[84:85], v[52:53], v[156:157] op_sel_hi:[0,1,1] neg_lo:[1,0,0] neg_hi:[1,0,0]
	v_pk_fma_f32 v[148:149], v[84:85], v[150:151], v[148:149] op_sel_hi:[0,1,1] neg_lo:[1,0,0] neg_hi:[1,0,0]
	v_pk_fma_f32 v[154:155], v[84:85], v[152:153], v[154:155] op_sel_hi:[0,1,1] neg_lo:[1,0,0] neg_hi:[1,0,0]
	v_pk_fma_f32 v[160:161], v[84:85], v[52:53], v[160:161] op_sel:[1,0,0] neg_lo:[1,0,0] neg_hi:[1,0,0]
	v_pk_fma_f32 v[162:163], v[84:85], v[150:151], v[162:163] op_sel:[1,0,0] neg_lo:[1,0,0] neg_hi:[1,0,0]
	v_pk_fma_f32 v[164:165], v[84:85], v[152:153], v[164:165] op_sel:[1,0,0] neg_lo:[1,0,0] neg_hi:[1,0,0]
	v_pk_fma_f32 v[166:167], v[86:87], v[52:53], v[166:167] op_sel_hi:[0,1,1] neg_lo:[1,0,0] neg_hi:[1,0,0]
	v_pk_fma_f32 v[168:169], v[86:87], v[150:151], v[168:169] op_sel_hi:[0,1,1] neg_lo:[1,0,0] neg_hi:[1,0,0]
	v_pk_fma_f32 v[170:171], v[86:87], v[152:153], v[170:171] op_sel_hi:[0,1,1] neg_lo:[1,0,0] neg_hi:[1,0,0]
	v_pk_mul_f32 v[132:133], v[86:87], v[156:157] op_sel:[1,0]
	v_pk_mul_f32 v[198:199], v[86:87], v[148:149] op_sel:[1,0]
	v_pk_mul_f32 v[204:205], v[86:87], v[154:155] op_sel:[1,0]
	s_waitcnt lgkmcnt(1)
	v_pk_mul_f32 v[172:173], v[88:89], v[156:157] op_sel_hi:[0,1]
	v_pk_mul_f32 v[200:201], v[88:89], v[148:149] op_sel_hi:[0,1]
	v_pk_mul_f32 v[206:207], v[88:89], v[154:155] op_sel_hi:[0,1]
	v_pk_mul_f32 v[196:197], v[88:89], v[156:157] op_sel:[1,0]
	v_pk_mul_f32 v[202:203], v[88:89], v[148:149] op_sel:[1,0]
	v_pk_mul_f32 v[208:209], v[88:89], v[154:155] op_sel:[1,0]
	v_pk_fma_f32 v[132:133], v[88:89], v[160:161], v[132:133] op_sel_hi:[0,1,1]
	v_pk_fma_f32 v[198:199], v[88:89], v[162:163], v[198:199] op_sel_hi:[0,1,1]
	v_pk_fma_f32 v[204:205], v[88:89], v[164:165], v[204:205] op_sel_hi:[0,1,1]
	v_pk_fma_f32 v[172:173], v[90:91], v[160:161], v[172:173] op_sel_hi:[0,1,1]
	v_pk_fma_f32 v[200:201], v[90:91], v[162:163], v[200:201] op_sel_hi:[0,1,1]
	v_pk_fma_f32 v[206:207], v[90:91], v[164:165], v[206:207] op_sel_hi:[0,1,1]
	v_pk_fma_f32 v[196:197], v[90:91], v[160:161], v[196:197] op_sel:[1,0,0]
	v_pk_fma_f32 v[202:203], v[90:91], v[162:163], v[202:203] op_sel:[1,0,0]
	v_pk_fma_f32 v[208:209], v[90:91], v[164:165], v[208:209] op_sel:[1,0,0]
	v_pk_fma_f32 v[132:133], v[88:89], v[166:167], v[132:133] op_sel:[1,0,0]
	v_pk_fma_f32 v[198:199], v[88:89], v[168:169], v[198:199] op_sel:[1,0,0]
	v_pk_fma_f32 v[204:205], v[88:89], v[170:171], v[204:205] op_sel:[1,0,0]
	v_pk_fma_f32 v[172:173], v[90:91], v[166:167], v[172:173] op_sel:[1,0,0]
	v_pk_fma_f32 v[200:201], v[90:91], v[168:169], v[200:201] op_sel:[1,0,0]
	v_pk_fma_f32 v[206:207], v[90:91], v[170:171], v[206:207] op_sel:[1,0,0]
	s_waitcnt lgkmcnt(0)
	v_pk_fma_f32 v[196:197], v[216:217], v[166:167], v[196:197] op_sel_hi:[0,1,1]
	v_pk_fma_f32 v[202:203], v[216:217], v[168:169], v[202:203] op_sel_hi:[0,1,1]
	v_pk_fma_f32 v[208:209], v[216:217], v[170:171], v[208:209] op_sel_hi:[0,1,1]
	v_pk_mul_f32 v[210:211], v[84:85], v[132:133] op_sel_hi:[0,1]
	v_pk_mul_f32 v[212:213], v[84:85], v[198:199] op_sel_hi:[0,1]
	v_pk_mul_f32 v[214:215], v[84:85], v[204:205] op_sel_hi:[0,1]
	v_pk_fma_f32 v[210:211], v[84:85], v[172:173], v[210:211] op_sel:[1,0,0]
	v_pk_fma_f32 v[212:213], v[84:85], v[200:201], v[212:213] op_sel:[1,0,0]
	v_pk_fma_f32 v[214:215], v[84:85], v[206:207], v[214:215] op_sel:[1,0,0]
	v_pk_fma_f32 v[210:211], v[86:87], v[196:197], v[210:211] op_sel_hi:[0,1,1]
	v_pk_fma_f32 v[212:213], v[86:87], v[202:203], v[212:213] op_sel_hi:[0,1,1]
	v_pk_fma_f32 v[214:215], v[86:87], v[208:209], v[214:215] op_sel_hi:[0,1,1]
	v_pk_fma_f32 v[210:211], v[216:217], v[52:53], v[210:211] op_sel:[1,0,0] neg_lo:[0,0,1] neg_hi:[0,0,1]
	v_pk_fma_f32 v[212:213], v[216:217], v[150:151], v[212:213] op_sel:[1,0,0] neg_lo:[0,0,1] neg_hi:[0,0,1]
	v_pk_fma_f32 v[214:215], v[216:217], v[152:153], v[214:215] op_sel:[1,0,0] neg_lo:[0,0,1] neg_hi:[0,0,1]
	v_cmp_eq_u32_e64 s[10:11], 1, v219
	v_cmp_eq_u32_e64 s[14:15], 2, v219
	v_cmp_eq_u32_e64 s[20:21], 3, v219
	v_cmp_eq_u32_e64 s[22:23], 4, v219
	v_cmp_eq_u32_e64 s[30:31], 5, v219
	v_cmp_eq_u32_e64 s[38:39], 6, v219
	v_pk_add_f32 v[52:53], v[106:107], v[132:133]
	v_pk_add_f32 v[148:149], v[108:109], v[52:53]
	v_pk_add_f32 v[106:107], v[222:223], v[198:199]
	v_pk_add_f32 v[108:109], v[178:179], v[106:107]
	v_pk_add_f32 v[150:151], v[228:229], v[204:205]
	v_pk_add_f32 v[152:153], v[184:185], v[150:151]
	v_pk_add_f32 v[154:155], v[158:159], v[172:173]
	v_pk_add_f32 v[156:157], v[174:175], v[154:155]
	v_pk_add_f32 v[158:159], v[224:225], v[200:201]
	v_pk_add_f32 v[160:161], v[180:181], v[158:159]
	v_pk_add_f32 v[162:163], v[230:231], v[206:207]
	v_pk_add_f32 v[164:165], v[186:187], v[162:163]
	v_pk_add_f32 v[166:167], v[220:221], v[196:197]
	v_pk_add_f32 v[168:169], v[176:177], v[166:167]
	v_pk_add_f32 v[170:171], v[226:227], v[202:203]
	v_pk_add_f32 v[174:175], v[182:183], v[170:171]
	v_pk_add_f32 v[176:177], v[232:233], v[208:209]
	v_pk_add_f32 v[178:179], v[188:189], v[176:177]
	v_pk_add_f32 v[180:181], v[234:235], v[210:211]
	v_pk_add_f32 v[182:183], v[190:191], v[180:181]
	v_pk_add_f32 v[184:185], v[236:237], v[212:213]
	v_pk_add_f32 v[186:187], v[192:193], v[184:185]
	v_pk_add_f32 v[188:189], v[238:239], v[214:215]
	v_pk_add_f32 v[190:191], v[194:195], v[188:189]
	v_pk_fma_f32 v[192:193], v[56:57], v[148:149], v[182:183] op_sel_hi:[0,1,1]
	v_pk_fma_f32 v[194:195], v[56:57], v[108:109], v[186:187] op_sel_hi:[0,1,1]
	v_pk_fma_f32 v[220:221], v[56:57], v[152:153], v[190:191] op_sel_hi:[0,1,1]
	v_pk_fma_f32 v[222:223], v[72:73], v[148:149], v[182:183] op_sel_hi:[0,1,1]
	v_pk_fma_f32 v[224:225], v[72:73], v[108:109], v[186:187] op_sel_hi:[0,1,1]
	v_pk_fma_f32 v[226:227], v[72:73], v[152:153], v[190:191] op_sel_hi:[0,1,1]
	v_pk_fma_f32 v[192:193], v[56:57], v[156:157], v[192:193] op_sel:[1,0,0]
	v_pk_fma_f32 v[194:195], v[56:57], v[160:161], v[194:195] op_sel:[1,0,0]
	v_pk_fma_f32 v[220:221], v[56:57], v[164:165], v[220:221] op_sel:[1,0,0]
	v_pk_fma_f32 v[222:223], v[72:73], v[156:157], v[222:223] op_sel:[1,0,0]
	v_pk_fma_f32 v[224:225], v[72:73], v[160:161], v[224:225] op_sel:[1,0,0]
	v_pk_fma_f32 v[226:227], v[72:73], v[164:165], v[226:227] op_sel:[1,0,0]
	v_pk_fma_f32 v[192:193], v[58:59], v[168:169], v[192:193] op_sel_hi:[0,1,1]
	v_pk_fma_f32 v[194:195], v[58:59], v[174:175], v[194:195] op_sel_hi:[0,1,1]
	v_pk_fma_f32 v[220:221], v[58:59], v[178:179], v[220:221] op_sel_hi:[0,1,1]
	v_pk_fma_f32 v[222:223], v[74:75], v[168:169], v[222:223] op_sel_hi:[0,1,1]
	v_pk_fma_f32 v[224:225], v[74:75], v[174:175], v[224:225] op_sel_hi:[0,1,1]
	v_pk_fma_f32 v[226:227], v[74:75], v[178:179], v[226:227] op_sel_hi:[0,1,1]
	v_pk_fma_f32 v[182:183], v[32:33], v[148:149], v[182:183] op_sel_hi:[0,1,1]
	v_pk_fma_f32 v[186:187], v[32:33], v[108:109], v[186:187] op_sel_hi:[0,1,1]
	v_pk_fma_f32 v[190:191], v[32:33], v[152:153], v[190:191] op_sel_hi:[0,1,1]
	v_pk_fma_f32 v[182:183], v[32:33], v[156:157], v[182:183] op_sel:[1,0,0]
	v_pk_fma_f32 v[186:187], v[32:33], v[160:161], v[186:187] op_sel:[1,0,0]
	v_pk_fma_f32 v[190:191], v[32:33], v[164:165], v[190:191] op_sel:[1,0,0]
	v_pk_fma_f32 v[182:183], v[34:35], v[168:169], v[182:183] op_sel_hi:[0,1,1]
	v_pk_fma_f32 v[186:187], v[34:35], v[174:175], v[186:187] op_sel_hi:[0,1,1]
	v_pk_fma_f32 v[190:191], v[34:35], v[178:179], v[190:191] op_sel_hi:[0,1,1]
	v_cndmask_b32_e64 v228, 0, v1, s[10:11]
	v_cndmask_b32_e64 v229, 0, v1, s[14:15]
	v_cndmask_b32_e64 v230, 0, v1, s[20:21]
	v_cndmask_b32_e64 v231, 0, v1, s[22:23]
	v_cndmask_b32_e64 v232, 0, v1, s[30:31]
	v_cndmask_b32_e64 v233, 0, v1, s[38:39]
	v_add_f32_dpp v182, v192, v182 wave_shl:1 row_mask:0xf bank_mask:0xf bound_ctrl:1
	v_add_f32_dpp v183, v193, v183 wave_shl:1 row_mask:0xf bank_mask:0xf bound_ctrl:1
	v_add_f32_dpp v186, v194, v186 wave_shl:1 row_mask:0xf bank_mask:0xf bound_ctrl:1
	v_add_f32_dpp v187, v195, v187 wave_shl:1 row_mask:0xf bank_mask:0xf bound_ctrl:1
	v_add_f32_dpp v190, v220, v190 wave_shl:1 row_mask:0xf bank_mask:0xf bound_ctrl:1
	v_add_f32_dpp v191, v221, v191 wave_shl:1 row_mask:0xf bank_mask:0xf bound_ctrl:1
	s_add_i32 s4, s34, 4
	s_cmpk_lt_i32 s4, 0x201
	s_cselect_b64 s[12:13], s[0:1], 0
	v_add_f32_dpp v182, v222, v182 wave_shr:1 row_mask:0xf bank_mask:0xf bound_ctrl:1
	v_add_f32_dpp v183, v223, v183 wave_shr:1 row_mask:0xf bank_mask:0xf bound_ctrl:1
	v_add_f32_dpp v186, v224, v186 wave_shr:1 row_mask:0xf bank_mask:0xf bound_ctrl:1
	v_add_f32_dpp v187, v225, v187 wave_shr:1 row_mask:0xf bank_mask:0xf bound_ctrl:1
	v_add_f32_dpp v190, v226, v190 wave_shr:1 row_mask:0xf bank_mask:0xf bound_ctrl:1
	v_add_f32_dpp v191, v227, v191 wave_shr:1 row_mask:0xf bank_mask:0xf bound_ctrl:1
	v_pk_fma_f32 v[182:183], v[12:13], v[218:219], v[182:183] op_sel_hi:[1,0,1] neg_lo:[0,0,1] neg_hi:[0,0,1]
	v_pk_fma_f32 v[186:187], v[14:15], v[218:219], v[186:187] op_sel_hi:[1,0,1] neg_lo:[0,0,1] neg_hi:[0,0,1]
	v_pk_fma_f32 v[190:191], v[16:17], v[218:219], v[190:191] op_sel_hi:[1,0,1] neg_lo:[0,0,1] neg_hi:[0,0,1]
	v_pk_add_f32 v[182:183], v[182:183], v[228:229] neg_lo:[0,1] neg_hi:[0,1]
	v_pk_add_f32 v[186:187], v[186:187], v[230:231] neg_lo:[0,1] neg_hi:[0,1]
	v_pk_add_f32 v[190:191], v[190:191], v[232:233] neg_lo:[0,1] neg_hi:[0,1]
	v_pk_mul_f32 v[234:235], v[182:183], v[182:183]
	v_pk_fma_f32 v[234:235], v[186:187], v[186:187], v[234:235]
	v_pk_fma_f32 v[234:235], v[190:191], v[190:191], v[234:235]
	v_add_f32_e32 v234, v234, v235
	v_cndmask_b32_e64 v235, 0, v234, s[12:13]
	v_add_f32_e32 v0, v0, v235
	s_add_i32 s4, s34, 9
	s_min_i32 s4, s4, 0x200
	s_mul_i32 s5, s4, 0x804
	s_add_i32 s5, s5, s35
	s_add_i32 s6, s5, 0x0
	s_add_i32 s7, s5, 0x101004
	s_add_i32 s8, s5, 0x202008
	s_add_i32 s11, s5, 0x30300c
	s_add_i32 s15, s5, 0x404010
	s_add_i32 s31, s5, 0x505014
	s_mul_i32 s9, s4, 0x180c
	s_add_i32 s9, s9, s33
	buffer_load_dword v12, v28, s[16:19], s6 offen nt
	buffer_load_dword v13, v28, s[16:19], s7 offen nt
	buffer_load_dword v14, v28, s[16:19], s8 offen nt
	buffer_load_dword v15, v28, s[16:19], s11 offen nt
	buffer_load_dword v16, v28, s[16:19], s15 offen nt
	buffer_load_dword v17, v28, s[16:19], s31 offen nt
	buffer_load_dwordx3 v[32:34], v27, s[24:27], s9 offen nt
	s_waitcnt vmcnt(14)
	v_mov_b32_dpp v56, v64 wave_shr:1 row_mask:0xf bank_mask:0xf bound_ctrl:1
	v_mov_b32_dpp v57, v65 wave_shr:1 row_mask:0xf bank_mask:0xf bound_ctrl:1
	v_mov_b32_dpp v58, v66 wave_shr:1 row_mask:0xf bank_mask:0xf bound_ctrl:1
	v_mov_b32_dpp v72, v64 wave_shl:1 row_mask:0xf bank_mask:0xf bound_ctrl:1
	v_mov_b32_dpp v73, v65 wave_shl:1 row_mask:0xf bank_mask:0xf bound_ctrl:1
	v_mov_b32_dpp v74, v66 wave_shl:1 row_mask:0xf bank_mask:0xf bound_ctrl:1
	v_mov_b32_dpp v84, v54 wave_shr:1 row_mask:0xf bank_mask:0xf bound_ctrl:1
	v_mov_b32_dpp v85, v55 wave_shr:1 row_mask:0xf bank_mask:0xf bound_ctrl:1
	v_mov_b32_dpp v86, v60 wave_shr:1 row_mask:0xf bank_mask:0xf bound_ctrl:1
	v_mov_b32_dpp v87, v61 wave_shr:1 row_mask:0xf bank_mask:0xf bound_ctrl:1
	v_mov_b32_dpp v88, v62 wave_shr:1 row_mask:0xf bank_mask:0xf bound_ctrl:1
	v_mov_b32_dpp v89, v63 wave_shr:1 row_mask:0xf bank_mask:0xf bound_ctrl:1
	v_mov_b32_dpp v90, v54 wave_shl:1 row_mask:0xf bank_mask:0xf bound_ctrl:1
	v_mov_b32_dpp v91, v55 wave_shl:1 row_mask:0xf bank_mask:0xf bound_ctrl:1
	v_mov_b32_dpp v108, v60 wave_shl:1 row_mask:0xf bank_mask:0xf bound_ctrl:1
	v_mov_b32_dpp v109, v61 wave_shl:1 row_mask:0xf bank_mask:0xf bound_ctrl:1
	v_mov_b32_dpp v148, v62 wave_shl:1 row_mask:0xf bank_mask:0xf bound_ctrl:1
	v_mov_b32_dpp v149, v63 wave_shl:1 row_mask:0xf bank_mask:0xf bound_ctrl:1
	v_pk_mul_f32 v[152:153], v[54:55], v[64:65] op_sel_hi:[1,0]
	v_pk_mul_f32 v[156:157], v[60:61], v[64:65] op_sel_hi:[1,0]
	v_pk_mul_f32 v[160:161], v[62:63], v[64:65] op_sel_hi:[1,0]
	v_pk_mul_f32 v[164:165], v[54:55], v[64:65] op_sel:[0,1]
	v_pk_mul_f32 v[168:169], v[60:61], v[64:65] op_sel:[0,1]
	v_pk_mul_f32 v[174:175], v[62:63], v[64:65] op_sel:[0,1]
	v_pk_mul_f32 v[178:179], v[54:55], v[66:67] op_sel_hi:[1,0]
	v_pk_mul_f32 v[182:183], v[60:61], v[66:67] op_sel_hi:[1,0]
	v_pk_mul_f32 v[186:187], v[62:63], v[66:67] op_sel_hi:[1,0]
	v_pk_add_f32 v[190:191], v[54:55], v[84:85]
	v_pk_add_f32 v[192:193], v[60:61], v[86:87]
	v_pk_add_f32 v[194:195], v[62:63], v[88:89]
	v_pk_fma_f32 v[152:153], v[84:85], v[56:57], v[152:153] op_sel_hi:[1,0,1]
	v_pk_fma_f32 v[156:157], v[86:87], v[56:57], v[156:157] op_sel_hi:[1,0,1]
	v_pk_fma_f32 v[160:161], v[88:89], v[56:57], v[160:161] op_sel_hi:[1,0,1]
	v_pk_fma_f32 v[164:165], v[84:85], v[56:57], v[164:165] op_sel:[0,1,0]
	v_pk_fma_f32 v[168:169], v[86:87], v[56:57], v[168:169] op_sel:[0,1,0]
	v_pk_fma_f32 v[174:175], v[88:89], v[56:57], v[174:175] op_sel:[0,1,0]
	v_pk_fma_f32 v[178:179], v[84:85], v[58:59], v[178:179] op_sel_hi:[1,0,1]
	v_pk_fma_f32 v[182:183], v[86:87], v[58:59], v[182:183] op_sel_hi:[1,0,1]
	v_pk_fma_f32 v[186:187], v[88:89], v[58:59], v[186:187] op_sel_hi:[1,0,1]
	v_pk_add_f32 v[190:191], v[190:191], v[90:91]
	v_pk_add_f32 v[192:193], v[192:193], v[108:109]
	v_pk_add_f32 v[194:195], v[194:195], v[148:149]
	v_pk_fma_f32 v[152:153], v[90:91], v[72:73], v[152:153] op_sel_hi:[1,0,1]
	v_pk_fma_f32 v[156:157], v[108:109], v[72:73], v[156:157] op_sel_hi:[1,0,1]
	v_pk_fma_f32 v[160:161], v[148:149], v[72:73], v[160:161] op_sel_hi:[1,0,1]
	v_pk_fma_f32 v[164:165], v[90:91], v[72:73], v[164:165] op_sel:[0,1,0]
	v_pk_fma_f32 v[168:169], v[108:109], v[72:73], v[168:169] op_sel:[0,1,0]
	v_pk_fma_f32 v[174:175], v[148:149], v[72:73], v[174:175] op_sel:[0,1,0]
	v_pk_fma_f32 v[178:179], v[90:91], v[74:75], v[178:179] op_sel_hi:[1,0,1]
	v_pk_fma_f32 v[182:183], v[108:109], v[74:75], v[182:183] op_sel_hi:[1,0,1]
	v_pk_fma_f32 v[186:187], v[148:149], v[74:75], v[186:187] op_sel_hi:[1,0,1]
	s_barrier
	ds_read_b128 v[84:87], v23 offset:3072
	ds_read_b128 v[88:91], v23 offset:4096
	ds_read_b128 v[216:219], v23 offset:5120
	v_pk_add_f32 v[108:109], v[46:47], v[190:191]
	v_pk_add_f32 v[46:47], v[134:135], v[192:193]
	v_pk_add_f32 v[134:135], v[136:137], v[194:195]
	v_pk_add_f32 v[136:137], v[142:143], v[152:153]
	v_pk_add_f32 v[142:143], v[116:117], v[156:157]
	v_pk_add_f32 v[116:117], v[118:119], v[160:161]
	v_pk_add_f32 v[118:119], v[120:121], v[164:165]
	v_pk_add_f32 v[120:121], v[122:123], v[168:169]
	v_pk_add_f32 v[122:123], v[124:125], v[174:175]
	v_pk_add_f32 v[124:125], v[126:127], v[178:179]
	v_pk_add_f32 v[126:127], v[128:129], v[182:183]
	v_pk_add_f32 v[128:129], v[130:131], v[186:187]
	s_waitcnt lgkmcnt(2)
	v_pk_fma_f32 v[136:137], v[84:85], v[108:109], v[136:137] op_sel_hi:[0,1,1] neg_lo:[1,0,0] neg_hi:[1,0,0]
	v_pk_fma_f32 v[142:143], v[84:85], v[46:47], v[142:143] op_sel_hi:[0,1,1] neg_lo:[1,0,0] neg_hi:[1,0,0]
	v_pk_fma_f32 v[116:117], v[84:85], v[134:135], v[116:117] op_sel_hi:[0,1,1] neg_lo:[1,0,0] neg_hi:[1,0,0]
	v_pk_fma_f32 v[118:119], v[84:85], v[108:109], v[118:119] op_sel:[1,0,0] neg_lo:[1,0,0] neg_hi:[1,0,0]
	v_pk_fma_f32 v[120:121], v[84:85], v[46:47], v[120:121] op_sel:[1,0,0] neg_lo:[1,0,0] neg_hi:[1,0,0]
	v_pk_fma_f32 v[122:123], v[84:85], v[134:135], v[122:123] op_sel:[1,0,0] neg_lo:[1,0,0] neg_hi:[1,0,0]
	v_pk_fma_f32 v[124:125], v[86:87], v[108:109], v[124:125] op_sel_hi:[0,1,1] neg_lo:[1,0,0] neg_hi:[1,0,0]
	v_pk_fma_f32 v[126:127], v[86:87], v[46:47], v[126:127] op_sel_hi:[0,1,1] neg_lo:[1,0,0] neg_hi:[1,0,0]
	v_pk_fma_f32 v[128:129], v[86:87], v[134:135], v[128:129] op_sel_hi:[0,1,1] neg_lo:[1,0,0] neg_hi:[1,0,0]
	v_pk_mul_f32 v[130:131], v[86:87], v[136:137] op_sel:[1,0]
	v_pk_mul_f32 v[222:223], v[86:87], v[142:143] op_sel:[1,0]
	v_pk_mul_f32 v[228:229], v[86:87], v[116:117] op_sel:[1,0]
	s_waitcnt lgkmcnt(1)
	v_pk_mul_f32 v[148:149], v[88:89], v[136:137] op_sel_hi:[0,1]
	v_pk_mul_f32 v[224:225], v[88:89], v[142:143] op_sel_hi:[0,1]
	v_pk_mul_f32 v[230:231], v[88:89], v[116:117] op_sel_hi:[0,1]
	v_pk_mul_f32 v[220:221], v[88:89], v[136:137] op_sel:[1,0]
	v_pk_mul_f32 v[226:227], v[88:89], v[142:143] op_sel:[1,0]
	v_pk_mul_f32 v[232:233], v[88:89], v[116:117] op_sel:[1,0]
	v_pk_fma_f32 v[130:131], v[88:89], v[118:119], v[130:131] op_sel_hi:[0,1,1]
	v_pk_fma_f32 v[222:223], v[88:89], v[120:121], v[222:223] op_sel_hi:[0,1,1]
	v_pk_fma_f32 v[228:229], v[88:89], v[122:123], v[228:229] op_sel_hi:[0,1,1]
	v_pk_fma_f32 v[148:149], v[90:91], v[118:119], v[148:149] op_sel_hi:[0,1,1]
	v_pk_fma_f32 v[224:225], v[90:91], v[120:121], v[224:225] op_sel_hi:[0,1,1]
	v_pk_fma_f32 v[230:231], v[90:91], v[122:123], v[230:231] op_sel_hi:[0,1,1]
	v_pk_fma_f32 v[220:221], v[90:91], v[118:119], v[220:221] op_sel:[1,0,0]
	v_pk_fma_f32 v[226:227], v[90:91], v[120:121], v[226:227] op_sel:[1,0,0]
	v_pk_fma_f32 v[232:233], v[90:91], v[122:123], v[232:233] op_sel:[1,0,0]
	v_pk_fma_f32 v[130:131], v[88:89], v[124:125], v[130:131] op_sel:[1,0,0]
	v_pk_fma_f32 v[222:223], v[88:89], v[126:127], v[222:223] op_sel:[1,0,0]
	v_pk_fma_f32 v[228:229], v[88:89], v[128:129], v[228:229] op_sel:[1,0,0]
	v_pk_fma_f32 v[148:149], v[90:91], v[124:125], v[148:149] op_sel:[1,0,0]
	v_pk_fma_f32 v[224:225], v[90:91], v[126:127], v[224:225] op_sel:[1,0,0]
	v_pk_fma_f32 v[230:231], v[90:91], v[128:129], v[230:231] op_sel:[1,0,0]
	s_waitcnt lgkmcnt(0)
	v_pk_fma_f32 v[220:221], v[216:217], v[124:125], v[220:221] op_sel_hi:[0,1,1]
	v_pk_fma_f32 v[226:227], v[216:217], v[126:127], v[226:227] op_sel_hi:[0,1,1]
	v_pk_fma_f32 v[232:233], v[216:217], v[128:129], v[232:233] op_sel_hi:[0,1,1]
	v_pk_mul_f32 v[234:235], v[84:85], v[130:131] op_sel_hi:[0,1]
	v_pk_mul_f32 v[236:237], v[84:85], v[222:223] op_sel_hi:[0,1]
	v_pk_mul_f32 v[238:239], v[84:85], v[228:229] op_sel_hi:[0,1]
	v_pk_fma_f32 v[234:235], v[84:85], v[148:149], v[234:235] op_sel:[1,0,0]
	v_pk_fma_f32 v[236:237], v[84:85], v[224:225], v[236:237] op_sel:[1,0,0]
	v_pk_fma_f32 v[238:239], v[84:85], v[230:231], v[238:239] op_sel:[1,0,0]
	v_pk_fma_f32 v[234:235], v[86:87], v[220:221], v[234:235] op_sel_hi:[0,1,1]
	v_pk_fma_f32 v[236:237], v[86:87], v[226:227], v[236:237] op_sel_hi:[0,1,1]
	v_pk_fma_f32 v[238:239], v[86:87], v[232:233], v[238:239] op_sel_hi:[0,1,1]
	v_pk_fma_f32 v[234:235], v[216:217], v[108:109], v[234:235] op_sel:[1,0,0] neg_lo:[0,0,1] neg_hi:[0,0,1]
	v_pk_fma_f32 v[236:237], v[216:217], v[46:47], v[236:237] op_sel:[1,0,0] neg_lo:[0,0,1] neg_hi:[0,0,1]
	v_pk_fma_f32 v[238:239], v[216:217], v[134:135], v[238:239] op_sel:[1,0,0] neg_lo:[0,0,1] neg_hi:[0,0,1]
	v_cmp_eq_u32_e64 s[10:11], 1, v219
	v_cmp_eq_u32_e64 s[14:15], 2, v219
	v_cmp_eq_u32_e64 s[20:21], 3, v219
	v_cmp_eq_u32_e64 s[22:23], 4, v219
	v_cmp_eq_u32_e64 s[30:31], 5, v219
	v_cmp_eq_u32_e64 s[38:39], 6, v219
	v_pk_add_f32 v[46:47], v[52:53], v[130:131]
	v_pk_add_f32 v[52:53], v[106:107], v[222:223]
	v_pk_add_f32 v[106:107], v[150:151], v[228:229]
	v_pk_add_f32 v[108:109], v[154:155], v[148:149]
	v_pk_add_f32 v[116:117], v[158:159], v[224:225]
	v_pk_add_f32 v[118:119], v[162:163], v[230:231]
	v_pk_add_f32 v[120:121], v[166:167], v[220:221]
	v_pk_add_f32 v[122:123], v[170:171], v[226:227]
	v_pk_add_f32 v[124:125], v[176:177], v[232:233]
	v_pk_add_f32 v[126:127], v[180:181], v[234:235]
	v_pk_add_f32 v[128:129], v[184:185], v[236:237]
	v_pk_add_f32 v[134:135], v[188:189], v[238:239]
	v_pk_fma_f32 v[136:137], v[76:77], v[46:47], v[126:127] op_sel_hi:[0,1,1]
	v_pk_fma_f32 v[142:143], v[76:77], v[52:53], v[128:129] op_sel_hi:[0,1,1]
	v_pk_fma_f32 v[150:151], v[76:77], v[106:107], v[134:135] op_sel_hi:[0,1,1]
	v_pk_fma_f32 v[154:155], v[92:93], v[46:47], v[126:127] op_sel_hi:[0,1,1]
	v_pk_fma_f32 v[158:159], v[92:93], v[52:53], v[128:129] op_sel_hi:[0,1,1]
	v_pk_fma_f32 v[162:163], v[92:93], v[106:107], v[134:135] op_sel_hi:[0,1,1]
	v_pk_fma_f32 v[136:137], v[76:77], v[108:109], v[136:137] op_sel:[1,0,0]
	v_pk_fma_f32 v[142:143], v[76:77], v[116:117], v[142:143] op_sel:[1,0,0]
	v_pk_fma_f32 v[150:151], v[76:77], v[118:119], v[150:151] op_sel:[1,0,0]
	v_pk_fma_f32 v[154:155], v[92:93], v[108:109], v[154:155] op_sel:[1,0,0]
	v_pk_fma_f32 v[158:159], v[92:93], v[116:117], v[158:159] op_sel:[1,0,0]
	v_pk_fma_f32 v[162:163], v[92:93], v[118:119], v[162:163] op_sel:[1,0,0]
	v_pk_fma_f32 v[136:137], v[78:79], v[120:121], v[136:137] op_sel_hi:[0,1,1]
	v_pk_fma_f32 v[142:143], v[78:79], v[122:123], v[142:143] op_sel_hi:[0,1,1]
	v_pk_fma_f32 v[150:151], v[78:79], v[124:125], v[150:151] op_sel_hi:[0,1,1]
	v_pk_fma_f32 v[154:155], v[94:95], v[120:121], v[154:155] op_sel_hi:[0,1,1]
	v_pk_fma_f32 v[158:159], v[94:95], v[122:123], v[158:159] op_sel_hi:[0,1,1]
	v_pk_fma_f32 v[162:163], v[94:95], v[124:125], v[162:163] op_sel_hi:[0,1,1]
	v_pk_fma_f32 v[126:127], v[36:37], v[46:47], v[126:127] op_sel_hi:[0,1,1]
	v_pk_fma_f32 v[128:129], v[36:37], v[52:53], v[128:129] op_sel_hi:[0,1,1]
	v_pk_fma_f32 v[134:135], v[36:37], v[106:107], v[134:135] op_sel_hi:[0,1,1]
	v_pk_fma_f32 v[126:127], v[36:37], v[108:109], v[126:127] op_sel:[1,0,0]
	v_pk_fma_f32 v[128:129], v[36:37], v[116:117], v[128:129] op_sel:[1,0,0]
	v_pk_fma_f32 v[134:135], v[36:37], v[118:119], v[134:135] op_sel:[1,0,0]
	v_pk_fma_f32 v[126:127], v[38:39], v[120:121], v[126:127] op_sel_hi:[0,1,1]
	v_pk_fma_f32 v[128:129], v[38:39], v[122:123], v[128:129] op_sel_hi:[0,1,1]
	v_pk_fma_f32 v[134:135], v[38:39], v[124:125], v[134:135] op_sel_hi:[0,1,1]
	v_cndmask_b32_e64 v166, 0, v1, s[10:11]
	v_cndmask_b32_e64 v167, 0, v1, s[14:15]
	v_cndmask_b32_e64 v170, 0, v1, s[20:21]
	v_cndmask_b32_e64 v171, 0, v1, s[22:23]
	v_cndmask_b32_e64 v176, 0, v1, s[30:31]
	v_cndmask_b32_e64 v177, 0, v1, s[38:39]
	v_add_f32_dpp v126, v136, v126 wave_shl:1 row_mask:0xf bank_mask:0xf bound_ctrl:1
	v_add_f32_dpp v127, v137, v127 wave_shl:1 row_mask:0xf bank_mask:0xf bound_ctrl:1
	v_add_f32_dpp v128, v142, v128 wave_shl:1 row_mask:0xf bank_mask:0xf bound_ctrl:1
	v_add_f32_dpp v129, v143, v129 wave_shl:1 row_mask:0xf bank_mask:0xf bound_ctrl:1
	v_add_f32_dpp v134, v150, v134 wave_shl:1 row_mask:0xf bank_mask:0xf bound_ctrl:1
	v_add_f32_dpp v135, v151, v135 wave_shl:1 row_mask:0xf bank_mask:0xf bound_ctrl:1
	s_add_i32 s4, s34, 5
	s_cmpk_lt_i32 s4, 0x201
	s_cselect_b64 s[12:13], s[0:1], 0
	v_add_f32_dpp v126, v154, v126 wave_shr:1 row_mask:0xf bank_mask:0xf bound_ctrl:1
	v_add_f32_dpp v127, v155, v127 wave_shr:1 row_mask:0xf bank_mask:0xf bound_ctrl:1
	v_add_f32_dpp v128, v158, v128 wave_shr:1 row_mask:0xf bank_mask:0xf bound_ctrl:1
	v_add_f32_dpp v129, v159, v129 wave_shr:1 row_mask:0xf bank_mask:0xf bound_ctrl:1
	v_add_f32_dpp v134, v162, v134 wave_shr:1 row_mask:0xf bank_mask:0xf bound_ctrl:1
	v_add_f32_dpp v135, v163, v135 wave_shr:1 row_mask:0xf bank_mask:0xf bound_ctrl:1
	v_pk_fma_f32 v[126:127], v[20:21], v[218:219], v[126:127] op_sel_hi:[1,0,1] neg_lo:[0,0,1] neg_hi:[0,0,1]
	v_pk_fma_f32 v[128:129], v[24:25], v[218:219], v[128:129] op_sel_hi:[1,0,1] neg_lo:[0,0,1] neg_hi:[0,0,1]
	v_pk_fma_f32 v[134:135], v[30:31], v[218:219], v[134:135] op_sel_hi:[1,0,1] neg_lo:[0,0,1] neg_hi:[0,0,1]
	v_pk_add_f32 v[126:127], v[126:127], v[166:167] neg_lo:[0,1] neg_hi:[0,1]
	v_pk_add_f32 v[128:129], v[128:129], v[170:171] neg_lo:[0,1] neg_hi:[0,1]
	v_pk_add_f32 v[134:135], v[134:135], v[176:177] neg_lo:[0,1] neg_hi:[0,1]
	v_pk_mul_f32 v[180:181], v[126:127], v[126:127]
	v_pk_fma_f32 v[180:181], v[128:129], v[128:129], v[180:181]
	v_pk_fma_f32 v[180:181], v[134:135], v[134:135], v[180:181]
	v_add_f32_e32 v180, v180, v181
	v_cndmask_b32_e64 v181, 0, v180, s[12:13]
	v_add_f32_e32 v0, v0, v181
	s_add_i32 s4, s34, 10
	s_min_i32 s4, s4, 0x200
	s_mul_i32 s5, s4, 0x804
	s_add_i32 s5, s5, s35
	s_add_i32 s6, s5, 0x0
	s_add_i32 s7, s5, 0x101004
	s_add_i32 s8, s5, 0x202008
	s_add_i32 s11, s5, 0x30300c
	s_add_i32 s15, s5, 0x404010
	s_add_i32 s31, s5, 0x505014
	s_mul_i32 s9, s4, 0x180c
	s_add_i32 s9, s9, s33
	buffer_load_dword v20, v28, s[16:19], s6 offen nt
	buffer_load_dword v21, v28, s[16:19], s7 offen nt
	buffer_load_dword v24, v28, s[16:19], s8 offen nt
	buffer_load_dword v25, v28, s[16:19], s11 offen nt
	buffer_load_dword v30, v28, s[16:19], s15 offen nt
	buffer_load_dword v31, v28, s[16:19], s31 offen nt
	buffer_load_dwordx3 v[36:38], v27, s[24:27], s9 offen nt
	s_waitcnt vmcnt(14)
	v_mov_b32_dpp v76, v8 wave_shr:1 row_mask:0xf bank_mask:0xf bound_ctrl:1
	v_mov_b32_dpp v77, v9 wave_shr:1 row_mask:0xf bank_mask:0xf bound_ctrl:1
	v_mov_b32_dpp v78, v10 wave_shr:1 row_mask:0xf bank_mask:0xf bound_ctrl:1
	v_mov_b32_dpp v84, v8 wave_shl:1 row_mask:0xf bank_mask:0xf bound_ctrl:1
	v_mov_b32_dpp v85, v9 wave_shl:1 row_mask:0xf bank_mask:0xf bound_ctrl:1
	v_mov_b32_dpp v86, v10 wave_shl:1 row_mask:0xf bank_mask:0xf bound_ctrl:1
	v_mov_b32_dpp v46, v2 wave_shr:1 row_mask:0xf bank_mask:0xf bound_ctrl:1
	v_mov_b32_dpp v47, v3 wave_shr:1 row_mask:0xf bank_mask:0xf bound_ctrl:1
	v_mov_b32_dpp v52, v4 wave_shr:1 row_mask:0xf bank_mask:0xf bound_ctrl:1
	v_mov_b32_dpp v53, v5 wave_shr:1 row_mask:0xf bank_mask:0xf bound_ctrl:1
	v_mov_b32_dpp v88, v6 wave_shr:1 row_mask:0xf bank_mask:0xf bound_ctrl:1
	v_mov_b32_dpp v89, v7 wave_shr:1 row_mask:0xf bank_mask:0xf bound_ctrl:1
	v_mov_b32_dpp v90, v2 wave_shl:1 row_mask:0xf bank_mask:0xf bound_ctrl:1
	v_mov_b32_dpp v91, v3 wave_shl:1 row_mask:0xf bank_mask:0xf bound_ctrl:1
	v_mov_b32_dpp v92, v4 wave_shl:1 row_mask:0xf bank_mask:0xf bound_ctrl:1
	v_mov_b32_dpp v93, v5 wave_shl:1 row_mask:0xf bank_mask:0xf bound_ctrl:1
	v_mov_b32_dpp v94, v6 wave_shl:1 row_mask:0xf bank_mask:0xf bound_ctrl:1
	v_mov_b32_dpp v95, v7 wave_shl:1 row_mask:0xf bank_mask:0xf bound_ctrl:1
	v_pk_mul_f32 v[106:107], v[2:3], v[8:9] op_sel_hi:[1,0]
	v_pk_mul_f32 v[108:109], v[4:5], v[8:9] op_sel_hi:[1,0]
	v_pk_mul_f32 v[116:117], v[6:7], v[8:9] op_sel_hi:[1,0]
	v_pk_mul_f32 v[118:119], v[2:3], v[8:9] op_sel:[0,1]
	v_pk_mul_f32 v[120:121], v[4:5], v[8:9] op_sel:[0,1]
	v_pk_mul_f32 v[122:123], v[6:7], v[8:9] op_sel:[0,1]
	v_pk_mul_f32 v[124:125], v[2:3], v[10:11] op_sel_hi:[1,0]
	v_pk_mul_f32 v[126:127], v[4:5], v[10:11] op_sel_hi:[1,0]
	v_pk_mul_f32 v[128:129], v[6:7], v[10:11] op_sel_hi:[1,0]
	v_pk_add_f32 v[134:135], v[2:3], v[46:47]
	v_pk_add_f32 v[136:137], v[4:5], v[52:53]
	v_pk_add_f32 v[142:143], v[6:7], v[88:89]
	v_pk_fma_f32 v[106:107], v[46:47], v[76:77], v[106:107] op_sel_hi:[1,0,1]
	v_pk_fma_f32 v[108:109], v[52:53], v[76:77], v[108:109] op_sel_hi:[1,0,1]
	v_pk_fma_f32 v[116:117], v[88:89], v[76:77], v[116:117] op_sel_hi:[1,0,1]
	v_pk_fma_f32 v[118:119], v[46:47], v[76:77], v[118:119] op_sel:[0,1,0]
	v_pk_fma_f32 v[120:121], v[52:53], v[76:77], v[120:121] op_sel:[0,1,0]
	v_pk_fma_f32 v[122:123], v[88:89], v[76:77], v[122:123] op_sel:[0,1,0]
	v_pk_fma_f32 v[124:125], v[46:47], v[78:79], v[124:125] op_sel_hi:[1,0,1]
	v_pk_fma_f32 v[126:127], v[52:53], v[78:79], v[126:127] op_sel_hi:[1,0,1]
	v_pk_fma_f32 v[128:129], v[88:89], v[78:79], v[128:129] op_sel_hi:[1,0,1]
	v_pk_add_f32 v[134:135], v[134:135], v[90:91]
	v_pk_add_f32 v[136:137], v[136:137], v[92:93]
	v_pk_add_f32 v[142:143], v[142:143], v[94:95]
	v_pk_fma_f32 v[106:107], v[90:91], v[84:85], v[106:107] op_sel_hi:[1,0,1]
	v_pk_fma_f32 v[108:109], v[92:93], v[84:85], v[108:109] op_sel_hi:[1,0,1]
	v_pk_fma_f32 v[116:117], v[94:95], v[84:85], v[116:117] op_sel_hi:[1,0,1]
	v_pk_fma_f32 v[118:119], v[90:91], v[84:85], v[118:119] op_sel:[0,1,0]
	v_pk_fma_f32 v[120:121], v[92:93], v[84:85], v[120:121] op_sel:[0,1,0]
	v_pk_fma_f32 v[122:123], v[94:95], v[84:85], v[122:123] op_sel:[0,1,0]
	v_pk_fma_f32 v[124:125], v[90:91], v[86:87], v[124:125] op_sel_hi:[1,0,1]
	v_pk_fma_f32 v[126:127], v[92:93], v[86:87], v[126:127] op_sel_hi:[1,0,1]
	v_pk_fma_f32 v[128:129], v[94:95], v[86:87], v[128:129] op_sel_hi:[1,0,1]
	s_barrier
	ds_read_b128 v[88:91], v23 offset:0
	ds_read_b128 v[92:95], v23 offset:1024
	ds_read_b128 v[216:219], v23 offset:2048
	v_pk_add_f32 v[46:47], v[190:191], v[134:135]
	v_pk_add_f32 v[52:53], v[140:141], v[46:47]
	v_pk_add_f32 v[140:141], v[192:193], v[136:137]
	v_pk_add_f32 v[150:151], v[144:145], v[140:141]
	v_pk_add_f32 v[144:145], v[194:195], v[142:143]
	v_pk_add_f32 v[154:155], v[146:147], v[144:145]
	v_pk_add_f32 v[146:147], v[152:153], v[106:107]
	v_pk_add_f32 v[158:159], v[96:97], v[146:147]
	v_pk_add_f32 v[96:97], v[156:157], v[108:109]
	v_pk_add_f32 v[152:153], v[98:99], v[96:97]
	v_pk_add_f32 v[98:99], v[160:161], v[116:117]
	v_pk_add_f32 v[156:157], v[100:101], v[98:99]
	v_pk_add_f32 v[100:101], v[164:165], v[118:119]
	v_pk_add_f32 v[160:161], v[102:103], v[100:101]
	v_pk_add_f32 v[102:103], v[168:169], v[120:121]
	v_pk_add_f32 v[162:163], v[104:105], v[102:103]
	v_pk_add_f32 v[104:105], v[174:175], v[122:123]
	v_pk_add_f32 v[164:165], v[110:111], v[104:105]
	v_pk_add_f32 v[110:111], v[178:179], v[124:125]
	v_pk_add_f32 v[166:167], v[112:113], v[110:111]
	v_pk_add_f32 v[112:113], v[182:183], v[126:127]
	v_pk_add_f32 v[168:169], v[114:115], v[112:113]
	v_pk_add_f32 v[114:115], v[186:187], v[128:129]
	v_pk_add_f32 v[170:171], v[138:139], v[114:115]
	s_waitcnt lgkmcnt(2)
	v_pk_fma_f32 v[158:159], v[88:89], v[52:53], v[158:159] op_sel_hi:[0,1,1] neg_lo:[1,0,0] neg_hi:[1,0,0]
	v_pk_fma_f32 v[152:153], v[88:89], v[150:151], v[152:153] op_sel_hi:[0,1,1] neg_lo:[1,0,0] neg_hi:[1,0,0]
	v_pk_fma_f32 v[156:157], v[88:89], v[154:155], v[156:157] op_sel_hi:[0,1,1] neg_lo:[1,0,0] neg_hi:[1,0,0]
	v_pk_fma_f32 v[160:161], v[88:89], v[52:53], v[160:161] op_sel:[1,0,0] neg_lo:[1,0,0] neg_hi:[1,0,0]
	v_pk_fma_f32 v[162:163], v[88:89], v[150:151], v[162:163] op_sel:[1,0,0] neg_lo:[1,0,0] neg_hi:[1,0,0]
	v_pk_fma_f32 v[164:165], v[88:89], v[154:155], v[164:165] op_sel:[1,0,0] neg_lo:[1,0,0] neg_hi:[1,0,0]
	v_pk_fma_f32 v[166:167], v[90:91], v[52:53], v[166:167] op_sel_hi:[0,1,1] neg_lo:[1,0,0] neg_hi:[1,0,0]
	v_pk_fma_f32 v[168:169], v[90:91], v[150:151], v[168:169] op_sel_hi:[0,1,1] neg_lo:[1,0,0] neg_hi:[1,0,0]
	v_pk_fma_f32 v[170:171], v[90:91], v[154:155], v[170:171] op_sel_hi:[0,1,1] neg_lo:[1,0,0] neg_hi:[1,0,0]
	v_pk_mul_f32 v[138:139], v[90:91], v[158:159] op_sel:[1,0]
	v_pk_mul_f32 v[178:179], v[90:91], v[152:153] op_sel:[1,0]
	v_pk_mul_f32 v[184:185], v[90:91], v[156:157] op_sel:[1,0]
	s_waitcnt lgkmcnt(1)
	v_pk_mul_f32 v[174:175], v[92:93], v[158:159] op_sel_hi:[0,1]
	v_pk_mul_f32 v[180:181], v[92:93], v[152:153] op_sel_hi:[0,1]
	v_pk_mul_f32 v[186:187], v[92:93], v[156:157] op_sel_hi:[0,1]
	v_pk_mul_f32 v[176:177], v[92:93], v[158:159] op_sel:[1,0]
	v_pk_mul_f32 v[182:183], v[92:93], v[152:153] op_sel:[1,0]
	v_pk_mul_f32 v[188:189], v[92:93], v[156:157] op_sel:[1,0]
	v_pk_fma_f32 v[138:139], v[92:93], v[160:161], v[138:139] op_sel_hi:[0,1,1]
	v_pk_fma_f32 v[178:179], v[92:93], v[162:163], v[178:179] op_sel_hi:[0,1,1]
	v_pk_fma_f32 v[184:185], v[92:93], v[164:165], v[184:185] op_sel_hi:[0,1,1]
	v_pk_fma_f32 v[174:175], v[94:95], v[160:161], v[174:175] op_sel_hi:[0,1,1]
	v_pk_fma_f32 v[180:181], v[94:95], v[162:163], v[180:181] op_sel_hi:[0,1,1]
	v_pk_fma_f32 v[186:187], v[94:95], v[164:165], v[186:187] op_sel_hi:[0,1,1]
	v_pk_fma_f32 v[176:177], v[94:95], v[160:161], v[176:177] op_sel:[1,0,0]
	v_pk_fma_f32 v[182:183], v[94:95], v[162:163], v[182:183] op_sel:[1,0,0]
	v_pk_fma_f32 v[188:189], v[94:95], v[164:165], v[188:189] op_sel:[1,0,0]
	v_pk_fma_f32 v[138:139], v[92:93], v[166:167], v[138:139] op_sel:[1,0,0]
	v_pk_fma_f32 v[178:179], v[92:93], v[168:169], v[178:179] op_sel:[1,0,0]
	v_pk_fma_f32 v[184:185], v[92:93], v[170:171], v[184:185] op_sel:[1,0,0]
	v_pk_fma_f32 v[174:175], v[94:95], v[166:167], v[174:175] op_sel:[1,0,0]
	v_pk_fma_f32 v[180:181], v[94:95], v[168:169], v[180:181] op_sel:[1,0,0]
	v_pk_fma_f32 v[186:187], v[94:95], v[170:171], v[186:187] op_sel:[1,0,0]
	s_waitcnt lgkmcnt(0)
	v_pk_fma_f32 v[176:177], v[216:217], v[166:167], v[176:177] op_sel_hi:[0,1,1]
	v_pk_fma_f32 v[182:183], v[216:217], v[168:169], v[182:183] op_sel_hi:[0,1,1]
	v_pk_fma_f32 v[188:189], v[216:217], v[170:171], v[188:189] op_sel_hi:[0,1,1]
	v_pk_mul_f32 v[190:191], v[88:89], v[138:139] op_sel_hi:[0,1]
	v_pk_mul_f32 v[192:193], v[88:89], v[178:179] op_sel_hi:[0,1]
	v_pk_mul_f32 v[194:195], v[88:89], v[184:185] op_sel_hi:[0,1]
	v_pk_fma_f32 v[190:191], v[88:89], v[174:175], v[190:191] op_sel:[1,0,0]
	v_pk_fma_f32 v[192:193], v[88:89], v[180:181], v[192:193] op_sel:[1,0,0]
	v_pk_fma_f32 v[194:195], v[88:89], v[186:187], v[194:195] op_sel:[1,0,0]
	v_pk_fma_f32 v[190:191], v[90:91], v[176:177], v[190:191] op_sel_hi:[0,1,1]
	v_pk_fma_f32 v[192:193], v[90:91], v[182:183], v[192:193] op_sel_hi:[0,1,1]
	v_pk_fma_f32 v[194:195], v[90:91], v[188:189], v[194:195] op_sel_hi:[0,1,1]
	v_pk_fma_f32 v[190:191], v[216:217], v[52:53], v[190:191] op_sel:[1,0,0] neg_lo:[0,0,1] neg_hi:[0,0,1]
	v_pk_fma_f32 v[192:193], v[216:217], v[150:151], v[192:193] op_sel:[1,0,0] neg_lo:[0,0,1] neg_hi:[0,0,1]
	v_pk_fma_f32 v[194:195], v[216:217], v[154:155], v[194:195] op_sel:[1,0,0] neg_lo:[0,0,1] neg_hi:[0,0,1]
	v_cmp_eq_u32_e64 s[10:11], 1, v219
	v_cmp_eq_u32_e64 s[14:15], 2, v219
	v_cmp_eq_u32_e64 s[20:21], 3, v219
	v_cmp_eq_u32_e64 s[22:23], 4, v219
	v_cmp_eq_u32_e64 s[30:31], 5, v219
	v_cmp_eq_u32_e64 s[38:39], 6, v219
	v_pk_add_f32 v[52:53], v[130:131], v[138:139]
	v_pk_add_f32 v[150:151], v[132:133], v[52:53]
	v_pk_add_f32 v[130:131], v[222:223], v[178:179]
	v_pk_add_f32 v[132:133], v[198:199], v[130:131]
	v_pk_add_f32 v[152:153], v[228:229], v[184:185]
	v_pk_add_f32 v[154:155], v[204:205], v[152:153]
	v_pk_add_f32 v[156:157], v[148:149], v[174:175]
	v_pk_add_f32 v[158:159], v[172:173], v[156:157]
	v_pk_add_f32 v[148:149], v[224:225], v[180:181]
	v_pk_add_f32 v[160:161], v[200:201], v[148:149]
	v_pk_add_f32 v[162:163], v[230:231], v[186:187]
	v_pk_add_f32 v[164:165], v[206:207], v[162:163]
	v_pk_add_f32 v[166:167], v[220:221], v[176:177]
	v_pk_add_f32 v[168:169], v[196:197], v[166:167]
	v_pk_add_f32 v[170:171], v[226:227], v[182:183]
	v_pk_add_f32 v[172:173], v[202:203], v[170:171]
	v_pk_add_f32 v[196:197], v[232:233], v[188:189]
	v_pk_add_f32 v[198:199], v[208:209], v[196:197]
	v_pk_add_f32 v[200:201], v[234:235], v[190:191]
	v_pk_add_f32 v[202:203], v[210:211], v[200:201]
	v_pk_add_f32 v[204:205], v[236:237], v[192:193]
	v_pk_add_f32 v[206:207], v[212:213], v[204:205]
	v_pk_add_f32 v[208:209], v[238:239], v[194:195]
	v_pk_add_f32 v[210:211], v[214:215], v[208:209]
	v_pk_fma_f32 v[212:213], v[68:69], v[150:151], v[202:203] op_sel_hi:[0,1,1]
	v_pk_fma_f32 v[214:215], v[68:69], v[132:133], v[206:207] op_sel_hi:[0,1,1]
	v_pk_fma_f32 v[220:221], v[68:69], v[154:155], v[210:211] op_sel_hi:[0,1,1]
	v_pk_fma_f32 v[222:223], v[80:81], v[150:151], v[202:203] op_sel_hi:[0,1,1]
	v_pk_fma_f32 v[224:225], v[80:81], v[132:133], v[206:207] op_sel_hi:[0,1,1]
	v_pk_fma_f32 v[226:227], v[80:81], v[154:155], v[210:211] op_sel_hi:[0,1,1]
	v_pk_fma_f32 v[212:213], v[68:69], v[158:159], v[212:213] op_sel:[1,0,0]
	v_pk_fma_f32 v[214:215], v[68:69], v[160:161], v[214:215] op_sel:[1,0,0]
	v_pk_fma_f32 v[220:221], v[68:69], v[164:165], v[220:221] op_sel:[1,0,0]
	v_pk_fma_f32 v[222:223], v[80:81], v[158:159], v[222:223] op_sel:[1,0,0]
	v_pk_fma_f32 v[224:225], v[80:81], v[160:161], v[224:225] op_sel:[1,0,0]
	v_pk_fma_f32 v[226:227], v[80:81], v[164:165], v[226:227] op_sel:[1,0,0]
	v_pk_fma_f32 v[212:213], v[70:71], v[168:169], v[212:213] op_sel_hi:[0,1,1]
	v_pk_fma_f32 v[214:215], v[70:71], v[172:173], v[214:215] op_sel_hi:[0,1,1]
	v_pk_fma_f32 v[220:221], v[70:71], v[198:199], v[220:221] op_sel_hi:[0,1,1]
	v_pk_fma_f32 v[222:223], v[82:83], v[168:169], v[222:223] op_sel_hi:[0,1,1]
	v_pk_fma_f32 v[224:225], v[82:83], v[172:173], v[224:225] op_sel_hi:[0,1,1]
	v_pk_fma_f32 v[226:227], v[82:83], v[198:199], v[226:227] op_sel_hi:[0,1,1]
	v_pk_fma_f32 v[202:203], v[48:49], v[150:151], v[202:203] op_sel_hi:[0,1,1]
	v_pk_fma_f32 v[206:207], v[48:49], v[132:133], v[206:207] op_sel_hi:[0,1,1]
	v_pk_fma_f32 v[210:211], v[48:49], v[154:155], v[210:211] op_sel_hi:[0,1,1]
	v_pk_fma_f32 v[202:203], v[48:49], v[158:159], v[202:203] op_sel:[1,0,0]
	v_pk_fma_f32 v[206:207], v[48:49], v[160:161], v[206:207] op_sel:[1,0,0]
	v_pk_fma_f32 v[210:211], v[48:49], v[164:165], v[210:211] op_sel:[1,0,0]
	v_pk_fma_f32 v[202:203], v[50:51], v[168:169], v[202:203] op_sel_hi:[0,1,1]
	v_pk_fma_f32 v[206:207], v[50:51], v[172:173], v[206:207] op_sel_hi:[0,1,1]
	v_pk_fma_f32 v[210:211], v[50:51], v[198:199], v[210:211] op_sel_hi:[0,1,1]
	v_cndmask_b32_e64 v228, 0, v1, s[10:11]
	v_cndmask_b32_e64 v229, 0, v1, s[14:15]
	v_cndmask_b32_e64 v230, 0, v1, s[20:21]
	v_cndmask_b32_e64 v231, 0, v1, s[22:23]
	v_cndmask_b32_e64 v232, 0, v1, s[30:31]
	v_cndmask_b32_e64 v233, 0, v1, s[38:39]
	v_add_f32_dpp v202, v212, v202 wave_shl:1 row_mask:0xf bank_mask:0xf bound_ctrl:1
	v_add_f32_dpp v203, v213, v203 wave_shl:1 row_mask:0xf bank_mask:0xf bound_ctrl:1
	v_add_f32_dpp v206, v214, v206 wave_shl:1 row_mask:0xf bank_mask:0xf bound_ctrl:1
	v_add_f32_dpp v207, v215, v207 wave_shl:1 row_mask:0xf bank_mask:0xf bound_ctrl:1
	v_add_f32_dpp v210, v220, v210 wave_shl:1 row_mask:0xf bank_mask:0xf bound_ctrl:1
	v_add_f32_dpp v211, v221, v211 wave_shl:1 row_mask:0xf bank_mask:0xf bound_ctrl:1
	s_add_i32 s4, s34, 6
	s_cmpk_lt_i32 s4, 0x201
	s_cselect_b64 s[12:13], s[0:1], 0
	v_add_f32_dpp v202, v222, v202 wave_shr:1 row_mask:0xf bank_mask:0xf bound_ctrl:1
	v_add_f32_dpp v203, v223, v203 wave_shr:1 row_mask:0xf bank_mask:0xf bound_ctrl:1
	v_add_f32_dpp v206, v224, v206 wave_shr:1 row_mask:0xf bank_mask:0xf bound_ctrl:1
	v_add_f32_dpp v207, v225, v207 wave_shr:1 row_mask:0xf bank_mask:0xf bound_ctrl:1
	v_add_f32_dpp v210, v226, v210 wave_shr:1 row_mask:0xf bank_mask:0xf bound_ctrl:1
	v_add_f32_dpp v211, v227, v211 wave_shr:1 row_mask:0xf bank_mask:0xf bound_ctrl:1
	v_pk_fma_f32 v[202:203], v[40:41], v[218:219], v[202:203] op_sel_hi:[1,0,1] neg_lo:[0,0,1] neg_hi:[0,0,1]
	v_pk_fma_f32 v[206:207], v[42:43], v[218:219], v[206:207] op_sel_hi:[1,0,1] neg_lo:[0,0,1] neg_hi:[0,0,1]
	v_pk_fma_f32 v[210:211], v[44:45], v[218:219], v[210:211] op_sel_hi:[1,0,1] neg_lo:[0,0,1] neg_hi:[0,0,1]
	v_pk_add_f32 v[202:203], v[202:203], v[228:229] neg_lo:[0,1] neg_hi:[0,1]
	v_pk_add_f32 v[206:207], v[206:207], v[230:231] neg_lo:[0,1] neg_hi:[0,1]
	v_pk_add_f32 v[210:211], v[210:211], v[232:233] neg_lo:[0,1] neg_hi:[0,1]
	v_pk_mul_f32 v[234:235], v[202:203], v[202:203]
	v_pk_fma_f32 v[234:235], v[206:207], v[206:207], v[234:235]
	v_pk_fma_f32 v[234:235], v[210:211], v[210:211], v[234:235]
	v_add_f32_e32 v234, v234, v235
	v_cndmask_b32_e64 v235, 0, v234, s[12:13]
	v_add_f32_e32 v0, v0, v235
	s_add_i32 s4, s34, 11
	s_min_i32 s4, s4, 0x200
	s_mul_i32 s5, s4, 0x804
	s_add_i32 s5, s5, s35
	s_add_i32 s6, s5, 0x0
	s_add_i32 s7, s5, 0x101004
	s_add_i32 s8, s5, 0x202008
	s_add_i32 s11, s5, 0x30300c
	s_add_i32 s15, s5, 0x404010
	s_add_i32 s31, s5, 0x505014
	s_mul_i32 s9, s4, 0x180c
	s_add_i32 s9, s9, s33
	buffer_load_dword v40, v28, s[16:19], s6 offen nt
	buffer_load_dword v41, v28, s[16:19], s7 offen nt
	buffer_load_dword v42, v28, s[16:19], s8 offen nt
	buffer_load_dword v43, v28, s[16:19], s11 offen nt
	buffer_load_dword v44, v28, s[16:19], s15 offen nt
	buffer_load_dword v45, v28, s[16:19], s31 offen nt
	buffer_load_dwordx3 v[48:50], v27, s[24:27], s9 offen nt
	s_waitcnt vmcnt(14)
	v_mov_b32_dpp v68, v32 wave_shr:1 row_mask:0xf bank_mask:0xf bound_ctrl:1
	v_mov_b32_dpp v69, v33 wave_shr:1 row_mask:0xf bank_mask:0xf bound_ctrl:1
	v_mov_b32_dpp v70, v34 wave_shr:1 row_mask:0xf bank_mask:0xf bound_ctrl:1
	v_mov_b32_dpp v80, v32 wave_shl:1 row_mask:0xf bank_mask:0xf bound_ctrl:1
	v_mov_b32_dpp v81, v33 wave_shl:1 row_mask:0xf bank_mask:0xf bound_ctrl:1
	v_mov_b32_dpp v82, v34 wave_shl:1 row_mask:0xf bank_mask:0xf bound_ctrl:1
	v_mov_b32_dpp v88, v12 wave_shr:1 row_mask:0xf bank_mask:0xf bound_ctrl:1
	v_mov_b32_dpp v89, v13 wave_shr:1 row_mask:0xf bank_mask:0xf bound_ctrl:1
	v_mov_b32_dpp v90, v14 wave_shr:1 row_mask:0xf bank_mask:0xf bound_ctrl:1
	v_mov_b32_dpp v91, v15 wave_shr:1 row_mask:0xf bank_mask:0xf bound_ctrl:1
	v_mov_b32_dpp v92, v16 wave_shr:1 row_mask:0xf bank_mask:0xf bound_ctrl:1
	v_mov_b32_dpp v93, v17 wave_shr:1 row_mask:0xf bank_mask:0xf bound_ctrl:1
	v_mov_b32_dpp v94, v12 wave_shl:1 row_mask:0xf bank_mask:0xf bound_ctrl:1
	v_mov_b32_dpp v95, v13 wave_shl:1 row_mask:0xf bank_mask:0xf bound_ctrl:1
	v_mov_b32_dpp v132, v14 wave_shl:1 row_mask:0xf bank_mask:0xf bound_ctrl:1
	v_mov_b32_dpp v133, v15 wave_shl:1 row_mask:0xf bank_mask:0xf bound_ctrl:1
	v_mov_b32_dpp v150, v16 wave_shl:1 row_mask:0xf bank_mask:0xf bound_ctrl:1
	v_mov_b32_dpp v151, v17 wave_shl:1 row_mask:0xf bank_mask:0xf bound_ctrl:1
	v_pk_mul_f32 v[154:155], v[12:13], v[32:33] op_sel_hi:[1,0]
	v_pk_mul_f32 v[158:159], v[14:15], v[32:33] op_sel_hi:[1,0]
	v_pk_mul_f32 v[160:161], v[16:17], v[32:33] op_sel_hi:[1,0]
	v_pk_mul_f32 v[164:165], v[12:13], v[32:33] op_sel:[0,1]
	v_pk_mul_f32 v[168:169], v[14:15], v[32:33] op_sel:[0,1]
	v_pk_mul_f32 v[172:173], v[16:17], v[32:33] op_sel:[0,1]
	v_pk_mul_f32 v[198:199], v[12:13], v[34:35] op_sel_hi:[1,0]
	v_pk_mul_f32 v[202:203], v[14:15], v[34:35] op_sel_hi:[1,0]
	v_pk_mul_f32 v[206:207], v[16:17], v[34:35] op_sel_hi:[1,0]
	v_pk_add_f32 v[210:211], v[12:13], v[88:89]
	v_pk_add_f32 v[212:213], v[14:15], v[90:91]
	v_pk_add_f32 v[214:215], v[16:17], v[92:93]
	v_pk_fma_f32 v[154:155], v[88:89], v[68:69], v[154:155] op_sel_hi:[1,0,1]
	v_pk_fma_f32 v[158:159], v[90:91], v[68:69], v[158:159] op_sel_hi:[1,0,1]
	v_pk_fma_f32 v[160:161], v[92:93], v[68:69], v[160:161] op_sel_hi:[1,0,1]
	v_pk_fma_f32 v[164:165], v[88:89], v[68:69], v[164:165] op_sel:[0,1,0]
	v_pk_fma_f32 v[168:169], v[90:91], v[68:69], v[168:169] op_sel:[0,1,0]
	v_pk_fma_f32 v[172:173], v[92:93], v[68:69], v[172:173] op_sel:[0,1,0]
	v_pk_fma_f32 v[198:199], v[88:89], v[70:71], v[198:199] op_sel_hi:[1,0,1]
	v_pk_fma_f32 v[202:203], v[90:91], v[70:71], v[202:203] op_sel_hi:[1,0,1]
	v_pk_fma_f32 v[206:207], v[92:93], v[70:71], v[206:207] op_sel_hi:[1,0,1]
	v_pk_add_f32 v[210:211], v[210:211], v[94:95]
	v_pk_add_f32 v[212:213], v[212:213], v[132:133]
	v_pk_add_f32 v[214:215], v[214:215], v[150:151]
	v_pk_fma_f32 v[154:155], v[94:95], v[80:81], v[154:155] op_sel_hi:[1,0,1]
	v_pk_fma_f32 v[158:159], v[132:133], v[80:81], v[158:159] op_sel_hi:[1,0,1]
	v_pk_fma_f32 v[160:161], v[150:151], v[80:81], v[160:161] op_sel_hi:[1,0,1]
	v_pk_fma_f32 v[164:165], v[94:95], v[80:81], v[164:165] op_sel:[0,1,0]
	v_pk_fma_f32 v[168:169], v[132:133], v[80:81], v[168:169] op_sel:[0,1,0]
	v_pk_fma_f32 v[172:173], v[150:151], v[80:81], v[172:173] op_sel:[0,1,0]
	v_pk_fma_f32 v[198:199], v[94:95], v[82:83], v[198:199] op_sel_hi:[1,0,1]
	v_pk_fma_f32 v[202:203], v[132:133], v[82:83], v[202:203] op_sel_hi:[1,0,1]
	v_pk_fma_f32 v[206:207], v[150:151], v[82:83], v[206:207] op_sel_hi:[1,0,1]
	s_barrier
	ds_read_b128 v[88:91], v23 offset:3072
	ds_read_b128 v[92:95], v23 offset:4096
	ds_read_b128 v[216:219], v23 offset:5120
	v_pk_add_f32 v[132:133], v[46:47], v[210:211]
	v_pk_add_f32 v[46:47], v[140:141], v[212:213]
	v_pk_add_f32 v[140:141], v[144:145], v[214:215]
	v_pk_add_f32 v[144:145], v[146:147], v[154:155]
	v_pk_add_f32 v[146:147], v[96:97], v[158:159]
	v_pk_add_f32 v[96:97], v[98:99], v[160:161]
	v_pk_add_f32 v[98:99], v[100:101], v[164:165]
	v_pk_add_f32 v[100:101], v[102:103], v[168:169]
	v_pk_add_f32 v[102:103], v[104:105], v[172:173]
	v_pk_add_f32 v[104:105], v[110:111], v[198:199]
	v_pk_add_f32 v[110:111], v[112:113], v[202:203]
	v_pk_add_f32 v[112:113], v[114:115], v[206:207]
	s_waitcnt lgkmcnt(2)
	v_pk_fma_f32 v[144:145], v[88:89], v[132:133], v[144:145] op_sel_hi:[0,1,1] neg_lo:[1,0,0] neg_hi:[1,0,0]
	v_pk_fma_f32 v[146:147], v[88:89], v[46:47], v[146:147] op_sel_hi:[0,1,1] neg_lo:[1,0,0] neg_hi:[1,0,0]
	v_pk_fma_f32 v[96:97], v[88:89], v[140:141], v[96:97] op_sel_hi:[0,1,1] neg_lo:[1,0,0] neg_hi:[1,0,0]
	v_pk_fma_f32 v[98:99], v[88:89], v[132:133], v[98:99] op_sel:[1,0,0] neg_lo:[1,0,0] neg_hi:[1,0,0]
	v_pk_fma_f32 v[100:101], v[88:89], v[46:47], v[100:101] op_sel:[1,0,0] neg_lo:[1,0,0] neg_hi:[1,0,0]
	v_pk_fma_f32 v[102:103], v[88:89], v[140:141], v[102:103] op_sel:[1,0,0] neg_lo:[1,0,0] neg_hi:[1,0,0]
	v_pk_fma_f32 v[104:105], v[90:91], v[132:133], v[104:105] op_sel_hi:[0,1,1] neg_lo:[1,0,0] neg_hi:[1,0,0]
	v_pk_fma_f32 v[110:111], v[90:91], v[46:47], v[110:111] op_sel_hi:[0,1,1] neg_lo:[1,0,0] neg_hi:[1,0,0]
	v_pk_fma_f32 v[112:113], v[90:91], v[140:141], v[112:113] op_sel_hi:[0,1,1] neg_lo:[1,0,0] neg_hi:[1,0,0]
	v_pk_mul_f32 v[114:115], v[90:91], v[144:145] op_sel:[1,0]
	v_pk_mul_f32 v[222:223], v[90:91], v[146:147] op_sel:[1,0]
	v_pk_mul_f32 v[228:229], v[90:91], v[96:97] op_sel:[1,0]
	s_waitcnt lgkmcnt(1)
	v_pk_mul_f32 v[150:151], v[92:93], v[144:145] op_sel_hi:[0,1]
	v_pk_mul_f32 v[224:225], v[92:93], v[146:147] op_sel_hi:[0,1]
	v_pk_mul_f32 v[230:231], v[92:93], v[96:97] op_sel_hi:[0,1]
	v_pk_mul_f32 v[220:221], v[92:93], v[144:145] op_sel:[1,0]
	v_pk_mul_f32 v[226:227], v[92:93], v[146:147] op_sel:[1,0]
	v_pk_mul_f32 v[232:233], v[92:93], v[96:97] op_sel:[1,0]
	v_pk_fma_f32 v[114:115], v[92:93], v[98:99], v[114:115] op_sel_hi:[0,1,1]
	v_pk_fma_f32 v[222:223], v[92:93], v[100:101], v[222:223] op_sel_hi:[0,1,1]
	v_pk_fma_f32 v[228:229], v[92:93], v[102:103], v[228:229] op_sel_hi:[0,1,1]
	v_pk_fma_f32 v[150:151], v[94:95], v[98:99], v[150:151] op_sel_hi:[0,1,1]
	v_pk_fma_f32 v[224:225], v[94:95], v[100:101], v[224:225] op_sel_hi:[0,1,1]
	v_pk_fma_f32 v[230:231], v[94:95], v[102:103], v[230:231] op_sel_hi:[0,1,1]
	v_pk_fma_f32 v[220:221], v[94:95], v[98:99], v[220:221] op_sel:[1,0,0]
	v_pk_fma_f32 v[226:227], v[94:95], v[100:101], v[226:227] op_sel:[1,0,0]
	v_pk_fma_f32 v[232:233], v[94:95], v[102:103], v[232:233] op_sel:[1,0,0]
	v_pk_fma_f32 v[114:115], v[92:93], v[104:105], v[114:115] op_sel:[1,0,0]
	v_pk_fma_f32 v[222:223], v[92:93], v[110:111], v[222:223] op_sel:[1,0,0]
	v_pk_fma_f32 v[228:229], v[92:93], v[112:113], v[228:229] op_sel:[1,0,0]
	v_pk_fma_f32 v[150:151], v[94:95], v[104:105], v[150:151] op_sel:[1,0,0]
	v_pk_fma_f32 v[224:225], v[94:95], v[110:111], v[224:225] op_sel:[1,0,0]
	v_pk_fma_f32 v[230:231], v[94:95], v[112:113], v[230:231] op_sel:[1,0,0]
	s_waitcnt lgkmcnt(0)
	v_pk_fma_f32 v[220:221], v[216:217], v[104:105], v[220:221] op_sel_hi:[0,1,1]
	v_pk_fma_f32 v[226:227], v[216:217], v[110:111], v[226:227] op_sel_hi:[0,1,1]
	v_pk_fma_f32 v[232:233], v[216:217], v[112:113], v[232:233] op_sel_hi:[0,1,1]
	v_pk_mul_f32 v[234:235], v[88:89], v[114:115] op_sel_hi:[0,1]
	v_pk_mul_f32 v[236:237], v[88:89], v[222:223] op_sel_hi:[0,1]
	v_pk_mul_f32 v[238:239], v[88:89], v[228:229] op_sel_hi:[0,1]
	v_pk_fma_f32 v[234:235], v[88:89], v[150:151], v[234:235] op_sel:[1,0,0]
	v_pk_fma_f32 v[236:237], v[88:89], v[224:225], v[236:237] op_sel:[1,0,0]
	v_pk_fma_f32 v[238:239], v[88:89], v[230:231], v[238:239] op_sel:[1,0,0]
	v_pk_fma_f32 v[234:235], v[90:91], v[220:221], v[234:235] op_sel_hi:[0,1,1]
	v_pk_fma_f32 v[236:237], v[90:91], v[226:227], v[236:237] op_sel_hi:[0,1,1]
	v_pk_fma_f32 v[238:239], v[90:91], v[232:233], v[238:239] op_sel_hi:[0,1,1]
	v_pk_fma_f32 v[234:235], v[216:217], v[132:133], v[234:235] op_sel:[1,0,0] neg_lo:[0,0,1] neg_hi:[0,0,1]
	v_pk_fma_f32 v[236:237], v[216:217], v[46:47], v[236:237] op_sel:[1,0,0] neg_lo:[0,0,1] neg_hi:[0,0,1]
	v_pk_fma_f32 v[238:239], v[216:217], v[140:141], v[238:239] op_sel:[1,0,0] neg_lo:[0,0,1] neg_hi:[0,0,1]
	v_cmp_eq_u32_e64 s[10:11], 1, v219
	v_cmp_eq_u32_e64 s[14:15], 2, v219
	v_cmp_eq_u32_e64 s[20:21], 3, v219
	v_cmp_eq_u32_e64 s[22:23], 4, v219
	v_cmp_eq_u32_e64 s[30:31], 5, v219
	v_cmp_eq_u32_e64 s[38:39], 6, v219
	v_pk_add_f32 v[46:47], v[52:53], v[114:115]
	v_pk_add_f32 v[52:53], v[130:131], v[222:223]
	v_pk_add_f32 v[96:97], v[152:153], v[228:229]
	v_pk_add_f32 v[98:99], v[156:157], v[150:151]
	v_pk_add_f32 v[100:101], v[148:149], v[224:225]
	v_pk_add_f32 v[102:103], v[162:163], v[230:231]
	v_pk_add_f32 v[104:105], v[166:167], v[220:221]
	v_pk_add_f32 v[110:111], v[170:171], v[226:227]
	v_pk_add_f32 v[112:113], v[196:197], v[232:233]
	v_pk_add_f32 v[130:131], v[200:201], v[234:235]
	v_pk_add_f32 v[132:133], v[204:205], v[236:237]
	v_pk_add_f32 v[140:141], v[208:209], v[238:239]
	v_pk_fma_f32 v[144:145], v[56:57], v[46:47], v[130:131] op_sel_hi:[0,1,1]
	v_pk_fma_f32 v[146:147], v[56:57], v[52:53], v[132:133] op_sel_hi:[0,1,1]
	v_pk_fma_f32 v[148:149], v[56:57], v[96:97], v[140:141] op_sel_hi:[0,1,1]
	v_pk_fma_f32 v[152:153], v[72:73], v[46:47], v[130:131] op_sel_hi:[0,1,1]
	v_pk_fma_f32 v[156:157], v[72:73], v[52:53], v[132:133] op_sel_hi:[0,1,1]
	v_pk_fma_f32 v[162:163], v[72:73], v[96:97], v[140:141] op_sel_hi:[0,1,1]
	v_pk_fma_f32 v[144:145], v[56:57], v[98:99], v[144:145] op_sel:[1,0,0]
	v_pk_fma_f32 v[146:147], v[56:57], v[100:101], v[146:147] op_sel:[1,0,0]
	v_pk_fma_f32 v[148:149], v[56:57], v[102:103], v[148:149] op_sel:[1,0,0]
	v_pk_fma_f32 v[152:153], v[72:73], v[98:99], v[152:153] op_sel:[1,0,0]
	v_pk_fma_f32 v[156:157], v[72:73], v[100:101], v[156:157] op_sel:[1,0,0]
	v_pk_fma_f32 v[162:163], v[72:73], v[102:103], v[162:163] op_sel:[1,0,0]
	v_pk_fma_f32 v[144:145], v[58:59], v[104:105], v[144:145] op_sel_hi:[0,1,1]
	v_pk_fma_f32 v[146:147], v[58:59], v[110:111], v[146:147] op_sel_hi:[0,1,1]
	v_pk_fma_f32 v[148:149], v[58:59], v[112:113], v[148:149] op_sel_hi:[0,1,1]
	v_pk_fma_f32 v[152:153], v[74:75], v[104:105], v[152:153] op_sel_hi:[0,1,1]
	v_pk_fma_f32 v[156:157], v[74:75], v[110:111], v[156:157] op_sel_hi:[0,1,1]
	v_pk_fma_f32 v[162:163], v[74:75], v[112:113], v[162:163] op_sel_hi:[0,1,1]
	v_pk_fma_f32 v[130:131], v[64:65], v[46:47], v[130:131] op_sel_hi:[0,1,1]
	v_pk_fma_f32 v[132:133], v[64:65], v[52:53], v[132:133] op_sel_hi:[0,1,1]
	v_pk_fma_f32 v[140:141], v[64:65], v[96:97], v[140:141] op_sel_hi:[0,1,1]
	v_pk_fma_f32 v[130:131], v[64:65], v[98:99], v[130:131] op_sel:[1,0,0]
	v_pk_fma_f32 v[132:133], v[64:65], v[100:101], v[132:133] op_sel:[1,0,0]
	v_pk_fma_f32 v[140:141], v[64:65], v[102:103], v[140:141] op_sel:[1,0,0]
	v_pk_fma_f32 v[130:131], v[66:67], v[104:105], v[130:131] op_sel_hi:[0,1,1]
	v_pk_fma_f32 v[132:133], v[66:67], v[110:111], v[132:133] op_sel_hi:[0,1,1]
	v_pk_fma_f32 v[140:141], v[66:67], v[112:113], v[140:141] op_sel_hi:[0,1,1]
	v_cndmask_b32_e64 v166, 0, v1, s[10:11]
	v_cndmask_b32_e64 v167, 0, v1, s[14:15]
	v_cndmask_b32_e64 v170, 0, v1, s[20:21]
	v_cndmask_b32_e64 v171, 0, v1, s[22:23]
	v_cndmask_b32_e64 v196, 0, v1, s[30:31]
	v_cndmask_b32_e64 v197, 0, v1, s[38:39]
	v_add_f32_dpp v130, v144, v130 wave_shl:1 row_mask:0xf bank_mask:0xf bound_ctrl:1
	v_add_f32_dpp v131, v145, v131 wave_shl:1 row_mask:0xf bank_mask:0xf bound_ctrl:1
	v_add_f32_dpp v132, v146, v132 wave_shl:1 row_mask:0xf bank_mask:0xf bound_ctrl:1
	v_add_f32_dpp v133, v147, v133 wave_shl:1 row_mask:0xf bank_mask:0xf bound_ctrl:1
	v_add_f32_dpp v140, v148, v140 wave_shl:1 row_mask:0xf bank_mask:0xf bound_ctrl:1
	v_add_f32_dpp v141, v149, v141 wave_shl:1 row_mask:0xf bank_mask:0xf bound_ctrl:1
	s_add_i32 s4, s34, 7
	s_cmpk_lt_i32 s4, 0x201
	s_cselect_b64 s[12:13], s[0:1], 0
	v_add_f32_dpp v130, v152, v130 wave_shr:1 row_mask:0xf bank_mask:0xf bound_ctrl:1
	v_add_f32_dpp v131, v153, v131 wave_shr:1 row_mask:0xf bank_mask:0xf bound_ctrl:1
	v_add_f32_dpp v132, v156, v132 wave_shr:1 row_mask:0xf bank_mask:0xf bound_ctrl:1
	v_add_f32_dpp v133, v157, v133 wave_shr:1 row_mask:0xf bank_mask:0xf bound_ctrl:1
	v_add_f32_dpp v140, v162, v140 wave_shr:1 row_mask:0xf bank_mask:0xf bound_ctrl:1
	v_add_f32_dpp v141, v163, v141 wave_shr:1 row_mask:0xf bank_mask:0xf bound_ctrl:1
	v_pk_fma_f32 v[130:131], v[54:55], v[218:219], v[130:131] op_sel_hi:[1,0,1] neg_lo:[0,0,1] neg_hi:[0,0,1]
	v_pk_fma_f32 v[132:133], v[60:61], v[218:219], v[132:133] op_sel_hi:[1,0,1] neg_lo:[0,0,1] neg_hi:[0,0,1]
	v_pk_fma_f32 v[140:141], v[62:63], v[218:219], v[140:141] op_sel_hi:[1,0,1] neg_lo:[0,0,1] neg_hi:[0,0,1]
	v_pk_add_f32 v[130:131], v[130:131], v[166:167] neg_lo:[0,1] neg_hi:[0,1]
	v_pk_add_f32 v[132:133], v[132:133], v[170:171] neg_lo:[0,1] neg_hi:[0,1]
	v_pk_add_f32 v[140:141], v[140:141], v[196:197] neg_lo:[0,1] neg_hi:[0,1]
	v_pk_mul_f32 v[200:201], v[130:131], v[130:131]
	v_pk_fma_f32 v[200:201], v[132:133], v[132:133], v[200:201]
	v_pk_fma_f32 v[200:201], v[140:141], v[140:141], v[200:201]
	v_add_f32_e32 v200, v200, v201
	v_cndmask_b32_e64 v201, 0, v200, s[12:13]
	v_add_f32_e32 v0, v0, v201
	s_waitcnt vmcnt(7)
	v_mov_b32_dpp v52, v36 wave_shr:1 row_mask:0xf bank_mask:0xf bound_ctrl:1
	v_mov_b32_dpp v53, v37 wave_shr:1 row_mask:0xf bank_mask:0xf bound_ctrl:1
	v_mov_b32_dpp v54, v38 wave_shr:1 row_mask:0xf bank_mask:0xf bound_ctrl:1
	v_mov_b32_dpp v56, v36 wave_shl:1 row_mask:0xf bank_mask:0xf bound_ctrl:1
	v_mov_b32_dpp v57, v37 wave_shl:1 row_mask:0xf bank_mask:0xf bound_ctrl:1
	v_mov_b32_dpp v58, v38 wave_shl:1 row_mask:0xf bank_mask:0xf bound_ctrl:1
	v_mov_b32_dpp v46, v20 wave_shr:1 row_mask:0xf bank_mask:0xf bound_ctrl:1
	v_mov_b32_dpp v47, v21 wave_shr:1 row_mask:0xf bank_mask:0xf bound_ctrl:1
	v_mov_b32_dpp v60, v24 wave_shr:1 row_mask:0xf bank_mask:0xf bound_ctrl:1
	v_mov_b32_dpp v61, v25 wave_shr:1 row_mask:0xf bank_mask:0xf bound_ctrl:1
	v_mov_b32_dpp v62, v30 wave_shr:1 row_mask:0xf bank_mask:0xf bound_ctrl:1
	v_mov_b32_dpp v63, v31 wave_shr:1 row_mask:0xf bank_mask:0xf bound_ctrl:1
	v_mov_b32_dpp v64, v20 wave_shl:1 row_mask:0xf bank_mask:0xf bound_ctrl:1
	v_mov_b32_dpp v65, v21 wave_shl:1 row_mask:0xf bank_mask:0xf bound_ctrl:1
	v_mov_b32_dpp v66, v24 wave_shl:1 row_mask:0xf bank_mask:0xf bound_ctrl:1
	v_mov_b32_dpp v67, v25 wave_shl:1 row_mask:0xf bank_mask:0xf bound_ctrl:1
	v_mov_b32_dpp v72, v30 wave_shl:1 row_mask:0xf bank_mask:0xf bound_ctrl:1
	v_mov_b32_dpp v73, v31 wave_shl:1 row_mask:0xf bank_mask:0xf bound_ctrl:1
	v_pk_mul_f32 v[74:75], v[20:21], v[36:37] op_sel_hi:[1,0]
	v_pk_mul_f32 v[88:89], v[24:25], v[36:37] op_sel_hi:[1,0]
	v_pk_mul_f32 v[90:91], v[30:31], v[36:37] op_sel_hi:[1,0]
	v_pk_mul_f32 v[92:93], v[20:21], v[36:37] op_sel:[0,1]
	v_pk_mul_f32 v[94:95], v[24:25], v[36:37] op_sel:[0,1]
	v_pk_mul_f32 v[96:97], v[30:31], v[36:37] op_sel:[0,1]
	v_pk_mul_f32 v[98:99], v[20:21], v[38:39] op_sel_hi:[1,0]
	v_pk_mul_f32 v[100:101], v[24:25], v[38:39] op_sel_hi:[1,0]
	v_pk_mul_f32 v[102:103], v[30:31], v[38:39] op_sel_hi:[1,0]
	v_pk_add_f32 v[104:105], v[20:21], v[46:47]
	v_pk_add_f32 v[110:111], v[24:25], v[60:61]
	v_pk_add_f32 v[112:113], v[30:31], v[62:63]
	v_pk_fma_f32 v[74:75], v[46:47], v[52:53], v[74:75] op_sel_hi:[1,0,1]
	v_pk_fma_f32 v[88:89], v[60:61], v[52:53], v[88:89] op_sel_hi:[1,0,1]
	v_pk_fma_f32 v[90:91], v[62:63], v[52:53], v[90:91] op_sel_hi:[1,0,1]
	v_pk_fma_f32 v[92:93], v[46:47], v[52:53], v[92:93] op_sel:[0,1,0]
	v_pk_fma_f32 v[94:95], v[60:61], v[52:53], v[94:95] op_sel:[0,1,0]
	v_pk_fma_f32 v[96:97], v[62:63], v[52:53], v[96:97] op_sel:[0,1,0]
	v_pk_fma_f32 v[98:99], v[46:47], v[54:55], v[98:99] op_sel_hi:[1,0,1]
	v_pk_fma_f32 v[100:101], v[60:61], v[54:55], v[100:101] op_sel_hi:[1,0,1]
	v_pk_fma_f32 v[102:103], v[62:63], v[54:55], v[102:103] op_sel_hi:[1,0,1]
	v_pk_add_f32 v[104:105], v[104:105], v[64:65]
	v_pk_add_f32 v[110:111], v[110:111], v[66:67]
	v_pk_add_f32 v[112:113], v[112:113], v[72:73]
	v_pk_fma_f32 v[74:75], v[64:65], v[56:57], v[74:75] op_sel_hi:[1,0,1]
	v_pk_fma_f32 v[88:89], v[66:67], v[56:57], v[88:89] op_sel_hi:[1,0,1]
	v_pk_fma_f32 v[90:91], v[72:73], v[56:57], v[90:91] op_sel_hi:[1,0,1]
	v_pk_fma_f32 v[92:93], v[64:65], v[56:57], v[92:93] op_sel:[0,1,0]
	v_pk_fma_f32 v[94:95], v[66:67], v[56:57], v[94:95] op_sel:[0,1,0]
	v_pk_fma_f32 v[96:97], v[72:73], v[56:57], v[96:97] op_sel:[0,1,0]
	v_pk_fma_f32 v[98:99], v[64:65], v[58:59], v[98:99] op_sel_hi:[1,0,1]
	v_pk_fma_f32 v[100:101], v[66:67], v[58:59], v[100:101] op_sel_hi:[1,0,1]
	v_pk_fma_f32 v[102:103], v[72:73], v[58:59], v[102:103] op_sel_hi:[1,0,1]
	s_barrier
	ds_read_b128 v[60:63], v23 offset:0
	ds_read_b128 v[64:67], v23 offset:1024
	ds_read_b128 v[144:147], v23 offset:2048
	v_pk_add_f32 v[46:47], v[210:211], v[104:105]
	v_pk_add_f32 v[72:73], v[134:135], v[46:47]
	v_pk_add_f32 v[130:131], v[212:213], v[110:111]
	v_pk_add_f32 v[132:133], v[136:137], v[130:131]
	v_pk_add_f32 v[134:135], v[214:215], v[112:113]
	v_pk_add_f32 v[136:137], v[142:143], v[134:135]
	v_pk_add_f32 v[140:141], v[154:155], v[74:75]
	v_pk_add_f32 v[142:143], v[106:107], v[140:141]
	v_pk_add_f32 v[106:107], v[158:159], v[88:89]
	v_pk_add_f32 v[148:149], v[108:109], v[106:107]
	v_pk_add_f32 v[108:109], v[160:161], v[90:91]
	v_pk_add_f32 v[152:153], v[116:117], v[108:109]
	v_pk_add_f32 v[116:117], v[164:165], v[92:93]
	v_pk_add_f32 v[154:155], v[118:119], v[116:117]
	v_pk_add_f32 v[118:119], v[168:169], v[94:95]
	v_pk_add_f32 v[156:157], v[120:121], v[118:119]
	v_pk_add_f32 v[120:121], v[172:173], v[96:97]
	v_pk_add_f32 v[158:159], v[122:123], v[120:121]
	v_pk_add_f32 v[122:123], v[198:199], v[98:99]
	v_pk_add_f32 v[160:161], v[124:125], v[122:123]
	v_pk_add_f32 v[124:125], v[202:203], v[100:101]
	v_pk_add_f32 v[162:163], v[126:127], v[124:125]
	v_pk_add_f32 v[126:127], v[206:207], v[102:103]
	v_pk_add_f32 v[164:165], v[128:129], v[126:127]
	s_waitcnt lgkmcnt(2)
	v_pk_fma_f32 v[142:143], v[60:61], v[72:73], v[142:143] op_sel_hi:[0,1,1] neg_lo:[1,0,0] neg_hi:[1,0,0]
	v_pk_fma_f32 v[148:149], v[60:61], v[132:133], v[148:149] op_sel_hi:[0,1,1] neg_lo:[1,0,0] neg_hi:[1,0,0]
	v_pk_fma_f32 v[152:153], v[60:61], v[136:137], v[152:153] op_sel_hi:[0,1,1] neg_lo:[1,0,0] neg_hi:[1,0,0]
	v_pk_fma_f32 v[154:155], v[60:61], v[72:73], v[154:155] op_sel:[1,0,0] neg_lo:[1,0,0] neg_hi:[1,0,0]
	v_pk_fma_f32 v[156:157], v[60:61], v[132:133], v[156:157] op_sel:[1,0,0] neg_lo:[1,0,0] neg_hi:[1,0,0]
	v_pk_fma_f32 v[158:159], v[60:61], v[136:137], v[158:159] op_sel:[1,0,0] neg_lo:[1,0,0] neg_hi:[1,0,0]
	v_pk_fma_f32 v[160:161], v[62:63], v[72:73], v[160:161] op_sel_hi:[0,1,1] neg_lo:[1,0,0] neg_hi:[1,0,0]
	v_pk_fma_f32 v[162:163], v[62:63], v[132:133], v[162:163] op_sel_hi:[0,1,1] neg_lo:[1,0,0] neg_hi:[1,0,0]
	v_pk_fma_f32 v[164:165], v[62:63], v[136:137], v[164:165] op_sel_hi:[0,1,1] neg_lo:[1,0,0] neg_hi:[1,0,0]
	v_pk_mul_f32 v[128:129], v[62:63], v[142:143] op_sel:[1,0]
	v_pk_mul_f32 v[170:171], v[62:63], v[148:149] op_sel:[1,0]
	v_pk_mul_f32 v[198:199], v[62:63], v[152:153] op_sel:[1,0]
	s_waitcnt lgkmcnt(1)
	v_pk_mul_f32 v[166:167], v[64:65], v[142:143] op_sel_hi:[0,1]
	v_pk_mul_f32 v[172:173], v[64:65], v[148:149] op_sel_hi:[0,1]
	v_pk_mul_f32 v[200:201], v[64:65], v[152:153] op_sel_hi:[0,1]
	v_pk_mul_f32 v[168:169], v[64:65], v[142:143] op_sel:[1,0]
	v_pk_mul_f32 v[196:197], v[64:65], v[148:149] op_sel:[1,0]
	v_pk_mul_f32 v[202:203], v[64:65], v[152:153] op_sel:[1,0]
	v_pk_fma_f32 v[128:129], v[64:65], v[154:155], v[128:129] op_sel_hi:[0,1,1]
	v_pk_fma_f32 v[170:171], v[64:65], v[156:157], v[170:171] op_sel_hi:[0,1,1]
	v_pk_fma_f32 v[198:199], v[64:65], v[158:159], v[198:199] op_sel_hi:[0,1,1]
	v_pk_fma_f32 v[166:167], v[66:67], v[154:155], v[166:167] op_sel_hi:[0,1,1]
	v_pk_fma_f32 v[172:173], v[66:67], v[156:157], v[172:173] op_sel_hi:[0,1,1]
	v_pk_fma_f32 v[200:201], v[66:67], v[158:159], v[200:201] op_sel_hi:[0,1,1]
	v_pk_fma_f32 v[168:169], v[66:67], v[154:155], v[168:169] op_sel:[1,0,0]
	v_pk_fma_f32 v[196:197], v[66:67], v[156:157], v[196:197] op_sel:[1,0,0]
	v_pk_fma_f32 v[202:203], v[66:67], v[158:159], v[202:203] op_sel:[1,0,0]
	v_pk_fma_f32 v[128:129], v[64:65], v[160:161], v[128:129] op_sel:[1,0,0]
	v_pk_fma_f32 v[170:171], v[64:65], v[162:163], v[170:171] op_sel:[1,0,0]
	v_pk_fma_f32 v[198:199], v[64:65], v[164:165], v[198:199] op_sel:[1,0,0]
	v_pk_fma_f32 v[166:167], v[66:67], v[160:161], v[166:167] op_sel:[1,0,0]
	v_pk_fma_f32 v[172:173], v[66:67], v[162:163], v[172:173] op_sel:[1,0,0]
	v_pk_fma_f32 v[200:201], v[66:67], v[164:165], v[200:201] op_sel:[1,0,0]
	s_waitcnt lgkmcnt(0)
	v_pk_fma_f32 v[168:169], v[144:145], v[160:161], v[168:169] op_sel_hi:[0,1,1]
	v_pk_fma_f32 v[196:197], v[144:145], v[162:163], v[196:197] op_sel_hi:[0,1,1]
	v_pk_fma_f32 v[202:203], v[144:145], v[164:165], v[202:203] op_sel_hi:[0,1,1]
	v_pk_mul_f32 v[204:205], v[60:61], v[128:129] op_sel_hi:[0,1]
	v_pk_mul_f32 v[206:207], v[60:61], v[170:171] op_sel_hi:[0,1]
	v_pk_mul_f32 v[208:209], v[60:61], v[198:199] op_sel_hi:[0,1]
	v_pk_fma_f32 v[204:205], v[60:61], v[166:167], v[204:205] op_sel:[1,0,0]
	v_pk_fma_f32 v[206:207], v[60:61], v[172:173], v[206:207] op_sel:[1,0,0]
	v_pk_fma_f32 v[208:209], v[60:61], v[200:201], v[208:209] op_sel:[1,0,0]
	v_pk_fma_f32 v[204:205], v[62:63], v[168:169], v[204:205] op_sel_hi:[0,1,1]
	v_pk_fma_f32 v[206:207], v[62:63], v[196:197], v[206:207] op_sel_hi:[0,1,1]
	v_pk_fma_f32 v[208:209], v[62:63], v[202:203], v[208:209] op_sel_hi:[0,1,1]
	v_pk_fma_f32 v[204:205], v[144:145], v[72:73], v[204:205] op_sel:[1,0,0] neg_lo:[0,0,1] neg_hi:[0,0,1]
	v_pk_fma_f32 v[206:207], v[144:145], v[132:133], v[206:207] op_sel:[1,0,0] neg_lo:[0,0,1] neg_hi:[0,0,1]
	v_pk_fma_f32 v[208:209], v[144:145], v[136:137], v[208:209] op_sel:[1,0,0] neg_lo:[0,0,1] neg_hi:[0,0,1]
	v_cmp_eq_u32_e64 s[10:11], 1, v147
	v_cmp_eq_u32_e64 s[14:15], 2, v147
	v_cmp_eq_u32_e64 s[20:21], 3, v147
	v_cmp_eq_u32_e64 s[22:23], 4, v147
	v_cmp_eq_u32_e64 s[30:31], 5, v147
	v_cmp_eq_u32_e64 s[38:39], 6, v147
	v_pk_add_f32 v[72:73], v[114:115], v[128:129]
	v_pk_add_f32 v[132:133], v[138:139], v[72:73]
	v_pk_add_f32 v[114:115], v[222:223], v[170:171]
	v_pk_add_f32 v[136:137], v[178:179], v[114:115]
	v_pk_add_f32 v[138:139], v[228:229], v[198:199]
	v_pk_add_f32 v[142:143], v[184:185], v[138:139]
	v_pk_add_f32 v[148:149], v[150:151], v[166:167]
	v_pk_add_f32 v[152:153], v[174:175], v[148:149]
	v_pk_add_f32 v[150:151], v[224:225], v[172:173]
	v_pk_add_f32 v[154:155], v[180:181], v[150:151]
	v_pk_add_f32 v[156:157], v[230:231], v[200:201]
	v_pk_add_f32 v[158:159], v[186:187], v[156:157]
	v_pk_add_f32 v[160:161], v[220:221], v[168:169]
	v_pk_add_f32 v[162:163], v[176:177], v[160:161]
	v_pk_add_f32 v[164:165], v[226:227], v[196:197]
	v_pk_add_f32 v[174:175], v[182:183], v[164:165]
	v_pk_add_f32 v[176:177], v[232:233], v[202:203]
	v_pk_add_f32 v[178:179], v[188:189], v[176:177]
	v_pk_add_f32 v[180:181], v[234:235], v[204:205]
	v_pk_add_f32 v[182:183], v[190:191], v[180:181]
	v_pk_add_f32 v[184:185], v[236:237], v[206:207]
	v_pk_add_f32 v[186:187], v[192:193], v[184:185]
	v_pk_add_f32 v[188:189], v[238:239], v[208:209]
	v_pk_add_f32 v[190:191], v[194:195], v[188:189]
	v_pk_fma_f32 v[192:193], v[76:77], v[132:133], v[182:183] op_sel_hi:[0,1,1]
	v_pk_fma_f32 v[194:195], v[76:77], v[136:137], v[186:187] op_sel_hi:[0,1,1]
	v_pk_fma_f32 v[210:211], v[76:77], v[142:143], v[190:191] op_sel_hi:[0,1,1]
	v_pk_fma_f32 v[212:213], v[84:85], v[132:133], v[182:183] op_sel_hi:[0,1,1]
	v_pk_fma_f32 v[214:215], v[84:85], v[136:137], v[186:187] op_sel_hi:[0,1,1]
	v_pk_fma_f32 v[216:217], v[84:85], v[142:143], v[190:191] op_sel_hi:[0,1,1]
	v_pk_fma_f32 v[192:193], v[76:77], v[152:153], v[192:193] op_sel:[1,0,0]
	v_pk_fma_f32 v[194:195], v[76:77], v[154:155], v[194:195] op_sel:[1,0,0]
	v_pk_fma_f32 v[210:211], v[76:77], v[158:159], v[210:211] op_sel:[1,0,0]
	v_pk_fma_f32 v[212:213], v[84:85], v[152:153], v[212:213] op_sel:[1,0,0]
	v_pk_fma_f32 v[214:215], v[84:85], v[154:155], v[214:215] op_sel:[1,0,0]
	v_pk_fma_f32 v[216:217], v[84:85], v[158:159], v[216:217] op_sel:[1,0,0]
	v_pk_fma_f32 v[192:193], v[78:79], v[162:163], v[192:193] op_sel_hi:[0,1,1]
	v_pk_fma_f32 v[194:195], v[78:79], v[174:175], v[194:195] op_sel_hi:[0,1,1]
	v_pk_fma_f32 v[210:211], v[78:79], v[178:179], v[210:211] op_sel_hi:[0,1,1]
	v_pk_fma_f32 v[212:213], v[86:87], v[162:163], v[212:213] op_sel_hi:[0,1,1]
	v_pk_fma_f32 v[214:215], v[86:87], v[174:175], v[214:215] op_sel_hi:[0,1,1]
	v_pk_fma_f32 v[216:217], v[86:87], v[178:179], v[216:217] op_sel_hi:[0,1,1]
	v_pk_fma_f32 v[182:183], v[8:9], v[132:133], v[182:183] op_sel_hi:[0,1,1]
	v_pk_fma_f32 v[186:187], v[8:9], v[136:137], v[186:187] op_sel_hi:[0,1,1]
	v_pk_fma_f32 v[190:191], v[8:9], v[142:143], v[190:191] op_sel_hi:[0,1,1]
	v_pk_fma_f32 v[182:183], v[8:9], v[152:153], v[182:183] op_sel:[1,0,0]
	v_pk_fma_f32 v[186:187], v[8:9], v[154:155], v[186:187] op_sel:[1,0,0]
	v_pk_fma_f32 v[190:191], v[8:9], v[158:159], v[190:191] op_sel:[1,0,0]
	v_pk_fma_f32 v[182:183], v[10:11], v[162:163], v[182:183] op_sel_hi:[0,1,1]
	v_pk_fma_f32 v[186:187], v[10:11], v[174:175], v[186:187] op_sel_hi:[0,1,1]
	v_pk_fma_f32 v[190:191], v[10:11], v[178:179], v[190:191] op_sel_hi:[0,1,1]
	v_cndmask_b32_e64 v218, 0, v1, s[10:11]
	v_cndmask_b32_e64 v219, 0, v1, s[14:15]
	v_cndmask_b32_e64 v220, 0, v1, s[20:21]
	v_cndmask_b32_e64 v221, 0, v1, s[22:23]
	v_cndmask_b32_e64 v222, 0, v1, s[30:31]
	v_cndmask_b32_e64 v223, 0, v1, s[38:39]
	v_add_f32_dpp v182, v192, v182 wave_shl:1 row_mask:0xf bank_mask:0xf bound_ctrl:1
	v_add_f32_dpp v183, v193, v183 wave_shl:1 row_mask:0xf bank_mask:0xf bound_ctrl:1
	v_add_f32_dpp v186, v194, v186 wave_shl:1 row_mask:0xf bank_mask:0xf bound_ctrl:1
	v_add_f32_dpp v187, v195, v187 wave_shl:1 row_mask:0xf bank_mask:0xf bound_ctrl:1
	v_add_f32_dpp v190, v210, v190 wave_shl:1 row_mask:0xf bank_mask:0xf bound_ctrl:1
	v_add_f32_dpp v191, v211, v191 wave_shl:1 row_mask:0xf bank_mask:0xf bound_ctrl:1
	s_add_i32 s4, s34, 8
	s_cmpk_lt_i32 s4, 0x201
	s_cselect_b64 s[12:13], s[0:1], 0
	v_add_f32_dpp v182, v212, v182 wave_shr:1 row_mask:0xf bank_mask:0xf bound_ctrl:1
	v_add_f32_dpp v183, v213, v183 wave_shr:1 row_mask:0xf bank_mask:0xf bound_ctrl:1
	v_add_f32_dpp v186, v214, v186 wave_shr:1 row_mask:0xf bank_mask:0xf bound_ctrl:1
	v_add_f32_dpp v187, v215, v187 wave_shr:1 row_mask:0xf bank_mask:0xf bound_ctrl:1
	v_add_f32_dpp v190, v216, v190 wave_shr:1 row_mask:0xf bank_mask:0xf bound_ctrl:1
	v_add_f32_dpp v191, v217, v191 wave_shr:1 row_mask:0xf bank_mask:0xf bound_ctrl:1
	v_pk_fma_f32 v[182:183], v[2:3], v[146:147], v[182:183] op_sel_hi:[1,0,1] neg_lo:[0,0,1] neg_hi:[0,0,1]
	v_pk_fma_f32 v[186:187], v[4:5], v[146:147], v[186:187] op_sel_hi:[1,0,1] neg_lo:[0,0,1] neg_hi:[0,0,1]
	v_pk_fma_f32 v[190:191], v[6:7], v[146:147], v[190:191] op_sel_hi:[1,0,1] neg_lo:[0,0,1] neg_hi:[0,0,1]
	v_pk_add_f32 v[182:183], v[182:183], v[218:219] neg_lo:[0,1] neg_hi:[0,1]
	v_pk_add_f32 v[186:187], v[186:187], v[220:221] neg_lo:[0,1] neg_hi:[0,1]
	v_pk_add_f32 v[190:191], v[190:191], v[222:223] neg_lo:[0,1] neg_hi:[0,1]
	v_pk_mul_f32 v[224:225], v[182:183], v[182:183]
	v_pk_fma_f32 v[224:225], v[186:187], v[186:187], v[224:225]
	v_pk_fma_f32 v[224:225], v[190:191], v[190:191], v[224:225]
	v_add_f32_e32 v224, v224, v225
	v_cndmask_b32_e64 v225, 0, v224, s[12:13]
	v_add_f32_e32 v0, v0, v225
	s_waitcnt vmcnt(0)
	v_mov_b32_dpp v4, v48 wave_shr:1 row_mask:0xf bank_mask:0xf bound_ctrl:1
	v_mov_b32_dpp v5, v49 wave_shr:1 row_mask:0xf bank_mask:0xf bound_ctrl:1
	v_mov_b32_dpp v6, v50 wave_shr:1 row_mask:0xf bank_mask:0xf bound_ctrl:1
	v_mov_b32_dpp v8, v48 wave_shl:1 row_mask:0xf bank_mask:0xf bound_ctrl:1
	v_mov_b32_dpp v9, v49 wave_shl:1 row_mask:0xf bank_mask:0xf bound_ctrl:1
	v_mov_b32_dpp v10, v50 wave_shl:1 row_mask:0xf bank_mask:0xf bound_ctrl:1
	v_mov_b32_dpp v2, v40 wave_shr:1 row_mask:0xf bank_mask:0xf bound_ctrl:1
	v_mov_b32_dpp v3, v41 wave_shr:1 row_mask:0xf bank_mask:0xf bound_ctrl:1
	v_mov_b32_dpp v60, v42 wave_shr:1 row_mask:0xf bank_mask:0xf bound_ctrl:1
	v_mov_b32_dpp v61, v43 wave_shr:1 row_mask:0xf bank_mask:0xf bound_ctrl:1
	v_mov_b32_dpp v62, v44 wave_shr:1 row_mask:0xf bank_mask:0xf bound_ctrl:1
	v_mov_b32_dpp v63, v45 wave_shr:1 row_mask:0xf bank_mask:0xf bound_ctrl:1
	v_mov_b32_dpp v64, v40 wave_shl:1 row_mask:0xf bank_mask:0xf bound_ctrl:1
	v_mov_b32_dpp v65, v41 wave_shl:1 row_mask:0xf bank_mask:0xf bound_ctrl:1
	v_mov_b32_dpp v66, v42 wave_shl:1 row_mask:0xf bank_mask:0xf bound_ctrl:1
	v_mov_b32_dpp v67, v43 wave_shl:1 row_mask:0xf bank_mask:0xf bound_ctrl:1
	v_mov_b32_dpp v76, v44 wave_shl:1 row_mask:0xf bank_mask:0xf bound_ctrl:1
	v_mov_b32_dpp v77, v45 wave_shl:1 row_mask:0xf bank_mask:0xf bound_ctrl:1
	v_pk_mul_f32 v[78:79], v[40:41], v[48:49] op_sel_hi:[1,0]
	v_pk_mul_f32 v[84:85], v[42:43], v[48:49] op_sel_hi:[1,0]
	v_pk_mul_f32 v[86:87], v[44:45], v[48:49] op_sel_hi:[1,0]
	v_pk_mul_f32 v[132:133], v[40:41], v[48:49] op_sel:[0,1]
	v_pk_mul_f32 v[136:137], v[42:43], v[48:49] op_sel:[0,1]
	v_pk_mul_f32 v[142:143], v[44:45], v[48:49] op_sel:[0,1]
	v_pk_mul_f32 v[144:145], v[40:41], v[50:51] op_sel_hi:[1,0]
	v_pk_mul_f32 v[146:147], v[42:43], v[50:51] op_sel_hi:[1,0]
	v_pk_mul_f32 v[152:153], v[44:45], v[50:51] op_sel_hi:[1,0]
	v_pk_add_f32 v[154:155], v[40:41], v[2:3]
	v_pk_add_f32 v[158:159], v[42:43], v[60:61]
	v_pk_add_f32 v[162:163], v[44:45], v[62:63]
	v_pk_fma_f32 v[78:79], v[2:3], v[4:5], v[78:79] op_sel_hi:[1,0,1]
	v_pk_fma_f32 v[84:85], v[60:61], v[4:5], v[84:85] op_sel_hi:[1,0,1]
	v_pk_fma_f32 v[86:87], v[62:63], v[4:5], v[86:87] op_sel_hi:[1,0,1]
	v_pk_fma_f32 v[132:133], v[2:3], v[4:5], v[132:133] op_sel:[0,1,0]
	v_pk_fma_f32 v[136:137], v[60:61], v[4:5], v[136:137] op_sel:[0,1,0]
	v_pk_fma_f32 v[142:143], v[62:63], v[4:5], v[142:143] op_sel:[0,1,0]
	v_pk_fma_f32 v[144:145], v[2:3], v[6:7], v[144:145] op_sel_hi:[1,0,1]
	v_pk_fma_f32 v[146:147], v[60:61], v[6:7], v[146:147] op_sel_hi:[1,0,1]
	v_pk_fma_f32 v[152:153], v[62:63], v[6:7], v[152:153] op_sel_hi:[1,0,1]
	v_pk_add_f32 v[154:155], v[154:155], v[64:65]
	v_pk_add_f32 v[158:159], v[158:159], v[66:67]
	v_pk_add_f32 v[162:163], v[162:163], v[76:77]
	v_pk_fma_f32 v[78:79], v[64:65], v[8:9], v[78:79] op_sel_hi:[1,0,1]
	v_pk_fma_f32 v[84:85], v[66:67], v[8:9], v[84:85] op_sel_hi:[1,0,1]
	v_pk_fma_f32 v[86:87], v[76:77], v[8:9], v[86:87] op_sel_hi:[1,0,1]
	v_pk_fma_f32 v[132:133], v[64:65], v[8:9], v[132:133] op_sel:[0,1,0]
	v_pk_fma_f32 v[136:137], v[66:67], v[8:9], v[136:137] op_sel:[0,1,0]
	v_pk_fma_f32 v[142:143], v[76:77], v[8:9], v[142:143] op_sel:[0,1,0]
	v_pk_fma_f32 v[144:145], v[64:65], v[10:11], v[144:145] op_sel_hi:[1,0,1]
	v_pk_fma_f32 v[146:147], v[66:67], v[10:11], v[146:147] op_sel_hi:[1,0,1]
	v_pk_fma_f32 v[152:153], v[76:77], v[10:11], v[152:153] op_sel_hi:[1,0,1]
	s_barrier
	ds_read_b128 v[60:63], v23 offset:3072
	ds_read_b128 v[64:67], v23 offset:4096
	ds_read_b128 v[192:195], v23 offset:5120
	v_pk_add_f32 v[2:3], v[46:47], v[154:155]
	v_pk_add_f32 v[46:47], v[130:131], v[158:159]
	v_pk_add_f32 v[76:77], v[134:135], v[162:163]
	v_pk_add_f32 v[130:131], v[140:141], v[78:79]
	v_pk_add_f32 v[134:135], v[106:107], v[84:85]
	v_pk_add_f32 v[106:107], v[108:109], v[86:87]
	v_pk_add_f32 v[108:109], v[116:117], v[132:133]
	v_pk_add_f32 v[116:117], v[118:119], v[136:137]
	v_pk_add_f32 v[118:119], v[120:121], v[142:143]
	v_pk_add_f32 v[120:121], v[122:123], v[144:145]
	v_pk_add_f32 v[122:123], v[124:125], v[146:147]
	v_pk_add_f32 v[124:125], v[126:127], v[152:153]
	s_waitcnt lgkmcnt(2)
	v_pk_fma_f32 v[130:131], v[60:61], v[2:3], v[130:131] op_sel_hi:[0,1,1] neg_lo:[1,0,0] neg_hi:[1,0,0]
	v_pk_fma_f32 v[134:135], v[60:61], v[46:47], v[134:135] op_sel_hi:[0,1,1] neg_lo:[1,0,0] neg_hi:[1,0,0]
	v_pk_fma_f32 v[106:107], v[60:61], v[76:77], v[106:107] op_sel_hi:[0,1,1] neg_lo:[1,0,0] neg_hi:[1,0,0]
	v_pk_fma_f32 v[108:109], v[60:61], v[2:3], v[108:109] op_sel:[1,0,0] neg_lo:[1,0,0] neg_hi:[1,0,0]
	v_pk_fma_f32 v[116:117], v[60:61], v[46:47], v[116:117] op_sel:[1,0,0] neg_lo:[1,0,0] neg_hi:[1,0,0]
	v_pk_fma_f32 v[118:119], v[60:61], v[76:77], v[118:119] op_sel:[1,0,0] neg_lo:[1,0,0] neg_hi:[1,0,0]
	v_pk_fma_f32 v[120:121], v[62:63], v[2:3], v[120:121] op_sel_hi:[0,1,1] neg_lo:[1,0,0] neg_hi:[1,0,0]
	v_pk_fma_f32 v[122:123], v[62:63], v[46:47], v[122:123] op_sel_hi:[0,1,1] neg_lo:[1,0,0] neg_hi:[1,0,0]
	v_pk_fma_f32 v[124:125], v[62:63], v[76:77], v[124:125] op_sel_hi:[0,1,1] neg_lo:[1,0,0] neg_hi:[1,0,0]
	v_pk_mul_f32 v[126:127], v[62:63], v[130:131] op_sel:[1,0]
	v_pk_mul_f32 v[178:179], v[62:63], v[134:135] op_sel:[1,0]
	v_pk_mul_f32 v[190:191], v[62:63], v[106:107] op_sel:[1,0]
	s_waitcnt lgkmcnt(1)
	v_pk_mul_f32 v[140:141], v[64:65], v[130:131] op_sel_hi:[0,1]
	v_pk_mul_f32 v[182:183], v[64:65], v[134:135] op_sel_hi:[0,1]
	v_pk_mul_f32 v[210:211], v[64:65], v[106:107] op_sel_hi:[0,1]
	v_pk_mul_f32 v[174:175], v[64:65], v[130:131] op_sel:[1,0]
	v_pk_mul_f32 v[186:187], v[64:65], v[134:135] op_sel:[1,0]
	v_pk_mul_f32 v[212:213], v[64:65], v[106:107] op_sel:[1,0]
	v_pk_fma_f32 v[126:127], v[64:65], v[108:109], v[126:127] op_sel_hi:[0,1,1]
	v_pk_fma_f32 v[178:179], v[64:65], v[116:117], v[178:179] op_sel_hi:[0,1,1]
	v_pk_fma_f32 v[190:191], v[64:65], v[118:119], v[190:191] op_sel_hi:[0,1,1]
	v_pk_fma_f32 v[140:141], v[66:67], v[108:109], v[140:141] op_sel_hi:[0,1,1]
	v_pk_fma_f32 v[182:183], v[66:67], v[116:117], v[182:183] op_sel_hi:[0,1,1]
	v_pk_fma_f32 v[210:211], v[66:67], v[118:119], v[210:211] op_sel_hi:[0,1,1]
	v_pk_fma_f32 v[174:175], v[66:67], v[108:109], v[174:175] op_sel:[1,0,0]
	v_pk_fma_f32 v[186:187], v[66:67], v[116:117], v[186:187] op_sel:[1,0,0]
	v_pk_fma_f32 v[212:213], v[66:67], v[118:119], v[212:213] op_sel:[1,0,0]
	v_pk_fma_f32 v[126:127], v[64:65], v[120:121], v[126:127] op_sel:[1,0,0]
	v_pk_fma_f32 v[178:179], v[64:65], v[122:123], v[178:179] op_sel:[1,0,0]
	v_pk_fma_f32 v[190:191], v[64:65], v[124:125], v[190:191] op_sel:[1,0,0]
	v_pk_fma_f32 v[140:141], v[66:67], v[120:121], v[140:141] op_sel:[1,0,0]
	v_pk_fma_f32 v[182:183], v[66:67], v[122:123], v[182:183] op_sel:[1,0,0]
	v_pk_fma_f32 v[210:211], v[66:67], v[124:125], v[210:211] op_sel:[1,0,0]
	s_waitcnt lgkmcnt(0)
	v_pk_fma_f32 v[174:175], v[192:193], v[120:121], v[174:175] op_sel_hi:[0,1,1]
	v_pk_fma_f32 v[186:187], v[192:193], v[122:123], v[186:187] op_sel_hi:[0,1,1]
	v_pk_fma_f32 v[212:213], v[192:193], v[124:125], v[212:213] op_sel_hi:[0,1,1]
	v_pk_mul_f32 v[214:215], v[60:61], v[126:127] op_sel_hi:[0,1]
	v_pk_mul_f32 v[216:217], v[60:61], v[178:179] op_sel_hi:[0,1]
	v_pk_mul_f32 v[218:219], v[60:61], v[190:191] op_sel_hi:[0,1]
	v_pk_fma_f32 v[214:215], v[60:61], v[140:141], v[214:215] op_sel:[1,0,0]
	v_pk_fma_f32 v[216:217], v[60:61], v[182:183], v[216:217] op_sel:[1,0,0]
	v_pk_fma_f32 v[218:219], v[60:61], v[210:211], v[218:219] op_sel:[1,0,0]
	v_pk_fma_f32 v[214:215], v[62:63], v[174:175], v[214:215] op_sel_hi:[0,1,1]
	v_pk_fma_f32 v[216:217], v[62:63], v[186:187], v[216:217] op_sel_hi:[0,1,1]
	v_pk_fma_f32 v[218:219], v[62:63], v[212:213], v[218:219] op_sel_hi:[0,1,1]
	v_pk_fma_f32 v[214:215], v[192:193], v[2:3], v[214:215] op_sel:[1,0,0] neg_lo:[0,0,1] neg_hi:[0,0,1]
	v_pk_fma_f32 v[216:217], v[192:193], v[46:47], v[216:217] op_sel:[1,0,0] neg_lo:[0,0,1] neg_hi:[0,0,1]
	v_pk_fma_f32 v[218:219], v[192:193], v[76:77], v[218:219] op_sel:[1,0,0] neg_lo:[0,0,1] neg_hi:[0,0,1]
	v_cmp_eq_u32_e64 s[10:11], 1, v195
	v_cmp_eq_u32_e64 s[14:15], 2, v195
	v_cmp_eq_u32_e64 s[20:21], 3, v195
	v_cmp_eq_u32_e64 s[22:23], 4, v195
	v_cmp_eq_u32_e64 s[30:31], 5, v195
	v_cmp_eq_u32_e64 s[38:39], 6, v195
	v_pk_add_f32 v[2:3], v[72:73], v[126:127]
	v_pk_add_f32 v[46:47], v[114:115], v[178:179]
	v_pk_add_f32 v[72:73], v[138:139], v[190:191]
	v_pk_add_f32 v[76:77], v[148:149], v[140:141]
	v_pk_add_f32 v[106:107], v[150:151], v[182:183]
	v_pk_add_f32 v[108:109], v[156:157], v[210:211]
	v_pk_add_f32 v[114:115], v[160:161], v[174:175]
	v_pk_add_f32 v[116:117], v[164:165], v[186:187]
	v_pk_add_f32 v[118:119], v[176:177], v[212:213]
	v_pk_add_f32 v[120:121], v[180:181], v[214:215]
	v_pk_add_f32 v[122:123], v[184:185], v[216:217]
	v_pk_add_f32 v[124:125], v[188:189], v[218:219]
	v_pk_fma_f32 v[130:131], v[68:69], v[2:3], v[120:121] op_sel_hi:[0,1,1]
	v_pk_fma_f32 v[134:135], v[68:69], v[46:47], v[122:123] op_sel_hi:[0,1,1]
	v_pk_fma_f32 v[138:139], v[68:69], v[72:73], v[124:125] op_sel_hi:[0,1,1]
	v_pk_fma_f32 v[148:149], v[80:81], v[2:3], v[120:121] op_sel_hi:[0,1,1]
	v_pk_fma_f32 v[150:151], v[80:81], v[46:47], v[122:123] op_sel_hi:[0,1,1]
	v_pk_fma_f32 v[156:157], v[80:81], v[72:73], v[124:125] op_sel_hi:[0,1,1]
	v_pk_fma_f32 v[130:131], v[68:69], v[76:77], v[130:131] op_sel:[1,0,0]
	v_pk_fma_f32 v[134:135], v[68:69], v[106:107], v[134:135] op_sel:[1,0,0]
	v_pk_fma_f32 v[138:139], v[68:69], v[108:109], v[138:139] op_sel:[1,0,0]
	v_pk_fma_f32 v[148:149], v[80:81], v[76:77], v[148:149] op_sel:[1,0,0]
	v_pk_fma_f32 v[150:151], v[80:81], v[106:107], v[150:151] op_sel:[1,0,0]
	v_pk_fma_f32 v[156:157], v[80:81], v[108:109], v[156:157] op_sel:[1,0,0]
	v_pk_fma_f32 v[130:131], v[70:71], v[114:115], v[130:131] op_sel_hi:[0,1,1]
	v_pk_fma_f32 v[134:135], v[70:71], v[116:117], v[134:135] op_sel_hi:[0,1,1]
	v_pk_fma_f32 v[138:139], v[70:71], v[118:119], v[138:139] op_sel_hi:[0,1,1]
	v_pk_fma_f32 v[148:149], v[82:83], v[114:115], v[148:149] op_sel_hi:[0,1,1]
	v_pk_fma_f32 v[150:151], v[82:83], v[116:117], v[150:151] op_sel_hi:[0,1,1]
	v_pk_fma_f32 v[156:157], v[82:83], v[118:119], v[156:157] op_sel_hi:[0,1,1]
	v_pk_fma_f32 v[120:121], v[32:33], v[2:3], v[120:121] op_sel_hi:[0,1,1]
	v_pk_fma_f32 v[122:123], v[32:33], v[46:47], v[122:123] op_sel_hi:[0,1,1]
	v_pk_fma_f32 v[124:125], v[32:33], v[72:73], v[124:125] op_sel_hi:[0,1,1]
	v_pk_fma_f32 v[120:121], v[32:33], v[76:77], v[120:121] op_sel:[1,0,0]
	v_pk_fma_f32 v[122:123], v[32:33], v[106:107], v[122:123] op_sel:[1,0,0]
	v_pk_fma_f32 v[124:125], v[32:33], v[108:109], v[124:125] op_sel:[1,0,0]
	v_pk_fma_f32 v[120:121], v[34:35], v[114:115], v[120:121] op_sel_hi:[0,1,1]
	v_pk_fma_f32 v[122:123], v[34:35], v[116:117], v[122:123] op_sel_hi:[0,1,1]
	v_pk_fma_f32 v[124:125], v[34:35], v[118:119], v[124:125] op_sel_hi:[0,1,1]
	v_cndmask_b32_e64 v160, 0, v1, s[10:11]
	v_cndmask_b32_e64 v161, 0, v1, s[14:15]
	v_cndmask_b32_e64 v164, 0, v1, s[20:21]
	v_cndmask_b32_e64 v165, 0, v1, s[22:23]
	v_cndmask_b32_e64 v176, 0, v1, s[30:31]
	v_cndmask_b32_e64 v177, 0, v1, s[38:39]
	v_add_f32_dpp v120, v130, v120 wave_shl:1 row_mask:0xf bank_mask:0xf bound_ctrl:1
	v_add_f32_dpp v121, v131, v121 wave_shl:1 row_mask:0xf bank_mask:0xf bound_ctrl:1
	v_add_f32_dpp v122, v134, v122 wave_shl:1 row_mask:0xf bank_mask:0xf bound_ctrl:1
	v_add_f32_dpp v123, v135, v123 wave_shl:1 row_mask:0xf bank_mask:0xf bound_ctrl:1
	v_add_f32_dpp v124, v138, v124 wave_shl:1 row_mask:0xf bank_mask:0xf bound_ctrl:1
	v_add_f32_dpp v125, v139, v125 wave_shl:1 row_mask:0xf bank_mask:0xf bound_ctrl:1
	s_add_i32 s4, s34, 9
	s_cmpk_lt_i32 s4, 0x201
	s_cselect_b64 s[12:13], s[0:1], 0
	v_add_f32_dpp v120, v148, v120 wave_shr:1 row_mask:0xf bank_mask:0xf bound_ctrl:1
	v_add_f32_dpp v121, v149, v121 wave_shr:1 row_mask:0xf bank_mask:0xf bound_ctrl:1
	v_add_f32_dpp v122, v150, v122 wave_shr:1 row_mask:0xf bank_mask:0xf bound_ctrl:1
	v_add_f32_dpp v123, v151, v123 wave_shr:1 row_mask:0xf bank_mask:0xf bound_ctrl:1
	v_add_f32_dpp v124, v156, v124 wave_shr:1 row_mask:0xf bank_mask:0xf bound_ctrl:1
	v_add_f32_dpp v125, v157, v125 wave_shr:1 row_mask:0xf bank_mask:0xf bound_ctrl:1
	v_pk_fma_f32 v[120:121], v[12:13], v[194:195], v[120:121] op_sel_hi:[1,0,1] neg_lo:[0,0,1] neg_hi:[0,0,1]
	v_pk_fma_f32 v[122:123], v[14:15], v[194:195], v[122:123] op_sel_hi:[1,0,1] neg_lo:[0,0,1] neg_hi:[0,0,1]
	v_pk_fma_f32 v[124:125], v[16:17], v[194:195], v[124:125] op_sel_hi:[1,0,1] neg_lo:[0,0,1] neg_hi:[0,0,1]
	v_pk_add_f32 v[120:121], v[120:121], v[160:161] neg_lo:[0,1] neg_hi:[0,1]
	v_pk_add_f32 v[122:123], v[122:123], v[164:165] neg_lo:[0,1] neg_hi:[0,1]
	v_pk_add_f32 v[124:125], v[124:125], v[176:177] neg_lo:[0,1] neg_hi:[0,1]
	v_pk_mul_f32 v[180:181], v[120:121], v[120:121]
	v_pk_fma_f32 v[180:181], v[122:123], v[122:123], v[180:181]
	v_pk_fma_f32 v[180:181], v[124:125], v[124:125], v[180:181]
	v_add_f32_e32 v180, v180, v181
	v_cndmask_b32_e64 v181, 0, v180, s[12:13]
	v_add_f32_e32 v0, v0, v181
